# shallower strip pipelines (16 rows / 2 steps in flight) together with the all-wave row sharing
# speedup vs baseline: 1.0084x; 1.0057x over previous
;     ...
;     for (int kb = 0; kb < D / 64; ++kb) {
; #pragma unroll
;         for (int i = 0; i < 8; ++i) { const int k = 64 * kb + 8 * i + kr; const f32x4 v = __builtin_nontemporal_load((const f32x4*)(W + (size_t)k * pitch)) * g[k];
;             mx[0] = __builtin_fmaxf(mx[0], __builtin_fabsf(v[0])); mx[1] = __builtin_fmaxf(mx[1], __builtin_fabsf(v[1])); mx[2] = __builtin_fmaxf(mx[2], __builtin_fabsf(v[2])); mx[3] = __builtin_fmaxf(mx[3], __builtin_fabsf(v[3])); } }
.LBB0_127:
	v_readfirstlane_b32 s4, v2
	v_readfirstlane_b32 s5, v3
	v_readfirstlane_b32 s6, v4
	v_readfirstlane_b32 s7, v5
	s_nop 1
	v_subrev_u32_e32 v250, s4, v2
	v_subrev_u32_e32 v251, s6, v4
	s_nop 4
	global_load_dwordx4 v[106:109], v250, s[4:5] nt
	global_load_dword v170, v251, s[6:7] offset:-480
	s_add_u32 s4, s4, 0x18000
	s_addc_u32 s5, s5, 0
	global_load_dwordx4 v[110:113], v250, s[4:5] nt
	global_load_dword v172, v251, s[6:7] offset:-448
	s_add_u32 s4, s4, 0x18000
	s_addc_u32 s5, s5, 0
	global_load_dwordx4 v[114:117], v250, s[4:5] nt
	global_load_dword v174, v251, s[6:7] offset:-416
	s_add_u32 s4, s4, 0x18000
	s_addc_u32 s5, s5, 0
	global_load_dwordx4 v[118:121], v250, s[4:5] nt
	global_load_dword v176, v251, s[6:7] offset:-384
	s_add_u32 s4, s4, 0x18000
	s_addc_u32 s5, s5, 0
	global_load_dwordx4 v[122:125], v250, s[4:5] nt
	global_load_dword v178, v251, s[6:7] offset:-352
	s_add_u32 s4, s4, 0x18000
	s_addc_u32 s5, s5, 0
	global_load_dwordx4 v[126:129], v250, s[4:5] nt
	global_load_dword v180, v251, s[6:7] offset:-320
	s_add_u32 s4, s4, 0x18000
	s_addc_u32 s5, s5, 0
	global_load_dwordx4 v[130:133], v250, s[4:5] nt
	global_load_dword v182, v251, s[6:7] offset:-288
	s_add_u32 s4, s4, 0x18000
	s_addc_u32 s5, s5, 0
	global_load_dwordx4 v[134:137], v250, s[4:5] nt
	global_load_dword v184, v251, s[6:7] offset:-256
	s_add_u32 s4, s4, 0x18000
	s_addc_u32 s5, s5, 0
	global_load_dwordx4 v[138:141], v250, s[4:5] nt
	global_load_dword v186, v251, s[6:7] offset:-224
	s_add_u32 s4, s4, 0x18000
	s_addc_u32 s5, s5, 0
	global_load_dwordx4 v[142:145], v250, s[4:5] nt
	global_load_dword v188, v251, s[6:7] offset:-192
	s_add_u32 s4, s4, 0x18000
	s_addc_u32 s5, s5, 0
	global_load_dwordx4 v[146:149], v250, s[4:5] nt
	global_load_dword v190, v251, s[6:7] offset:-160
	s_add_u32 s4, s4, 0x18000
	s_addc_u32 s5, s5, 0
	global_load_dwordx4 v[150:153], v250, s[4:5] nt
	global_load_dword v192, v251, s[6:7] offset:-128
	s_add_u32 s4, s4, 0x18000
	s_addc_u32 s5, s5, 0
	global_load_dwordx4 v[154:157], v250, s[4:5] nt
	global_load_dword v194, v251, s[6:7] offset:-96
	s_add_u32 s4, s4, 0x18000
	s_addc_u32 s5, s5, 0
	global_load_dwordx4 v[158:161], v250, s[4:5] nt
	global_load_dword v196, v251, s[6:7] offset:-64
	s_add_u32 s4, s4, 0x18000
	s_addc_u32 s5, s5, 0
	global_load_dwordx4 v[162:165], v250, s[4:5] nt
	global_load_dword v198, v251, s[6:7] offset:-32
	s_add_u32 s4, s4, 0x18000
	s_addc_u32 s5, s5, 0
	global_load_dwordx4 v[166:169], v250, s[4:5] nt
	global_load_dword v200, v251, s[6:7]
	s_waitcnt vmcnt(28)
	v_pk_mul_f32 v[16:17], v[106:107], v[170:171] op_sel_hi:[1,0]
	v_pk_mul_f32 v[18:19], v[108:109], v[170:171] op_sel_hi:[1,0]
	v_pk_mul_f32 v[20:21], v[110:111], v[172:173] op_sel_hi:[1,0]
	v_pk_mul_f32 v[22:23], v[112:113], v[172:173] op_sel_hi:[1,0]
	v_max3_f32 v15, v15, |v16|, |v20|
	v_max3_f32 v13, v13, |v17|, |v21|
	v_max3_f32 v9, v9, |v18|, |v22|
	v_max3_f32 v7, v7, |v19|, |v23|
	s_add_u32 s4, s4, 0x18000
	s_addc_u32 s5, s5, 0
	global_load_dwordx4 v[106:109], v250, s[4:5] nt
	global_load_dword v170, v251, s[6:7] offset:32
	s_add_u32 s4, s4, 0x18000
	s_addc_u32 s5, s5, 0
	global_load_dwordx4 v[110:113], v250, s[4:5] nt
	global_load_dword v172, v251, s[6:7] offset:64
	s_waitcnt vmcnt(28)
	v_pk_mul_f32 v[16:17], v[114:115], v[174:175] op_sel_hi:[1,0]
	v_pk_mul_f32 v[18:19], v[116:117], v[174:175] op_sel_hi:[1,0]
	v_pk_mul_f32 v[20:21], v[118:119], v[176:177] op_sel_hi:[1,0]
	v_pk_mul_f32 v[22:23], v[120:121], v[176:177] op_sel_hi:[1,0]
	v_max3_f32 v15, v15, |v16|, |v20|
	v_max3_f32 v13, v13, |v17|, |v21|
	v_max3_f32 v9, v9, |v18|, |v22|
	v_max3_f32 v7, v7, |v19|, |v23|
	s_add_u32 s4, s4, 0x18000
	s_addc_u32 s5, s5, 0
	global_load_dwordx4 v[114:117], v250, s[4:5] nt
	global_load_dword v174, v251, s[6:7] offset:96
	s_add_u32 s4, s4, 0x18000
	s_addc_u32 s5, s5, 0
	global_load_dwordx4 v[118:121], v250, s[4:5] nt
	global_load_dword v176, v251, s[6:7] offset:128
	s_waitcnt vmcnt(28)
	v_pk_mul_f32 v[16:17], v[122:123], v[178:179] op_sel_hi:[1,0]
	v_pk_mul_f32 v[18:19], v[124:125], v[178:179] op_sel_hi:[1,0]
	v_pk_mul_f32 v[20:21], v[126:127], v[180:181] op_sel_hi:[1,0]
	v_pk_mul_f32 v[22:23], v[128:129], v[180:181] op_sel_hi:[1,0]
	v_max3_f32 v15, v15, |v16|, |v20|
	v_max3_f32 v13, v13, |v17|, |v21|
	v_max3_f32 v9, v9, |v18|, |v22|
	v_max3_f32 v7, v7, |v19|, |v23|
	s_add_u32 s4, s4, 0x18000
	s_addc_u32 s5, s5, 0
	global_load_dwordx4 v[122:125], v250, s[4:5] nt
	global_load_dword v178, v251, s[6:7] offset:160
	s_add_u32 s4, s4, 0x18000
	s_addc_u32 s5, s5, 0
	global_load_dwordx4 v[126:129], v250, s[4:5] nt
	global_load_dword v180, v251, s[6:7] offset:192
	s_waitcnt vmcnt(28)
	v_pk_mul_f32 v[16:17], v[130:131], v[182:183] op_sel_hi:[1,0]
	v_pk_mul_f32 v[18:19], v[132:133], v[182:183] op_sel_hi:[1,0]
	v_pk_mul_f32 v[20:21], v[134:135], v[184:185] op_sel_hi:[1,0]
	v_pk_mul_f32 v[22:23], v[136:137], v[184:185] op_sel_hi:[1,0]
	v_max3_f32 v15, v15, |v16|, |v20|
	v_max3_f32 v13, v13, |v17|, |v21|
	v_max3_f32 v9, v9, |v18|, |v22|
	v_max3_f32 v7, v7, |v19|, |v23|
	s_add_u32 s4, s4, 0x18000
	s_addc_u32 s5, s5, 0
	global_load_dwordx4 v[130:133], v250, s[4:5] nt
	global_load_dword v182, v251, s[6:7] offset:224
	s_add_u32 s4, s4, 0x18000
	s_addc_u32 s5, s5, 0
	global_load_dwordx4 v[134:137], v250, s[4:5] nt
	global_load_dword v184, v251, s[6:7] offset:256
	s_waitcnt vmcnt(28)
;     ...
;     for (int kb = 0; kb < D / 64; ++kb) {
; #pragma unroll
;         for (int i = 0; i < 8; ++i) { const int k = 64 * kb + 8 * i + kr; const f32x4 v = __builtin_nontemporal_load((const f32x4*)(W + (size_t)k * pitch)) * g[k];
;             mx[0] = __builtin_fmaxf(mx[0], __builtin_fabsf(v[0])); mx[1] = __builtin_fmaxf(mx[1], __builtin_fabsf(v[1])); mx[2] = __builtin_fmaxf(mx[2], __builtin_fabsf(v[2])); mx[3] = __builtin_fmaxf(mx[3], __builtin_fabsf(v[3])); } }
	v_pk_mul_f32 v[16:17], v[138:139], v[186:187] op_sel_hi:[1,0]
	v_pk_mul_f32 v[18:19], v[140:141], v[186:187] op_sel_hi:[1,0]
	v_pk_mul_f32 v[20:21], v[142:143], v[188:189] op_sel_hi:[1,0]
	v_pk_mul_f32 v[22:23], v[144:145], v[188:189] op_sel_hi:[1,0]
	v_max3_f32 v15, v15, |v16|, |v20|
	v_max3_f32 v13, v13, |v17|, |v21|
	v_max3_f32 v9, v9, |v18|, |v22|
	v_max3_f32 v7, v7, |v19|, |v23|
	s_add_u32 s4, s4, 0x18000
	s_addc_u32 s5, s5, 0
	global_load_dwordx4 v[138:141], v250, s[4:5] nt
	global_load_dword v186, v251, s[6:7] offset:288
	s_add_u32 s4, s4, 0x18000
	s_addc_u32 s5, s5, 0
	global_load_dwordx4 v[142:145], v250, s[4:5] nt
	global_load_dword v188, v251, s[6:7] offset:320
	s_waitcnt vmcnt(28)
	v_pk_mul_f32 v[16:17], v[146:147], v[190:191] op_sel_hi:[1,0]
	v_pk_mul_f32 v[18:19], v[148:149], v[190:191] op_sel_hi:[1,0]
	v_pk_mul_f32 v[20:21], v[150:151], v[192:193] op_sel_hi:[1,0]
	v_pk_mul_f32 v[22:23], v[152:153], v[192:193] op_sel_hi:[1,0]
	v_max3_f32 v15, v15, |v16|, |v20|
	v_max3_f32 v13, v13, |v17|, |v21|
	v_max3_f32 v9, v9, |v18|, |v22|
	v_max3_f32 v7, v7, |v19|, |v23|
	s_add_u32 s4, s4, 0x18000
	s_addc_u32 s5, s5, 0
	global_load_dwordx4 v[146:149], v250, s[4:5] nt
	global_load_dword v190, v251, s[6:7] offset:352
	s_add_u32 s4, s4, 0x18000
	s_addc_u32 s5, s5, 0
	global_load_dwordx4 v[150:153], v250, s[4:5] nt
	global_load_dword v192, v251, s[6:7] offset:384
	s_waitcnt vmcnt(28)
	v_pk_mul_f32 v[16:17], v[154:155], v[194:195] op_sel_hi:[1,0]
	v_pk_mul_f32 v[18:19], v[156:157], v[194:195] op_sel_hi:[1,0]
	v_pk_mul_f32 v[20:21], v[158:159], v[196:197] op_sel_hi:[1,0]
	v_pk_mul_f32 v[22:23], v[160:161], v[196:197] op_sel_hi:[1,0]
	v_max3_f32 v15, v15, |v16|, |v20|
	v_max3_f32 v13, v13, |v17|, |v21|
	v_max3_f32 v9, v9, |v18|, |v22|
	v_max3_f32 v7, v7, |v19|, |v23|
	s_add_u32 s4, s4, 0x18000
	s_addc_u32 s5, s5, 0
	global_load_dwordx4 v[154:157], v250, s[4:5] nt
	global_load_dword v194, v251, s[6:7] offset:416
	s_add_u32 s4, s4, 0x18000
	s_addc_u32 s5, s5, 0
	global_load_dwordx4 v[158:161], v250, s[4:5] nt
	global_load_dword v196, v251, s[6:7] offset:448
	s_waitcnt vmcnt(28)
	v_pk_mul_f32 v[16:17], v[162:163], v[198:199] op_sel_hi:[1,0]
	v_pk_mul_f32 v[18:19], v[164:165], v[198:199] op_sel_hi:[1,0]
	v_pk_mul_f32 v[20:21], v[166:167], v[200:201] op_sel_hi:[1,0]
	v_pk_mul_f32 v[22:23], v[168:169], v[200:201] op_sel_hi:[1,0]
	v_max3_f32 v15, v15, |v16|, |v20|
	v_max3_f32 v13, v13, |v17|, |v21|
	v_max3_f32 v9, v9, |v18|, |v22|
	v_max3_f32 v7, v7, |v19|, |v23|
	s_add_u32 s4, s4, 0x18000
	s_addc_u32 s5, s5, 0
	global_load_dwordx4 v[162:165], v250, s[4:5] nt
	global_load_dword v198, v251, s[6:7] offset:480
	s_add_u32 s4, s4, 0x18000
	s_addc_u32 s5, s5, 0
	global_load_dwordx4 v[166:169], v250, s[4:5] nt
	global_load_dword v200, v251, s[6:7] offset:512
	s_waitcnt vmcnt(28)
	v_pk_mul_f32 v[16:17], v[106:107], v[170:171] op_sel_hi:[1,0]
	v_pk_mul_f32 v[18:19], v[108:109], v[170:171] op_sel_hi:[1,0]
	v_pk_mul_f32 v[20:21], v[110:111], v[172:173] op_sel_hi:[1,0]
	v_pk_mul_f32 v[22:23], v[112:113], v[172:173] op_sel_hi:[1,0]
	v_max3_f32 v15, v15, |v16|, |v20|
	v_max3_f32 v13, v13, |v17|, |v21|
	v_max3_f32 v9, v9, |v18|, |v22|
	v_max3_f32 v7, v7, |v19|, |v23|
	s_add_u32 s4, s4, 0x18000
	s_addc_u32 s5, s5, 0
	global_load_dwordx4 v[106:109], v250, s[4:5] nt
	global_load_dword v170, v251, s[6:7] offset:544
	s_add_u32 s4, s4, 0x18000
	s_addc_u32 s5, s5, 0
	global_load_dwordx4 v[110:113], v250, s[4:5] nt
	global_load_dword v172, v251, s[6:7] offset:576
	s_waitcnt vmcnt(28)
	v_pk_mul_f32 v[16:17], v[114:115], v[174:175] op_sel_hi:[1,0]
	v_pk_mul_f32 v[18:19], v[116:117], v[174:175] op_sel_hi:[1,0]
	v_pk_mul_f32 v[20:21], v[118:119], v[176:177] op_sel_hi:[1,0]
	v_pk_mul_f32 v[22:23], v[120:121], v[176:177] op_sel_hi:[1,0]
	v_max3_f32 v15, v15, |v16|, |v20|
	v_max3_f32 v13, v13, |v17|, |v21|
	v_max3_f32 v9, v9, |v18|, |v22|
	v_max3_f32 v7, v7, |v19|, |v23|
	s_add_u32 s4, s4, 0x18000
	s_addc_u32 s5, s5, 0
	global_load_dwordx4 v[114:117], v250, s[4:5] nt
	global_load_dword v174, v251, s[6:7] offset:608
	s_add_u32 s4, s4, 0x18000
	s_addc_u32 s5, s5, 0
	global_load_dwordx4 v[118:121], v250, s[4:5] nt
	global_load_dword v176, v251, s[6:7] offset:640
	s_waitcnt vmcnt(28)
	v_pk_mul_f32 v[16:17], v[122:123], v[178:179] op_sel_hi:[1,0]
	v_pk_mul_f32 v[18:19], v[124:125], v[178:179] op_sel_hi:[1,0]
	v_pk_mul_f32 v[20:21], v[126:127], v[180:181] op_sel_hi:[1,0]
	v_pk_mul_f32 v[22:23], v[128:129], v[180:181] op_sel_hi:[1,0]
	v_max3_f32 v15, v15, |v16|, |v20|
	v_max3_f32 v13, v13, |v17|, |v21|
	v_max3_f32 v9, v9, |v18|, |v22|
	v_max3_f32 v7, v7, |v19|, |v23|
	s_add_u32 s4, s4, 0x18000
	s_addc_u32 s5, s5, 0
	global_load_dwordx4 v[122:125], v250, s[4:5] nt
	global_load_dword v178, v251, s[6:7] offset:672
	s_add_u32 s4, s4, 0x18000
	s_addc_u32 s5, s5, 0
	global_load_dwordx4 v[126:129], v250, s[4:5] nt
	global_load_dword v180, v251, s[6:7] offset:704
	s_waitcnt vmcnt(28)
	v_pk_mul_f32 v[16:17], v[130:131], v[182:183] op_sel_hi:[1,0]
	v_pk_mul_f32 v[18:19], v[132:133], v[182:183] op_sel_hi:[1,0]
	v_pk_mul_f32 v[20:21], v[134:135], v[184:185] op_sel_hi:[1,0]
	v_pk_mul_f32 v[22:23], v[136:137], v[184:185] op_sel_hi:[1,0]
	v_max3_f32 v15, v15, |v16|, |v20|
	v_max3_f32 v13, v13, |v17|, |v21|
	v_max3_f32 v9, v9, |v18|, |v22|
	v_max3_f32 v7, v7, |v19|, |v23|
	s_add_u32 s4, s4, 0x18000
	s_addc_u32 s5, s5, 0
	global_load_dwordx4 v[130:133], v250, s[4:5] nt
	global_load_dword v182, v251, s[6:7] offset:736
	s_add_u32 s4, s4, 0x18000
	s_addc_u32 s5, s5, 0
	global_load_dwordx4 v[134:137], v250, s[4:5] nt
	global_load_dword v184, v251, s[6:7] offset:768
	s_waitcnt vmcnt(28)
;     ...
;     for (int kb = 0; kb < D / 64; ++kb) {
; #pragma unroll
;         for (int i = 0; i < 8; ++i) { const int k = 64 * kb + 8 * i + kr; const f32x4 v = __builtin_nontemporal_load((const f32x4*)(W + (size_t)k * pitch)) * g[k];
;             mx[0] = __builtin_fmaxf(mx[0], __builtin_fabsf(v[0])); mx[1] = __builtin_fmaxf(mx[1], __builtin_fabsf(v[1])); mx[2] = __builtin_fmaxf(mx[2], __builtin_fabsf(v[2])); mx[3] = __builtin_fmaxf(mx[3], __builtin_fabsf(v[3])); } }
	v_pk_mul_f32 v[16:17], v[138:139], v[186:187] op_sel_hi:[1,0]
	v_pk_mul_f32 v[18:19], v[140:141], v[186:187] op_sel_hi:[1,0]
	v_pk_mul_f32 v[20:21], v[142:143], v[188:189] op_sel_hi:[1,0]
	v_pk_mul_f32 v[22:23], v[144:145], v[188:189] op_sel_hi:[1,0]
	v_max3_f32 v15, v15, |v16|, |v20|
	v_max3_f32 v13, v13, |v17|, |v21|
	v_max3_f32 v9, v9, |v18|, |v22|
	v_max3_f32 v7, v7, |v19|, |v23|
	s_add_u32 s4, s4, 0x18000
	s_addc_u32 s5, s5, 0
	global_load_dwordx4 v[138:141], v250, s[4:5] nt
	global_load_dword v186, v251, s[6:7] offset:800
	s_add_u32 s4, s4, 0x18000
	s_addc_u32 s5, s5, 0
	global_load_dwordx4 v[142:145], v250, s[4:5] nt
	global_load_dword v188, v251, s[6:7] offset:832
	s_waitcnt vmcnt(28)
	v_pk_mul_f32 v[16:17], v[146:147], v[190:191] op_sel_hi:[1,0]
	v_pk_mul_f32 v[18:19], v[148:149], v[190:191] op_sel_hi:[1,0]
	v_pk_mul_f32 v[20:21], v[150:151], v[192:193] op_sel_hi:[1,0]
	v_pk_mul_f32 v[22:23], v[152:153], v[192:193] op_sel_hi:[1,0]
	v_max3_f32 v15, v15, |v16|, |v20|
	v_max3_f32 v13, v13, |v17|, |v21|
	v_max3_f32 v9, v9, |v18|, |v22|
	v_max3_f32 v7, v7, |v19|, |v23|
	s_add_u32 s4, s4, 0x18000
	s_addc_u32 s5, s5, 0
	global_load_dwordx4 v[146:149], v250, s[4:5] nt
	global_load_dword v190, v251, s[6:7] offset:864
	s_add_u32 s4, s4, 0x18000
	s_addc_u32 s5, s5, 0
	global_load_dwordx4 v[150:153], v250, s[4:5] nt
	global_load_dword v192, v251, s[6:7] offset:896
	s_waitcnt vmcnt(28)
	v_pk_mul_f32 v[16:17], v[154:155], v[194:195] op_sel_hi:[1,0]
	v_pk_mul_f32 v[18:19], v[156:157], v[194:195] op_sel_hi:[1,0]
	v_pk_mul_f32 v[20:21], v[158:159], v[196:197] op_sel_hi:[1,0]
	v_pk_mul_f32 v[22:23], v[160:161], v[196:197] op_sel_hi:[1,0]
	v_max3_f32 v15, v15, |v16|, |v20|
	v_max3_f32 v13, v13, |v17|, |v21|
	v_max3_f32 v9, v9, |v18|, |v22|
	v_max3_f32 v7, v7, |v19|, |v23|
	s_add_u32 s4, s4, 0x18000
	s_addc_u32 s5, s5, 0
	global_load_dwordx4 v[154:157], v250, s[4:5] nt
	global_load_dword v194, v251, s[6:7] offset:928
	s_add_u32 s4, s4, 0x18000
	s_addc_u32 s5, s5, 0
	global_load_dwordx4 v[158:161], v250, s[4:5] nt
	global_load_dword v196, v251, s[6:7] offset:960
	s_waitcnt vmcnt(28)
	v_pk_mul_f32 v[16:17], v[162:163], v[198:199] op_sel_hi:[1,0]
	v_pk_mul_f32 v[18:19], v[164:165], v[198:199] op_sel_hi:[1,0]
	v_pk_mul_f32 v[20:21], v[166:167], v[200:201] op_sel_hi:[1,0]
	v_pk_mul_f32 v[22:23], v[168:169], v[200:201] op_sel_hi:[1,0]
	v_max3_f32 v15, v15, |v16|, |v20|
	v_max3_f32 v13, v13, |v17|, |v21|
	v_max3_f32 v9, v9, |v18|, |v22|
	v_max3_f32 v7, v7, |v19|, |v23|
	s_add_u32 s4, s4, 0x18000
	s_addc_u32 s5, s5, 0
	global_load_dwordx4 v[162:165], v250, s[4:5] nt
	global_load_dword v198, v251, s[6:7] offset:992
	s_add_u32 s4, s4, 0x18000
	s_addc_u32 s5, s5, 0
	global_load_dwordx4 v[166:169], v250, s[4:5] nt
	global_load_dword v200, v251, s[6:7] offset:1024
	s_waitcnt vmcnt(28)
	v_pk_mul_f32 v[16:17], v[106:107], v[170:171] op_sel_hi:[1,0]
	v_pk_mul_f32 v[18:19], v[108:109], v[170:171] op_sel_hi:[1,0]
	v_pk_mul_f32 v[20:21], v[110:111], v[172:173] op_sel_hi:[1,0]
	v_pk_mul_f32 v[22:23], v[112:113], v[172:173] op_sel_hi:[1,0]
	v_max3_f32 v15, v15, |v16|, |v20|
	v_max3_f32 v13, v13, |v17|, |v21|
	v_max3_f32 v9, v9, |v18|, |v22|
	v_max3_f32 v7, v7, |v19|, |v23|
	s_add_u32 s4, s4, 0x18000
	s_addc_u32 s5, s5, 0
	global_load_dwordx4 v[106:109], v250, s[4:5] nt
	global_load_dword v170, v251, s[6:7] offset:1056
	s_add_u32 s4, s4, 0x18000
	s_addc_u32 s5, s5, 0
	global_load_dwordx4 v[110:113], v250, s[4:5] nt
	global_load_dword v172, v251, s[6:7] offset:1088
	s_waitcnt vmcnt(28)
	v_pk_mul_f32 v[16:17], v[114:115], v[174:175] op_sel_hi:[1,0]
	v_pk_mul_f32 v[18:19], v[116:117], v[174:175] op_sel_hi:[1,0]
	v_pk_mul_f32 v[20:21], v[118:119], v[176:177] op_sel_hi:[1,0]
	v_pk_mul_f32 v[22:23], v[120:121], v[176:177] op_sel_hi:[1,0]
	v_max3_f32 v15, v15, |v16|, |v20|
	v_max3_f32 v13, v13, |v17|, |v21|
	v_max3_f32 v9, v9, |v18|, |v22|
	v_max3_f32 v7, v7, |v19|, |v23|
	s_add_u32 s4, s4, 0x18000
	s_addc_u32 s5, s5, 0
	global_load_dwordx4 v[114:117], v250, s[4:5] nt
	global_load_dword v174, v251, s[6:7] offset:1120
	s_add_u32 s4, s4, 0x18000
	s_addc_u32 s5, s5, 0
	global_load_dwordx4 v[118:121], v250, s[4:5] nt
	global_load_dword v176, v251, s[6:7] offset:1152
	s_waitcnt vmcnt(28)
	v_pk_mul_f32 v[16:17], v[122:123], v[178:179] op_sel_hi:[1,0]
	v_pk_mul_f32 v[18:19], v[124:125], v[178:179] op_sel_hi:[1,0]
	v_pk_mul_f32 v[20:21], v[126:127], v[180:181] op_sel_hi:[1,0]
	v_pk_mul_f32 v[22:23], v[128:129], v[180:181] op_sel_hi:[1,0]
	v_max3_f32 v15, v15, |v16|, |v20|
	v_max3_f32 v13, v13, |v17|, |v21|
	v_max3_f32 v9, v9, |v18|, |v22|
	v_max3_f32 v7, v7, |v19|, |v23|
	s_add_u32 s4, s4, 0x18000
	s_addc_u32 s5, s5, 0
	global_load_dwordx4 v[122:125], v250, s[4:5] nt
	global_load_dword v178, v251, s[6:7] offset:1184
	s_add_u32 s4, s4, 0x18000
	s_addc_u32 s5, s5, 0
	global_load_dwordx4 v[126:129], v250, s[4:5] nt
	global_load_dword v180, v251, s[6:7] offset:1216
	s_waitcnt vmcnt(28)
	v_pk_mul_f32 v[16:17], v[130:131], v[182:183] op_sel_hi:[1,0]
	v_pk_mul_f32 v[18:19], v[132:133], v[182:183] op_sel_hi:[1,0]
	v_pk_mul_f32 v[20:21], v[134:135], v[184:185] op_sel_hi:[1,0]
	v_pk_mul_f32 v[22:23], v[136:137], v[184:185] op_sel_hi:[1,0]
	v_max3_f32 v15, v15, |v16|, |v20|
	v_max3_f32 v13, v13, |v17|, |v21|
	v_max3_f32 v9, v9, |v18|, |v22|
	v_max3_f32 v7, v7, |v19|, |v23|
	s_add_u32 s4, s4, 0x18000
	s_addc_u32 s5, s5, 0
	global_load_dwordx4 v[130:133], v250, s[4:5] nt
	global_load_dword v182, v251, s[6:7] offset:1248
	s_add_u32 s4, s4, 0x18000
	s_addc_u32 s5, s5, 0
	global_load_dwordx4 v[134:137], v250, s[4:5] nt
	global_load_dword v184, v251, s[6:7] offset:1280
	s_waitcnt vmcnt(28)
;     ...
;     for (int kb = 0; kb < D / 64; ++kb) {
; #pragma unroll
;         for (int i = 0; i < 8; ++i) { const int k = 64 * kb + 8 * i + kr; const f32x4 v = __builtin_nontemporal_load((const f32x4*)(W + (size_t)k * pitch)) * g[k];
;             mx[0] = __builtin_fmaxf(mx[0], __builtin_fabsf(v[0])); mx[1] = __builtin_fmaxf(mx[1], __builtin_fabsf(v[1])); mx[2] = __builtin_fmaxf(mx[2], __builtin_fabsf(v[2])); mx[3] = __builtin_fmaxf(mx[3], __builtin_fabsf(v[3])); } }
	v_pk_mul_f32 v[16:17], v[138:139], v[186:187] op_sel_hi:[1,0]
	v_pk_mul_f32 v[18:19], v[140:141], v[186:187] op_sel_hi:[1,0]
	v_pk_mul_f32 v[20:21], v[142:143], v[188:189] op_sel_hi:[1,0]
	v_pk_mul_f32 v[22:23], v[144:145], v[188:189] op_sel_hi:[1,0]
	v_max3_f32 v15, v15, |v16|, |v20|
	v_max3_f32 v13, v13, |v17|, |v21|
	v_max3_f32 v9, v9, |v18|, |v22|
	v_max3_f32 v7, v7, |v19|, |v23|
	s_add_u32 s4, s4, 0x18000
	s_addc_u32 s5, s5, 0
	global_load_dwordx4 v[138:141], v250, s[4:5] nt
	global_load_dword v186, v251, s[6:7] offset:1312
	s_add_u32 s4, s4, 0x18000
	s_addc_u32 s5, s5, 0
	global_load_dwordx4 v[142:145], v250, s[4:5] nt
	global_load_dword v188, v251, s[6:7] offset:1344
	s_waitcnt vmcnt(28)
	v_pk_mul_f32 v[16:17], v[146:147], v[190:191] op_sel_hi:[1,0]
	v_pk_mul_f32 v[18:19], v[148:149], v[190:191] op_sel_hi:[1,0]
	v_pk_mul_f32 v[20:21], v[150:151], v[192:193] op_sel_hi:[1,0]
	v_pk_mul_f32 v[22:23], v[152:153], v[192:193] op_sel_hi:[1,0]
	v_max3_f32 v15, v15, |v16|, |v20|
	v_max3_f32 v13, v13, |v17|, |v21|
	v_max3_f32 v9, v9, |v18|, |v22|
	v_max3_f32 v7, v7, |v19|, |v23|
	s_add_u32 s4, s4, 0x18000
	s_addc_u32 s5, s5, 0
	global_load_dwordx4 v[146:149], v250, s[4:5] nt
	global_load_dword v190, v251, s[6:7] offset:1376
	s_add_u32 s4, s4, 0x18000
	s_addc_u32 s5, s5, 0
	global_load_dwordx4 v[150:153], v250, s[4:5] nt
	global_load_dword v192, v251, s[6:7] offset:1408
	s_waitcnt vmcnt(28)
	v_pk_mul_f32 v[16:17], v[154:155], v[194:195] op_sel_hi:[1,0]
	v_pk_mul_f32 v[18:19], v[156:157], v[194:195] op_sel_hi:[1,0]
	v_pk_mul_f32 v[20:21], v[158:159], v[196:197] op_sel_hi:[1,0]
	v_pk_mul_f32 v[22:23], v[160:161], v[196:197] op_sel_hi:[1,0]
	v_max3_f32 v15, v15, |v16|, |v20|
	v_max3_f32 v13, v13, |v17|, |v21|
	v_max3_f32 v9, v9, |v18|, |v22|
	v_max3_f32 v7, v7, |v19|, |v23|
	s_add_u32 s4, s4, 0x18000
	s_addc_u32 s5, s5, 0
	global_load_dwordx4 v[154:157], v250, s[4:5] nt
	global_load_dword v194, v251, s[6:7] offset:1440
	s_add_u32 s4, s4, 0x18000
	s_addc_u32 s5, s5, 0
	global_load_dwordx4 v[158:161], v250, s[4:5] nt
	global_load_dword v196, v251, s[6:7] offset:1472
	s_waitcnt vmcnt(28)
	v_pk_mul_f32 v[16:17], v[162:163], v[198:199] op_sel_hi:[1,0]
	v_pk_mul_f32 v[18:19], v[164:165], v[198:199] op_sel_hi:[1,0]
	v_pk_mul_f32 v[20:21], v[166:167], v[200:201] op_sel_hi:[1,0]
	v_pk_mul_f32 v[22:23], v[168:169], v[200:201] op_sel_hi:[1,0]
	v_max3_f32 v15, v15, |v16|, |v20|
	v_max3_f32 v13, v13, |v17|, |v21|
	v_max3_f32 v9, v9, |v18|, |v22|
	v_max3_f32 v7, v7, |v19|, |v23|
	s_add_u32 s4, s4, 0x18000
	s_addc_u32 s5, s5, 0
	global_load_dwordx4 v[162:165], v250, s[4:5] nt
	global_load_dword v198, v251, s[6:7] offset:1504
	s_add_u32 s4, s4, 0x18000
	s_addc_u32 s5, s5, 0
	global_load_dwordx4 v[166:169], v250, s[4:5] nt
	global_load_dword v200, v251, s[6:7] offset:1536
	s_waitcnt vmcnt(28)
	v_pk_mul_f32 v[16:17], v[106:107], v[170:171] op_sel_hi:[1,0]
	v_pk_mul_f32 v[18:19], v[108:109], v[170:171] op_sel_hi:[1,0]
	v_pk_mul_f32 v[20:21], v[110:111], v[172:173] op_sel_hi:[1,0]
	v_pk_mul_f32 v[22:23], v[112:113], v[172:173] op_sel_hi:[1,0]
	v_max3_f32 v15, v15, |v16|, |v20|
	v_max3_f32 v13, v13, |v17|, |v21|
	v_max3_f32 v9, v9, |v18|, |v22|
	v_max3_f32 v7, v7, |v19|, |v23|
	s_add_u32 s4, s4, 0x18000
	s_addc_u32 s5, s5, 0
	global_load_dwordx4 v[106:109], v250, s[4:5] nt
	global_load_dword v170, v251, s[6:7] offset:1568
	s_add_u32 s4, s4, 0x18000
	s_addc_u32 s5, s5, 0
	global_load_dwordx4 v[110:113], v250, s[4:5] nt
	global_load_dword v172, v251, s[6:7] offset:1600
	s_waitcnt vmcnt(28)
	v_pk_mul_f32 v[16:17], v[114:115], v[174:175] op_sel_hi:[1,0]
	v_pk_mul_f32 v[18:19], v[116:117], v[174:175] op_sel_hi:[1,0]
	v_pk_mul_f32 v[20:21], v[118:119], v[176:177] op_sel_hi:[1,0]
	v_pk_mul_f32 v[22:23], v[120:121], v[176:177] op_sel_hi:[1,0]
	v_max3_f32 v15, v15, |v16|, |v20|
	v_max3_f32 v13, v13, |v17|, |v21|
	v_max3_f32 v9, v9, |v18|, |v22|
	v_max3_f32 v7, v7, |v19|, |v23|
	s_add_u32 s4, s4, 0x18000
	s_addc_u32 s5, s5, 0
	global_load_dwordx4 v[114:117], v250, s[4:5] nt
	global_load_dword v174, v251, s[6:7] offset:1632
	s_add_u32 s4, s4, 0x18000
	s_addc_u32 s5, s5, 0
	global_load_dwordx4 v[118:121], v250, s[4:5] nt
	global_load_dword v176, v251, s[6:7] offset:1664
	s_waitcnt vmcnt(28)
	v_pk_mul_f32 v[16:17], v[122:123], v[178:179] op_sel_hi:[1,0]
	v_pk_mul_f32 v[18:19], v[124:125], v[178:179] op_sel_hi:[1,0]
	v_pk_mul_f32 v[20:21], v[126:127], v[180:181] op_sel_hi:[1,0]
	v_pk_mul_f32 v[22:23], v[128:129], v[180:181] op_sel_hi:[1,0]
	v_max3_f32 v15, v15, |v16|, |v20|
	v_max3_f32 v13, v13, |v17|, |v21|
	v_max3_f32 v9, v9, |v18|, |v22|
	v_max3_f32 v7, v7, |v19|, |v23|
	s_add_u32 s4, s4, 0x18000
	s_addc_u32 s5, s5, 0
	global_load_dwordx4 v[122:125], v250, s[4:5] nt
	global_load_dword v178, v251, s[6:7] offset:1696
	s_add_u32 s4, s4, 0x18000
	s_addc_u32 s5, s5, 0
	global_load_dwordx4 v[126:129], v250, s[4:5] nt
	global_load_dword v180, v251, s[6:7] offset:1728
	s_waitcnt vmcnt(28)
	v_pk_mul_f32 v[16:17], v[130:131], v[182:183] op_sel_hi:[1,0]
	v_pk_mul_f32 v[18:19], v[132:133], v[182:183] op_sel_hi:[1,0]
	v_pk_mul_f32 v[20:21], v[134:135], v[184:185] op_sel_hi:[1,0]
	v_pk_mul_f32 v[22:23], v[136:137], v[184:185] op_sel_hi:[1,0]
	v_max3_f32 v15, v15, |v16|, |v20|
	v_max3_f32 v13, v13, |v17|, |v21|
	v_max3_f32 v9, v9, |v18|, |v22|
	v_max3_f32 v7, v7, |v19|, |v23|
	s_add_u32 s4, s4, 0x18000
	s_addc_u32 s5, s5, 0
	global_load_dwordx4 v[130:133], v250, s[4:5] nt
	global_load_dword v182, v251, s[6:7] offset:1760
	s_add_u32 s4, s4, 0x18000
	s_addc_u32 s5, s5, 0
	global_load_dwordx4 v[134:137], v250, s[4:5] nt
	global_load_dword v184, v251, s[6:7] offset:1792
	s_waitcnt vmcnt(28)
;     ...
;     for (int kb = 0; kb < D / 64; ++kb) {
; #pragma unroll
;         for (int i = 0; i < 8; ++i) { const int k = 64 * kb + 8 * i + kr; const f32x4 v = __builtin_nontemporal_load((const f32x4*)(W + (size_t)k * pitch)) * g[k];
;             mx[0] = __builtin_fmaxf(mx[0], __builtin_fabsf(v[0])); mx[1] = __builtin_fmaxf(mx[1], __builtin_fabsf(v[1])); mx[2] = __builtin_fmaxf(mx[2], __builtin_fabsf(v[2])); mx[3] = __builtin_fmaxf(mx[3], __builtin_fabsf(v[3])); } }
	v_pk_mul_f32 v[16:17], v[138:139], v[186:187] op_sel_hi:[1,0]
	v_pk_mul_f32 v[18:19], v[140:141], v[186:187] op_sel_hi:[1,0]
	v_pk_mul_f32 v[20:21], v[142:143], v[188:189] op_sel_hi:[1,0]
	v_pk_mul_f32 v[22:23], v[144:145], v[188:189] op_sel_hi:[1,0]
	v_max3_f32 v15, v15, |v16|, |v20|
	v_max3_f32 v13, v13, |v17|, |v21|
	v_max3_f32 v9, v9, |v18|, |v22|
	v_max3_f32 v7, v7, |v19|, |v23|
	s_add_u32 s4, s4, 0x18000
	s_addc_u32 s5, s5, 0
	global_load_dwordx4 v[138:141], v250, s[4:5] nt
	global_load_dword v186, v251, s[6:7] offset:1824
	s_add_u32 s4, s4, 0x18000
	s_addc_u32 s5, s5, 0
	global_load_dwordx4 v[142:145], v250, s[4:5] nt
	global_load_dword v188, v251, s[6:7] offset:1856
	s_waitcnt vmcnt(28)
	v_pk_mul_f32 v[16:17], v[146:147], v[190:191] op_sel_hi:[1,0]
	v_pk_mul_f32 v[18:19], v[148:149], v[190:191] op_sel_hi:[1,0]
	v_pk_mul_f32 v[20:21], v[150:151], v[192:193] op_sel_hi:[1,0]
	v_pk_mul_f32 v[22:23], v[152:153], v[192:193] op_sel_hi:[1,0]
	v_max3_f32 v15, v15, |v16|, |v20|
	v_max3_f32 v13, v13, |v17|, |v21|
	v_max3_f32 v9, v9, |v18|, |v22|
	v_max3_f32 v7, v7, |v19|, |v23|
	s_add_u32 s4, s4, 0x18000
	s_addc_u32 s5, s5, 0
	global_load_dwordx4 v[146:149], v250, s[4:5] nt
	global_load_dword v190, v251, s[6:7] offset:1888
	s_add_u32 s4, s4, 0x18000
	s_addc_u32 s5, s5, 0
	global_load_dwordx4 v[150:153], v250, s[4:5] nt
	global_load_dword v192, v251, s[6:7] offset:1920
	s_waitcnt vmcnt(28)
	v_pk_mul_f32 v[16:17], v[154:155], v[194:195] op_sel_hi:[1,0]
	v_pk_mul_f32 v[18:19], v[156:157], v[194:195] op_sel_hi:[1,0]
	v_pk_mul_f32 v[20:21], v[158:159], v[196:197] op_sel_hi:[1,0]
	v_pk_mul_f32 v[22:23], v[160:161], v[196:197] op_sel_hi:[1,0]
	v_max3_f32 v15, v15, |v16|, |v20|
	v_max3_f32 v13, v13, |v17|, |v21|
	v_max3_f32 v9, v9, |v18|, |v22|
	v_max3_f32 v7, v7, |v19|, |v23|
	s_add_u32 s4, s4, 0x18000
	s_addc_u32 s5, s5, 0
	global_load_dwordx4 v[154:157], v250, s[4:5] nt
	global_load_dword v194, v251, s[6:7] offset:1952
	s_add_u32 s4, s4, 0x18000
	s_addc_u32 s5, s5, 0
	global_load_dwordx4 v[158:161], v250, s[4:5] nt
	global_load_dword v196, v251, s[6:7] offset:1984
	s_waitcnt vmcnt(28)
	v_pk_mul_f32 v[16:17], v[162:163], v[198:199] op_sel_hi:[1,0]
	v_pk_mul_f32 v[18:19], v[164:165], v[198:199] op_sel_hi:[1,0]
	v_pk_mul_f32 v[20:21], v[166:167], v[200:201] op_sel_hi:[1,0]
	v_pk_mul_f32 v[22:23], v[168:169], v[200:201] op_sel_hi:[1,0]
	v_max3_f32 v15, v15, |v16|, |v20|
	v_max3_f32 v13, v13, |v17|, |v21|
	v_max3_f32 v9, v9, |v18|, |v22|
	v_max3_f32 v7, v7, |v19|, |v23|
	s_add_u32 s4, s4, 0x18000
	s_addc_u32 s5, s5, 0
	global_load_dwordx4 v[162:165], v250, s[4:5] nt
	global_load_dword v198, v251, s[6:7] offset:2016
	s_add_u32 s4, s4, 0x18000
	s_addc_u32 s5, s5, 0
	global_load_dwordx4 v[166:169], v250, s[4:5] nt
	global_load_dword v200, v251, s[6:7] offset:2048
	s_waitcnt vmcnt(28)
	v_pk_mul_f32 v[16:17], v[106:107], v[170:171] op_sel_hi:[1,0]
	v_pk_mul_f32 v[18:19], v[108:109], v[170:171] op_sel_hi:[1,0]
	v_pk_mul_f32 v[20:21], v[110:111], v[172:173] op_sel_hi:[1,0]
	v_pk_mul_f32 v[22:23], v[112:113], v[172:173] op_sel_hi:[1,0]
	v_max3_f32 v15, v15, |v16|, |v20|
	v_max3_f32 v13, v13, |v17|, |v21|
	v_max3_f32 v9, v9, |v18|, |v22|
	v_max3_f32 v7, v7, |v19|, |v23|
	s_add_u32 s4, s4, 0x18000
	s_addc_u32 s5, s5, 0
	global_load_dwordx4 v[106:109], v250, s[4:5] nt
	global_load_dword v170, v251, s[6:7] offset:2080
	s_add_u32 s4, s4, 0x18000
	s_addc_u32 s5, s5, 0
	global_load_dwordx4 v[110:113], v250, s[4:5] nt
	global_load_dword v172, v251, s[6:7] offset:2112
	s_waitcnt vmcnt(28)
	v_pk_mul_f32 v[16:17], v[114:115], v[174:175] op_sel_hi:[1,0]
	v_pk_mul_f32 v[18:19], v[116:117], v[174:175] op_sel_hi:[1,0]
	v_pk_mul_f32 v[20:21], v[118:119], v[176:177] op_sel_hi:[1,0]
	v_pk_mul_f32 v[22:23], v[120:121], v[176:177] op_sel_hi:[1,0]
	v_max3_f32 v15, v15, |v16|, |v20|
	v_max3_f32 v13, v13, |v17|, |v21|
	v_max3_f32 v9, v9, |v18|, |v22|
	v_max3_f32 v7, v7, |v19|, |v23|
	s_add_u32 s4, s4, 0x18000
	s_addc_u32 s5, s5, 0
	global_load_dwordx4 v[114:117], v250, s[4:5] nt
	global_load_dword v174, v251, s[6:7] offset:2144
	s_add_u32 s4, s4, 0x18000
	s_addc_u32 s5, s5, 0
	global_load_dwordx4 v[118:121], v250, s[4:5] nt
	global_load_dword v176, v251, s[6:7] offset:2176
	s_waitcnt vmcnt(28)
	v_pk_mul_f32 v[16:17], v[122:123], v[178:179] op_sel_hi:[1,0]
	v_pk_mul_f32 v[18:19], v[124:125], v[178:179] op_sel_hi:[1,0]
	v_pk_mul_f32 v[20:21], v[126:127], v[180:181] op_sel_hi:[1,0]
	v_pk_mul_f32 v[22:23], v[128:129], v[180:181] op_sel_hi:[1,0]
	v_max3_f32 v15, v15, |v16|, |v20|
	v_max3_f32 v13, v13, |v17|, |v21|
	v_max3_f32 v9, v9, |v18|, |v22|
	v_max3_f32 v7, v7, |v19|, |v23|
	s_add_u32 s4, s4, 0x18000
	s_addc_u32 s5, s5, 0
	global_load_dwordx4 v[122:125], v250, s[4:5] nt
	global_load_dword v178, v251, s[6:7] offset:2208
	s_add_u32 s4, s4, 0x18000
	s_addc_u32 s5, s5, 0
	global_load_dwordx4 v[126:129], v250, s[4:5] nt
	global_load_dword v180, v251, s[6:7] offset:2240
	s_waitcnt vmcnt(28)
	v_pk_mul_f32 v[16:17], v[130:131], v[182:183] op_sel_hi:[1,0]
	v_pk_mul_f32 v[18:19], v[132:133], v[182:183] op_sel_hi:[1,0]
	v_pk_mul_f32 v[20:21], v[134:135], v[184:185] op_sel_hi:[1,0]
	v_pk_mul_f32 v[22:23], v[136:137], v[184:185] op_sel_hi:[1,0]
	v_max3_f32 v15, v15, |v16|, |v20|
	v_max3_f32 v13, v13, |v17|, |v21|
	v_max3_f32 v9, v9, |v18|, |v22|
	v_max3_f32 v7, v7, |v19|, |v23|
	s_add_u32 s4, s4, 0x18000
	s_addc_u32 s5, s5, 0
	global_load_dwordx4 v[130:133], v250, s[4:5] nt
	global_load_dword v182, v251, s[6:7] offset:2272
	s_add_u32 s4, s4, 0x18000
	s_addc_u32 s5, s5, 0
	global_load_dwordx4 v[134:137], v250, s[4:5] nt
	global_load_dword v184, v251, s[6:7] offset:2304
	s_waitcnt vmcnt(28)
;     ...
;     for (int kb = 0; kb < D / 64; ++kb) {
; #pragma unroll
;         for (int i = 0; i < 8; ++i) { const int k = 64 * kb + 8 * i + kr; const f32x4 v = __builtin_nontemporal_load((const f32x4*)(W + (size_t)k * pitch)) * g[k];
;             mx[0] = __builtin_fmaxf(mx[0], __builtin_fabsf(v[0])); mx[1] = __builtin_fmaxf(mx[1], __builtin_fabsf(v[1])); mx[2] = __builtin_fmaxf(mx[2], __builtin_fabsf(v[2])); mx[3] = __builtin_fmaxf(mx[3], __builtin_fabsf(v[3])); } }
	v_pk_mul_f32 v[16:17], v[138:139], v[186:187] op_sel_hi:[1,0]
	v_pk_mul_f32 v[18:19], v[140:141], v[186:187] op_sel_hi:[1,0]
	v_pk_mul_f32 v[20:21], v[142:143], v[188:189] op_sel_hi:[1,0]
	v_pk_mul_f32 v[22:23], v[144:145], v[188:189] op_sel_hi:[1,0]
	v_max3_f32 v15, v15, |v16|, |v20|
	v_max3_f32 v13, v13, |v17|, |v21|
	v_max3_f32 v9, v9, |v18|, |v22|
	v_max3_f32 v7, v7, |v19|, |v23|
	s_add_u32 s4, s4, 0x18000
	s_addc_u32 s5, s5, 0
	global_load_dwordx4 v[138:141], v250, s[4:5] nt
	global_load_dword v186, v251, s[6:7] offset:2336
	s_add_u32 s4, s4, 0x18000
	s_addc_u32 s5, s5, 0
	global_load_dwordx4 v[142:145], v250, s[4:5] nt
	global_load_dword v188, v251, s[6:7] offset:2368
	s_waitcnt vmcnt(28)
	v_pk_mul_f32 v[16:17], v[146:147], v[190:191] op_sel_hi:[1,0]
	v_pk_mul_f32 v[18:19], v[148:149], v[190:191] op_sel_hi:[1,0]
	v_pk_mul_f32 v[20:21], v[150:151], v[192:193] op_sel_hi:[1,0]
	v_pk_mul_f32 v[22:23], v[152:153], v[192:193] op_sel_hi:[1,0]
	v_max3_f32 v15, v15, |v16|, |v20|
	v_max3_f32 v13, v13, |v17|, |v21|
	v_max3_f32 v9, v9, |v18|, |v22|
	v_max3_f32 v7, v7, |v19|, |v23|
	s_add_u32 s4, s4, 0x18000
	s_addc_u32 s5, s5, 0
	global_load_dwordx4 v[146:149], v250, s[4:5] nt
	global_load_dword v190, v251, s[6:7] offset:2400
	s_add_u32 s4, s4, 0x18000
	s_addc_u32 s5, s5, 0
	global_load_dwordx4 v[150:153], v250, s[4:5] nt
	global_load_dword v192, v251, s[6:7] offset:2432
	s_waitcnt vmcnt(28)
	v_pk_mul_f32 v[16:17], v[154:155], v[194:195] op_sel_hi:[1,0]
	v_pk_mul_f32 v[18:19], v[156:157], v[194:195] op_sel_hi:[1,0]
	v_pk_mul_f32 v[20:21], v[158:159], v[196:197] op_sel_hi:[1,0]
	v_pk_mul_f32 v[22:23], v[160:161], v[196:197] op_sel_hi:[1,0]
	v_max3_f32 v15, v15, |v16|, |v20|
	v_max3_f32 v13, v13, |v17|, |v21|
	v_max3_f32 v9, v9, |v18|, |v22|
	v_max3_f32 v7, v7, |v19|, |v23|
	s_add_u32 s4, s4, 0x18000
	s_addc_u32 s5, s5, 0
	global_load_dwordx4 v[154:157], v250, s[4:5] nt
	global_load_dword v194, v251, s[6:7] offset:2464
	s_add_u32 s4, s4, 0x18000
	s_addc_u32 s5, s5, 0
	global_load_dwordx4 v[158:161], v250, s[4:5] nt
	global_load_dword v196, v251, s[6:7] offset:2496
	s_waitcnt vmcnt(28)
	v_pk_mul_f32 v[16:17], v[162:163], v[198:199] op_sel_hi:[1,0]
	v_pk_mul_f32 v[18:19], v[164:165], v[198:199] op_sel_hi:[1,0]
	v_pk_mul_f32 v[20:21], v[166:167], v[200:201] op_sel_hi:[1,0]
	v_pk_mul_f32 v[22:23], v[168:169], v[200:201] op_sel_hi:[1,0]
	v_max3_f32 v15, v15, |v16|, |v20|
	v_max3_f32 v13, v13, |v17|, |v21|
	v_max3_f32 v9, v9, |v18|, |v22|
	v_max3_f32 v7, v7, |v19|, |v23|
	s_add_u32 s4, s4, 0x18000
	s_addc_u32 s5, s5, 0
	global_load_dwordx4 v[162:165], v250, s[4:5] nt
	global_load_dword v198, v251, s[6:7] offset:2528
	s_add_u32 s4, s4, 0x18000
	s_addc_u32 s5, s5, 0
	global_load_dwordx4 v[166:169], v250, s[4:5] nt
	global_load_dword v200, v251, s[6:7] offset:2560
	s_waitcnt vmcnt(28)
	v_pk_mul_f32 v[16:17], v[106:107], v[170:171] op_sel_hi:[1,0]
	v_pk_mul_f32 v[18:19], v[108:109], v[170:171] op_sel_hi:[1,0]
	v_pk_mul_f32 v[20:21], v[110:111], v[172:173] op_sel_hi:[1,0]
	v_pk_mul_f32 v[22:23], v[112:113], v[172:173] op_sel_hi:[1,0]
	v_max3_f32 v15, v15, |v16|, |v20|
	v_max3_f32 v13, v13, |v17|, |v21|
	v_max3_f32 v9, v9, |v18|, |v22|
	v_max3_f32 v7, v7, |v19|, |v23|
	s_add_u32 s4, s4, 0x18000
	s_addc_u32 s5, s5, 0
	global_load_dwordx4 v[106:109], v250, s[4:5] nt
	global_load_dword v170, v251, s[6:7] offset:2592
	s_add_u32 s4, s4, 0x18000
	s_addc_u32 s5, s5, 0
	global_load_dwordx4 v[110:113], v250, s[4:5] nt
	global_load_dword v172, v251, s[6:7] offset:2624
	s_waitcnt vmcnt(28)
	v_pk_mul_f32 v[16:17], v[114:115], v[174:175] op_sel_hi:[1,0]
	v_pk_mul_f32 v[18:19], v[116:117], v[174:175] op_sel_hi:[1,0]
	v_pk_mul_f32 v[20:21], v[118:119], v[176:177] op_sel_hi:[1,0]
	v_pk_mul_f32 v[22:23], v[120:121], v[176:177] op_sel_hi:[1,0]
	v_max3_f32 v15, v15, |v16|, |v20|
	v_max3_f32 v13, v13, |v17|, |v21|
	v_max3_f32 v9, v9, |v18|, |v22|
	v_max3_f32 v7, v7, |v19|, |v23|
	s_add_u32 s4, s4, 0x18000
	s_addc_u32 s5, s5, 0
	global_load_dwordx4 v[114:117], v250, s[4:5] nt
	global_load_dword v174, v251, s[6:7] offset:2656
	s_add_u32 s4, s4, 0x18000
	s_addc_u32 s5, s5, 0
	global_load_dwordx4 v[118:121], v250, s[4:5] nt
	global_load_dword v176, v251, s[6:7] offset:2688
	s_waitcnt vmcnt(28)
	v_pk_mul_f32 v[16:17], v[122:123], v[178:179] op_sel_hi:[1,0]
	v_pk_mul_f32 v[18:19], v[124:125], v[178:179] op_sel_hi:[1,0]
	v_pk_mul_f32 v[20:21], v[126:127], v[180:181] op_sel_hi:[1,0]
	v_pk_mul_f32 v[22:23], v[128:129], v[180:181] op_sel_hi:[1,0]
	v_max3_f32 v15, v15, |v16|, |v20|
	v_max3_f32 v13, v13, |v17|, |v21|
	v_max3_f32 v9, v9, |v18|, |v22|
	v_max3_f32 v7, v7, |v19|, |v23|
	s_add_u32 s4, s4, 0x18000
	s_addc_u32 s5, s5, 0
	global_load_dwordx4 v[122:125], v250, s[4:5] nt
	global_load_dword v178, v251, s[6:7] offset:2720
	s_add_u32 s4, s4, 0x18000
	s_addc_u32 s5, s5, 0
	global_load_dwordx4 v[126:129], v250, s[4:5] nt
	global_load_dword v180, v251, s[6:7] offset:2752
	s_waitcnt vmcnt(28)
	v_pk_mul_f32 v[16:17], v[130:131], v[182:183] op_sel_hi:[1,0]
	v_pk_mul_f32 v[18:19], v[132:133], v[182:183] op_sel_hi:[1,0]
	v_pk_mul_f32 v[20:21], v[134:135], v[184:185] op_sel_hi:[1,0]
	v_pk_mul_f32 v[22:23], v[136:137], v[184:185] op_sel_hi:[1,0]
	v_max3_f32 v15, v15, |v16|, |v20|
	v_max3_f32 v13, v13, |v17|, |v21|
	v_max3_f32 v9, v9, |v18|, |v22|
	v_max3_f32 v7, v7, |v19|, |v23|
	s_add_u32 s4, s4, 0x18000
	s_addc_u32 s5, s5, 0
	global_load_dwordx4 v[130:133], v250, s[4:5] nt
	global_load_dword v182, v251, s[6:7] offset:2784
	s_add_u32 s4, s4, 0x18000
	s_addc_u32 s5, s5, 0
	global_load_dwordx4 v[134:137], v250, s[4:5] nt
	global_load_dword v184, v251, s[6:7] offset:2816
	s_waitcnt vmcnt(28)
;     ...
;     for (int kb = 0; kb < D / 64; ++kb) {
; #pragma unroll
;         for (int i = 0; i < 8; ++i) { const int k = 64 * kb + 8 * i + kr; const f32x4 v = __builtin_nontemporal_load((const f32x4*)(W + (size_t)k * pitch)) * g[k];
;             mx[0] = __builtin_fmaxf(mx[0], __builtin_fabsf(v[0])); mx[1] = __builtin_fmaxf(mx[1], __builtin_fabsf(v[1])); mx[2] = __builtin_fmaxf(mx[2], __builtin_fabsf(v[2])); mx[3] = __builtin_fmaxf(mx[3], __builtin_fabsf(v[3])); } }
	v_pk_mul_f32 v[16:17], v[138:139], v[186:187] op_sel_hi:[1,0]
	v_pk_mul_f32 v[18:19], v[140:141], v[186:187] op_sel_hi:[1,0]
	v_pk_mul_f32 v[20:21], v[142:143], v[188:189] op_sel_hi:[1,0]
	v_pk_mul_f32 v[22:23], v[144:145], v[188:189] op_sel_hi:[1,0]
	v_max3_f32 v15, v15, |v16|, |v20|
	v_max3_f32 v13, v13, |v17|, |v21|
	v_max3_f32 v9, v9, |v18|, |v22|
	v_max3_f32 v7, v7, |v19|, |v23|
	s_add_u32 s4, s4, 0x18000
	s_addc_u32 s5, s5, 0
	global_load_dwordx4 v[138:141], v250, s[4:5] nt
	global_load_dword v186, v251, s[6:7] offset:2848
	s_add_u32 s4, s4, 0x18000
	s_addc_u32 s5, s5, 0
	global_load_dwordx4 v[142:145], v250, s[4:5] nt
	global_load_dword v188, v251, s[6:7] offset:2880
	s_waitcnt vmcnt(28)
	v_pk_mul_f32 v[16:17], v[146:147], v[190:191] op_sel_hi:[1,0]
	v_pk_mul_f32 v[18:19], v[148:149], v[190:191] op_sel_hi:[1,0]
	v_pk_mul_f32 v[20:21], v[150:151], v[192:193] op_sel_hi:[1,0]
	v_pk_mul_f32 v[22:23], v[152:153], v[192:193] op_sel_hi:[1,0]
	v_max3_f32 v15, v15, |v16|, |v20|
	v_max3_f32 v13, v13, |v17|, |v21|
	v_max3_f32 v9, v9, |v18|, |v22|
	v_max3_f32 v7, v7, |v19|, |v23|
	s_add_u32 s4, s4, 0x18000
	s_addc_u32 s5, s5, 0
	global_load_dwordx4 v[146:149], v250, s[4:5] nt
	global_load_dword v190, v251, s[6:7] offset:2912
	s_add_u32 s4, s4, 0x18000
	s_addc_u32 s5, s5, 0
	global_load_dwordx4 v[150:153], v250, s[4:5] nt
	global_load_dword v192, v251, s[6:7] offset:2944
	s_waitcnt vmcnt(28)
	v_pk_mul_f32 v[16:17], v[154:155], v[194:195] op_sel_hi:[1,0]
	v_pk_mul_f32 v[18:19], v[156:157], v[194:195] op_sel_hi:[1,0]
	v_pk_mul_f32 v[20:21], v[158:159], v[196:197] op_sel_hi:[1,0]
	v_pk_mul_f32 v[22:23], v[160:161], v[196:197] op_sel_hi:[1,0]
	v_max3_f32 v15, v15, |v16|, |v20|
	v_max3_f32 v13, v13, |v17|, |v21|
	v_max3_f32 v9, v9, |v18|, |v22|
	v_max3_f32 v7, v7, |v19|, |v23|
	s_add_u32 s4, s4, 0x18000
	s_addc_u32 s5, s5, 0
	global_load_dwordx4 v[154:157], v250, s[4:5] nt
	global_load_dword v194, v251, s[6:7] offset:2976
	s_add_u32 s4, s4, 0x18000
	s_addc_u32 s5, s5, 0
	global_load_dwordx4 v[158:161], v250, s[4:5] nt
	global_load_dword v196, v251, s[6:7] offset:3008
	s_waitcnt vmcnt(28)
	v_pk_mul_f32 v[16:17], v[162:163], v[198:199] op_sel_hi:[1,0]
	v_pk_mul_f32 v[18:19], v[164:165], v[198:199] op_sel_hi:[1,0]
	v_pk_mul_f32 v[20:21], v[166:167], v[200:201] op_sel_hi:[1,0]
	v_pk_mul_f32 v[22:23], v[168:169], v[200:201] op_sel_hi:[1,0]
	v_max3_f32 v15, v15, |v16|, |v20|
	v_max3_f32 v13, v13, |v17|, |v21|
	v_max3_f32 v9, v9, |v18|, |v22|
	v_max3_f32 v7, v7, |v19|, |v23|
	s_add_u32 s4, s4, 0x18000
	s_addc_u32 s5, s5, 0
	global_load_dwordx4 v[162:165], v250, s[4:5] nt
	global_load_dword v198, v251, s[6:7] offset:3040
	s_add_u32 s4, s4, 0x18000
	s_addc_u32 s5, s5, 0
	global_load_dwordx4 v[166:169], v250, s[4:5] nt
	global_load_dword v200, v251, s[6:7] offset:3072
	s_waitcnt vmcnt(28)
	v_pk_mul_f32 v[16:17], v[106:107], v[170:171] op_sel_hi:[1,0]
	v_pk_mul_f32 v[18:19], v[108:109], v[170:171] op_sel_hi:[1,0]
	v_pk_mul_f32 v[20:21], v[110:111], v[172:173] op_sel_hi:[1,0]
	v_pk_mul_f32 v[22:23], v[112:113], v[172:173] op_sel_hi:[1,0]
	v_max3_f32 v15, v15, |v16|, |v20|
	v_max3_f32 v13, v13, |v17|, |v21|
	v_max3_f32 v9, v9, |v18|, |v22|
	v_max3_f32 v7, v7, |v19|, |v23|
	s_add_u32 s4, s4, 0x18000
	s_addc_u32 s5, s5, 0
	global_load_dwordx4 v[106:109], v250, s[4:5] nt
	global_load_dword v170, v251, s[6:7] offset:3104
	s_add_u32 s4, s4, 0x18000
	s_addc_u32 s5, s5, 0
	global_load_dwordx4 v[110:113], v250, s[4:5] nt
	global_load_dword v172, v251, s[6:7] offset:3136
	s_waitcnt vmcnt(28)
	v_pk_mul_f32 v[16:17], v[114:115], v[174:175] op_sel_hi:[1,0]
	v_pk_mul_f32 v[18:19], v[116:117], v[174:175] op_sel_hi:[1,0]
	v_pk_mul_f32 v[20:21], v[118:119], v[176:177] op_sel_hi:[1,0]
	v_pk_mul_f32 v[22:23], v[120:121], v[176:177] op_sel_hi:[1,0]
	v_max3_f32 v15, v15, |v16|, |v20|
	v_max3_f32 v13, v13, |v17|, |v21|
	v_max3_f32 v9, v9, |v18|, |v22|
	v_max3_f32 v7, v7, |v19|, |v23|
	s_add_u32 s4, s4, 0x18000
	s_addc_u32 s5, s5, 0
	global_load_dwordx4 v[114:117], v250, s[4:5] nt
	global_load_dword v174, v251, s[6:7] offset:3168
	s_add_u32 s4, s4, 0x18000
	s_addc_u32 s5, s5, 0
	global_load_dwordx4 v[118:121], v250, s[4:5] nt
	global_load_dword v176, v251, s[6:7] offset:3200
	s_waitcnt vmcnt(28)
	v_pk_mul_f32 v[16:17], v[122:123], v[178:179] op_sel_hi:[1,0]
	v_pk_mul_f32 v[18:19], v[124:125], v[178:179] op_sel_hi:[1,0]
	v_pk_mul_f32 v[20:21], v[126:127], v[180:181] op_sel_hi:[1,0]
	v_pk_mul_f32 v[22:23], v[128:129], v[180:181] op_sel_hi:[1,0]
	v_max3_f32 v15, v15, |v16|, |v20|
	v_max3_f32 v13, v13, |v17|, |v21|
	v_max3_f32 v9, v9, |v18|, |v22|
	v_max3_f32 v7, v7, |v19|, |v23|
	s_add_u32 s4, s4, 0x18000
	s_addc_u32 s5, s5, 0
	global_load_dwordx4 v[122:125], v250, s[4:5] nt
	global_load_dword v178, v251, s[6:7] offset:3232
	s_add_u32 s4, s4, 0x18000
	s_addc_u32 s5, s5, 0
	global_load_dwordx4 v[126:129], v250, s[4:5] nt
	global_load_dword v180, v251, s[6:7] offset:3264
	s_waitcnt vmcnt(28)
	v_pk_mul_f32 v[16:17], v[130:131], v[182:183] op_sel_hi:[1,0]
	v_pk_mul_f32 v[18:19], v[132:133], v[182:183] op_sel_hi:[1,0]
	v_pk_mul_f32 v[20:21], v[134:135], v[184:185] op_sel_hi:[1,0]
	v_pk_mul_f32 v[22:23], v[136:137], v[184:185] op_sel_hi:[1,0]
	v_max3_f32 v15, v15, |v16|, |v20|
	v_max3_f32 v13, v13, |v17|, |v21|
	v_max3_f32 v9, v9, |v18|, |v22|
	v_max3_f32 v7, v7, |v19|, |v23|
	s_add_u32 s4, s4, 0x18000
	s_addc_u32 s5, s5, 0
	global_load_dwordx4 v[130:133], v250, s[4:5] nt
	global_load_dword v182, v251, s[6:7] offset:3296
	s_add_u32 s4, s4, 0x18000
	s_addc_u32 s5, s5, 0
	global_load_dwordx4 v[134:137], v250, s[4:5] nt
	global_load_dword v184, v251, s[6:7] offset:3328
	s_waitcnt vmcnt(28)
;     ...
;     for (int kb = 0; kb < D / 64; ++kb) {
; #pragma unroll
;         for (int i = 0; i < 8; ++i) { const int k = 64 * kb + 8 * i + kr; const f32x4 v = __builtin_nontemporal_load((const f32x4*)(W + (size_t)k * pitch)) * g[k];
;             mx[0] = __builtin_fmaxf(mx[0], __builtin_fabsf(v[0])); mx[1] = __builtin_fmaxf(mx[1], __builtin_fabsf(v[1])); mx[2] = __builtin_fmaxf(mx[2], __builtin_fabsf(v[2])); mx[3] = __builtin_fmaxf(mx[3], __builtin_fabsf(v[3])); } }
	v_pk_mul_f32 v[16:17], v[138:139], v[186:187] op_sel_hi:[1,0]
	v_pk_mul_f32 v[18:19], v[140:141], v[186:187] op_sel_hi:[1,0]
	v_pk_mul_f32 v[20:21], v[142:143], v[188:189] op_sel_hi:[1,0]
	v_pk_mul_f32 v[22:23], v[144:145], v[188:189] op_sel_hi:[1,0]
	v_max3_f32 v15, v15, |v16|, |v20|
	v_max3_f32 v13, v13, |v17|, |v21|
	v_max3_f32 v9, v9, |v18|, |v22|
	v_max3_f32 v7, v7, |v19|, |v23|
	s_add_u32 s4, s4, 0x18000
	s_addc_u32 s5, s5, 0
	global_load_dwordx4 v[138:141], v250, s[4:5] nt
	global_load_dword v186, v251, s[6:7] offset:3360
	s_add_u32 s4, s4, 0x18000
	s_addc_u32 s5, s5, 0
	global_load_dwordx4 v[142:145], v250, s[4:5] nt
	global_load_dword v188, v251, s[6:7] offset:3392
	s_waitcnt vmcnt(28)
	v_pk_mul_f32 v[16:17], v[146:147], v[190:191] op_sel_hi:[1,0]
	v_pk_mul_f32 v[18:19], v[148:149], v[190:191] op_sel_hi:[1,0]
	v_pk_mul_f32 v[20:21], v[150:151], v[192:193] op_sel_hi:[1,0]
	v_pk_mul_f32 v[22:23], v[152:153], v[192:193] op_sel_hi:[1,0]
	v_max3_f32 v15, v15, |v16|, |v20|
	v_max3_f32 v13, v13, |v17|, |v21|
	v_max3_f32 v9, v9, |v18|, |v22|
	v_max3_f32 v7, v7, |v19|, |v23|
	s_add_u32 s4, s4, 0x18000
	s_addc_u32 s5, s5, 0
	global_load_dwordx4 v[146:149], v250, s[4:5] nt
	global_load_dword v190, v251, s[6:7] offset:3424
	s_add_u32 s4, s4, 0x18000
	s_addc_u32 s5, s5, 0
	global_load_dwordx4 v[150:153], v250, s[4:5] nt
	global_load_dword v192, v251, s[6:7] offset:3456
	s_waitcnt vmcnt(28)
	v_pk_mul_f32 v[16:17], v[154:155], v[194:195] op_sel_hi:[1,0]
	v_pk_mul_f32 v[18:19], v[156:157], v[194:195] op_sel_hi:[1,0]
	v_pk_mul_f32 v[20:21], v[158:159], v[196:197] op_sel_hi:[1,0]
	v_pk_mul_f32 v[22:23], v[160:161], v[196:197] op_sel_hi:[1,0]
	v_max3_f32 v15, v15, |v16|, |v20|
	v_max3_f32 v13, v13, |v17|, |v21|
	v_max3_f32 v9, v9, |v18|, |v22|
	v_max3_f32 v7, v7, |v19|, |v23|
	s_add_u32 s4, s4, 0x18000
	s_addc_u32 s5, s5, 0
	global_load_dwordx4 v[154:157], v250, s[4:5] nt
	global_load_dword v194, v251, s[6:7] offset:3488
	s_add_u32 s4, s4, 0x18000
	s_addc_u32 s5, s5, 0
	global_load_dwordx4 v[158:161], v250, s[4:5] nt
	global_load_dword v196, v251, s[6:7] offset:3520
	s_waitcnt vmcnt(28)
	v_pk_mul_f32 v[16:17], v[162:163], v[198:199] op_sel_hi:[1,0]
	v_pk_mul_f32 v[18:19], v[164:165], v[198:199] op_sel_hi:[1,0]
	v_pk_mul_f32 v[20:21], v[166:167], v[200:201] op_sel_hi:[1,0]
	v_pk_mul_f32 v[22:23], v[168:169], v[200:201] op_sel_hi:[1,0]
	v_max3_f32 v15, v15, |v16|, |v20|
	v_max3_f32 v13, v13, |v17|, |v21|
	v_max3_f32 v9, v9, |v18|, |v22|
	v_max3_f32 v7, v7, |v19|, |v23|
	s_add_u32 s4, s4, 0x18000
	s_addc_u32 s5, s5, 0
	global_load_dwordx4 v[162:165], v250, s[4:5] nt
	global_load_dword v198, v251, s[6:7] offset:3552
	s_add_u32 s4, s4, 0x18000
	s_addc_u32 s5, s5, 0
	global_load_dwordx4 v[166:169], v250, s[4:5] nt
	global_load_dword v200, v251, s[6:7] offset:3584
	s_waitcnt vmcnt(28)
	v_pk_mul_f32 v[16:17], v[106:107], v[170:171] op_sel_hi:[1,0]
	v_pk_mul_f32 v[18:19], v[108:109], v[170:171] op_sel_hi:[1,0]
	v_pk_mul_f32 v[20:21], v[110:111], v[172:173] op_sel_hi:[1,0]
	v_pk_mul_f32 v[22:23], v[112:113], v[172:173] op_sel_hi:[1,0]
	v_max3_f32 v15, v15, |v16|, |v20|
	v_max3_f32 v13, v13, |v17|, |v21|
	v_max3_f32 v9, v9, |v18|, |v22|
	v_max3_f32 v7, v7, |v19|, |v23|
	s_waitcnt vmcnt(24)
	v_pk_mul_f32 v[16:17], v[114:115], v[174:175] op_sel_hi:[1,0]
	v_pk_mul_f32 v[18:19], v[116:117], v[174:175] op_sel_hi:[1,0]
	v_pk_mul_f32 v[20:21], v[118:119], v[176:177] op_sel_hi:[1,0]
	v_pk_mul_f32 v[22:23], v[120:121], v[176:177] op_sel_hi:[1,0]
	v_max3_f32 v15, v15, |v16|, |v20|
	v_max3_f32 v13, v13, |v17|, |v21|
	v_max3_f32 v9, v9, |v18|, |v22|
	v_max3_f32 v7, v7, |v19|, |v23|
	s_waitcnt vmcnt(20)
	v_pk_mul_f32 v[16:17], v[122:123], v[178:179] op_sel_hi:[1,0]
	v_pk_mul_f32 v[18:19], v[124:125], v[178:179] op_sel_hi:[1,0]
	v_pk_mul_f32 v[20:21], v[126:127], v[180:181] op_sel_hi:[1,0]
	v_pk_mul_f32 v[22:23], v[128:129], v[180:181] op_sel_hi:[1,0]
	v_max3_f32 v15, v15, |v16|, |v20|
	v_max3_f32 v13, v13, |v17|, |v21|
	v_max3_f32 v9, v9, |v18|, |v22|
	v_max3_f32 v7, v7, |v19|, |v23|
	s_waitcnt vmcnt(16)
; __device__ __forceinline__ float shfl_xor_f(float v, int mask, int lane) { return __int_as_float(__builtin_amdgcn_ds_bpermute((lane ^ mask) << 2, __float_as_int(v))); }
;     ...
;             mx[0] = __builtin_fmaxf(mx[0], __builtin_fabsf(v[0])); mx[1] = __builtin_fmaxf(mx[1], __builtin_fabsf(v[1])); mx[2] = __builtin_fmaxf(mx[2], __builtin_fabsf(v[2])); mx[3] = __builtin_fmaxf(mx[3], __builtin_fabsf(v[3])); } }
; #pragma unroll
;     for (int c = 0; c < 4; ++c) { float m = mx[c]; m = __builtin_fmaxf(m, shfl_xor_f(m, 8, lane)); m = __builtin_fmaxf(m, shfl_xor_f(m, 16, lane)); m = __builtin_fmaxf(m, shfl_xor_f(m, 32, lane)); mx[c] = m; }
;     f32x4 inv, step;
; #pragma unroll
;     for (int c = 0; c < 4; ++c) { step[c] = mx[c] > 0.f ? mx[c] * (1.0f / 127.0f) : 1.0f; inv[c] = mx[c] > 0.f ? 127.0f / mx[c] : 0.f; }
;     if (lane < 8) *(f32x4*)(sw + n0 + 4 * lane) = step * swm;
	v_pk_mul_f32 v[16:17], v[130:131], v[182:183] op_sel_hi:[1,0]
	v_pk_mul_f32 v[18:19], v[132:133], v[182:183] op_sel_hi:[1,0]
	v_pk_mul_f32 v[20:21], v[134:135], v[184:185] op_sel_hi:[1,0]
	v_pk_mul_f32 v[22:23], v[136:137], v[184:185] op_sel_hi:[1,0]
	v_max3_f32 v15, v15, |v16|, |v20|
	v_max3_f32 v13, v13, |v17|, |v21|
	v_max3_f32 v9, v9, |v18|, |v22|
	v_max3_f32 v7, v7, |v19|, |v23|
	s_waitcnt vmcnt(12)
	v_pk_mul_f32 v[16:17], v[138:139], v[186:187] op_sel_hi:[1,0]
	v_pk_mul_f32 v[18:19], v[140:141], v[186:187] op_sel_hi:[1,0]
	v_pk_mul_f32 v[20:21], v[142:143], v[188:189] op_sel_hi:[1,0]
	v_pk_mul_f32 v[22:23], v[144:145], v[188:189] op_sel_hi:[1,0]
	v_max3_f32 v15, v15, |v16|, |v20|
	v_max3_f32 v13, v13, |v17|, |v21|
	v_max3_f32 v9, v9, |v18|, |v22|
	v_max3_f32 v7, v7, |v19|, |v23|
	s_waitcnt vmcnt(8)
	v_pk_mul_f32 v[16:17], v[146:147], v[190:191] op_sel_hi:[1,0]
	v_pk_mul_f32 v[18:19], v[148:149], v[190:191] op_sel_hi:[1,0]
	v_pk_mul_f32 v[20:21], v[150:151], v[192:193] op_sel_hi:[1,0]
	v_pk_mul_f32 v[22:23], v[152:153], v[192:193] op_sel_hi:[1,0]
	v_max3_f32 v15, v15, |v16|, |v20|
	v_max3_f32 v13, v13, |v17|, |v21|
	v_max3_f32 v9, v9, |v18|, |v22|
	v_max3_f32 v7, v7, |v19|, |v23|
	s_waitcnt vmcnt(4)
	v_pk_mul_f32 v[16:17], v[154:155], v[194:195] op_sel_hi:[1,0]
	v_pk_mul_f32 v[18:19], v[156:157], v[194:195] op_sel_hi:[1,0]
	v_pk_mul_f32 v[20:21], v[158:159], v[196:197] op_sel_hi:[1,0]
	v_pk_mul_f32 v[22:23], v[160:161], v[196:197] op_sel_hi:[1,0]
	v_max3_f32 v15, v15, |v16|, |v20|
	v_max3_f32 v13, v13, |v17|, |v21|
	v_max3_f32 v9, v9, |v18|, |v22|
	v_max3_f32 v7, v7, |v19|, |v23|
	s_waitcnt vmcnt(0)
	v_pk_mul_f32 v[16:17], v[162:163], v[198:199] op_sel_hi:[1,0]
	v_pk_mul_f32 v[18:19], v[164:165], v[198:199] op_sel_hi:[1,0]
	v_pk_mul_f32 v[20:21], v[166:167], v[200:201] op_sel_hi:[1,0]
	v_pk_mul_f32 v[22:23], v[168:169], v[200:201] op_sel_hi:[1,0]
	v_max3_f32 v15, v15, |v16|, |v20|
	v_max3_f32 v13, v13, |v17|, |v21|
	v_max3_f32 v9, v9, |v18|, |v22|
	v_max3_f32 v7, v7, |v19|, |v23|
	v_lshlrev_b32_e32 v2, 2, v68
	v_xor_b32_e32 v3, 32, v2
	ds_bpermute_b32 v4, v3, v15
	v_max_f32_e32 v5, v15, v15
	v_xor_b32_e32 v8, 64, v2
	ds_bpermute_b32 v10, v3, v13
	v_max_f32_e32 v6, v13, v13
	s_waitcnt lgkmcnt(1)
	v_max_f32_e32 v4, v4, v4
	v_max_f32_e32 v4, v5, v4
	ds_bpermute_b32 v5, v8, v4
	s_waitcnt lgkmcnt(1)
	v_max_f32_e32 v10, v10, v10
	v_xor_b32_e32 v11, 0x80, v2
	v_max_f32_e32 v6, v6, v10
	ds_bpermute_b32 v10, v8, v6
	s_waitcnt lgkmcnt(1)
	v_max_f32_e32 v5, v5, v5
	v_max_f32_e32 v4, v4, v5
	ds_bpermute_b32 v5, v11, v4
	ds_bpermute_b32 v12, v3, v9
	ds_bpermute_b32 v3, v3, v7
	s_waitcnt lgkmcnt(3)
	v_max_f32_e32 v10, v10, v10
	v_max_f32_e32 v10, v6, v10
	s_waitcnt lgkmcnt(2)
	v_max_f32_e32 v5, v5, v5
	v_max_f32_e32 v6, v4, v5
	s_waitcnt lgkmcnt(1)
	v_max_f32_e32 v4, v12, v12
	v_max_f32_e32 v5, v9, v9
	v_max_f32_e32 v4, v5, v4
	s_waitcnt lgkmcnt(0)
	v_max_f32_e32 v3, v3, v3
	v_max_f32_e32 v7, v7, v7
	ds_bpermute_b32 v5, v8, v4
	v_max_f32_e32 v3, v7, v3
	ds_bpermute_b32 v7, v8, v3
	ds_bpermute_b32 v8, v11, v10
	v_cmp_lt_f32_e64 s[10:11], 0, v6
	s_waitcnt lgkmcnt(2)
	v_max_f32_e32 v5, v5, v5
	v_max_f32_e32 v4, v4, v5
	s_waitcnt lgkmcnt(1)
	v_max_f32_e32 v5, v7, v7
	v_max_f32_e32 v3, v3, v5
	ds_bpermute_b32 v9, v11, v4
	ds_bpermute_b32 v7, v11, v3
	s_waitcnt lgkmcnt(2)
	v_max_f32_e32 v5, v8, v8
	v_max_f32_e32 v5, v10, v5
	v_cmp_lt_f32_e64 s[8:9], 0, v5
	s_waitcnt lgkmcnt(1)
	v_max_f32_e32 v8, v9, v9
	s_waitcnt lgkmcnt(0)
	v_max_f32_e32 v7, v7, v7
	v_max_f32_e32 v4, v4, v8
	v_max_f32_e32 v3, v3, v7
	v_cmp_lt_f32_e64 s[6:7], 0, v4
	v_cmp_lt_f32_e64 s[4:5], 0, v3
	v_cmp_gt_u32_e32 vcc, 8, v68
	s_and_saveexec_b64 s[38:39], vcc
	s_cbranch_execz .LBB0_130
	s_mul_i32 s40, s28, 0x3000
	s_mul_hi_u32 s29, s28, 0x3000
	s_add_u32 s40, s14, s40
	s_addc_u32 s29, s15, s29
	v_mul_f32_e32 v7, 0x3c010204, v6
	s_add_u32 s40, s40, s30
	v_cndmask_b32_e64 v8, 1.0, v7, s[10:11]
	v_mul_f32_e32 v7, 0x3c010204, v5
	s_addc_u32 s41, s29, s31
	v_lshlrev_b32_e32 v12, 2, v2
	v_mov_b32_e32 v13, 0
	v_cndmask_b32_e64 v9, 1.0, v7, s[8:9]
	v_mul_f32_e32 v7, 0x3c010204, v4
	v_lshl_add_u64 v[12:13], s[40:41], 0, v[12:13]
	v_cndmask_b32_e64 v10, 1.0, v7, s[6:7]
	v_mul_f32_e32 v7, 0x3c010204, v3
	v_add_co_u32_e32 v12, vcc, 0x80000, v12
	v_cndmask_b32_e64 v11, 1.0, v7, s[4:5]
	s_nop 0
	v_addc_co_u32_e32 v13, vcc, 0, v13, vcc
	global_store_dwordx4 v[12:13], v[8:11], off

; #define LAS __attribute__((address_space(3)))
; #define LDS_WAIT() asm volatile("s_waitcnt lgkmcnt(0)" ::: "memory")
;     ...
;     for (int kb = 0; kb < D / 64; ++kb) {
; #pragma unroll
;         for (int i = 0; i < 8; ++i) { const int kk = 8 * i + kr; const int k = 64 * kb + kk; const f32x4 v = __builtin_nontemporal_load((const f32x4*)(W + (size_t)k * pitch)) * g[k];
;             LAS float* p = scr + kk * 33 + 4 * (lane & 7); p[0] = __builtin_rintf(v[0] * inv[0]); p[1] = __builtin_rintf(v[1] * inv[1]); p[2] = __builtin_rintf(v[2] * inv[2]); p[3] = __builtin_rintf(v[3] * inv[3]); }
;         LDS_WAIT(); asm volatile("" ::: "memory");
.LBB0_131:
	v_readfirstlane_b32 s4, v0
	v_readfirstlane_b32 s5, v1
	v_readfirstlane_b32 s6, v2
	v_readfirstlane_b32 s7, v3
	s_nop 1
	v_subrev_u32_e32 v250, s4, v0
	v_subrev_u32_e32 v251, s6, v2
	s_add_u32 s4, s4, 0xfff58000
	s_addc_u32 s5, s5, -1
	s_add_u32 s6, s6, 0x1000
	s_addc_u32 s7, s7, 0
	s_nop 4
	global_load_dwordx4 v[106:109], v250, s[4:5] nt
	global_load_dword v170, v251, s[6:7]
	s_add_u32 s4, s4, 0x18000
	s_addc_u32 s5, s5, 0
	global_load_dwordx4 v[110:113], v250, s[4:5] nt
	global_load_dword v172, v251, s[6:7] offset:32
	s_add_u32 s4, s4, 0x18000
	s_addc_u32 s5, s5, 0
	global_load_dwordx4 v[114:117], v250, s[4:5] nt
	global_load_dword v174, v251, s[6:7] offset:64
	s_add_u32 s4, s4, 0x18000
	s_addc_u32 s5, s5, 0
	global_load_dwordx4 v[118:121], v250, s[4:5] nt
	global_load_dword v176, v251, s[6:7] offset:96
	s_add_u32 s4, s4, 0x18000
	s_addc_u32 s5, s5, 0
	global_load_dwordx4 v[122:125], v250, s[4:5] nt
	global_load_dword v178, v251, s[6:7] offset:128
	s_add_u32 s4, s4, 0x18000
	s_addc_u32 s5, s5, 0
	global_load_dwordx4 v[126:129], v250, s[4:5] nt
	global_load_dword v180, v251, s[6:7] offset:160
	s_add_u32 s4, s4, 0x18000
	s_addc_u32 s5, s5, 0
	global_load_dwordx4 v[130:133], v250, s[4:5] nt
	global_load_dword v182, v251, s[6:7] offset:192
	s_add_u32 s4, s4, 0x18000
	s_addc_u32 s5, s5, 0
	global_load_dwordx4 v[134:137], v250, s[4:5] nt
	global_load_dword v184, v251, s[6:7] offset:224
	s_add_u32 s4, s4, 0x18000
	s_addc_u32 s5, s5, 0
	global_load_dwordx4 v[138:141], v250, s[4:5] nt
	global_load_dword v186, v251, s[6:7] offset:256
	s_add_u32 s4, s4, 0x18000
	s_addc_u32 s5, s5, 0
	global_load_dwordx4 v[142:145], v250, s[4:5] nt
	global_load_dword v188, v251, s[6:7] offset:288
	s_add_u32 s4, s4, 0x18000
	s_addc_u32 s5, s5, 0
	global_load_dwordx4 v[146:149], v250, s[4:5] nt
	global_load_dword v190, v251, s[6:7] offset:320
	s_add_u32 s4, s4, 0x18000
	s_addc_u32 s5, s5, 0
	global_load_dwordx4 v[150:153], v250, s[4:5] nt
	global_load_dword v192, v251, s[6:7] offset:352
	s_add_u32 s4, s4, 0x18000
	s_addc_u32 s5, s5, 0
	global_load_dwordx4 v[154:157], v250, s[4:5] nt
	global_load_dword v194, v251, s[6:7] offset:384
	s_add_u32 s4, s4, 0x18000
	s_addc_u32 s5, s5, 0
	global_load_dwordx4 v[158:161], v250, s[4:5] nt
	global_load_dword v196, v251, s[6:7] offset:416
	s_add_u32 s4, s4, 0x18000
	s_addc_u32 s5, s5, 0
	global_load_dwordx4 v[162:165], v250, s[4:5] nt
	global_load_dword v198, v251, s[6:7] offset:448
	s_add_u32 s4, s4, 0x18000
	s_addc_u32 s5, s5, 0
	global_load_dwordx4 v[166:169], v250, s[4:5] nt
	global_load_dword v200, v251, s[6:7] offset:480
	v_add_u32_e32 v87, 0x14a0, v31
	v_add_u32_e32 v88, 0x14a8, v31
	v_add_u32_e32 v89, 0x18c0, v31
	v_add_u32_e32 v90, 0x18c8, v31
	v_add_u32_e32 v91, 0x1ce0, v31
	v_add_u32_e32 v92, 0x1ce8, v31
	v_lshl_add_u64 v[18:19], v[6:7], 0, v[12:13]
	v_lshl_add_u64 v[22:23], v[6:7], 0, v[10:11]
	v_lshl_add_u64 v[82:83], v[6:7], 0, v[8:9]
	v_lshl_add_u64 v[84:85], v[6:7], 0, v[4:5]
	v_lshl_add_u64 v[6:7], v[6:7], 0, 64
	s_waitcnt vmcnt(16)
	v_pk_mul_f32 v[46:47], v[112:113], v[172:173] op_sel_hi:[1,0]
	v_pk_mul_f32 v[20:21], v[110:111], v[172:173] op_sel_hi:[1,0]
	v_pk_mul_f32 v[44:45], v[116:117], v[174:175] op_sel_hi:[1,0]
	v_pk_mul_f32 v[24:25], v[114:115], v[174:175] op_sel_hi:[1,0]
	v_pk_mul_f32 v[48:49], v[120:121], v[176:177] op_sel_hi:[1,0]
	v_pk_mul_f32 v[16:17], v[108:109], v[170:171] op_sel_hi:[1,0]
	v_pk_mul_f32 v[14:15], v[106:107], v[170:171] op_sel_hi:[1,0]
	v_pk_mul_f32 v[50:51], v[118:119], v[176:177] op_sel_hi:[1,0]
	v_pk_mul_f32 v[52:53], v[124:125], v[178:179] op_sel_hi:[1,0]
	v_pk_mul_f32 v[54:55], v[122:123], v[178:179] op_sel_hi:[1,0]
	v_pk_mul_f32 v[56:57], v[128:129], v[180:181] op_sel_hi:[1,0]
	v_pk_mul_f32 v[58:59], v[126:127], v[180:181] op_sel_hi:[1,0]
	v_pk_mul_f32 v[60:61], v[132:133], v[182:183] op_sel_hi:[1,0]
	v_pk_mul_f32 v[62:63], v[130:131], v[182:183] op_sel_hi:[1,0]
	v_pk_mul_f32 v[42:43], v[136:137], v[184:185] op_sel_hi:[1,0]
	v_pk_mul_f32 v[40:41], v[134:135], v[184:185] op_sel_hi:[1,0]
	s_add_u32 s4, s4, 0x18000
	s_addc_u32 s5, s5, 0
	global_load_dwordx4 v[106:109], v250, s[4:5] nt
	global_load_dword v170, v251, s[6:7] offset:512
	s_add_u32 s4, s4, 0x18000
	s_addc_u32 s5, s5, 0
	global_load_dwordx4 v[110:113], v250, s[4:5] nt
	global_load_dword v172, v251, s[6:7] offset:544
	s_add_u32 s4, s4, 0x18000
	s_addc_u32 s5, s5, 0
	global_load_dwordx4 v[114:117], v250, s[4:5] nt
	global_load_dword v174, v251, s[6:7] offset:576
	s_add_u32 s4, s4, 0x18000
	s_addc_u32 s5, s5, 0
	global_load_dwordx4 v[118:121], v250, s[4:5] nt
	global_load_dword v176, v251, s[6:7] offset:608
	s_add_u32 s4, s4, 0x18000
	s_addc_u32 s5, s5, 0
	global_load_dwordx4 v[122:125], v250, s[4:5] nt
	global_load_dword v178, v251, s[6:7] offset:640
	s_add_u32 s4, s4, 0x18000
	s_addc_u32 s5, s5, 0
	global_load_dwordx4 v[126:129], v250, s[4:5] nt
	global_load_dword v180, v251, s[6:7] offset:672
	s_add_u32 s4, s4, 0x18000
	s_addc_u32 s5, s5, 0
	global_load_dwordx4 v[130:133], v250, s[4:5] nt
	global_load_dword v182, v251, s[6:7] offset:704
	s_add_u32 s4, s4, 0x18000
	s_addc_u32 s5, s5, 0
	global_load_dwordx4 v[134:137], v250, s[4:5] nt
	global_load_dword v184, v251, s[6:7] offset:736
	v_mul_f32_e32 v14, v26, v14
	v_mul_f32_e32 v15, v27, v15
	v_mul_f32_e32 v16, v28, v16
	v_mul_f32_e32 v17, v29, v17
	v_mul_f32_e32 v20, v26, v20
	v_mul_f32_e32 v21, v27, v21
	v_mul_f32_e32 v46, v28, v46
	v_mul_f32_e32 v47, v29, v47
	v_mul_f32_e32 v24, v26, v24
	v_mul_f32_e32 v25, v27, v25
	v_mul_f32_e32 v44, v28, v44
	v_mul_f32_e32 v45, v29, v45
	v_mul_f32_e32 v50, v26, v50
	v_mul_f32_e32 v51, v27, v51
	v_mul_f32_e32 v48, v28, v48
; #define LAS __attribute__((address_space(3)))
; #define GAS __attribute__((address_space(1)))
; #define LDS_WAIT() asm volatile("s_waitcnt lgkmcnt(0)" ::: "memory")
;     ...
;         for (int i = 0; i < 8; ++i) { const int kk = 8 * i + kr; const int k = 64 * kb + kk; const f32x4 v = __builtin_nontemporal_load((const f32x4*)(W + (size_t)k * pitch)) * g[k];
;             LAS float* p = scr + kk * 33 + 4 * (lane & 7); p[0] = __builtin_rintf(v[0] * inv[0]); p[1] = __builtin_rintf(v[1] * inv[1]); p[2] = __builtin_rintf(v[2] * inv[2]); p[3] = __builtin_rintf(v[3] * inv[3]); }
;         LDS_WAIT(); asm volatile("" ::: "memory");
;         const int c = lane & 7;
; #pragma unroll
;         for (int j = 0; j < 4; ++j) { const int n = (lane >> 3) + 8 * j; const LAS float* sp = scr + (8 * c) * 33 + n;
;             u32x2 o;
;             o.x = ((unsigned)(int)sp[0 * 33] & 0xFFu) | (((unsigned)(int)sp[1 * 33] & 0xFFu) << 8) | (((unsigned)(int)sp[2 * 33] & 0xFFu) << 16) | (((unsigned)(int)sp[3 * 33] & 0xFFu) << 24);
;             o.y = ((unsigned)(int)sp[4 * 33] & 0xFFu) | (((unsigned)(int)sp[5 * 33] & 0xFFu) << 8) | (((unsigned)(int)sp[6 * 33] & 0xFFu) << 16) | (((unsigned)(int)sp[7 * 33] & 0xFFu) << 24);
;             *(GAS u32x2*)(dst + (size_t)(n0 + n) * D + 64 * kb + 8 * c) = o; }
;         LDS_WAIT(); asm volatile("" ::: "memory");
	v_mul_f32_e32 v49, v29, v49
	v_mul_f32_e32 v54, v26, v54
	v_mul_f32_e32 v55, v27, v55
	v_mul_f32_e32 v52, v28, v52
	v_mul_f32_e32 v53, v29, v53
	v_mul_f32_e32 v58, v26, v58
	v_mul_f32_e32 v59, v27, v59
	v_mul_f32_e32 v56, v28, v56
	v_mul_f32_e32 v57, v29, v57
	v_mul_f32_e32 v62, v26, v62
	v_mul_f32_e32 v63, v27, v63
	v_mul_f32_e32 v60, v28, v60
	v_mul_f32_e32 v61, v29, v61
	v_mul_f32_e32 v40, v26, v40
	v_mul_f32_e32 v41, v27, v41
	v_mul_f32_e32 v42, v28, v42
	v_mul_f32_e32 v43, v29, v43
	v_rndne_f32_e32 v14, v14
	v_rndne_f32_e32 v15, v15
	v_rndne_f32_e32 v16, v16
	v_rndne_f32_e32 v17, v17
	v_rndne_f32_e32 v20, v20
	v_rndne_f32_e32 v21, v21
	v_rndne_f32_e32 v46, v46
	v_rndne_f32_e32 v47, v47
	v_rndne_f32_e32 v24, v24
	v_rndne_f32_e32 v25, v25
	v_rndne_f32_e32 v44, v44
	v_rndne_f32_e32 v45, v45
	v_rndne_f32_e32 v50, v50
	v_rndne_f32_e32 v51, v51
	v_rndne_f32_e32 v48, v48
	v_rndne_f32_e32 v49, v49
	v_rndne_f32_e32 v54, v54
	v_rndne_f32_e32 v55, v55
	v_rndne_f32_e32 v52, v52
	v_rndne_f32_e32 v53, v53
	v_rndne_f32_e32 v58, v58
	v_rndne_f32_e32 v59, v59
	v_rndne_f32_e32 v56, v56
	v_rndne_f32_e32 v57, v57
	v_rndne_f32_e32 v62, v62
	v_rndne_f32_e32 v63, v63
	v_rndne_f32_e32 v60, v60
	v_rndne_f32_e32 v61, v61
	v_rndne_f32_e32 v40, v40
	v_rndne_f32_e32 v41, v41
	v_rndne_f32_e32 v42, v42
	v_rndne_f32_e32 v43, v43
	ds_write2_b32 v31, v14, v15 offset1:1
	ds_write2_b32 v31, v16, v17 offset0:2 offset1:3
	ds_write2_b32 v32, v20, v21 offset1:1
	ds_write2_b32 v33, v46, v47 offset1:1
	ds_write2_b32 v34, v24, v25 offset1:1
	ds_write2_b32 v35, v44, v45 offset1:1
	ds_write2_b32 v36, v50, v51 offset1:1
	ds_write2_b32 v37, v48, v49 offset1:1
	ds_write2_b32 v38, v54, v55 offset1:1
	ds_write2_b32 v39, v52, v53 offset1:1
	ds_write2_b32 v87, v58, v59 offset1:1
	ds_write2_b32 v88, v56, v57 offset1:1
	ds_write2_b32 v89, v62, v63 offset1:1
	ds_write2_b32 v90, v60, v61 offset1:1
	ds_write2_b32 v91, v40, v41 offset1:1
	ds_write2_b32 v92, v42, v43 offset1:1
	s_waitcnt lgkmcnt(0)
	ds_read2_b32 v[14:15], v30 offset1:8
	ds_read2_b32 v[16:17], v30 offset0:33 offset1:41
	ds_read2_b32 v[20:21], v30 offset0:66 offset1:74
	ds_read2_b32 v[24:25], v30 offset0:99 offset1:107
	ds_read2_b32 v[40:41], v30 offset0:132 offset1:140
	ds_read2_b32 v[42:43], v30 offset0:165 offset1:173
	ds_read2_b32 v[44:45], v30 offset0:198 offset1:206
	ds_read2_b32 v[46:47], v30 offset0:231 offset1:239
	ds_read2_b32 v[48:49], v30 offset0:16 offset1:24
	ds_read2_b32 v[50:51], v30 offset0:49 offset1:57
	ds_read2_b32 v[52:53], v30 offset0:82 offset1:90
	ds_read2_b32 v[54:55], v30 offset0:115 offset1:123
	ds_read2_b32 v[56:57], v30 offset0:148 offset1:156
	ds_read2_b32 v[58:59], v30 offset0:181 offset1:189
	ds_read2_b32 v[60:61], v30 offset0:214 offset1:222
	ds_read2_b32 v[62:63], v30 offset0:247 offset1:255
	s_waitcnt lgkmcnt(14)
	v_cvt_i32_f32_e32 v16, v16
	s_waitcnt lgkmcnt(10)
	v_cvt_i32_f32_e32 v42, v42
	v_cvt_i32_f32_e32 v14, v14
	v_cvt_i32_f32_sdwa v20, v20 dst_sel:WORD_1 dst_unused:UNUSED_PAD src0_sel:DWORD
	v_cvt_i32_f32_e32 v40, v40
	s_waitcnt lgkmcnt(9)
	v_cvt_i32_f32_sdwa v44, v44 dst_sel:WORD_1 dst_unused:UNUSED_PAD src0_sel:DWORD
	v_cvt_i32_f32_e32 v17, v17
	v_cvt_i32_f32_e32 v43, v43
	s_waitcnt lgkmcnt(6)
	v_cvt_i32_f32_e32 v50, v50
	s_waitcnt lgkmcnt(2)
	v_cvt_i32_f32_e32 v58, v58
	v_cvt_i32_f32_e32 v51, v51
	v_cvt_i32_f32_e32 v59, v59
	v_cvt_i32_f32_sdwa v24, v24 dst_sel:BYTE_3 dst_unused:UNUSED_PAD src0_sel:DWORD
	v_cvt_i32_f32_sdwa v46, v46 dst_sel:BYTE_3 dst_unused:UNUSED_PAD src0_sel:DWORD
	v_cvt_i32_f32_e32 v15, v15
	v_cvt_i32_f32_sdwa v21, v21 dst_sel:WORD_1 dst_unused:UNUSED_PAD src0_sel:DWORD
	v_cvt_i32_f32_e32 v41, v41
	v_cvt_i32_f32_sdwa v45, v45 dst_sel:WORD_1 dst_unused:UNUSED_PAD src0_sel:DWORD
	v_cvt_i32_f32_e32 v48, v48
	v_cvt_i32_f32_sdwa v52, v52 dst_sel:WORD_1 dst_unused:UNUSED_PAD src0_sel:DWORD
	v_cvt_i32_f32_e32 v56, v56
	s_waitcnt lgkmcnt(1)
	v_cvt_i32_f32_sdwa v60, v60 dst_sel:WORD_1 dst_unused:UNUSED_PAD src0_sel:DWORD
	v_cvt_i32_f32_e32 v49, v49
	v_cvt_i32_f32_sdwa v53, v53 dst_sel:WORD_1 dst_unused:UNUSED_PAD src0_sel:DWORD
	v_cvt_i32_f32_e32 v57, v57
	v_cvt_i32_f32_sdwa v61, v61 dst_sel:WORD_1 dst_unused:UNUSED_PAD src0_sel:DWORD
	v_cvt_i32_f32_sdwa v25, v25 dst_sel:BYTE_3 dst_unused:UNUSED_PAD src0_sel:DWORD
	v_cvt_i32_f32_sdwa v47, v47 dst_sel:BYTE_3 dst_unused:UNUSED_PAD src0_sel:DWORD
	v_cvt_i32_f32_sdwa v54, v54 dst_sel:BYTE_3 dst_unused:UNUSED_PAD src0_sel:DWORD
	s_waitcnt lgkmcnt(0)
	v_cvt_i32_f32_sdwa v62, v62 dst_sel:BYTE_3 dst_unused:UNUSED_PAD src0_sel:DWORD
	v_cvt_i32_f32_sdwa v55, v55 dst_sel:BYTE_3 dst_unused:UNUSED_PAD src0_sel:DWORD
	v_cvt_i32_f32_sdwa v63, v63 dst_sel:BYTE_3 dst_unused:UNUSED_PAD src0_sel:DWORD
	v_lshlrev_b32_e32 v16, 8, v16
	v_lshlrev_b32_e32 v42, 8, v42
	v_and_b32_e32 v20, 0xff0000, v20
	v_and_b32_e32 v44, 0xff0000, v44
	v_lshlrev_b32_e32 v17, 8, v17
	v_lshlrev_b32_e32 v43, 8, v43
	v_lshlrev_b32_e32 v50, 8, v50
	v_lshlrev_b32_e32 v58, 8, v58
	v_lshlrev_b32_e32 v51, 8, v51
	v_lshlrev_b32_e32 v59, 8, v59
	v_perm_b32 v14, v16, v14, s28
	v_perm_b32 v16, v42, v40, s28
	v_and_b32_e32 v21, 0xff0000, v21
	v_and_b32_e32 v45, 0xff0000, v45
	v_and_b32_e32 v52, 0xff0000, v52
	v_and_b32_e32 v60, 0xff0000, v60
	v_and_b32_e32 v53, 0xff0000, v53
	v_and_b32_e32 v61, 0xff0000, v61
	v_perm_b32 v17, v17, v15, s28
	v_perm_b32 v40, v43, v41, s28
	v_perm_b32 v41, v50, v48, s28
	v_perm_b32 v42, v58, v56, s28
	v_perm_b32 v43, v51, v49, s28
	v_perm_b32 v48, v59, v57, s28
	v_or3_b32 v14, v14, v20, v24
	v_or3_b32 v15, v16, v44, v46
	v_or3_b32 v16, v17, v21, v25
	v_or3_b32 v17, v40, v45, v47
	v_or3_b32 v20, v41, v52, v54
	v_or3_b32 v21, v42, v60, v62
	v_or3_b32 v24, v43, v53, v55
	v_or3_b32 v25, v48, v61, v63
	global_store_dwordx2 v[18:19], v[14:15], off
	global_store_dwordx2 v[22:23], v[16:17], off
	global_store_dwordx2 v[82:83], v[20:21], off
	global_store_dwordx2 v[84:85], v[24:25], off
	s_waitcnt lgkmcnt(0)
; #define LAS __attribute__((address_space(3)))
; #define GAS __attribute__((address_space(1)))
; #define LDS_WAIT() asm volatile("s_waitcnt lgkmcnt(0)" ::: "memory")
;     ...
;     for (int kb = 0; kb < D / 64; ++kb) {
; #pragma unroll
;         for (int i = 0; i < 8; ++i) { const int kk = 8 * i + kr; const int k = 64 * kb + kk; const f32x4 v = __builtin_nontemporal_load((const f32x4*)(W + (size_t)k * pitch)) * g[k];
;             LAS float* p = scr + kk * 33 + 4 * (lane & 7); p[0] = __builtin_rintf(v[0] * inv[0]); p[1] = __builtin_rintf(v[1] * inv[1]); p[2] = __builtin_rintf(v[2] * inv[2]); p[3] = __builtin_rintf(v[3] * inv[3]); }
;         LDS_WAIT(); asm volatile("" ::: "memory");
;         const int c = lane & 7;
; #pragma unroll
;         for (int j = 0; j < 4; ++j) { const int n = (lane >> 3) + 8 * j; const LAS float* sp = scr + (8 * c) * 33 + n;
;             u32x2 o;
;             o.x = ((unsigned)(int)sp[0 * 33] & 0xFFu) | (((unsigned)(int)sp[1 * 33] & 0xFFu) << 8) | (((unsigned)(int)sp[2 * 33] & 0xFFu) << 16) | (((unsigned)(int)sp[3 * 33] & 0xFFu) << 24);
;             o.y = ((unsigned)(int)sp[4 * 33] & 0xFFu) | (((unsigned)(int)sp[5 * 33] & 0xFFu) << 8) | (((unsigned)(int)sp[6 * 33] & 0xFFu) << 16) | (((unsigned)(int)sp[7 * 33] & 0xFFu) << 24);
;             *(GAS u32x2*)(dst + (size_t)(n0 + n) * D + 64 * kb + 8 * c) = o; }
;         LDS_WAIT(); asm volatile("" ::: "memory");
	v_add_u32_e32 v87, 0x14a0, v31
	v_add_u32_e32 v88, 0x14a8, v31
	v_add_u32_e32 v89, 0x18c0, v31
	v_add_u32_e32 v90, 0x18c8, v31
	v_add_u32_e32 v91, 0x1ce0, v31
	v_add_u32_e32 v92, 0x1ce8, v31
	v_lshl_add_u64 v[18:19], v[6:7], 0, v[12:13]
	v_lshl_add_u64 v[22:23], v[6:7], 0, v[10:11]
	v_lshl_add_u64 v[82:83], v[6:7], 0, v[8:9]
	v_lshl_add_u64 v[84:85], v[6:7], 0, v[4:5]
	v_lshl_add_u64 v[6:7], v[6:7], 0, 64
	s_waitcnt vmcnt(20)
	v_pk_mul_f32 v[46:47], v[144:145], v[188:189] op_sel_hi:[1,0]
	v_pk_mul_f32 v[20:21], v[142:143], v[188:189] op_sel_hi:[1,0]
	v_pk_mul_f32 v[44:45], v[148:149], v[190:191] op_sel_hi:[1,0]
	v_pk_mul_f32 v[24:25], v[146:147], v[190:191] op_sel_hi:[1,0]
	v_pk_mul_f32 v[48:49], v[152:153], v[192:193] op_sel_hi:[1,0]
	v_pk_mul_f32 v[16:17], v[140:141], v[186:187] op_sel_hi:[1,0]
	v_pk_mul_f32 v[14:15], v[138:139], v[186:187] op_sel_hi:[1,0]
	v_pk_mul_f32 v[50:51], v[150:151], v[192:193] op_sel_hi:[1,0]
	v_pk_mul_f32 v[52:53], v[156:157], v[194:195] op_sel_hi:[1,0]
	v_pk_mul_f32 v[54:55], v[154:155], v[194:195] op_sel_hi:[1,0]
	v_pk_mul_f32 v[56:57], v[160:161], v[196:197] op_sel_hi:[1,0]
	v_pk_mul_f32 v[58:59], v[158:159], v[196:197] op_sel_hi:[1,0]
	v_pk_mul_f32 v[60:61], v[164:165], v[198:199] op_sel_hi:[1,0]
	v_pk_mul_f32 v[62:63], v[162:163], v[198:199] op_sel_hi:[1,0]
	v_pk_mul_f32 v[42:43], v[168:169], v[200:201] op_sel_hi:[1,0]
	v_pk_mul_f32 v[40:41], v[166:167], v[200:201] op_sel_hi:[1,0]
	s_add_u32 s4, s4, 0x18000
	s_addc_u32 s5, s5, 0
	global_load_dwordx4 v[138:141], v250, s[4:5] nt
	global_load_dword v186, v251, s[6:7] offset:768
	s_add_u32 s4, s4, 0x18000
	s_addc_u32 s5, s5, 0
	global_load_dwordx4 v[142:145], v250, s[4:5] nt
	global_load_dword v188, v251, s[6:7] offset:800
	s_add_u32 s4, s4, 0x18000
	s_addc_u32 s5, s5, 0
	global_load_dwordx4 v[146:149], v250, s[4:5] nt
	global_load_dword v190, v251, s[6:7] offset:832
	s_add_u32 s4, s4, 0x18000
	s_addc_u32 s5, s5, 0
	global_load_dwordx4 v[150:153], v250, s[4:5] nt
	global_load_dword v192, v251, s[6:7] offset:864
	s_add_u32 s4, s4, 0x18000
	s_addc_u32 s5, s5, 0
	global_load_dwordx4 v[154:157], v250, s[4:5] nt
	global_load_dword v194, v251, s[6:7] offset:896
	s_add_u32 s4, s4, 0x18000
	s_addc_u32 s5, s5, 0
	global_load_dwordx4 v[158:161], v250, s[4:5] nt
	global_load_dword v196, v251, s[6:7] offset:928
	s_add_u32 s4, s4, 0x18000
	s_addc_u32 s5, s5, 0
	global_load_dwordx4 v[162:165], v250, s[4:5] nt
	global_load_dword v198, v251, s[6:7] offset:960
	s_add_u32 s4, s4, 0x18000
	s_addc_u32 s5, s5, 0
	global_load_dwordx4 v[166:169], v250, s[4:5] nt
	global_load_dword v200, v251, s[6:7] offset:992
	v_mul_f32_e32 v14, v26, v14
	v_mul_f32_e32 v15, v27, v15
	v_mul_f32_e32 v16, v28, v16
	v_mul_f32_e32 v17, v29, v17
	v_mul_f32_e32 v20, v26, v20
	v_mul_f32_e32 v21, v27, v21
	v_mul_f32_e32 v46, v28, v46
	v_mul_f32_e32 v47, v29, v47
	v_mul_f32_e32 v24, v26, v24
	v_mul_f32_e32 v25, v27, v25
	v_mul_f32_e32 v44, v28, v44
	v_mul_f32_e32 v45, v29, v45
	v_mul_f32_e32 v50, v26, v50
	v_mul_f32_e32 v51, v27, v51
	v_mul_f32_e32 v48, v28, v48
	v_mul_f32_e32 v49, v29, v49
	v_mul_f32_e32 v54, v26, v54
	v_mul_f32_e32 v55, v27, v55
	v_mul_f32_e32 v52, v28, v52
	v_mul_f32_e32 v53, v29, v53
	v_mul_f32_e32 v58, v26, v58
	v_mul_f32_e32 v59, v27, v59
	v_mul_f32_e32 v56, v28, v56
	v_mul_f32_e32 v57, v29, v57
	v_mul_f32_e32 v62, v26, v62
	v_mul_f32_e32 v63, v27, v63
	v_mul_f32_e32 v60, v28, v60
	v_mul_f32_e32 v61, v29, v61
	v_mul_f32_e32 v40, v26, v40
	v_mul_f32_e32 v41, v27, v41
	v_mul_f32_e32 v42, v28, v42
	v_mul_f32_e32 v43, v29, v43
	v_rndne_f32_e32 v14, v14
	v_rndne_f32_e32 v15, v15
	v_rndne_f32_e32 v16, v16
	v_rndne_f32_e32 v17, v17
	v_rndne_f32_e32 v20, v20
	v_rndne_f32_e32 v21, v21
	v_rndne_f32_e32 v46, v46
	v_rndne_f32_e32 v47, v47
	v_rndne_f32_e32 v24, v24
	v_rndne_f32_e32 v25, v25
	v_rndne_f32_e32 v44, v44
	v_rndne_f32_e32 v45, v45
	v_rndne_f32_e32 v50, v50
	v_rndne_f32_e32 v51, v51
	v_rndne_f32_e32 v48, v48
	v_rndne_f32_e32 v49, v49
	v_rndne_f32_e32 v54, v54
	v_rndne_f32_e32 v55, v55
	v_rndne_f32_e32 v52, v52
	v_rndne_f32_e32 v53, v53
	v_rndne_f32_e32 v58, v58
	v_rndne_f32_e32 v59, v59
	v_rndne_f32_e32 v56, v56
	v_rndne_f32_e32 v57, v57
	v_rndne_f32_e32 v62, v62
	v_rndne_f32_e32 v63, v63
	v_rndne_f32_e32 v60, v60
	v_rndne_f32_e32 v61, v61
	v_rndne_f32_e32 v40, v40
	v_rndne_f32_e32 v41, v41
	v_rndne_f32_e32 v42, v42
	v_rndne_f32_e32 v43, v43
	ds_write2_b32 v31, v14, v15 offset1:1
	ds_write2_b32 v31, v16, v17 offset0:2 offset1:3
	ds_write2_b32 v32, v20, v21 offset1:1
	ds_write2_b32 v33, v46, v47 offset1:1
	ds_write2_b32 v34, v24, v25 offset1:1
	ds_write2_b32 v35, v44, v45 offset1:1
	ds_write2_b32 v36, v50, v51 offset1:1
	ds_write2_b32 v37, v48, v49 offset1:1
	ds_write2_b32 v38, v54, v55 offset1:1
	ds_write2_b32 v39, v52, v53 offset1:1
	ds_write2_b32 v87, v58, v59 offset1:1
	ds_write2_b32 v88, v56, v57 offset1:1
	ds_write2_b32 v89, v62, v63 offset1:1
	ds_write2_b32 v90, v60, v61 offset1:1
	ds_write2_b32 v91, v40, v41 offset1:1
	ds_write2_b32 v92, v42, v43 offset1:1
	s_waitcnt lgkmcnt(0)
	ds_read2_b32 v[14:15], v30 offset1:8
	ds_read2_b32 v[16:17], v30 offset0:33 offset1:41
	ds_read2_b32 v[20:21], v30 offset0:66 offset1:74
	ds_read2_b32 v[24:25], v30 offset0:99 offset1:107
	ds_read2_b32 v[40:41], v30 offset0:132 offset1:140
	ds_read2_b32 v[42:43], v30 offset0:165 offset1:173
	ds_read2_b32 v[44:45], v30 offset0:198 offset1:206
	ds_read2_b32 v[46:47], v30 offset0:231 offset1:239
	ds_read2_b32 v[48:49], v30 offset0:16 offset1:24
	ds_read2_b32 v[50:51], v30 offset0:49 offset1:57
	ds_read2_b32 v[52:53], v30 offset0:82 offset1:90
	ds_read2_b32 v[54:55], v30 offset0:115 offset1:123
	ds_read2_b32 v[56:57], v30 offset0:148 offset1:156
	ds_read2_b32 v[58:59], v30 offset0:181 offset1:189
	ds_read2_b32 v[60:61], v30 offset0:214 offset1:222
	ds_read2_b32 v[62:63], v30 offset0:247 offset1:255
	s_waitcnt lgkmcnt(14)
; #define LAS __attribute__((address_space(3)))
; #define GAS __attribute__((address_space(1)))
; #define LDS_WAIT() asm volatile("s_waitcnt lgkmcnt(0)" ::: "memory")
;     ...
;     for (int kb = 0; kb < D / 64; ++kb) {
; #pragma unroll
;         for (int i = 0; i < 8; ++i) { const int kk = 8 * i + kr; const int k = 64 * kb + kk; const f32x4 v = __builtin_nontemporal_load((const f32x4*)(W + (size_t)k * pitch)) * g[k];
;             LAS float* p = scr + kk * 33 + 4 * (lane & 7); p[0] = __builtin_rintf(v[0] * inv[0]); p[1] = __builtin_rintf(v[1] * inv[1]); p[2] = __builtin_rintf(v[2] * inv[2]); p[3] = __builtin_rintf(v[3] * inv[3]); }
;         LDS_WAIT(); asm volatile("" ::: "memory");
;         const int c = lane & 7;
; #pragma unroll
;         for (int j = 0; j < 4; ++j) { const int n = (lane >> 3) + 8 * j; const LAS float* sp = scr + (8 * c) * 33 + n;
;             u32x2 o;
;             o.x = ((unsigned)(int)sp[0 * 33] & 0xFFu) | (((unsigned)(int)sp[1 * 33] & 0xFFu) << 8) | (((unsigned)(int)sp[2 * 33] & 0xFFu) << 16) | (((unsigned)(int)sp[3 * 33] & 0xFFu) << 24);
;             o.y = ((unsigned)(int)sp[4 * 33] & 0xFFu) | (((unsigned)(int)sp[5 * 33] & 0xFFu) << 8) | (((unsigned)(int)sp[6 * 33] & 0xFFu) << 16) | (((unsigned)(int)sp[7 * 33] & 0xFFu) << 24);
;             *(GAS u32x2*)(dst + (size_t)(n0 + n) * D + 64 * kb + 8 * c) = o; }
;         LDS_WAIT(); asm volatile("" ::: "memory");
;     }
	v_cvt_i32_f32_e32 v16, v16
	s_waitcnt lgkmcnt(10)
	v_cvt_i32_f32_e32 v42, v42
	v_cvt_i32_f32_e32 v14, v14
	v_cvt_i32_f32_sdwa v20, v20 dst_sel:WORD_1 dst_unused:UNUSED_PAD src0_sel:DWORD
	v_cvt_i32_f32_e32 v40, v40
	s_waitcnt lgkmcnt(9)
	v_cvt_i32_f32_sdwa v44, v44 dst_sel:WORD_1 dst_unused:UNUSED_PAD src0_sel:DWORD
	v_cvt_i32_f32_e32 v17, v17
	v_cvt_i32_f32_e32 v43, v43
	s_waitcnt lgkmcnt(6)
	v_cvt_i32_f32_e32 v50, v50
	s_waitcnt lgkmcnt(2)
	v_cvt_i32_f32_e32 v58, v58
	v_cvt_i32_f32_e32 v51, v51
	v_cvt_i32_f32_e32 v59, v59
	v_cvt_i32_f32_sdwa v24, v24 dst_sel:BYTE_3 dst_unused:UNUSED_PAD src0_sel:DWORD
	v_cvt_i32_f32_sdwa v46, v46 dst_sel:BYTE_3 dst_unused:UNUSED_PAD src0_sel:DWORD
	v_cvt_i32_f32_e32 v15, v15
	v_cvt_i32_f32_sdwa v21, v21 dst_sel:WORD_1 dst_unused:UNUSED_PAD src0_sel:DWORD
	v_cvt_i32_f32_e32 v41, v41
	v_cvt_i32_f32_sdwa v45, v45 dst_sel:WORD_1 dst_unused:UNUSED_PAD src0_sel:DWORD
	v_cvt_i32_f32_e32 v48, v48
	v_cvt_i32_f32_sdwa v52, v52 dst_sel:WORD_1 dst_unused:UNUSED_PAD src0_sel:DWORD
	v_cvt_i32_f32_e32 v56, v56
	s_waitcnt lgkmcnt(1)
	v_cvt_i32_f32_sdwa v60, v60 dst_sel:WORD_1 dst_unused:UNUSED_PAD src0_sel:DWORD
	v_cvt_i32_f32_e32 v49, v49
	v_cvt_i32_f32_sdwa v53, v53 dst_sel:WORD_1 dst_unused:UNUSED_PAD src0_sel:DWORD
	v_cvt_i32_f32_e32 v57, v57
	v_cvt_i32_f32_sdwa v61, v61 dst_sel:WORD_1 dst_unused:UNUSED_PAD src0_sel:DWORD
	v_cvt_i32_f32_sdwa v25, v25 dst_sel:BYTE_3 dst_unused:UNUSED_PAD src0_sel:DWORD
	v_cvt_i32_f32_sdwa v47, v47 dst_sel:BYTE_3 dst_unused:UNUSED_PAD src0_sel:DWORD
	v_cvt_i32_f32_sdwa v54, v54 dst_sel:BYTE_3 dst_unused:UNUSED_PAD src0_sel:DWORD
	s_waitcnt lgkmcnt(0)
	v_cvt_i32_f32_sdwa v62, v62 dst_sel:BYTE_3 dst_unused:UNUSED_PAD src0_sel:DWORD
	v_cvt_i32_f32_sdwa v55, v55 dst_sel:BYTE_3 dst_unused:UNUSED_PAD src0_sel:DWORD
	v_cvt_i32_f32_sdwa v63, v63 dst_sel:BYTE_3 dst_unused:UNUSED_PAD src0_sel:DWORD
	v_lshlrev_b32_e32 v16, 8, v16
	v_lshlrev_b32_e32 v42, 8, v42
	v_and_b32_e32 v20, 0xff0000, v20
	v_and_b32_e32 v44, 0xff0000, v44
	v_lshlrev_b32_e32 v17, 8, v17
	v_lshlrev_b32_e32 v43, 8, v43
	v_lshlrev_b32_e32 v50, 8, v50
	v_lshlrev_b32_e32 v58, 8, v58
	v_lshlrev_b32_e32 v51, 8, v51
	v_lshlrev_b32_e32 v59, 8, v59
	v_perm_b32 v14, v16, v14, s28
	v_perm_b32 v16, v42, v40, s28
	v_and_b32_e32 v21, 0xff0000, v21
	v_and_b32_e32 v45, 0xff0000, v45
	v_and_b32_e32 v52, 0xff0000, v52
	v_and_b32_e32 v60, 0xff0000, v60
	v_and_b32_e32 v53, 0xff0000, v53
	v_and_b32_e32 v61, 0xff0000, v61
	v_perm_b32 v17, v17, v15, s28
	v_perm_b32 v40, v43, v41, s28
	v_perm_b32 v41, v50, v48, s28
	v_perm_b32 v42, v58, v56, s28
	v_perm_b32 v43, v51, v49, s28
	v_perm_b32 v48, v59, v57, s28
	v_or3_b32 v14, v14, v20, v24
	v_or3_b32 v15, v16, v44, v46
	v_or3_b32 v16, v17, v21, v25
	v_or3_b32 v17, v40, v45, v47
	v_or3_b32 v20, v41, v52, v54
	v_or3_b32 v21, v42, v60, v62
	v_or3_b32 v24, v43, v53, v55
	v_or3_b32 v25, v48, v61, v63
	global_store_dwordx2 v[18:19], v[14:15], off
	global_store_dwordx2 v[22:23], v[16:17], off
	global_store_dwordx2 v[82:83], v[20:21], off
	global_store_dwordx2 v[84:85], v[24:25], off
	s_waitcnt lgkmcnt(0)
	v_add_u32_e32 v87, 0x14a0, v31
	v_add_u32_e32 v88, 0x14a8, v31
	v_add_u32_e32 v89, 0x18c0, v31
	v_add_u32_e32 v90, 0x18c8, v31
	v_add_u32_e32 v91, 0x1ce0, v31
	v_add_u32_e32 v92, 0x1ce8, v31
	v_lshl_add_u64 v[18:19], v[6:7], 0, v[12:13]
	v_lshl_add_u64 v[22:23], v[6:7], 0, v[10:11]
	v_lshl_add_u64 v[82:83], v[6:7], 0, v[8:9]
	v_lshl_add_u64 v[84:85], v[6:7], 0, v[4:5]
	v_lshl_add_u64 v[6:7], v[6:7], 0, 64
	s_waitcnt vmcnt(24)
	v_pk_mul_f32 v[46:47], v[112:113], v[172:173] op_sel_hi:[1,0]
	v_pk_mul_f32 v[20:21], v[110:111], v[172:173] op_sel_hi:[1,0]
	v_pk_mul_f32 v[44:45], v[116:117], v[174:175] op_sel_hi:[1,0]
	v_pk_mul_f32 v[24:25], v[114:115], v[174:175] op_sel_hi:[1,0]
	v_pk_mul_f32 v[48:49], v[120:121], v[176:177] op_sel_hi:[1,0]
	v_pk_mul_f32 v[16:17], v[108:109], v[170:171] op_sel_hi:[1,0]
	v_pk_mul_f32 v[14:15], v[106:107], v[170:171] op_sel_hi:[1,0]
	v_pk_mul_f32 v[50:51], v[118:119], v[176:177] op_sel_hi:[1,0]
	v_pk_mul_f32 v[52:53], v[124:125], v[178:179] op_sel_hi:[1,0]
	v_pk_mul_f32 v[54:55], v[122:123], v[178:179] op_sel_hi:[1,0]
	v_pk_mul_f32 v[56:57], v[128:129], v[180:181] op_sel_hi:[1,0]
	v_pk_mul_f32 v[58:59], v[126:127], v[180:181] op_sel_hi:[1,0]
	v_pk_mul_f32 v[60:61], v[132:133], v[182:183] op_sel_hi:[1,0]
	v_pk_mul_f32 v[62:63], v[130:131], v[182:183] op_sel_hi:[1,0]
	v_pk_mul_f32 v[42:43], v[136:137], v[184:185] op_sel_hi:[1,0]
	v_pk_mul_f32 v[40:41], v[134:135], v[184:185] op_sel_hi:[1,0]
	s_add_u32 s4, s4, 0x18000
	s_addc_u32 s5, s5, 0
	global_load_dwordx4 v[106:109], v250, s[4:5] nt
	global_load_dword v170, v251, s[6:7] offset:1024
	s_add_u32 s4, s4, 0x18000
	s_addc_u32 s5, s5, 0
	global_load_dwordx4 v[110:113], v250, s[4:5] nt
	global_load_dword v172, v251, s[6:7] offset:1056
	s_add_u32 s4, s4, 0x18000
	s_addc_u32 s5, s5, 0
	global_load_dwordx4 v[114:117], v250, s[4:5] nt
	global_load_dword v174, v251, s[6:7] offset:1088
	s_add_u32 s4, s4, 0x18000
	s_addc_u32 s5, s5, 0
	global_load_dwordx4 v[118:121], v250, s[4:5] nt
	global_load_dword v176, v251, s[6:7] offset:1120
	s_add_u32 s4, s4, 0x18000
	s_addc_u32 s5, s5, 0
	global_load_dwordx4 v[122:125], v250, s[4:5] nt
	global_load_dword v178, v251, s[6:7] offset:1152
	s_add_u32 s4, s4, 0x18000
	s_addc_u32 s5, s5, 0
	global_load_dwordx4 v[126:129], v250, s[4:5] nt
	global_load_dword v180, v251, s[6:7] offset:1184
	s_add_u32 s4, s4, 0x18000
	s_addc_u32 s5, s5, 0
	global_load_dwordx4 v[130:133], v250, s[4:5] nt
	global_load_dword v182, v251, s[6:7] offset:1216
	s_add_u32 s4, s4, 0x18000
	s_addc_u32 s5, s5, 0
	global_load_dwordx4 v[134:137], v250, s[4:5] nt
; #define LAS __attribute__((address_space(3)))
; #define GAS __attribute__((address_space(1)))
; #define LDS_WAIT() asm volatile("s_waitcnt lgkmcnt(0)" ::: "memory")
;     ...
;         for (int i = 0; i < 8; ++i) { const int kk = 8 * i + kr; const int k = 64 * kb + kk; const f32x4 v = __builtin_nontemporal_load((const f32x4*)(W + (size_t)k * pitch)) * g[k];
;             LAS float* p = scr + kk * 33 + 4 * (lane & 7); p[0] = __builtin_rintf(v[0] * inv[0]); p[1] = __builtin_rintf(v[1] * inv[1]); p[2] = __builtin_rintf(v[2] * inv[2]); p[3] = __builtin_rintf(v[3] * inv[3]); }
;         LDS_WAIT(); asm volatile("" ::: "memory");
;         const int c = lane & 7;
; #pragma unroll
;         for (int j = 0; j < 4; ++j) { const int n = (lane >> 3) + 8 * j; const LAS float* sp = scr + (8 * c) * 33 + n;
;             u32x2 o;
;             o.x = ((unsigned)(int)sp[0 * 33] & 0xFFu) | (((unsigned)(int)sp[1 * 33] & 0xFFu) << 8) | (((unsigned)(int)sp[2 * 33] & 0xFFu) << 16) | (((unsigned)(int)sp[3 * 33] & 0xFFu) << 24);
;             o.y = ((unsigned)(int)sp[4 * 33] & 0xFFu) | (((unsigned)(int)sp[5 * 33] & 0xFFu) << 8) | (((unsigned)(int)sp[6 * 33] & 0xFFu) << 16) | (((unsigned)(int)sp[7 * 33] & 0xFFu) << 24);
;             *(GAS u32x2*)(dst + (size_t)(n0 + n) * D + 64 * kb + 8 * c) = o; }
;         LDS_WAIT(); asm volatile("" ::: "memory");
	global_load_dword v184, v251, s[6:7] offset:1248
	v_mul_f32_e32 v14, v26, v14
	v_mul_f32_e32 v15, v27, v15
	v_mul_f32_e32 v16, v28, v16
	v_mul_f32_e32 v17, v29, v17
	v_mul_f32_e32 v20, v26, v20
	v_mul_f32_e32 v21, v27, v21
	v_mul_f32_e32 v46, v28, v46
	v_mul_f32_e32 v47, v29, v47
	v_mul_f32_e32 v24, v26, v24
	v_mul_f32_e32 v25, v27, v25
	v_mul_f32_e32 v44, v28, v44
	v_mul_f32_e32 v45, v29, v45
	v_mul_f32_e32 v50, v26, v50
	v_mul_f32_e32 v51, v27, v51
	v_mul_f32_e32 v48, v28, v48
	v_mul_f32_e32 v49, v29, v49
	v_mul_f32_e32 v54, v26, v54
	v_mul_f32_e32 v55, v27, v55
	v_mul_f32_e32 v52, v28, v52
	v_mul_f32_e32 v53, v29, v53
	v_mul_f32_e32 v58, v26, v58
	v_mul_f32_e32 v59, v27, v59
	v_mul_f32_e32 v56, v28, v56
	v_mul_f32_e32 v57, v29, v57
	v_mul_f32_e32 v62, v26, v62
	v_mul_f32_e32 v63, v27, v63
	v_mul_f32_e32 v60, v28, v60
	v_mul_f32_e32 v61, v29, v61
	v_mul_f32_e32 v40, v26, v40
	v_mul_f32_e32 v41, v27, v41
	v_mul_f32_e32 v42, v28, v42
	v_mul_f32_e32 v43, v29, v43
	v_rndne_f32_e32 v14, v14
	v_rndne_f32_e32 v15, v15
	v_rndne_f32_e32 v16, v16
	v_rndne_f32_e32 v17, v17
	v_rndne_f32_e32 v20, v20
	v_rndne_f32_e32 v21, v21
	v_rndne_f32_e32 v46, v46
	v_rndne_f32_e32 v47, v47
	v_rndne_f32_e32 v24, v24
	v_rndne_f32_e32 v25, v25
	v_rndne_f32_e32 v44, v44
	v_rndne_f32_e32 v45, v45
	v_rndne_f32_e32 v50, v50
	v_rndne_f32_e32 v51, v51
	v_rndne_f32_e32 v48, v48
	v_rndne_f32_e32 v49, v49
	v_rndne_f32_e32 v54, v54
	v_rndne_f32_e32 v55, v55
	v_rndne_f32_e32 v52, v52
	v_rndne_f32_e32 v53, v53
	v_rndne_f32_e32 v58, v58
	v_rndne_f32_e32 v59, v59
	v_rndne_f32_e32 v56, v56
	v_rndne_f32_e32 v57, v57
	v_rndne_f32_e32 v62, v62
	v_rndne_f32_e32 v63, v63
	v_rndne_f32_e32 v60, v60
	v_rndne_f32_e32 v61, v61
	v_rndne_f32_e32 v40, v40
	v_rndne_f32_e32 v41, v41
	v_rndne_f32_e32 v42, v42
	v_rndne_f32_e32 v43, v43
	ds_write2_b32 v31, v14, v15 offset1:1
	ds_write2_b32 v31, v16, v17 offset0:2 offset1:3
	ds_write2_b32 v32, v20, v21 offset1:1
	ds_write2_b32 v33, v46, v47 offset1:1
	ds_write2_b32 v34, v24, v25 offset1:1
	ds_write2_b32 v35, v44, v45 offset1:1
	ds_write2_b32 v36, v50, v51 offset1:1
	ds_write2_b32 v37, v48, v49 offset1:1
	ds_write2_b32 v38, v54, v55 offset1:1
	ds_write2_b32 v39, v52, v53 offset1:1
	ds_write2_b32 v87, v58, v59 offset1:1
	ds_write2_b32 v88, v56, v57 offset1:1
	ds_write2_b32 v89, v62, v63 offset1:1
	ds_write2_b32 v90, v60, v61 offset1:1
	ds_write2_b32 v91, v40, v41 offset1:1
	ds_write2_b32 v92, v42, v43 offset1:1
	s_waitcnt lgkmcnt(0)
	ds_read2_b32 v[14:15], v30 offset1:8
	ds_read2_b32 v[16:17], v30 offset0:33 offset1:41
	ds_read2_b32 v[20:21], v30 offset0:66 offset1:74
	ds_read2_b32 v[24:25], v30 offset0:99 offset1:107
	ds_read2_b32 v[40:41], v30 offset0:132 offset1:140
	ds_read2_b32 v[42:43], v30 offset0:165 offset1:173
	ds_read2_b32 v[44:45], v30 offset0:198 offset1:206
	ds_read2_b32 v[46:47], v30 offset0:231 offset1:239
	ds_read2_b32 v[48:49], v30 offset0:16 offset1:24
	ds_read2_b32 v[50:51], v30 offset0:49 offset1:57
	ds_read2_b32 v[52:53], v30 offset0:82 offset1:90
	ds_read2_b32 v[54:55], v30 offset0:115 offset1:123
	ds_read2_b32 v[56:57], v30 offset0:148 offset1:156
	ds_read2_b32 v[58:59], v30 offset0:181 offset1:189
	ds_read2_b32 v[60:61], v30 offset0:214 offset1:222
	ds_read2_b32 v[62:63], v30 offset0:247 offset1:255
	s_waitcnt lgkmcnt(14)
	v_cvt_i32_f32_e32 v16, v16
	s_waitcnt lgkmcnt(10)
	v_cvt_i32_f32_e32 v42, v42
	v_cvt_i32_f32_e32 v14, v14
	v_cvt_i32_f32_sdwa v20, v20 dst_sel:WORD_1 dst_unused:UNUSED_PAD src0_sel:DWORD
	v_cvt_i32_f32_e32 v40, v40
	s_waitcnt lgkmcnt(9)
	v_cvt_i32_f32_sdwa v44, v44 dst_sel:WORD_1 dst_unused:UNUSED_PAD src0_sel:DWORD
	v_cvt_i32_f32_e32 v17, v17
	v_cvt_i32_f32_e32 v43, v43
	s_waitcnt lgkmcnt(6)
	v_cvt_i32_f32_e32 v50, v50
	s_waitcnt lgkmcnt(2)
	v_cvt_i32_f32_e32 v58, v58
	v_cvt_i32_f32_e32 v51, v51
	v_cvt_i32_f32_e32 v59, v59
	v_cvt_i32_f32_sdwa v24, v24 dst_sel:BYTE_3 dst_unused:UNUSED_PAD src0_sel:DWORD
	v_cvt_i32_f32_sdwa v46, v46 dst_sel:BYTE_3 dst_unused:UNUSED_PAD src0_sel:DWORD
	v_cvt_i32_f32_e32 v15, v15
	v_cvt_i32_f32_sdwa v21, v21 dst_sel:WORD_1 dst_unused:UNUSED_PAD src0_sel:DWORD
	v_cvt_i32_f32_e32 v41, v41
	v_cvt_i32_f32_sdwa v45, v45 dst_sel:WORD_1 dst_unused:UNUSED_PAD src0_sel:DWORD
	v_cvt_i32_f32_e32 v48, v48
	v_cvt_i32_f32_sdwa v52, v52 dst_sel:WORD_1 dst_unused:UNUSED_PAD src0_sel:DWORD
	v_cvt_i32_f32_e32 v56, v56
	s_waitcnt lgkmcnt(1)
	v_cvt_i32_f32_sdwa v60, v60 dst_sel:WORD_1 dst_unused:UNUSED_PAD src0_sel:DWORD
	v_cvt_i32_f32_e32 v49, v49
	v_cvt_i32_f32_sdwa v53, v53 dst_sel:WORD_1 dst_unused:UNUSED_PAD src0_sel:DWORD
	v_cvt_i32_f32_e32 v57, v57
	v_cvt_i32_f32_sdwa v61, v61 dst_sel:WORD_1 dst_unused:UNUSED_PAD src0_sel:DWORD
	v_cvt_i32_f32_sdwa v25, v25 dst_sel:BYTE_3 dst_unused:UNUSED_PAD src0_sel:DWORD
	v_cvt_i32_f32_sdwa v47, v47 dst_sel:BYTE_3 dst_unused:UNUSED_PAD src0_sel:DWORD
	v_cvt_i32_f32_sdwa v54, v54 dst_sel:BYTE_3 dst_unused:UNUSED_PAD src0_sel:DWORD
	s_waitcnt lgkmcnt(0)
; #define LAS __attribute__((address_space(3)))
; #define GAS __attribute__((address_space(1)))
; #define LDS_WAIT() asm volatile("s_waitcnt lgkmcnt(0)" ::: "memory")
;     ...
;         for (int i = 0; i < 8; ++i) { const int kk = 8 * i + kr; const int k = 64 * kb + kk; const f32x4 v = __builtin_nontemporal_load((const f32x4*)(W + (size_t)k * pitch)) * g[k];
;             LAS float* p = scr + kk * 33 + 4 * (lane & 7); p[0] = __builtin_rintf(v[0] * inv[0]); p[1] = __builtin_rintf(v[1] * inv[1]); p[2] = __builtin_rintf(v[2] * inv[2]); p[3] = __builtin_rintf(v[3] * inv[3]); }
;         LDS_WAIT(); asm volatile("" ::: "memory");
;         const int c = lane & 7;
; #pragma unroll
;         for (int j = 0; j < 4; ++j) { const int n = (lane >> 3) + 8 * j; const LAS float* sp = scr + (8 * c) * 33 + n;
;             u32x2 o;
;             o.x = ((unsigned)(int)sp[0 * 33] & 0xFFu) | (((unsigned)(int)sp[1 * 33] & 0xFFu) << 8) | (((unsigned)(int)sp[2 * 33] & 0xFFu) << 16) | (((unsigned)(int)sp[3 * 33] & 0xFFu) << 24);
;             o.y = ((unsigned)(int)sp[4 * 33] & 0xFFu) | (((unsigned)(int)sp[5 * 33] & 0xFFu) << 8) | (((unsigned)(int)sp[6 * 33] & 0xFFu) << 16) | (((unsigned)(int)sp[7 * 33] & 0xFFu) << 24);
;             *(GAS u32x2*)(dst + (size_t)(n0 + n) * D + 64 * kb + 8 * c) = o; }
;         LDS_WAIT(); asm volatile("" ::: "memory");
	v_cvt_i32_f32_sdwa v62, v62 dst_sel:BYTE_3 dst_unused:UNUSED_PAD src0_sel:DWORD
	v_cvt_i32_f32_sdwa v55, v55 dst_sel:BYTE_3 dst_unused:UNUSED_PAD src0_sel:DWORD
	v_cvt_i32_f32_sdwa v63, v63 dst_sel:BYTE_3 dst_unused:UNUSED_PAD src0_sel:DWORD
	v_lshlrev_b32_e32 v16, 8, v16
	v_lshlrev_b32_e32 v42, 8, v42
	v_and_b32_e32 v20, 0xff0000, v20
	v_and_b32_e32 v44, 0xff0000, v44
	v_lshlrev_b32_e32 v17, 8, v17
	v_lshlrev_b32_e32 v43, 8, v43
	v_lshlrev_b32_e32 v50, 8, v50
	v_lshlrev_b32_e32 v58, 8, v58
	v_lshlrev_b32_e32 v51, 8, v51
	v_lshlrev_b32_e32 v59, 8, v59
	v_perm_b32 v14, v16, v14, s28
	v_perm_b32 v16, v42, v40, s28
	v_and_b32_e32 v21, 0xff0000, v21
	v_and_b32_e32 v45, 0xff0000, v45
	v_and_b32_e32 v52, 0xff0000, v52
	v_and_b32_e32 v60, 0xff0000, v60
	v_and_b32_e32 v53, 0xff0000, v53
	v_and_b32_e32 v61, 0xff0000, v61
	v_perm_b32 v17, v17, v15, s28
	v_perm_b32 v40, v43, v41, s28
	v_perm_b32 v41, v50, v48, s28
	v_perm_b32 v42, v58, v56, s28
	v_perm_b32 v43, v51, v49, s28
	v_perm_b32 v48, v59, v57, s28
	v_or3_b32 v14, v14, v20, v24
	v_or3_b32 v15, v16, v44, v46
	v_or3_b32 v16, v17, v21, v25
	v_or3_b32 v17, v40, v45, v47
	v_or3_b32 v20, v41, v52, v54
	v_or3_b32 v21, v42, v60, v62
	v_or3_b32 v24, v43, v53, v55
	v_or3_b32 v25, v48, v61, v63
	global_store_dwordx2 v[18:19], v[14:15], off
	global_store_dwordx2 v[22:23], v[16:17], off
	global_store_dwordx2 v[82:83], v[20:21], off
	global_store_dwordx2 v[84:85], v[24:25], off
	s_waitcnt lgkmcnt(0)
	v_add_u32_e32 v87, 0x14a0, v31
	v_add_u32_e32 v88, 0x14a8, v31
	v_add_u32_e32 v89, 0x18c0, v31
	v_add_u32_e32 v90, 0x18c8, v31
	v_add_u32_e32 v91, 0x1ce0, v31
	v_add_u32_e32 v92, 0x1ce8, v31
	v_lshl_add_u64 v[18:19], v[6:7], 0, v[12:13]
	v_lshl_add_u64 v[22:23], v[6:7], 0, v[10:11]
	v_lshl_add_u64 v[82:83], v[6:7], 0, v[8:9]
	v_lshl_add_u64 v[84:85], v[6:7], 0, v[4:5]
	v_lshl_add_u64 v[6:7], v[6:7], 0, 64
	s_waitcnt vmcnt(24)
	v_pk_mul_f32 v[46:47], v[144:145], v[188:189] op_sel_hi:[1,0]
	v_pk_mul_f32 v[20:21], v[142:143], v[188:189] op_sel_hi:[1,0]
	v_pk_mul_f32 v[44:45], v[148:149], v[190:191] op_sel_hi:[1,0]
	v_pk_mul_f32 v[24:25], v[146:147], v[190:191] op_sel_hi:[1,0]
	v_pk_mul_f32 v[48:49], v[152:153], v[192:193] op_sel_hi:[1,0]
	v_pk_mul_f32 v[16:17], v[140:141], v[186:187] op_sel_hi:[1,0]
	v_pk_mul_f32 v[14:15], v[138:139], v[186:187] op_sel_hi:[1,0]
	v_pk_mul_f32 v[50:51], v[150:151], v[192:193] op_sel_hi:[1,0]
	v_pk_mul_f32 v[52:53], v[156:157], v[194:195] op_sel_hi:[1,0]
	v_pk_mul_f32 v[54:55], v[154:155], v[194:195] op_sel_hi:[1,0]
	v_pk_mul_f32 v[56:57], v[160:161], v[196:197] op_sel_hi:[1,0]
	v_pk_mul_f32 v[58:59], v[158:159], v[196:197] op_sel_hi:[1,0]
	v_pk_mul_f32 v[60:61], v[164:165], v[198:199] op_sel_hi:[1,0]
	v_pk_mul_f32 v[62:63], v[162:163], v[198:199] op_sel_hi:[1,0]
	v_pk_mul_f32 v[42:43], v[168:169], v[200:201] op_sel_hi:[1,0]
	v_pk_mul_f32 v[40:41], v[166:167], v[200:201] op_sel_hi:[1,0]
	s_add_u32 s4, s4, 0x18000
	s_addc_u32 s5, s5, 0
	global_load_dwordx4 v[138:141], v250, s[4:5] nt
	global_load_dword v186, v251, s[6:7] offset:1280
	s_add_u32 s4, s4, 0x18000
	s_addc_u32 s5, s5, 0
	global_load_dwordx4 v[142:145], v250, s[4:5] nt
	global_load_dword v188, v251, s[6:7] offset:1312
	s_add_u32 s4, s4, 0x18000
	s_addc_u32 s5, s5, 0
	global_load_dwordx4 v[146:149], v250, s[4:5] nt
	global_load_dword v190, v251, s[6:7] offset:1344
	s_add_u32 s4, s4, 0x18000
	s_addc_u32 s5, s5, 0
	global_load_dwordx4 v[150:153], v250, s[4:5] nt
	global_load_dword v192, v251, s[6:7] offset:1376
	s_add_u32 s4, s4, 0x18000
	s_addc_u32 s5, s5, 0
	global_load_dwordx4 v[154:157], v250, s[4:5] nt
	global_load_dword v194, v251, s[6:7] offset:1408
	s_add_u32 s4, s4, 0x18000
	s_addc_u32 s5, s5, 0
	global_load_dwordx4 v[158:161], v250, s[4:5] nt
	global_load_dword v196, v251, s[6:7] offset:1440
	s_add_u32 s4, s4, 0x18000
	s_addc_u32 s5, s5, 0
	global_load_dwordx4 v[162:165], v250, s[4:5] nt
	global_load_dword v198, v251, s[6:7] offset:1472
	s_add_u32 s4, s4, 0x18000
	s_addc_u32 s5, s5, 0
	global_load_dwordx4 v[166:169], v250, s[4:5] nt
	global_load_dword v200, v251, s[6:7] offset:1504
	v_mul_f32_e32 v14, v26, v14
	v_mul_f32_e32 v15, v27, v15
	v_mul_f32_e32 v16, v28, v16
	v_mul_f32_e32 v17, v29, v17
	v_mul_f32_e32 v20, v26, v20
	v_mul_f32_e32 v21, v27, v21
	v_mul_f32_e32 v46, v28, v46
	v_mul_f32_e32 v47, v29, v47
	v_mul_f32_e32 v24, v26, v24
	v_mul_f32_e32 v25, v27, v25
	v_mul_f32_e32 v44, v28, v44
	v_mul_f32_e32 v45, v29, v45
	v_mul_f32_e32 v50, v26, v50
	v_mul_f32_e32 v51, v27, v51
	v_mul_f32_e32 v48, v28, v48
	v_mul_f32_e32 v49, v29, v49
	v_mul_f32_e32 v54, v26, v54
	v_mul_f32_e32 v55, v27, v55
	v_mul_f32_e32 v52, v28, v52
	v_mul_f32_e32 v53, v29, v53
	v_mul_f32_e32 v58, v26, v58
	v_mul_f32_e32 v59, v27, v59
	v_mul_f32_e32 v56, v28, v56
	v_mul_f32_e32 v57, v29, v57
	v_mul_f32_e32 v62, v26, v62
	v_mul_f32_e32 v63, v27, v63
	v_mul_f32_e32 v60, v28, v60
	v_mul_f32_e32 v61, v29, v61
	v_mul_f32_e32 v40, v26, v40
	v_mul_f32_e32 v41, v27, v41
	v_mul_f32_e32 v42, v28, v42
	v_mul_f32_e32 v43, v29, v43
	v_rndne_f32_e32 v14, v14
	v_rndne_f32_e32 v15, v15
	v_rndne_f32_e32 v16, v16
	v_rndne_f32_e32 v17, v17
	v_rndne_f32_e32 v20, v20
	v_rndne_f32_e32 v21, v21
	v_rndne_f32_e32 v46, v46
	v_rndne_f32_e32 v47, v47
	v_rndne_f32_e32 v24, v24
	v_rndne_f32_e32 v25, v25
	v_rndne_f32_e32 v44, v44
	v_rndne_f32_e32 v45, v45
	v_rndne_f32_e32 v50, v50
	v_rndne_f32_e32 v51, v51
	v_rndne_f32_e32 v48, v48
	v_rndne_f32_e32 v49, v49
	v_rndne_f32_e32 v54, v54
	v_rndne_f32_e32 v55, v55
	v_rndne_f32_e32 v52, v52
	v_rndne_f32_e32 v53, v53
	v_rndne_f32_e32 v58, v58
	v_rndne_f32_e32 v59, v59
	v_rndne_f32_e32 v56, v56
	v_rndne_f32_e32 v57, v57
	v_rndne_f32_e32 v62, v62
	v_rndne_f32_e32 v63, v63
	v_rndne_f32_e32 v60, v60
	v_rndne_f32_e32 v61, v61
	v_rndne_f32_e32 v40, v40
	v_rndne_f32_e32 v41, v41
	v_rndne_f32_e32 v42, v42
	v_rndne_f32_e32 v43, v43
	ds_write2_b32 v31, v14, v15 offset1:1
	ds_write2_b32 v31, v16, v17 offset0:2 offset1:3
	ds_write2_b32 v32, v20, v21 offset1:1
	ds_write2_b32 v33, v46, v47 offset1:1
	ds_write2_b32 v34, v24, v25 offset1:1
	ds_write2_b32 v35, v44, v45 offset1:1
	ds_write2_b32 v36, v50, v51 offset1:1
	ds_write2_b32 v37, v48, v49 offset1:1
	ds_write2_b32 v38, v54, v55 offset1:1
	ds_write2_b32 v39, v52, v53 offset1:1
	ds_write2_b32 v87, v58, v59 offset1:1
	ds_write2_b32 v88, v56, v57 offset1:1
	ds_write2_b32 v89, v62, v63 offset1:1
	ds_write2_b32 v90, v60, v61 offset1:1
	ds_write2_b32 v91, v40, v41 offset1:1
	ds_write2_b32 v92, v42, v43 offset1:1
	s_waitcnt lgkmcnt(0)
; #define LAS __attribute__((address_space(3)))
; #define GAS __attribute__((address_space(1)))
; #define LDS_WAIT() asm volatile("s_waitcnt lgkmcnt(0)" ::: "memory")
;     ...
;         const int c = lane & 7;
; #pragma unroll
;         for (int j = 0; j < 4; ++j) { const int n = (lane >> 3) + 8 * j; const LAS float* sp = scr + (8 * c) * 33 + n;
;             u32x2 o;
;             o.x = ((unsigned)(int)sp[0 * 33] & 0xFFu) | (((unsigned)(int)sp[1 * 33] & 0xFFu) << 8) | (((unsigned)(int)sp[2 * 33] & 0xFFu) << 16) | (((unsigned)(int)sp[3 * 33] & 0xFFu) << 24);
;             o.y = ((unsigned)(int)sp[4 * 33] & 0xFFu) | (((unsigned)(int)sp[5 * 33] & 0xFFu) << 8) | (((unsigned)(int)sp[6 * 33] & 0xFFu) << 16) | (((unsigned)(int)sp[7 * 33] & 0xFFu) << 24);
;             *(GAS u32x2*)(dst + (size_t)(n0 + n) * D + 64 * kb + 8 * c) = o; }
;         LDS_WAIT(); asm volatile("" ::: "memory");
	ds_read2_b32 v[14:15], v30 offset1:8
	ds_read2_b32 v[16:17], v30 offset0:33 offset1:41
	ds_read2_b32 v[20:21], v30 offset0:66 offset1:74
	ds_read2_b32 v[24:25], v30 offset0:99 offset1:107
	ds_read2_b32 v[40:41], v30 offset0:132 offset1:140
	ds_read2_b32 v[42:43], v30 offset0:165 offset1:173
	ds_read2_b32 v[44:45], v30 offset0:198 offset1:206
	ds_read2_b32 v[46:47], v30 offset0:231 offset1:239
	ds_read2_b32 v[48:49], v30 offset0:16 offset1:24
	ds_read2_b32 v[50:51], v30 offset0:49 offset1:57
	ds_read2_b32 v[52:53], v30 offset0:82 offset1:90
	ds_read2_b32 v[54:55], v30 offset0:115 offset1:123
	ds_read2_b32 v[56:57], v30 offset0:148 offset1:156
	ds_read2_b32 v[58:59], v30 offset0:181 offset1:189
	ds_read2_b32 v[60:61], v30 offset0:214 offset1:222
	ds_read2_b32 v[62:63], v30 offset0:247 offset1:255
	s_waitcnt lgkmcnt(14)
	v_cvt_i32_f32_e32 v16, v16
	s_waitcnt lgkmcnt(10)
	v_cvt_i32_f32_e32 v42, v42
	v_cvt_i32_f32_e32 v14, v14
	v_cvt_i32_f32_sdwa v20, v20 dst_sel:WORD_1 dst_unused:UNUSED_PAD src0_sel:DWORD
	v_cvt_i32_f32_e32 v40, v40
	s_waitcnt lgkmcnt(9)
	v_cvt_i32_f32_sdwa v44, v44 dst_sel:WORD_1 dst_unused:UNUSED_PAD src0_sel:DWORD
	v_cvt_i32_f32_e32 v17, v17
	v_cvt_i32_f32_e32 v43, v43
	s_waitcnt lgkmcnt(6)
	v_cvt_i32_f32_e32 v50, v50
	s_waitcnt lgkmcnt(2)
	v_cvt_i32_f32_e32 v58, v58
	v_cvt_i32_f32_e32 v51, v51
	v_cvt_i32_f32_e32 v59, v59
	v_cvt_i32_f32_sdwa v24, v24 dst_sel:BYTE_3 dst_unused:UNUSED_PAD src0_sel:DWORD
	v_cvt_i32_f32_sdwa v46, v46 dst_sel:BYTE_3 dst_unused:UNUSED_PAD src0_sel:DWORD
	v_cvt_i32_f32_e32 v15, v15
	v_cvt_i32_f32_sdwa v21, v21 dst_sel:WORD_1 dst_unused:UNUSED_PAD src0_sel:DWORD
	v_cvt_i32_f32_e32 v41, v41
	v_cvt_i32_f32_sdwa v45, v45 dst_sel:WORD_1 dst_unused:UNUSED_PAD src0_sel:DWORD
	v_cvt_i32_f32_e32 v48, v48
	v_cvt_i32_f32_sdwa v52, v52 dst_sel:WORD_1 dst_unused:UNUSED_PAD src0_sel:DWORD
	v_cvt_i32_f32_e32 v56, v56
	s_waitcnt lgkmcnt(1)
	v_cvt_i32_f32_sdwa v60, v60 dst_sel:WORD_1 dst_unused:UNUSED_PAD src0_sel:DWORD
	v_cvt_i32_f32_e32 v49, v49
	v_cvt_i32_f32_sdwa v53, v53 dst_sel:WORD_1 dst_unused:UNUSED_PAD src0_sel:DWORD
	v_cvt_i32_f32_e32 v57, v57
	v_cvt_i32_f32_sdwa v61, v61 dst_sel:WORD_1 dst_unused:UNUSED_PAD src0_sel:DWORD
	v_cvt_i32_f32_sdwa v25, v25 dst_sel:BYTE_3 dst_unused:UNUSED_PAD src0_sel:DWORD
	v_cvt_i32_f32_sdwa v47, v47 dst_sel:BYTE_3 dst_unused:UNUSED_PAD src0_sel:DWORD
	v_cvt_i32_f32_sdwa v54, v54 dst_sel:BYTE_3 dst_unused:UNUSED_PAD src0_sel:DWORD
	s_waitcnt lgkmcnt(0)
	v_cvt_i32_f32_sdwa v62, v62 dst_sel:BYTE_3 dst_unused:UNUSED_PAD src0_sel:DWORD
	v_cvt_i32_f32_sdwa v55, v55 dst_sel:BYTE_3 dst_unused:UNUSED_PAD src0_sel:DWORD
	v_cvt_i32_f32_sdwa v63, v63 dst_sel:BYTE_3 dst_unused:UNUSED_PAD src0_sel:DWORD
	v_lshlrev_b32_e32 v16, 8, v16
	v_lshlrev_b32_e32 v42, 8, v42
	v_and_b32_e32 v20, 0xff0000, v20
	v_and_b32_e32 v44, 0xff0000, v44
	v_lshlrev_b32_e32 v17, 8, v17
	v_lshlrev_b32_e32 v43, 8, v43
	v_lshlrev_b32_e32 v50, 8, v50
	v_lshlrev_b32_e32 v58, 8, v58
	v_lshlrev_b32_e32 v51, 8, v51
	v_lshlrev_b32_e32 v59, 8, v59
	v_perm_b32 v14, v16, v14, s28
	v_perm_b32 v16, v42, v40, s28
	v_and_b32_e32 v21, 0xff0000, v21
	v_and_b32_e32 v45, 0xff0000, v45
	v_and_b32_e32 v52, 0xff0000, v52
	v_and_b32_e32 v60, 0xff0000, v60
	v_and_b32_e32 v53, 0xff0000, v53
	v_and_b32_e32 v61, 0xff0000, v61
	v_perm_b32 v17, v17, v15, s28
	v_perm_b32 v40, v43, v41, s28
	v_perm_b32 v41, v50, v48, s28
	v_perm_b32 v42, v58, v56, s28
	v_perm_b32 v43, v51, v49, s28
	v_perm_b32 v48, v59, v57, s28
	v_or3_b32 v14, v14, v20, v24
	v_or3_b32 v15, v16, v44, v46
	v_or3_b32 v16, v17, v21, v25
	v_or3_b32 v17, v40, v45, v47
	v_or3_b32 v20, v41, v52, v54
	v_or3_b32 v21, v42, v60, v62
	v_or3_b32 v24, v43, v53, v55
	v_or3_b32 v25, v48, v61, v63
	global_store_dwordx2 v[18:19], v[14:15], off
	global_store_dwordx2 v[22:23], v[16:17], off
	global_store_dwordx2 v[82:83], v[20:21], off
	global_store_dwordx2 v[84:85], v[24:25], off
	s_waitcnt lgkmcnt(0)
	v_add_u32_e32 v87, 0x14a0, v31
	v_add_u32_e32 v88, 0x14a8, v31
	v_add_u32_e32 v89, 0x18c0, v31
	v_add_u32_e32 v90, 0x18c8, v31
	v_add_u32_e32 v91, 0x1ce0, v31
	v_add_u32_e32 v92, 0x1ce8, v31
	v_lshl_add_u64 v[18:19], v[6:7], 0, v[12:13]
	v_lshl_add_u64 v[22:23], v[6:7], 0, v[10:11]
	v_lshl_add_u64 v[82:83], v[6:7], 0, v[8:9]
	v_lshl_add_u64 v[84:85], v[6:7], 0, v[4:5]
	v_lshl_add_u64 v[6:7], v[6:7], 0, 64
	s_waitcnt vmcnt(24)
; #define LAS __attribute__((address_space(3)))
; #define GAS __attribute__((address_space(1)))
; #define LDS_WAIT() asm volatile("s_waitcnt lgkmcnt(0)" ::: "memory")
;     ...
;         for (int i = 0; i < 8; ++i) { const int kk = 8 * i + kr; const int k = 64 * kb + kk; const f32x4 v = __builtin_nontemporal_load((const f32x4*)(W + (size_t)k * pitch)) * g[k];
;             LAS float* p = scr + kk * 33 + 4 * (lane & 7); p[0] = __builtin_rintf(v[0] * inv[0]); p[1] = __builtin_rintf(v[1] * inv[1]); p[2] = __builtin_rintf(v[2] * inv[2]); p[3] = __builtin_rintf(v[3] * inv[3]); }
;         LDS_WAIT(); asm volatile("" ::: "memory");
;         const int c = lane & 7;
; #pragma unroll
;         for (int j = 0; j < 4; ++j) { const int n = (lane >> 3) + 8 * j; const LAS float* sp = scr + (8 * c) * 33 + n;
;             u32x2 o;
;             o.x = ((unsigned)(int)sp[0 * 33] & 0xFFu) | (((unsigned)(int)sp[1 * 33] & 0xFFu) << 8) | (((unsigned)(int)sp[2 * 33] & 0xFFu) << 16) | (((unsigned)(int)sp[3 * 33] & 0xFFu) << 24);
;             o.y = ((unsigned)(int)sp[4 * 33] & 0xFFu) | (((unsigned)(int)sp[5 * 33] & 0xFFu) << 8) | (((unsigned)(int)sp[6 * 33] & 0xFFu) << 16) | (((unsigned)(int)sp[7 * 33] & 0xFFu) << 24);
;             *(GAS u32x2*)(dst + (size_t)(n0 + n) * D + 64 * kb + 8 * c) = o; }
;         LDS_WAIT(); asm volatile("" ::: "memory");
	v_pk_mul_f32 v[46:47], v[112:113], v[172:173] op_sel_hi:[1,0]
	v_pk_mul_f32 v[20:21], v[110:111], v[172:173] op_sel_hi:[1,0]
	v_pk_mul_f32 v[44:45], v[116:117], v[174:175] op_sel_hi:[1,0]
	v_pk_mul_f32 v[24:25], v[114:115], v[174:175] op_sel_hi:[1,0]
	v_pk_mul_f32 v[48:49], v[120:121], v[176:177] op_sel_hi:[1,0]
	v_pk_mul_f32 v[16:17], v[108:109], v[170:171] op_sel_hi:[1,0]
	v_pk_mul_f32 v[14:15], v[106:107], v[170:171] op_sel_hi:[1,0]
	v_pk_mul_f32 v[50:51], v[118:119], v[176:177] op_sel_hi:[1,0]
	v_pk_mul_f32 v[52:53], v[124:125], v[178:179] op_sel_hi:[1,0]
	v_pk_mul_f32 v[54:55], v[122:123], v[178:179] op_sel_hi:[1,0]
	v_pk_mul_f32 v[56:57], v[128:129], v[180:181] op_sel_hi:[1,0]
	v_pk_mul_f32 v[58:59], v[126:127], v[180:181] op_sel_hi:[1,0]
	v_pk_mul_f32 v[60:61], v[132:133], v[182:183] op_sel_hi:[1,0]
	v_pk_mul_f32 v[62:63], v[130:131], v[182:183] op_sel_hi:[1,0]
	v_pk_mul_f32 v[42:43], v[136:137], v[184:185] op_sel_hi:[1,0]
	v_pk_mul_f32 v[40:41], v[134:135], v[184:185] op_sel_hi:[1,0]
	s_add_u32 s4, s4, 0x18000
	s_addc_u32 s5, s5, 0
	global_load_dwordx4 v[106:109], v250, s[4:5] nt
	global_load_dword v170, v251, s[6:7] offset:1536
	s_add_u32 s4, s4, 0x18000
	s_addc_u32 s5, s5, 0
	global_load_dwordx4 v[110:113], v250, s[4:5] nt
	global_load_dword v172, v251, s[6:7] offset:1568
	s_add_u32 s4, s4, 0x18000
	s_addc_u32 s5, s5, 0
	global_load_dwordx4 v[114:117], v250, s[4:5] nt
	global_load_dword v174, v251, s[6:7] offset:1600
	s_add_u32 s4, s4, 0x18000
	s_addc_u32 s5, s5, 0
	global_load_dwordx4 v[118:121], v250, s[4:5] nt
	global_load_dword v176, v251, s[6:7] offset:1632
	s_add_u32 s4, s4, 0x18000
	s_addc_u32 s5, s5, 0
	global_load_dwordx4 v[122:125], v250, s[4:5] nt
	global_load_dword v178, v251, s[6:7] offset:1664
	s_add_u32 s4, s4, 0x18000
	s_addc_u32 s5, s5, 0
	global_load_dwordx4 v[126:129], v250, s[4:5] nt
	global_load_dword v180, v251, s[6:7] offset:1696
	s_add_u32 s4, s4, 0x18000
	s_addc_u32 s5, s5, 0
	global_load_dwordx4 v[130:133], v250, s[4:5] nt
	global_load_dword v182, v251, s[6:7] offset:1728
	s_add_u32 s4, s4, 0x18000
	s_addc_u32 s5, s5, 0
	global_load_dwordx4 v[134:137], v250, s[4:5] nt
	global_load_dword v184, v251, s[6:7] offset:1760
	v_mul_f32_e32 v14, v26, v14
	v_mul_f32_e32 v15, v27, v15
	v_mul_f32_e32 v16, v28, v16
	v_mul_f32_e32 v17, v29, v17
	v_mul_f32_e32 v20, v26, v20
	v_mul_f32_e32 v21, v27, v21
	v_mul_f32_e32 v46, v28, v46
	v_mul_f32_e32 v47, v29, v47
	v_mul_f32_e32 v24, v26, v24
	v_mul_f32_e32 v25, v27, v25
	v_mul_f32_e32 v44, v28, v44
	v_mul_f32_e32 v45, v29, v45
	v_mul_f32_e32 v50, v26, v50
	v_mul_f32_e32 v51, v27, v51
	v_mul_f32_e32 v48, v28, v48
	v_mul_f32_e32 v49, v29, v49
	v_mul_f32_e32 v54, v26, v54
	v_mul_f32_e32 v55, v27, v55
	v_mul_f32_e32 v52, v28, v52
	v_mul_f32_e32 v53, v29, v53
	v_mul_f32_e32 v58, v26, v58
	v_mul_f32_e32 v59, v27, v59
	v_mul_f32_e32 v56, v28, v56
	v_mul_f32_e32 v57, v29, v57
	v_mul_f32_e32 v62, v26, v62
	v_mul_f32_e32 v63, v27, v63
	v_mul_f32_e32 v60, v28, v60
	v_mul_f32_e32 v61, v29, v61
	v_mul_f32_e32 v40, v26, v40
	v_mul_f32_e32 v41, v27, v41
	v_mul_f32_e32 v42, v28, v42
	v_mul_f32_e32 v43, v29, v43
	v_rndne_f32_e32 v14, v14
	v_rndne_f32_e32 v15, v15
	v_rndne_f32_e32 v16, v16
	v_rndne_f32_e32 v17, v17
	v_rndne_f32_e32 v20, v20
	v_rndne_f32_e32 v21, v21
	v_rndne_f32_e32 v46, v46
	v_rndne_f32_e32 v47, v47
	v_rndne_f32_e32 v24, v24
	v_rndne_f32_e32 v25, v25
	v_rndne_f32_e32 v44, v44
	v_rndne_f32_e32 v45, v45
	v_rndne_f32_e32 v50, v50
	v_rndne_f32_e32 v51, v51
	v_rndne_f32_e32 v48, v48
	v_rndne_f32_e32 v49, v49
	v_rndne_f32_e32 v54, v54
	v_rndne_f32_e32 v55, v55
	v_rndne_f32_e32 v52, v52
	v_rndne_f32_e32 v53, v53
	v_rndne_f32_e32 v58, v58
	v_rndne_f32_e32 v59, v59
	v_rndne_f32_e32 v56, v56
	v_rndne_f32_e32 v57, v57
	v_rndne_f32_e32 v62, v62
	v_rndne_f32_e32 v63, v63
	v_rndne_f32_e32 v60, v60
	v_rndne_f32_e32 v61, v61
	v_rndne_f32_e32 v40, v40
	v_rndne_f32_e32 v41, v41
	v_rndne_f32_e32 v42, v42
	v_rndne_f32_e32 v43, v43
	ds_write2_b32 v31, v14, v15 offset1:1
	ds_write2_b32 v31, v16, v17 offset0:2 offset1:3
	ds_write2_b32 v32, v20, v21 offset1:1
	ds_write2_b32 v33, v46, v47 offset1:1
	ds_write2_b32 v34, v24, v25 offset1:1
	ds_write2_b32 v35, v44, v45 offset1:1
	ds_write2_b32 v36, v50, v51 offset1:1
	ds_write2_b32 v37, v48, v49 offset1:1
	ds_write2_b32 v38, v54, v55 offset1:1
	ds_write2_b32 v39, v52, v53 offset1:1
	ds_write2_b32 v87, v58, v59 offset1:1
	ds_write2_b32 v88, v56, v57 offset1:1
	ds_write2_b32 v89, v62, v63 offset1:1
	ds_write2_b32 v90, v60, v61 offset1:1
	ds_write2_b32 v91, v40, v41 offset1:1
	ds_write2_b32 v92, v42, v43 offset1:1
	s_waitcnt lgkmcnt(0)
	ds_read2_b32 v[14:15], v30 offset1:8
	ds_read2_b32 v[16:17], v30 offset0:33 offset1:41
	ds_read2_b32 v[20:21], v30 offset0:66 offset1:74
	ds_read2_b32 v[24:25], v30 offset0:99 offset1:107
	ds_read2_b32 v[40:41], v30 offset0:132 offset1:140
	ds_read2_b32 v[42:43], v30 offset0:165 offset1:173
	ds_read2_b32 v[44:45], v30 offset0:198 offset1:206
	ds_read2_b32 v[46:47], v30 offset0:231 offset1:239
	ds_read2_b32 v[48:49], v30 offset0:16 offset1:24
	ds_read2_b32 v[50:51], v30 offset0:49 offset1:57
	ds_read2_b32 v[52:53], v30 offset0:82 offset1:90
	ds_read2_b32 v[54:55], v30 offset0:115 offset1:123
	ds_read2_b32 v[56:57], v30 offset0:148 offset1:156
	ds_read2_b32 v[58:59], v30 offset0:181 offset1:189
	ds_read2_b32 v[60:61], v30 offset0:214 offset1:222
	ds_read2_b32 v[62:63], v30 offset0:247 offset1:255
	s_waitcnt lgkmcnt(14)
	v_cvt_i32_f32_e32 v16, v16
	s_waitcnt lgkmcnt(10)
	v_cvt_i32_f32_e32 v42, v42
	v_cvt_i32_f32_e32 v14, v14
	v_cvt_i32_f32_sdwa v20, v20 dst_sel:WORD_1 dst_unused:UNUSED_PAD src0_sel:DWORD
	v_cvt_i32_f32_e32 v40, v40
	s_waitcnt lgkmcnt(9)
; #define LAS __attribute__((address_space(3)))
; #define GAS __attribute__((address_space(1)))
; #define LDS_WAIT() asm volatile("s_waitcnt lgkmcnt(0)" ::: "memory")
;     ...
;         for (int i = 0; i < 8; ++i) { const int kk = 8 * i + kr; const int k = 64 * kb + kk; const f32x4 v = __builtin_nontemporal_load((const f32x4*)(W + (size_t)k * pitch)) * g[k];
;             LAS float* p = scr + kk * 33 + 4 * (lane & 7); p[0] = __builtin_rintf(v[0] * inv[0]); p[1] = __builtin_rintf(v[1] * inv[1]); p[2] = __builtin_rintf(v[2] * inv[2]); p[3] = __builtin_rintf(v[3] * inv[3]); }
;         LDS_WAIT(); asm volatile("" ::: "memory");
;         const int c = lane & 7;
; #pragma unroll
;         for (int j = 0; j < 4; ++j) { const int n = (lane >> 3) + 8 * j; const LAS float* sp = scr + (8 * c) * 33 + n;
;             u32x2 o;
;             o.x = ((unsigned)(int)sp[0 * 33] & 0xFFu) | (((unsigned)(int)sp[1 * 33] & 0xFFu) << 8) | (((unsigned)(int)sp[2 * 33] & 0xFFu) << 16) | (((unsigned)(int)sp[3 * 33] & 0xFFu) << 24);
;             o.y = ((unsigned)(int)sp[4 * 33] & 0xFFu) | (((unsigned)(int)sp[5 * 33] & 0xFFu) << 8) | (((unsigned)(int)sp[6 * 33] & 0xFFu) << 16) | (((unsigned)(int)sp[7 * 33] & 0xFFu) << 24);
;             *(GAS u32x2*)(dst + (size_t)(n0 + n) * D + 64 * kb + 8 * c) = o; }
;         LDS_WAIT(); asm volatile("" ::: "memory");
	v_cvt_i32_f32_sdwa v44, v44 dst_sel:WORD_1 dst_unused:UNUSED_PAD src0_sel:DWORD
	v_cvt_i32_f32_e32 v17, v17
	v_cvt_i32_f32_e32 v43, v43
	s_waitcnt lgkmcnt(6)
	v_cvt_i32_f32_e32 v50, v50
	s_waitcnt lgkmcnt(2)
	v_cvt_i32_f32_e32 v58, v58
	v_cvt_i32_f32_e32 v51, v51
	v_cvt_i32_f32_e32 v59, v59
	v_cvt_i32_f32_sdwa v24, v24 dst_sel:BYTE_3 dst_unused:UNUSED_PAD src0_sel:DWORD
	v_cvt_i32_f32_sdwa v46, v46 dst_sel:BYTE_3 dst_unused:UNUSED_PAD src0_sel:DWORD
	v_cvt_i32_f32_e32 v15, v15
	v_cvt_i32_f32_sdwa v21, v21 dst_sel:WORD_1 dst_unused:UNUSED_PAD src0_sel:DWORD
	v_cvt_i32_f32_e32 v41, v41
	v_cvt_i32_f32_sdwa v45, v45 dst_sel:WORD_1 dst_unused:UNUSED_PAD src0_sel:DWORD
	v_cvt_i32_f32_e32 v48, v48
	v_cvt_i32_f32_sdwa v52, v52 dst_sel:WORD_1 dst_unused:UNUSED_PAD src0_sel:DWORD
	v_cvt_i32_f32_e32 v56, v56
	s_waitcnt lgkmcnt(1)
	v_cvt_i32_f32_sdwa v60, v60 dst_sel:WORD_1 dst_unused:UNUSED_PAD src0_sel:DWORD
	v_cvt_i32_f32_e32 v49, v49
	v_cvt_i32_f32_sdwa v53, v53 dst_sel:WORD_1 dst_unused:UNUSED_PAD src0_sel:DWORD
	v_cvt_i32_f32_e32 v57, v57
	v_cvt_i32_f32_sdwa v61, v61 dst_sel:WORD_1 dst_unused:UNUSED_PAD src0_sel:DWORD
	v_cvt_i32_f32_sdwa v25, v25 dst_sel:BYTE_3 dst_unused:UNUSED_PAD src0_sel:DWORD
	v_cvt_i32_f32_sdwa v47, v47 dst_sel:BYTE_3 dst_unused:UNUSED_PAD src0_sel:DWORD
	v_cvt_i32_f32_sdwa v54, v54 dst_sel:BYTE_3 dst_unused:UNUSED_PAD src0_sel:DWORD
	s_waitcnt lgkmcnt(0)
	v_cvt_i32_f32_sdwa v62, v62 dst_sel:BYTE_3 dst_unused:UNUSED_PAD src0_sel:DWORD
	v_cvt_i32_f32_sdwa v55, v55 dst_sel:BYTE_3 dst_unused:UNUSED_PAD src0_sel:DWORD
	v_cvt_i32_f32_sdwa v63, v63 dst_sel:BYTE_3 dst_unused:UNUSED_PAD src0_sel:DWORD
	v_lshlrev_b32_e32 v16, 8, v16
	v_lshlrev_b32_e32 v42, 8, v42
	v_and_b32_e32 v20, 0xff0000, v20
	v_and_b32_e32 v44, 0xff0000, v44
	v_lshlrev_b32_e32 v17, 8, v17
	v_lshlrev_b32_e32 v43, 8, v43
	v_lshlrev_b32_e32 v50, 8, v50
	v_lshlrev_b32_e32 v58, 8, v58
	v_lshlrev_b32_e32 v51, 8, v51
	v_lshlrev_b32_e32 v59, 8, v59
	v_perm_b32 v14, v16, v14, s28
	v_perm_b32 v16, v42, v40, s28
	v_and_b32_e32 v21, 0xff0000, v21
	v_and_b32_e32 v45, 0xff0000, v45
	v_and_b32_e32 v52, 0xff0000, v52
	v_and_b32_e32 v60, 0xff0000, v60
	v_and_b32_e32 v53, 0xff0000, v53
	v_and_b32_e32 v61, 0xff0000, v61
	v_perm_b32 v17, v17, v15, s28
	v_perm_b32 v40, v43, v41, s28
	v_perm_b32 v41, v50, v48, s28
	v_perm_b32 v42, v58, v56, s28
	v_perm_b32 v43, v51, v49, s28
	v_perm_b32 v48, v59, v57, s28
	v_or3_b32 v14, v14, v20, v24
	v_or3_b32 v15, v16, v44, v46
	v_or3_b32 v16, v17, v21, v25
	v_or3_b32 v17, v40, v45, v47
	v_or3_b32 v20, v41, v52, v54
	v_or3_b32 v21, v42, v60, v62
	v_or3_b32 v24, v43, v53, v55
	v_or3_b32 v25, v48, v61, v63
	global_store_dwordx2 v[18:19], v[14:15], off
	global_store_dwordx2 v[22:23], v[16:17], off
	global_store_dwordx2 v[82:83], v[20:21], off
	global_store_dwordx2 v[84:85], v[24:25], off
	s_waitcnt lgkmcnt(0)
	v_add_u32_e32 v87, 0x14a0, v31
	v_add_u32_e32 v88, 0x14a8, v31
	v_add_u32_e32 v89, 0x18c0, v31
	v_add_u32_e32 v90, 0x18c8, v31
	v_add_u32_e32 v91, 0x1ce0, v31
	v_add_u32_e32 v92, 0x1ce8, v31
	v_lshl_add_u64 v[18:19], v[6:7], 0, v[12:13]
	v_lshl_add_u64 v[22:23], v[6:7], 0, v[10:11]
	v_lshl_add_u64 v[82:83], v[6:7], 0, v[8:9]
	v_lshl_add_u64 v[84:85], v[6:7], 0, v[4:5]
	v_lshl_add_u64 v[6:7], v[6:7], 0, 64
	s_waitcnt vmcnt(24)
	v_pk_mul_f32 v[46:47], v[144:145], v[188:189] op_sel_hi:[1,0]
	v_pk_mul_f32 v[20:21], v[142:143], v[188:189] op_sel_hi:[1,0]
	v_pk_mul_f32 v[44:45], v[148:149], v[190:191] op_sel_hi:[1,0]
	v_pk_mul_f32 v[24:25], v[146:147], v[190:191] op_sel_hi:[1,0]
	v_pk_mul_f32 v[48:49], v[152:153], v[192:193] op_sel_hi:[1,0]
	v_pk_mul_f32 v[16:17], v[140:141], v[186:187] op_sel_hi:[1,0]
	v_pk_mul_f32 v[14:15], v[138:139], v[186:187] op_sel_hi:[1,0]
	v_pk_mul_f32 v[50:51], v[150:151], v[192:193] op_sel_hi:[1,0]
	v_pk_mul_f32 v[52:53], v[156:157], v[194:195] op_sel_hi:[1,0]
	v_pk_mul_f32 v[54:55], v[154:155], v[194:195] op_sel_hi:[1,0]
	v_pk_mul_f32 v[56:57], v[160:161], v[196:197] op_sel_hi:[1,0]
	v_pk_mul_f32 v[58:59], v[158:159], v[196:197] op_sel_hi:[1,0]
	v_pk_mul_f32 v[60:61], v[164:165], v[198:199] op_sel_hi:[1,0]
	v_pk_mul_f32 v[62:63], v[162:163], v[198:199] op_sel_hi:[1,0]
	v_pk_mul_f32 v[42:43], v[168:169], v[200:201] op_sel_hi:[1,0]
	v_pk_mul_f32 v[40:41], v[166:167], v[200:201] op_sel_hi:[1,0]
	s_add_u32 s4, s4, 0x18000
	s_addc_u32 s5, s5, 0
	global_load_dwordx4 v[138:141], v250, s[4:5] nt
	global_load_dword v186, v251, s[6:7] offset:1792
	s_add_u32 s4, s4, 0x18000
	s_addc_u32 s5, s5, 0
	global_load_dwordx4 v[142:145], v250, s[4:5] nt
	global_load_dword v188, v251, s[6:7] offset:1824
	s_add_u32 s4, s4, 0x18000
	s_addc_u32 s5, s5, 0
	global_load_dwordx4 v[146:149], v250, s[4:5] nt
	global_load_dword v190, v251, s[6:7] offset:1856
	s_add_u32 s4, s4, 0x18000
	s_addc_u32 s5, s5, 0
	global_load_dwordx4 v[150:153], v250, s[4:5] nt
	global_load_dword v192, v251, s[6:7] offset:1888
	s_add_u32 s4, s4, 0x18000
	s_addc_u32 s5, s5, 0
	global_load_dwordx4 v[154:157], v250, s[4:5] nt
	global_load_dword v194, v251, s[6:7] offset:1920
	s_add_u32 s4, s4, 0x18000
	s_addc_u32 s5, s5, 0
	global_load_dwordx4 v[158:161], v250, s[4:5] nt
	global_load_dword v196, v251, s[6:7] offset:1952
	s_add_u32 s4, s4, 0x18000
	s_addc_u32 s5, s5, 0
	global_load_dwordx4 v[162:165], v250, s[4:5] nt
	global_load_dword v198, v251, s[6:7] offset:1984
	s_add_u32 s4, s4, 0x18000
	s_addc_u32 s5, s5, 0
	global_load_dwordx4 v[166:169], v250, s[4:5] nt
	global_load_dword v200, v251, s[6:7] offset:2016
	v_mul_f32_e32 v14, v26, v14
	v_mul_f32_e32 v15, v27, v15
	v_mul_f32_e32 v16, v28, v16
	v_mul_f32_e32 v17, v29, v17
	v_mul_f32_e32 v20, v26, v20
	v_mul_f32_e32 v21, v27, v21
; #define LAS __attribute__((address_space(3)))
; #define GAS __attribute__((address_space(1)))
; #define LDS_WAIT() asm volatile("s_waitcnt lgkmcnt(0)" ::: "memory")
;     ...
;         for (int i = 0; i < 8; ++i) { const int kk = 8 * i + kr; const int k = 64 * kb + kk; const f32x4 v = __builtin_nontemporal_load((const f32x4*)(W + (size_t)k * pitch)) * g[k];
;             LAS float* p = scr + kk * 33 + 4 * (lane & 7); p[0] = __builtin_rintf(v[0] * inv[0]); p[1] = __builtin_rintf(v[1] * inv[1]); p[2] = __builtin_rintf(v[2] * inv[2]); p[3] = __builtin_rintf(v[3] * inv[3]); }
;         LDS_WAIT(); asm volatile("" ::: "memory");
;         const int c = lane & 7;
; #pragma unroll
;         for (int j = 0; j < 4; ++j) { const int n = (lane >> 3) + 8 * j; const LAS float* sp = scr + (8 * c) * 33 + n;
;             u32x2 o;
;             o.x = ((unsigned)(int)sp[0 * 33] & 0xFFu) | (((unsigned)(int)sp[1 * 33] & 0xFFu) << 8) | (((unsigned)(int)sp[2 * 33] & 0xFFu) << 16) | (((unsigned)(int)sp[3 * 33] & 0xFFu) << 24);
;             o.y = ((unsigned)(int)sp[4 * 33] & 0xFFu) | (((unsigned)(int)sp[5 * 33] & 0xFFu) << 8) | (((unsigned)(int)sp[6 * 33] & 0xFFu) << 16) | (((unsigned)(int)sp[7 * 33] & 0xFFu) << 24);
;             *(GAS u32x2*)(dst + (size_t)(n0 + n) * D + 64 * kb + 8 * c) = o; }
;         LDS_WAIT(); asm volatile("" ::: "memory");
	v_mul_f32_e32 v46, v28, v46
	v_mul_f32_e32 v47, v29, v47
	v_mul_f32_e32 v24, v26, v24
	v_mul_f32_e32 v25, v27, v25
	v_mul_f32_e32 v44, v28, v44
	v_mul_f32_e32 v45, v29, v45
	v_mul_f32_e32 v50, v26, v50
	v_mul_f32_e32 v51, v27, v51
	v_mul_f32_e32 v48, v28, v48
	v_mul_f32_e32 v49, v29, v49
	v_mul_f32_e32 v54, v26, v54
	v_mul_f32_e32 v55, v27, v55
	v_mul_f32_e32 v52, v28, v52
	v_mul_f32_e32 v53, v29, v53
	v_mul_f32_e32 v58, v26, v58
	v_mul_f32_e32 v59, v27, v59
	v_mul_f32_e32 v56, v28, v56
	v_mul_f32_e32 v57, v29, v57
	v_mul_f32_e32 v62, v26, v62
	v_mul_f32_e32 v63, v27, v63
	v_mul_f32_e32 v60, v28, v60
	v_mul_f32_e32 v61, v29, v61
	v_mul_f32_e32 v40, v26, v40
	v_mul_f32_e32 v41, v27, v41
	v_mul_f32_e32 v42, v28, v42
	v_mul_f32_e32 v43, v29, v43
	v_rndne_f32_e32 v14, v14
	v_rndne_f32_e32 v15, v15
	v_rndne_f32_e32 v16, v16
	v_rndne_f32_e32 v17, v17
	v_rndne_f32_e32 v20, v20
	v_rndne_f32_e32 v21, v21
	v_rndne_f32_e32 v46, v46
	v_rndne_f32_e32 v47, v47
	v_rndne_f32_e32 v24, v24
	v_rndne_f32_e32 v25, v25
	v_rndne_f32_e32 v44, v44
	v_rndne_f32_e32 v45, v45
	v_rndne_f32_e32 v50, v50
	v_rndne_f32_e32 v51, v51
	v_rndne_f32_e32 v48, v48
	v_rndne_f32_e32 v49, v49
	v_rndne_f32_e32 v54, v54
	v_rndne_f32_e32 v55, v55
	v_rndne_f32_e32 v52, v52
	v_rndne_f32_e32 v53, v53
	v_rndne_f32_e32 v58, v58
	v_rndne_f32_e32 v59, v59
	v_rndne_f32_e32 v56, v56
	v_rndne_f32_e32 v57, v57
	v_rndne_f32_e32 v62, v62
	v_rndne_f32_e32 v63, v63
	v_rndne_f32_e32 v60, v60
	v_rndne_f32_e32 v61, v61
	v_rndne_f32_e32 v40, v40
	v_rndne_f32_e32 v41, v41
	v_rndne_f32_e32 v42, v42
	v_rndne_f32_e32 v43, v43
	ds_write2_b32 v31, v14, v15 offset1:1
	ds_write2_b32 v31, v16, v17 offset0:2 offset1:3
	ds_write2_b32 v32, v20, v21 offset1:1
	ds_write2_b32 v33, v46, v47 offset1:1
	ds_write2_b32 v34, v24, v25 offset1:1
	ds_write2_b32 v35, v44, v45 offset1:1
	ds_write2_b32 v36, v50, v51 offset1:1
	ds_write2_b32 v37, v48, v49 offset1:1
	ds_write2_b32 v38, v54, v55 offset1:1
	ds_write2_b32 v39, v52, v53 offset1:1
	ds_write2_b32 v87, v58, v59 offset1:1
	ds_write2_b32 v88, v56, v57 offset1:1
	ds_write2_b32 v89, v62, v63 offset1:1
	ds_write2_b32 v90, v60, v61 offset1:1
	ds_write2_b32 v91, v40, v41 offset1:1
	ds_write2_b32 v92, v42, v43 offset1:1
	s_waitcnt lgkmcnt(0)
	ds_read2_b32 v[14:15], v30 offset1:8
	ds_read2_b32 v[16:17], v30 offset0:33 offset1:41
	ds_read2_b32 v[20:21], v30 offset0:66 offset1:74
	ds_read2_b32 v[24:25], v30 offset0:99 offset1:107
	ds_read2_b32 v[40:41], v30 offset0:132 offset1:140
	ds_read2_b32 v[42:43], v30 offset0:165 offset1:173
	ds_read2_b32 v[44:45], v30 offset0:198 offset1:206
	ds_read2_b32 v[46:47], v30 offset0:231 offset1:239
	ds_read2_b32 v[48:49], v30 offset0:16 offset1:24
	ds_read2_b32 v[50:51], v30 offset0:49 offset1:57
	ds_read2_b32 v[52:53], v30 offset0:82 offset1:90
	ds_read2_b32 v[54:55], v30 offset0:115 offset1:123
	ds_read2_b32 v[56:57], v30 offset0:148 offset1:156
	ds_read2_b32 v[58:59], v30 offset0:181 offset1:189
	ds_read2_b32 v[60:61], v30 offset0:214 offset1:222
	ds_read2_b32 v[62:63], v30 offset0:247 offset1:255
	s_waitcnt lgkmcnt(14)
	v_cvt_i32_f32_e32 v16, v16
	s_waitcnt lgkmcnt(10)
	v_cvt_i32_f32_e32 v42, v42
	v_cvt_i32_f32_e32 v14, v14
	v_cvt_i32_f32_sdwa v20, v20 dst_sel:WORD_1 dst_unused:UNUSED_PAD src0_sel:DWORD
	v_cvt_i32_f32_e32 v40, v40
	s_waitcnt lgkmcnt(9)
	v_cvt_i32_f32_sdwa v44, v44 dst_sel:WORD_1 dst_unused:UNUSED_PAD src0_sel:DWORD
	v_cvt_i32_f32_e32 v17, v17
	v_cvt_i32_f32_e32 v43, v43
	s_waitcnt lgkmcnt(6)
	v_cvt_i32_f32_e32 v50, v50
	s_waitcnt lgkmcnt(2)
	v_cvt_i32_f32_e32 v58, v58
	v_cvt_i32_f32_e32 v51, v51
	v_cvt_i32_f32_e32 v59, v59
	v_cvt_i32_f32_sdwa v24, v24 dst_sel:BYTE_3 dst_unused:UNUSED_PAD src0_sel:DWORD
	v_cvt_i32_f32_sdwa v46, v46 dst_sel:BYTE_3 dst_unused:UNUSED_PAD src0_sel:DWORD
	v_cvt_i32_f32_e32 v15, v15
	v_cvt_i32_f32_sdwa v21, v21 dst_sel:WORD_1 dst_unused:UNUSED_PAD src0_sel:DWORD
	v_cvt_i32_f32_e32 v41, v41
	v_cvt_i32_f32_sdwa v45, v45 dst_sel:WORD_1 dst_unused:UNUSED_PAD src0_sel:DWORD
	v_cvt_i32_f32_e32 v48, v48
	v_cvt_i32_f32_sdwa v52, v52 dst_sel:WORD_1 dst_unused:UNUSED_PAD src0_sel:DWORD
	v_cvt_i32_f32_e32 v56, v56
	s_waitcnt lgkmcnt(1)
	v_cvt_i32_f32_sdwa v60, v60 dst_sel:WORD_1 dst_unused:UNUSED_PAD src0_sel:DWORD
	v_cvt_i32_f32_e32 v49, v49
	v_cvt_i32_f32_sdwa v53, v53 dst_sel:WORD_1 dst_unused:UNUSED_PAD src0_sel:DWORD
	v_cvt_i32_f32_e32 v57, v57
	v_cvt_i32_f32_sdwa v61, v61 dst_sel:WORD_1 dst_unused:UNUSED_PAD src0_sel:DWORD
	v_cvt_i32_f32_sdwa v25, v25 dst_sel:BYTE_3 dst_unused:UNUSED_PAD src0_sel:DWORD
	v_cvt_i32_f32_sdwa v47, v47 dst_sel:BYTE_3 dst_unused:UNUSED_PAD src0_sel:DWORD
	v_cvt_i32_f32_sdwa v54, v54 dst_sel:BYTE_3 dst_unused:UNUSED_PAD src0_sel:DWORD
	s_waitcnt lgkmcnt(0)
	v_cvt_i32_f32_sdwa v62, v62 dst_sel:BYTE_3 dst_unused:UNUSED_PAD src0_sel:DWORD
	v_cvt_i32_f32_sdwa v55, v55 dst_sel:BYTE_3 dst_unused:UNUSED_PAD src0_sel:DWORD
	v_cvt_i32_f32_sdwa v63, v63 dst_sel:BYTE_3 dst_unused:UNUSED_PAD src0_sel:DWORD
	v_lshlrev_b32_e32 v16, 8, v16
	v_lshlrev_b32_e32 v42, 8, v42
	v_and_b32_e32 v20, 0xff0000, v20
	v_and_b32_e32 v44, 0xff0000, v44
	v_lshlrev_b32_e32 v17, 8, v17
	v_lshlrev_b32_e32 v43, 8, v43
	v_lshlrev_b32_e32 v50, 8, v50
	v_lshlrev_b32_e32 v58, 8, v58
	v_lshlrev_b32_e32 v51, 8, v51
	v_lshlrev_b32_e32 v59, 8, v59
	v_perm_b32 v14, v16, v14, s28
	v_perm_b32 v16, v42, v40, s28
	v_and_b32_e32 v21, 0xff0000, v21
	v_and_b32_e32 v45, 0xff0000, v45
	v_and_b32_e32 v52, 0xff0000, v52
	v_and_b32_e32 v60, 0xff0000, v60
	v_and_b32_e32 v53, 0xff0000, v53
	v_and_b32_e32 v61, 0xff0000, v61
	v_perm_b32 v17, v17, v15, s28
	v_perm_b32 v40, v43, v41, s28
	v_perm_b32 v41, v50, v48, s28
	v_perm_b32 v42, v58, v56, s28
	v_perm_b32 v43, v51, v49, s28
	v_perm_b32 v48, v59, v57, s28
	v_or3_b32 v14, v14, v20, v24
	v_or3_b32 v15, v16, v44, v46
	v_or3_b32 v16, v17, v21, v25
	v_or3_b32 v17, v40, v45, v47
	v_or3_b32 v20, v41, v52, v54
	v_or3_b32 v21, v42, v60, v62
	v_or3_b32 v24, v43, v53, v55
	v_or3_b32 v25, v48, v61, v63
	global_store_dwordx2 v[18:19], v[14:15], off
	global_store_dwordx2 v[22:23], v[16:17], off
	global_store_dwordx2 v[82:83], v[20:21], off
	global_store_dwordx2 v[84:85], v[24:25], off
	s_waitcnt lgkmcnt(0)
; #define LAS __attribute__((address_space(3)))
; #define GAS __attribute__((address_space(1)))
; #define LDS_WAIT() asm volatile("s_waitcnt lgkmcnt(0)" ::: "memory")
;     ...
;         for (int i = 0; i < 8; ++i) { const int kk = 8 * i + kr; const int k = 64 * kb + kk; const f32x4 v = __builtin_nontemporal_load((const f32x4*)(W + (size_t)k * pitch)) * g[k];
;             LAS float* p = scr + kk * 33 + 4 * (lane & 7); p[0] = __builtin_rintf(v[0] * inv[0]); p[1] = __builtin_rintf(v[1] * inv[1]); p[2] = __builtin_rintf(v[2] * inv[2]); p[3] = __builtin_rintf(v[3] * inv[3]); }
;         LDS_WAIT(); asm volatile("" ::: "memory");
;         const int c = lane & 7;
; #pragma unroll
;         for (int j = 0; j < 4; ++j) { const int n = (lane >> 3) + 8 * j; const LAS float* sp = scr + (8 * c) * 33 + n;
;             u32x2 o;
;             o.x = ((unsigned)(int)sp[0 * 33] & 0xFFu) | (((unsigned)(int)sp[1 * 33] & 0xFFu) << 8) | (((unsigned)(int)sp[2 * 33] & 0xFFu) << 16) | (((unsigned)(int)sp[3 * 33] & 0xFFu) << 24);
;             o.y = ((unsigned)(int)sp[4 * 33] & 0xFFu) | (((unsigned)(int)sp[5 * 33] & 0xFFu) << 8) | (((unsigned)(int)sp[6 * 33] & 0xFFu) << 16) | (((unsigned)(int)sp[7 * 33] & 0xFFu) << 24);
;             *(GAS u32x2*)(dst + (size_t)(n0 + n) * D + 64 * kb + 8 * c) = o; }
;         LDS_WAIT(); asm volatile("" ::: "memory");
	v_add_u32_e32 v87, 0x14a0, v31
	v_add_u32_e32 v88, 0x14a8, v31
	v_add_u32_e32 v89, 0x18c0, v31
	v_add_u32_e32 v90, 0x18c8, v31
	v_add_u32_e32 v91, 0x1ce0, v31
	v_add_u32_e32 v92, 0x1ce8, v31
	v_lshl_add_u64 v[18:19], v[6:7], 0, v[12:13]
	v_lshl_add_u64 v[22:23], v[6:7], 0, v[10:11]
	v_lshl_add_u64 v[82:83], v[6:7], 0, v[8:9]
	v_lshl_add_u64 v[84:85], v[6:7], 0, v[4:5]
	v_lshl_add_u64 v[6:7], v[6:7], 0, 64
	s_waitcnt vmcnt(24)
	v_pk_mul_f32 v[46:47], v[112:113], v[172:173] op_sel_hi:[1,0]
	v_pk_mul_f32 v[20:21], v[110:111], v[172:173] op_sel_hi:[1,0]
	v_pk_mul_f32 v[44:45], v[116:117], v[174:175] op_sel_hi:[1,0]
	v_pk_mul_f32 v[24:25], v[114:115], v[174:175] op_sel_hi:[1,0]
	v_pk_mul_f32 v[48:49], v[120:121], v[176:177] op_sel_hi:[1,0]
	v_pk_mul_f32 v[16:17], v[108:109], v[170:171] op_sel_hi:[1,0]
	v_pk_mul_f32 v[14:15], v[106:107], v[170:171] op_sel_hi:[1,0]
	v_pk_mul_f32 v[50:51], v[118:119], v[176:177] op_sel_hi:[1,0]
	v_pk_mul_f32 v[52:53], v[124:125], v[178:179] op_sel_hi:[1,0]
	v_pk_mul_f32 v[54:55], v[122:123], v[178:179] op_sel_hi:[1,0]
	v_pk_mul_f32 v[56:57], v[128:129], v[180:181] op_sel_hi:[1,0]
	v_pk_mul_f32 v[58:59], v[126:127], v[180:181] op_sel_hi:[1,0]
	v_pk_mul_f32 v[60:61], v[132:133], v[182:183] op_sel_hi:[1,0]
	v_pk_mul_f32 v[62:63], v[130:131], v[182:183] op_sel_hi:[1,0]
	v_pk_mul_f32 v[42:43], v[136:137], v[184:185] op_sel_hi:[1,0]
	v_pk_mul_f32 v[40:41], v[134:135], v[184:185] op_sel_hi:[1,0]
	s_add_u32 s4, s4, 0x18000
	s_addc_u32 s5, s5, 0
	global_load_dwordx4 v[106:109], v250, s[4:5] nt
	global_load_dword v170, v251, s[6:7] offset:2048
	s_add_u32 s4, s4, 0x18000
	s_addc_u32 s5, s5, 0
	global_load_dwordx4 v[110:113], v250, s[4:5] nt
	global_load_dword v172, v251, s[6:7] offset:2080
	s_add_u32 s4, s4, 0x18000
	s_addc_u32 s5, s5, 0
	global_load_dwordx4 v[114:117], v250, s[4:5] nt
	global_load_dword v174, v251, s[6:7] offset:2112
	s_add_u32 s4, s4, 0x18000
	s_addc_u32 s5, s5, 0
	global_load_dwordx4 v[118:121], v250, s[4:5] nt
	global_load_dword v176, v251, s[6:7] offset:2144
	s_add_u32 s4, s4, 0x18000
	s_addc_u32 s5, s5, 0
	global_load_dwordx4 v[122:125], v250, s[4:5] nt
	global_load_dword v178, v251, s[6:7] offset:2176
	s_add_u32 s4, s4, 0x18000
	s_addc_u32 s5, s5, 0
	global_load_dwordx4 v[126:129], v250, s[4:5] nt
	global_load_dword v180, v251, s[6:7] offset:2208
	s_add_u32 s4, s4, 0x18000
	s_addc_u32 s5, s5, 0
	global_load_dwordx4 v[130:133], v250, s[4:5] nt
	global_load_dword v182, v251, s[6:7] offset:2240
	s_add_u32 s4, s4, 0x18000
	s_addc_u32 s5, s5, 0
	global_load_dwordx4 v[134:137], v250, s[4:5] nt
	global_load_dword v184, v251, s[6:7] offset:2272
	v_mul_f32_e32 v14, v26, v14
	v_mul_f32_e32 v15, v27, v15
	v_mul_f32_e32 v16, v28, v16
	v_mul_f32_e32 v17, v29, v17
	v_mul_f32_e32 v20, v26, v20
	v_mul_f32_e32 v21, v27, v21
	v_mul_f32_e32 v46, v28, v46
	v_mul_f32_e32 v47, v29, v47
	v_mul_f32_e32 v24, v26, v24
	v_mul_f32_e32 v25, v27, v25
	v_mul_f32_e32 v44, v28, v44
	v_mul_f32_e32 v45, v29, v45
	v_mul_f32_e32 v50, v26, v50
	v_mul_f32_e32 v51, v27, v51
	v_mul_f32_e32 v48, v28, v48
	v_mul_f32_e32 v49, v29, v49
	v_mul_f32_e32 v54, v26, v54
	v_mul_f32_e32 v55, v27, v55
	v_mul_f32_e32 v52, v28, v52
	v_mul_f32_e32 v53, v29, v53
	v_mul_f32_e32 v58, v26, v58
	v_mul_f32_e32 v59, v27, v59
	v_mul_f32_e32 v56, v28, v56
	v_mul_f32_e32 v57, v29, v57
	v_mul_f32_e32 v62, v26, v62
	v_mul_f32_e32 v63, v27, v63
	v_mul_f32_e32 v60, v28, v60
	v_mul_f32_e32 v61, v29, v61
	v_mul_f32_e32 v40, v26, v40
	v_mul_f32_e32 v41, v27, v41
	v_mul_f32_e32 v42, v28, v42
	v_mul_f32_e32 v43, v29, v43
	v_rndne_f32_e32 v14, v14
	v_rndne_f32_e32 v15, v15
	v_rndne_f32_e32 v16, v16
	v_rndne_f32_e32 v17, v17
	v_rndne_f32_e32 v20, v20
	v_rndne_f32_e32 v21, v21
	v_rndne_f32_e32 v46, v46
	v_rndne_f32_e32 v47, v47
	v_rndne_f32_e32 v24, v24
	v_rndne_f32_e32 v25, v25
	v_rndne_f32_e32 v44, v44
	v_rndne_f32_e32 v45, v45
	v_rndne_f32_e32 v50, v50
	v_rndne_f32_e32 v51, v51
	v_rndne_f32_e32 v48, v48
	v_rndne_f32_e32 v49, v49
	v_rndne_f32_e32 v54, v54
	v_rndne_f32_e32 v55, v55
	v_rndne_f32_e32 v52, v52
	v_rndne_f32_e32 v53, v53
	v_rndne_f32_e32 v58, v58
	v_rndne_f32_e32 v59, v59
	v_rndne_f32_e32 v56, v56
	v_rndne_f32_e32 v57, v57
	v_rndne_f32_e32 v62, v62
	v_rndne_f32_e32 v63, v63
	v_rndne_f32_e32 v60, v60
	v_rndne_f32_e32 v61, v61
	v_rndne_f32_e32 v40, v40
	v_rndne_f32_e32 v41, v41
	v_rndne_f32_e32 v42, v42
	v_rndne_f32_e32 v43, v43
	ds_write2_b32 v31, v14, v15 offset1:1
	ds_write2_b32 v31, v16, v17 offset0:2 offset1:3
	ds_write2_b32 v32, v20, v21 offset1:1
	ds_write2_b32 v33, v46, v47 offset1:1
	ds_write2_b32 v34, v24, v25 offset1:1
	ds_write2_b32 v35, v44, v45 offset1:1
	ds_write2_b32 v36, v50, v51 offset1:1
	ds_write2_b32 v37, v48, v49 offset1:1
	ds_write2_b32 v38, v54, v55 offset1:1
	ds_write2_b32 v39, v52, v53 offset1:1
	ds_write2_b32 v87, v58, v59 offset1:1
	ds_write2_b32 v88, v56, v57 offset1:1
	ds_write2_b32 v89, v62, v63 offset1:1
	ds_write2_b32 v90, v60, v61 offset1:1
	ds_write2_b32 v91, v40, v41 offset1:1
	ds_write2_b32 v92, v42, v43 offset1:1
	s_waitcnt lgkmcnt(0)
	ds_read2_b32 v[14:15], v30 offset1:8
	ds_read2_b32 v[16:17], v30 offset0:33 offset1:41
	ds_read2_b32 v[20:21], v30 offset0:66 offset1:74
	ds_read2_b32 v[24:25], v30 offset0:99 offset1:107
	ds_read2_b32 v[40:41], v30 offset0:132 offset1:140
	ds_read2_b32 v[42:43], v30 offset0:165 offset1:173
	ds_read2_b32 v[44:45], v30 offset0:198 offset1:206
	ds_read2_b32 v[46:47], v30 offset0:231 offset1:239
	ds_read2_b32 v[48:49], v30 offset0:16 offset1:24
	ds_read2_b32 v[50:51], v30 offset0:49 offset1:57
	ds_read2_b32 v[52:53], v30 offset0:82 offset1:90
	ds_read2_b32 v[54:55], v30 offset0:115 offset1:123
	ds_read2_b32 v[56:57], v30 offset0:148 offset1:156
	ds_read2_b32 v[58:59], v30 offset0:181 offset1:189
	ds_read2_b32 v[60:61], v30 offset0:214 offset1:222
	ds_read2_b32 v[62:63], v30 offset0:247 offset1:255
	s_waitcnt lgkmcnt(14)
; #define LAS __attribute__((address_space(3)))
; #define GAS __attribute__((address_space(1)))
; #define LDS_WAIT() asm volatile("s_waitcnt lgkmcnt(0)" ::: "memory")
;     ...
;         for (int i = 0; i < 8; ++i) { const int kk = 8 * i + kr; const int k = 64 * kb + kk; const f32x4 v = __builtin_nontemporal_load((const f32x4*)(W + (size_t)k * pitch)) * g[k];
;             LAS float* p = scr + kk * 33 + 4 * (lane & 7); p[0] = __builtin_rintf(v[0] * inv[0]); p[1] = __builtin_rintf(v[1] * inv[1]); p[2] = __builtin_rintf(v[2] * inv[2]); p[3] = __builtin_rintf(v[3] * inv[3]); }
;         LDS_WAIT(); asm volatile("" ::: "memory");
;         const int c = lane & 7;
; #pragma unroll
;         for (int j = 0; j < 4; ++j) { const int n = (lane >> 3) + 8 * j; const LAS float* sp = scr + (8 * c) * 33 + n;
;             u32x2 o;
;             o.x = ((unsigned)(int)sp[0 * 33] & 0xFFu) | (((unsigned)(int)sp[1 * 33] & 0xFFu) << 8) | (((unsigned)(int)sp[2 * 33] & 0xFFu) << 16) | (((unsigned)(int)sp[3 * 33] & 0xFFu) << 24);
;             o.y = ((unsigned)(int)sp[4 * 33] & 0xFFu) | (((unsigned)(int)sp[5 * 33] & 0xFFu) << 8) | (((unsigned)(int)sp[6 * 33] & 0xFFu) << 16) | (((unsigned)(int)sp[7 * 33] & 0xFFu) << 24);
;             *(GAS u32x2*)(dst + (size_t)(n0 + n) * D + 64 * kb + 8 * c) = o; }
;         LDS_WAIT(); asm volatile("" ::: "memory");
	v_cvt_i32_f32_e32 v16, v16
	s_waitcnt lgkmcnt(10)
	v_cvt_i32_f32_e32 v42, v42
	v_cvt_i32_f32_e32 v14, v14
	v_cvt_i32_f32_sdwa v20, v20 dst_sel:WORD_1 dst_unused:UNUSED_PAD src0_sel:DWORD
	v_cvt_i32_f32_e32 v40, v40
	s_waitcnt lgkmcnt(9)
	v_cvt_i32_f32_sdwa v44, v44 dst_sel:WORD_1 dst_unused:UNUSED_PAD src0_sel:DWORD
	v_cvt_i32_f32_e32 v17, v17
	v_cvt_i32_f32_e32 v43, v43
	s_waitcnt lgkmcnt(6)
	v_cvt_i32_f32_e32 v50, v50
	s_waitcnt lgkmcnt(2)
	v_cvt_i32_f32_e32 v58, v58
	v_cvt_i32_f32_e32 v51, v51
	v_cvt_i32_f32_e32 v59, v59
	v_cvt_i32_f32_sdwa v24, v24 dst_sel:BYTE_3 dst_unused:UNUSED_PAD src0_sel:DWORD
	v_cvt_i32_f32_sdwa v46, v46 dst_sel:BYTE_3 dst_unused:UNUSED_PAD src0_sel:DWORD
	v_cvt_i32_f32_e32 v15, v15
	v_cvt_i32_f32_sdwa v21, v21 dst_sel:WORD_1 dst_unused:UNUSED_PAD src0_sel:DWORD
	v_cvt_i32_f32_e32 v41, v41
	v_cvt_i32_f32_sdwa v45, v45 dst_sel:WORD_1 dst_unused:UNUSED_PAD src0_sel:DWORD
	v_cvt_i32_f32_e32 v48, v48
	v_cvt_i32_f32_sdwa v52, v52 dst_sel:WORD_1 dst_unused:UNUSED_PAD src0_sel:DWORD
	v_cvt_i32_f32_e32 v56, v56
	s_waitcnt lgkmcnt(1)
	v_cvt_i32_f32_sdwa v60, v60 dst_sel:WORD_1 dst_unused:UNUSED_PAD src0_sel:DWORD
	v_cvt_i32_f32_e32 v49, v49
	v_cvt_i32_f32_sdwa v53, v53 dst_sel:WORD_1 dst_unused:UNUSED_PAD src0_sel:DWORD
	v_cvt_i32_f32_e32 v57, v57
	v_cvt_i32_f32_sdwa v61, v61 dst_sel:WORD_1 dst_unused:UNUSED_PAD src0_sel:DWORD
	v_cvt_i32_f32_sdwa v25, v25 dst_sel:BYTE_3 dst_unused:UNUSED_PAD src0_sel:DWORD
	v_cvt_i32_f32_sdwa v47, v47 dst_sel:BYTE_3 dst_unused:UNUSED_PAD src0_sel:DWORD
	v_cvt_i32_f32_sdwa v54, v54 dst_sel:BYTE_3 dst_unused:UNUSED_PAD src0_sel:DWORD
	s_waitcnt lgkmcnt(0)
	v_cvt_i32_f32_sdwa v62, v62 dst_sel:BYTE_3 dst_unused:UNUSED_PAD src0_sel:DWORD
	v_cvt_i32_f32_sdwa v55, v55 dst_sel:BYTE_3 dst_unused:UNUSED_PAD src0_sel:DWORD
	v_cvt_i32_f32_sdwa v63, v63 dst_sel:BYTE_3 dst_unused:UNUSED_PAD src0_sel:DWORD
	v_lshlrev_b32_e32 v16, 8, v16
	v_lshlrev_b32_e32 v42, 8, v42
	v_and_b32_e32 v20, 0xff0000, v20
	v_and_b32_e32 v44, 0xff0000, v44
	v_lshlrev_b32_e32 v17, 8, v17
	v_lshlrev_b32_e32 v43, 8, v43
	v_lshlrev_b32_e32 v50, 8, v50
	v_lshlrev_b32_e32 v58, 8, v58
	v_lshlrev_b32_e32 v51, 8, v51
	v_lshlrev_b32_e32 v59, 8, v59
	v_perm_b32 v14, v16, v14, s28
	v_perm_b32 v16, v42, v40, s28
	v_and_b32_e32 v21, 0xff0000, v21
	v_and_b32_e32 v45, 0xff0000, v45
	v_and_b32_e32 v52, 0xff0000, v52
	v_and_b32_e32 v60, 0xff0000, v60
	v_and_b32_e32 v53, 0xff0000, v53
	v_and_b32_e32 v61, 0xff0000, v61
	v_perm_b32 v17, v17, v15, s28
	v_perm_b32 v40, v43, v41, s28
	v_perm_b32 v41, v50, v48, s28
	v_perm_b32 v42, v58, v56, s28
	v_perm_b32 v43, v51, v49, s28
	v_perm_b32 v48, v59, v57, s28
	v_or3_b32 v14, v14, v20, v24
	v_or3_b32 v15, v16, v44, v46
	v_or3_b32 v16, v17, v21, v25
	v_or3_b32 v17, v40, v45, v47
	v_or3_b32 v20, v41, v52, v54
	v_or3_b32 v21, v42, v60, v62
	v_or3_b32 v24, v43, v53, v55
	v_or3_b32 v25, v48, v61, v63
	global_store_dwordx2 v[18:19], v[14:15], off
	global_store_dwordx2 v[22:23], v[16:17], off
	global_store_dwordx2 v[82:83], v[20:21], off
	global_store_dwordx2 v[84:85], v[24:25], off
	s_waitcnt lgkmcnt(0)
	v_add_u32_e32 v87, 0x14a0, v31
	v_add_u32_e32 v88, 0x14a8, v31
	v_add_u32_e32 v89, 0x18c0, v31
	v_add_u32_e32 v90, 0x18c8, v31
	v_add_u32_e32 v91, 0x1ce0, v31
	v_add_u32_e32 v92, 0x1ce8, v31
	v_lshl_add_u64 v[18:19], v[6:7], 0, v[12:13]
	v_lshl_add_u64 v[22:23], v[6:7], 0, v[10:11]
	v_lshl_add_u64 v[82:83], v[6:7], 0, v[8:9]
	v_lshl_add_u64 v[84:85], v[6:7], 0, v[4:5]
	v_lshl_add_u64 v[6:7], v[6:7], 0, 64
	s_waitcnt vmcnt(24)
	v_pk_mul_f32 v[46:47], v[144:145], v[188:189] op_sel_hi:[1,0]
	v_pk_mul_f32 v[20:21], v[142:143], v[188:189] op_sel_hi:[1,0]
	v_pk_mul_f32 v[44:45], v[148:149], v[190:191] op_sel_hi:[1,0]
	v_pk_mul_f32 v[24:25], v[146:147], v[190:191] op_sel_hi:[1,0]
	v_pk_mul_f32 v[48:49], v[152:153], v[192:193] op_sel_hi:[1,0]
	v_pk_mul_f32 v[16:17], v[140:141], v[186:187] op_sel_hi:[1,0]
	v_pk_mul_f32 v[14:15], v[138:139], v[186:187] op_sel_hi:[1,0]
	v_pk_mul_f32 v[50:51], v[150:151], v[192:193] op_sel_hi:[1,0]
	v_pk_mul_f32 v[52:53], v[156:157], v[194:195] op_sel_hi:[1,0]
	v_pk_mul_f32 v[54:55], v[154:155], v[194:195] op_sel_hi:[1,0]
	v_pk_mul_f32 v[56:57], v[160:161], v[196:197] op_sel_hi:[1,0]
	v_pk_mul_f32 v[58:59], v[158:159], v[196:197] op_sel_hi:[1,0]
	v_pk_mul_f32 v[60:61], v[164:165], v[198:199] op_sel_hi:[1,0]
	v_pk_mul_f32 v[62:63], v[162:163], v[198:199] op_sel_hi:[1,0]
	v_pk_mul_f32 v[42:43], v[168:169], v[200:201] op_sel_hi:[1,0]
	v_pk_mul_f32 v[40:41], v[166:167], v[200:201] op_sel_hi:[1,0]
	s_add_u32 s4, s4, 0x18000
	s_addc_u32 s5, s5, 0
	global_load_dwordx4 v[138:141], v250, s[4:5] nt
	global_load_dword v186, v251, s[6:7] offset:2304
	s_add_u32 s4, s4, 0x18000
	s_addc_u32 s5, s5, 0
	global_load_dwordx4 v[142:145], v250, s[4:5] nt
	global_load_dword v188, v251, s[6:7] offset:2336
	s_add_u32 s4, s4, 0x18000
	s_addc_u32 s5, s5, 0
	global_load_dwordx4 v[146:149], v250, s[4:5] nt
	global_load_dword v190, v251, s[6:7] offset:2368
	s_add_u32 s4, s4, 0x18000
	s_addc_u32 s5, s5, 0
	global_load_dwordx4 v[150:153], v250, s[4:5] nt
	global_load_dword v192, v251, s[6:7] offset:2400
	s_add_u32 s4, s4, 0x18000
	s_addc_u32 s5, s5, 0
	global_load_dwordx4 v[154:157], v250, s[4:5] nt
	global_load_dword v194, v251, s[6:7] offset:2432
	s_add_u32 s4, s4, 0x18000
	s_addc_u32 s5, s5, 0
	global_load_dwordx4 v[158:161], v250, s[4:5] nt
	global_load_dword v196, v251, s[6:7] offset:2464
	s_add_u32 s4, s4, 0x18000
	s_addc_u32 s5, s5, 0
	global_load_dwordx4 v[162:165], v250, s[4:5] nt
	global_load_dword v198, v251, s[6:7] offset:2496
	s_add_u32 s4, s4, 0x18000
	s_addc_u32 s5, s5, 0
	global_load_dwordx4 v[166:169], v250, s[4:5] nt
; #define LAS __attribute__((address_space(3)))
; #define GAS __attribute__((address_space(1)))
; #define LDS_WAIT() asm volatile("s_waitcnt lgkmcnt(0)" ::: "memory")
;     ...
;         for (int i = 0; i < 8; ++i) { const int kk = 8 * i + kr; const int k = 64 * kb + kk; const f32x4 v = __builtin_nontemporal_load((const f32x4*)(W + (size_t)k * pitch)) * g[k];
;             LAS float* p = scr + kk * 33 + 4 * (lane & 7); p[0] = __builtin_rintf(v[0] * inv[0]); p[1] = __builtin_rintf(v[1] * inv[1]); p[2] = __builtin_rintf(v[2] * inv[2]); p[3] = __builtin_rintf(v[3] * inv[3]); }
;         LDS_WAIT(); asm volatile("" ::: "memory");
;         const int c = lane & 7;
; #pragma unroll
;         for (int j = 0; j < 4; ++j) { const int n = (lane >> 3) + 8 * j; const LAS float* sp = scr + (8 * c) * 33 + n;
;             u32x2 o;
;             o.x = ((unsigned)(int)sp[0 * 33] & 0xFFu) | (((unsigned)(int)sp[1 * 33] & 0xFFu) << 8) | (((unsigned)(int)sp[2 * 33] & 0xFFu) << 16) | (((unsigned)(int)sp[3 * 33] & 0xFFu) << 24);
;             o.y = ((unsigned)(int)sp[4 * 33] & 0xFFu) | (((unsigned)(int)sp[5 * 33] & 0xFFu) << 8) | (((unsigned)(int)sp[6 * 33] & 0xFFu) << 16) | (((unsigned)(int)sp[7 * 33] & 0xFFu) << 24);
;             *(GAS u32x2*)(dst + (size_t)(n0 + n) * D + 64 * kb + 8 * c) = o; }
;         LDS_WAIT(); asm volatile("" ::: "memory");
	global_load_dword v200, v251, s[6:7] offset:2528
	v_mul_f32_e32 v14, v26, v14
	v_mul_f32_e32 v15, v27, v15
	v_mul_f32_e32 v16, v28, v16
	v_mul_f32_e32 v17, v29, v17
	v_mul_f32_e32 v20, v26, v20
	v_mul_f32_e32 v21, v27, v21
	v_mul_f32_e32 v46, v28, v46
	v_mul_f32_e32 v47, v29, v47
	v_mul_f32_e32 v24, v26, v24
	v_mul_f32_e32 v25, v27, v25
	v_mul_f32_e32 v44, v28, v44
	v_mul_f32_e32 v45, v29, v45
	v_mul_f32_e32 v50, v26, v50
	v_mul_f32_e32 v51, v27, v51
	v_mul_f32_e32 v48, v28, v48
	v_mul_f32_e32 v49, v29, v49
	v_mul_f32_e32 v54, v26, v54
	v_mul_f32_e32 v55, v27, v55
	v_mul_f32_e32 v52, v28, v52
	v_mul_f32_e32 v53, v29, v53
	v_mul_f32_e32 v58, v26, v58
	v_mul_f32_e32 v59, v27, v59
	v_mul_f32_e32 v56, v28, v56
	v_mul_f32_e32 v57, v29, v57
	v_mul_f32_e32 v62, v26, v62
	v_mul_f32_e32 v63, v27, v63
	v_mul_f32_e32 v60, v28, v60
	v_mul_f32_e32 v61, v29, v61
	v_mul_f32_e32 v40, v26, v40
	v_mul_f32_e32 v41, v27, v41
	v_mul_f32_e32 v42, v28, v42
	v_mul_f32_e32 v43, v29, v43
	v_rndne_f32_e32 v14, v14
	v_rndne_f32_e32 v15, v15
	v_rndne_f32_e32 v16, v16
	v_rndne_f32_e32 v17, v17
	v_rndne_f32_e32 v20, v20
	v_rndne_f32_e32 v21, v21
	v_rndne_f32_e32 v46, v46
	v_rndne_f32_e32 v47, v47
	v_rndne_f32_e32 v24, v24
	v_rndne_f32_e32 v25, v25
	v_rndne_f32_e32 v44, v44
	v_rndne_f32_e32 v45, v45
	v_rndne_f32_e32 v50, v50
	v_rndne_f32_e32 v51, v51
	v_rndne_f32_e32 v48, v48
	v_rndne_f32_e32 v49, v49
	v_rndne_f32_e32 v54, v54
	v_rndne_f32_e32 v55, v55
	v_rndne_f32_e32 v52, v52
	v_rndne_f32_e32 v53, v53
	v_rndne_f32_e32 v58, v58
	v_rndne_f32_e32 v59, v59
	v_rndne_f32_e32 v56, v56
	v_rndne_f32_e32 v57, v57
	v_rndne_f32_e32 v62, v62
	v_rndne_f32_e32 v63, v63
	v_rndne_f32_e32 v60, v60
	v_rndne_f32_e32 v61, v61
	v_rndne_f32_e32 v40, v40
	v_rndne_f32_e32 v41, v41
	v_rndne_f32_e32 v42, v42
	v_rndne_f32_e32 v43, v43
	ds_write2_b32 v31, v14, v15 offset1:1
	ds_write2_b32 v31, v16, v17 offset0:2 offset1:3
	ds_write2_b32 v32, v20, v21 offset1:1
	ds_write2_b32 v33, v46, v47 offset1:1
	ds_write2_b32 v34, v24, v25 offset1:1
	ds_write2_b32 v35, v44, v45 offset1:1
	ds_write2_b32 v36, v50, v51 offset1:1
	ds_write2_b32 v37, v48, v49 offset1:1
	ds_write2_b32 v38, v54, v55 offset1:1
	ds_write2_b32 v39, v52, v53 offset1:1
	ds_write2_b32 v87, v58, v59 offset1:1
	ds_write2_b32 v88, v56, v57 offset1:1
	ds_write2_b32 v89, v62, v63 offset1:1
	ds_write2_b32 v90, v60, v61 offset1:1
	ds_write2_b32 v91, v40, v41 offset1:1
	ds_write2_b32 v92, v42, v43 offset1:1
	s_waitcnt lgkmcnt(0)
	ds_read2_b32 v[14:15], v30 offset1:8
	ds_read2_b32 v[16:17], v30 offset0:33 offset1:41
	ds_read2_b32 v[20:21], v30 offset0:66 offset1:74
	ds_read2_b32 v[24:25], v30 offset0:99 offset1:107
	ds_read2_b32 v[40:41], v30 offset0:132 offset1:140
	ds_read2_b32 v[42:43], v30 offset0:165 offset1:173
	ds_read2_b32 v[44:45], v30 offset0:198 offset1:206
	ds_read2_b32 v[46:47], v30 offset0:231 offset1:239
	ds_read2_b32 v[48:49], v30 offset0:16 offset1:24
	ds_read2_b32 v[50:51], v30 offset0:49 offset1:57
	ds_read2_b32 v[52:53], v30 offset0:82 offset1:90
	ds_read2_b32 v[54:55], v30 offset0:115 offset1:123
	ds_read2_b32 v[56:57], v30 offset0:148 offset1:156
	ds_read2_b32 v[58:59], v30 offset0:181 offset1:189
	ds_read2_b32 v[60:61], v30 offset0:214 offset1:222
	ds_read2_b32 v[62:63], v30 offset0:247 offset1:255
	s_waitcnt lgkmcnt(14)
	v_cvt_i32_f32_e32 v16, v16
	s_waitcnt lgkmcnt(10)
	v_cvt_i32_f32_e32 v42, v42
	v_cvt_i32_f32_e32 v14, v14
	v_cvt_i32_f32_sdwa v20, v20 dst_sel:WORD_1 dst_unused:UNUSED_PAD src0_sel:DWORD
	v_cvt_i32_f32_e32 v40, v40
	s_waitcnt lgkmcnt(9)
	v_cvt_i32_f32_sdwa v44, v44 dst_sel:WORD_1 dst_unused:UNUSED_PAD src0_sel:DWORD
	v_cvt_i32_f32_e32 v17, v17
	v_cvt_i32_f32_e32 v43, v43
	s_waitcnt lgkmcnt(6)
	v_cvt_i32_f32_e32 v50, v50
	s_waitcnt lgkmcnt(2)
	v_cvt_i32_f32_e32 v58, v58
	v_cvt_i32_f32_e32 v51, v51
	v_cvt_i32_f32_e32 v59, v59
	v_cvt_i32_f32_sdwa v24, v24 dst_sel:BYTE_3 dst_unused:UNUSED_PAD src0_sel:DWORD
	v_cvt_i32_f32_sdwa v46, v46 dst_sel:BYTE_3 dst_unused:UNUSED_PAD src0_sel:DWORD
	v_cvt_i32_f32_e32 v15, v15
	v_cvt_i32_f32_sdwa v21, v21 dst_sel:WORD_1 dst_unused:UNUSED_PAD src0_sel:DWORD
	v_cvt_i32_f32_e32 v41, v41
	v_cvt_i32_f32_sdwa v45, v45 dst_sel:WORD_1 dst_unused:UNUSED_PAD src0_sel:DWORD
	v_cvt_i32_f32_e32 v48, v48
	v_cvt_i32_f32_sdwa v52, v52 dst_sel:WORD_1 dst_unused:UNUSED_PAD src0_sel:DWORD
	v_cvt_i32_f32_e32 v56, v56
	s_waitcnt lgkmcnt(1)
	v_cvt_i32_f32_sdwa v60, v60 dst_sel:WORD_1 dst_unused:UNUSED_PAD src0_sel:DWORD
	v_cvt_i32_f32_e32 v49, v49
	v_cvt_i32_f32_sdwa v53, v53 dst_sel:WORD_1 dst_unused:UNUSED_PAD src0_sel:DWORD
	v_cvt_i32_f32_e32 v57, v57
	v_cvt_i32_f32_sdwa v61, v61 dst_sel:WORD_1 dst_unused:UNUSED_PAD src0_sel:DWORD
	v_cvt_i32_f32_sdwa v25, v25 dst_sel:BYTE_3 dst_unused:UNUSED_PAD src0_sel:DWORD
	v_cvt_i32_f32_sdwa v47, v47 dst_sel:BYTE_3 dst_unused:UNUSED_PAD src0_sel:DWORD
	v_cvt_i32_f32_sdwa v54, v54 dst_sel:BYTE_3 dst_unused:UNUSED_PAD src0_sel:DWORD
	s_waitcnt lgkmcnt(0)
; #define LAS __attribute__((address_space(3)))
; #define GAS __attribute__((address_space(1)))
; #define LDS_WAIT() asm volatile("s_waitcnt lgkmcnt(0)" ::: "memory")
;     ...
;         for (int i = 0; i < 8; ++i) { const int kk = 8 * i + kr; const int k = 64 * kb + kk; const f32x4 v = __builtin_nontemporal_load((const f32x4*)(W + (size_t)k * pitch)) * g[k];
;             LAS float* p = scr + kk * 33 + 4 * (lane & 7); p[0] = __builtin_rintf(v[0] * inv[0]); p[1] = __builtin_rintf(v[1] * inv[1]); p[2] = __builtin_rintf(v[2] * inv[2]); p[3] = __builtin_rintf(v[3] * inv[3]); }
;         LDS_WAIT(); asm volatile("" ::: "memory");
;         const int c = lane & 7;
; #pragma unroll
;         for (int j = 0; j < 4; ++j) { const int n = (lane >> 3) + 8 * j; const LAS float* sp = scr + (8 * c) * 33 + n;
;             u32x2 o;
;             o.x = ((unsigned)(int)sp[0 * 33] & 0xFFu) | (((unsigned)(int)sp[1 * 33] & 0xFFu) << 8) | (((unsigned)(int)sp[2 * 33] & 0xFFu) << 16) | (((unsigned)(int)sp[3 * 33] & 0xFFu) << 24);
;             o.y = ((unsigned)(int)sp[4 * 33] & 0xFFu) | (((unsigned)(int)sp[5 * 33] & 0xFFu) << 8) | (((unsigned)(int)sp[6 * 33] & 0xFFu) << 16) | (((unsigned)(int)sp[7 * 33] & 0xFFu) << 24);
;             *(GAS u32x2*)(dst + (size_t)(n0 + n) * D + 64 * kb + 8 * c) = o; }
;         LDS_WAIT(); asm volatile("" ::: "memory");
	v_cvt_i32_f32_sdwa v62, v62 dst_sel:BYTE_3 dst_unused:UNUSED_PAD src0_sel:DWORD
	v_cvt_i32_f32_sdwa v55, v55 dst_sel:BYTE_3 dst_unused:UNUSED_PAD src0_sel:DWORD
	v_cvt_i32_f32_sdwa v63, v63 dst_sel:BYTE_3 dst_unused:UNUSED_PAD src0_sel:DWORD
	v_lshlrev_b32_e32 v16, 8, v16
	v_lshlrev_b32_e32 v42, 8, v42
	v_and_b32_e32 v20, 0xff0000, v20
	v_and_b32_e32 v44, 0xff0000, v44
	v_lshlrev_b32_e32 v17, 8, v17
	v_lshlrev_b32_e32 v43, 8, v43
	v_lshlrev_b32_e32 v50, 8, v50
	v_lshlrev_b32_e32 v58, 8, v58
	v_lshlrev_b32_e32 v51, 8, v51
	v_lshlrev_b32_e32 v59, 8, v59
	v_perm_b32 v14, v16, v14, s28
	v_perm_b32 v16, v42, v40, s28
	v_and_b32_e32 v21, 0xff0000, v21
	v_and_b32_e32 v45, 0xff0000, v45
	v_and_b32_e32 v52, 0xff0000, v52
	v_and_b32_e32 v60, 0xff0000, v60
	v_and_b32_e32 v53, 0xff0000, v53
	v_and_b32_e32 v61, 0xff0000, v61
	v_perm_b32 v17, v17, v15, s28
	v_perm_b32 v40, v43, v41, s28
	v_perm_b32 v41, v50, v48, s28
	v_perm_b32 v42, v58, v56, s28
	v_perm_b32 v43, v51, v49, s28
	v_perm_b32 v48, v59, v57, s28
	v_or3_b32 v14, v14, v20, v24
	v_or3_b32 v15, v16, v44, v46
	v_or3_b32 v16, v17, v21, v25
	v_or3_b32 v17, v40, v45, v47
	v_or3_b32 v20, v41, v52, v54
	v_or3_b32 v21, v42, v60, v62
	v_or3_b32 v24, v43, v53, v55
	v_or3_b32 v25, v48, v61, v63
	global_store_dwordx2 v[18:19], v[14:15], off
	global_store_dwordx2 v[22:23], v[16:17], off
	global_store_dwordx2 v[82:83], v[20:21], off
	global_store_dwordx2 v[84:85], v[24:25], off
	s_waitcnt lgkmcnt(0)
	v_add_u32_e32 v87, 0x14a0, v31
	v_add_u32_e32 v88, 0x14a8, v31
	v_add_u32_e32 v89, 0x18c0, v31
	v_add_u32_e32 v90, 0x18c8, v31
	v_add_u32_e32 v91, 0x1ce0, v31
	v_add_u32_e32 v92, 0x1ce8, v31
	v_lshl_add_u64 v[18:19], v[6:7], 0, v[12:13]
	v_lshl_add_u64 v[22:23], v[6:7], 0, v[10:11]
	v_lshl_add_u64 v[82:83], v[6:7], 0, v[8:9]
	v_lshl_add_u64 v[84:85], v[6:7], 0, v[4:5]
	v_lshl_add_u64 v[6:7], v[6:7], 0, 64
	s_waitcnt vmcnt(24)
	v_pk_mul_f32 v[46:47], v[112:113], v[172:173] op_sel_hi:[1,0]
	v_pk_mul_f32 v[20:21], v[110:111], v[172:173] op_sel_hi:[1,0]
	v_pk_mul_f32 v[44:45], v[116:117], v[174:175] op_sel_hi:[1,0]
	v_pk_mul_f32 v[24:25], v[114:115], v[174:175] op_sel_hi:[1,0]
	v_pk_mul_f32 v[48:49], v[120:121], v[176:177] op_sel_hi:[1,0]
	v_pk_mul_f32 v[16:17], v[108:109], v[170:171] op_sel_hi:[1,0]
	v_pk_mul_f32 v[14:15], v[106:107], v[170:171] op_sel_hi:[1,0]
	v_pk_mul_f32 v[50:51], v[118:119], v[176:177] op_sel_hi:[1,0]
	v_pk_mul_f32 v[52:53], v[124:125], v[178:179] op_sel_hi:[1,0]
	v_pk_mul_f32 v[54:55], v[122:123], v[178:179] op_sel_hi:[1,0]
	v_pk_mul_f32 v[56:57], v[128:129], v[180:181] op_sel_hi:[1,0]
	v_pk_mul_f32 v[58:59], v[126:127], v[180:181] op_sel_hi:[1,0]
	v_pk_mul_f32 v[60:61], v[132:133], v[182:183] op_sel_hi:[1,0]
	v_pk_mul_f32 v[62:63], v[130:131], v[182:183] op_sel_hi:[1,0]
	v_pk_mul_f32 v[42:43], v[136:137], v[184:185] op_sel_hi:[1,0]
	v_pk_mul_f32 v[40:41], v[134:135], v[184:185] op_sel_hi:[1,0]
	s_add_u32 s4, s4, 0x18000
	s_addc_u32 s5, s5, 0
	global_load_dwordx4 v[106:109], v250, s[4:5] nt
	global_load_dword v170, v251, s[6:7] offset:2560
	s_add_u32 s4, s4, 0x18000
	s_addc_u32 s5, s5, 0
	global_load_dwordx4 v[110:113], v250, s[4:5] nt
	global_load_dword v172, v251, s[6:7] offset:2592
	s_add_u32 s4, s4, 0x18000
	s_addc_u32 s5, s5, 0
	global_load_dwordx4 v[114:117], v250, s[4:5] nt
	global_load_dword v174, v251, s[6:7] offset:2624
	s_add_u32 s4, s4, 0x18000
	s_addc_u32 s5, s5, 0
	global_load_dwordx4 v[118:121], v250, s[4:5] nt
	global_load_dword v176, v251, s[6:7] offset:2656
	s_add_u32 s4, s4, 0x18000
	s_addc_u32 s5, s5, 0
	global_load_dwordx4 v[122:125], v250, s[4:5] nt
	global_load_dword v178, v251, s[6:7] offset:2688
	s_add_u32 s4, s4, 0x18000
	s_addc_u32 s5, s5, 0
	global_load_dwordx4 v[126:129], v250, s[4:5] nt
	global_load_dword v180, v251, s[6:7] offset:2720
	s_add_u32 s4, s4, 0x18000
	s_addc_u32 s5, s5, 0
	global_load_dwordx4 v[130:133], v250, s[4:5] nt
	global_load_dword v182, v251, s[6:7] offset:2752
	s_add_u32 s4, s4, 0x18000
	s_addc_u32 s5, s5, 0
	global_load_dwordx4 v[134:137], v250, s[4:5] nt
	global_load_dword v184, v251, s[6:7] offset:2784
	v_mul_f32_e32 v14, v26, v14
	v_mul_f32_e32 v15, v27, v15
	v_mul_f32_e32 v16, v28, v16
	v_mul_f32_e32 v17, v29, v17
	v_mul_f32_e32 v20, v26, v20
	v_mul_f32_e32 v21, v27, v21
	v_mul_f32_e32 v46, v28, v46
	v_mul_f32_e32 v47, v29, v47
	v_mul_f32_e32 v24, v26, v24
	v_mul_f32_e32 v25, v27, v25
	v_mul_f32_e32 v44, v28, v44
	v_mul_f32_e32 v45, v29, v45
	v_mul_f32_e32 v50, v26, v50
	v_mul_f32_e32 v51, v27, v51
	v_mul_f32_e32 v48, v28, v48
	v_mul_f32_e32 v49, v29, v49
	v_mul_f32_e32 v54, v26, v54
	v_mul_f32_e32 v55, v27, v55
	v_mul_f32_e32 v52, v28, v52
	v_mul_f32_e32 v53, v29, v53
	v_mul_f32_e32 v58, v26, v58
	v_mul_f32_e32 v59, v27, v59
	v_mul_f32_e32 v56, v28, v56
	v_mul_f32_e32 v57, v29, v57
	v_mul_f32_e32 v62, v26, v62
	v_mul_f32_e32 v63, v27, v63
	v_mul_f32_e32 v60, v28, v60
	v_mul_f32_e32 v61, v29, v61
	v_mul_f32_e32 v40, v26, v40
	v_mul_f32_e32 v41, v27, v41
	v_mul_f32_e32 v42, v28, v42
	v_mul_f32_e32 v43, v29, v43
	v_rndne_f32_e32 v14, v14
	v_rndne_f32_e32 v15, v15
	v_rndne_f32_e32 v16, v16
	v_rndne_f32_e32 v17, v17
	v_rndne_f32_e32 v20, v20
	v_rndne_f32_e32 v21, v21
	v_rndne_f32_e32 v46, v46
	v_rndne_f32_e32 v47, v47
	v_rndne_f32_e32 v24, v24
	v_rndne_f32_e32 v25, v25
	v_rndne_f32_e32 v44, v44
	v_rndne_f32_e32 v45, v45
	v_rndne_f32_e32 v50, v50
	v_rndne_f32_e32 v51, v51
	v_rndne_f32_e32 v48, v48
	v_rndne_f32_e32 v49, v49
	v_rndne_f32_e32 v54, v54
	v_rndne_f32_e32 v55, v55
	v_rndne_f32_e32 v52, v52
	v_rndne_f32_e32 v53, v53
	v_rndne_f32_e32 v58, v58
	v_rndne_f32_e32 v59, v59
	v_rndne_f32_e32 v56, v56
	v_rndne_f32_e32 v57, v57
	v_rndne_f32_e32 v62, v62
	v_rndne_f32_e32 v63, v63
	v_rndne_f32_e32 v60, v60
	v_rndne_f32_e32 v61, v61
	v_rndne_f32_e32 v40, v40
	v_rndne_f32_e32 v41, v41
	v_rndne_f32_e32 v42, v42
	v_rndne_f32_e32 v43, v43
	ds_write2_b32 v31, v14, v15 offset1:1
	ds_write2_b32 v31, v16, v17 offset0:2 offset1:3
	ds_write2_b32 v32, v20, v21 offset1:1
	ds_write2_b32 v33, v46, v47 offset1:1
	ds_write2_b32 v34, v24, v25 offset1:1
	ds_write2_b32 v35, v44, v45 offset1:1
	ds_write2_b32 v36, v50, v51 offset1:1
	ds_write2_b32 v37, v48, v49 offset1:1
	ds_write2_b32 v38, v54, v55 offset1:1
	ds_write2_b32 v39, v52, v53 offset1:1
	ds_write2_b32 v87, v58, v59 offset1:1
	ds_write2_b32 v88, v56, v57 offset1:1
	ds_write2_b32 v89, v62, v63 offset1:1
	ds_write2_b32 v90, v60, v61 offset1:1
	ds_write2_b32 v91, v40, v41 offset1:1
	ds_write2_b32 v92, v42, v43 offset1:1
	s_waitcnt lgkmcnt(0)
; #define LAS __attribute__((address_space(3)))
; #define GAS __attribute__((address_space(1)))
; #define LDS_WAIT() asm volatile("s_waitcnt lgkmcnt(0)" ::: "memory")
;     ...
;         const int c = lane & 7;
; #pragma unroll
;         for (int j = 0; j < 4; ++j) { const int n = (lane >> 3) + 8 * j; const LAS float* sp = scr + (8 * c) * 33 + n;
;             u32x2 o;
;             o.x = ((unsigned)(int)sp[0 * 33] & 0xFFu) | (((unsigned)(int)sp[1 * 33] & 0xFFu) << 8) | (((unsigned)(int)sp[2 * 33] & 0xFFu) << 16) | (((unsigned)(int)sp[3 * 33] & 0xFFu) << 24);
;             o.y = ((unsigned)(int)sp[4 * 33] & 0xFFu) | (((unsigned)(int)sp[5 * 33] & 0xFFu) << 8) | (((unsigned)(int)sp[6 * 33] & 0xFFu) << 16) | (((unsigned)(int)sp[7 * 33] & 0xFFu) << 24);
;             *(GAS u32x2*)(dst + (size_t)(n0 + n) * D + 64 * kb + 8 * c) = o; }
;         LDS_WAIT(); asm volatile("" ::: "memory");
	ds_read2_b32 v[14:15], v30 offset1:8
	ds_read2_b32 v[16:17], v30 offset0:33 offset1:41
	ds_read2_b32 v[20:21], v30 offset0:66 offset1:74
	ds_read2_b32 v[24:25], v30 offset0:99 offset1:107
	ds_read2_b32 v[40:41], v30 offset0:132 offset1:140
	ds_read2_b32 v[42:43], v30 offset0:165 offset1:173
	ds_read2_b32 v[44:45], v30 offset0:198 offset1:206
	ds_read2_b32 v[46:47], v30 offset0:231 offset1:239
	ds_read2_b32 v[48:49], v30 offset0:16 offset1:24
	ds_read2_b32 v[50:51], v30 offset0:49 offset1:57
	ds_read2_b32 v[52:53], v30 offset0:82 offset1:90
	ds_read2_b32 v[54:55], v30 offset0:115 offset1:123
	ds_read2_b32 v[56:57], v30 offset0:148 offset1:156
	ds_read2_b32 v[58:59], v30 offset0:181 offset1:189
	ds_read2_b32 v[60:61], v30 offset0:214 offset1:222
	ds_read2_b32 v[62:63], v30 offset0:247 offset1:255
	s_waitcnt lgkmcnt(14)
	v_cvt_i32_f32_e32 v16, v16
	s_waitcnt lgkmcnt(10)
	v_cvt_i32_f32_e32 v42, v42
	v_cvt_i32_f32_e32 v14, v14
	v_cvt_i32_f32_sdwa v20, v20 dst_sel:WORD_1 dst_unused:UNUSED_PAD src0_sel:DWORD
	v_cvt_i32_f32_e32 v40, v40
	s_waitcnt lgkmcnt(9)
	v_cvt_i32_f32_sdwa v44, v44 dst_sel:WORD_1 dst_unused:UNUSED_PAD src0_sel:DWORD
	v_cvt_i32_f32_e32 v17, v17
	v_cvt_i32_f32_e32 v43, v43
	s_waitcnt lgkmcnt(6)
	v_cvt_i32_f32_e32 v50, v50
	s_waitcnt lgkmcnt(2)
	v_cvt_i32_f32_e32 v58, v58
	v_cvt_i32_f32_e32 v51, v51
	v_cvt_i32_f32_e32 v59, v59
	v_cvt_i32_f32_sdwa v24, v24 dst_sel:BYTE_3 dst_unused:UNUSED_PAD src0_sel:DWORD
	v_cvt_i32_f32_sdwa v46, v46 dst_sel:BYTE_3 dst_unused:UNUSED_PAD src0_sel:DWORD
	v_cvt_i32_f32_e32 v15, v15
	v_cvt_i32_f32_sdwa v21, v21 dst_sel:WORD_1 dst_unused:UNUSED_PAD src0_sel:DWORD
	v_cvt_i32_f32_e32 v41, v41
	v_cvt_i32_f32_sdwa v45, v45 dst_sel:WORD_1 dst_unused:UNUSED_PAD src0_sel:DWORD
	v_cvt_i32_f32_e32 v48, v48
	v_cvt_i32_f32_sdwa v52, v52 dst_sel:WORD_1 dst_unused:UNUSED_PAD src0_sel:DWORD
	v_cvt_i32_f32_e32 v56, v56
	s_waitcnt lgkmcnt(1)
	v_cvt_i32_f32_sdwa v60, v60 dst_sel:WORD_1 dst_unused:UNUSED_PAD src0_sel:DWORD
	v_cvt_i32_f32_e32 v49, v49
	v_cvt_i32_f32_sdwa v53, v53 dst_sel:WORD_1 dst_unused:UNUSED_PAD src0_sel:DWORD
	v_cvt_i32_f32_e32 v57, v57
	v_cvt_i32_f32_sdwa v61, v61 dst_sel:WORD_1 dst_unused:UNUSED_PAD src0_sel:DWORD
	v_cvt_i32_f32_sdwa v25, v25 dst_sel:BYTE_3 dst_unused:UNUSED_PAD src0_sel:DWORD
	v_cvt_i32_f32_sdwa v47, v47 dst_sel:BYTE_3 dst_unused:UNUSED_PAD src0_sel:DWORD
	v_cvt_i32_f32_sdwa v54, v54 dst_sel:BYTE_3 dst_unused:UNUSED_PAD src0_sel:DWORD
	s_waitcnt lgkmcnt(0)
	v_cvt_i32_f32_sdwa v62, v62 dst_sel:BYTE_3 dst_unused:UNUSED_PAD src0_sel:DWORD
	v_cvt_i32_f32_sdwa v55, v55 dst_sel:BYTE_3 dst_unused:UNUSED_PAD src0_sel:DWORD
	v_cvt_i32_f32_sdwa v63, v63 dst_sel:BYTE_3 dst_unused:UNUSED_PAD src0_sel:DWORD
	v_lshlrev_b32_e32 v16, 8, v16
	v_lshlrev_b32_e32 v42, 8, v42
	v_and_b32_e32 v20, 0xff0000, v20
	v_and_b32_e32 v44, 0xff0000, v44
	v_lshlrev_b32_e32 v17, 8, v17
	v_lshlrev_b32_e32 v43, 8, v43
	v_lshlrev_b32_e32 v50, 8, v50
	v_lshlrev_b32_e32 v58, 8, v58
	v_lshlrev_b32_e32 v51, 8, v51
	v_lshlrev_b32_e32 v59, 8, v59
	v_perm_b32 v14, v16, v14, s28
	v_perm_b32 v16, v42, v40, s28
	v_and_b32_e32 v21, 0xff0000, v21
	v_and_b32_e32 v45, 0xff0000, v45
	v_and_b32_e32 v52, 0xff0000, v52
	v_and_b32_e32 v60, 0xff0000, v60
	v_and_b32_e32 v53, 0xff0000, v53
	v_and_b32_e32 v61, 0xff0000, v61
	v_perm_b32 v17, v17, v15, s28
	v_perm_b32 v40, v43, v41, s28
	v_perm_b32 v41, v50, v48, s28
	v_perm_b32 v42, v58, v56, s28
	v_perm_b32 v43, v51, v49, s28
	v_perm_b32 v48, v59, v57, s28
	v_or3_b32 v14, v14, v20, v24
	v_or3_b32 v15, v16, v44, v46
	v_or3_b32 v16, v17, v21, v25
	v_or3_b32 v17, v40, v45, v47
	v_or3_b32 v20, v41, v52, v54
	v_or3_b32 v21, v42, v60, v62
	v_or3_b32 v24, v43, v53, v55
	v_or3_b32 v25, v48, v61, v63
	global_store_dwordx2 v[18:19], v[14:15], off
	global_store_dwordx2 v[22:23], v[16:17], off
	global_store_dwordx2 v[82:83], v[20:21], off
	global_store_dwordx2 v[84:85], v[24:25], off
	s_waitcnt lgkmcnt(0)
	v_add_u32_e32 v87, 0x14a0, v31
	v_add_u32_e32 v88, 0x14a8, v31
	v_add_u32_e32 v89, 0x18c0, v31
	v_add_u32_e32 v90, 0x18c8, v31
	v_add_u32_e32 v91, 0x1ce0, v31
	v_add_u32_e32 v92, 0x1ce8, v31
	v_lshl_add_u64 v[18:19], v[6:7], 0, v[12:13]
	v_lshl_add_u64 v[22:23], v[6:7], 0, v[10:11]
	v_lshl_add_u64 v[82:83], v[6:7], 0, v[8:9]
	v_lshl_add_u64 v[84:85], v[6:7], 0, v[4:5]
	v_lshl_add_u64 v[6:7], v[6:7], 0, 64
	s_waitcnt vmcnt(24)
; #define LAS __attribute__((address_space(3)))
; #define GAS __attribute__((address_space(1)))
; #define LDS_WAIT() asm volatile("s_waitcnt lgkmcnt(0)" ::: "memory")
;     ...
;         for (int i = 0; i < 8; ++i) { const int kk = 8 * i + kr; const int k = 64 * kb + kk; const f32x4 v = __builtin_nontemporal_load((const f32x4*)(W + (size_t)k * pitch)) * g[k];
;             LAS float* p = scr + kk * 33 + 4 * (lane & 7); p[0] = __builtin_rintf(v[0] * inv[0]); p[1] = __builtin_rintf(v[1] * inv[1]); p[2] = __builtin_rintf(v[2] * inv[2]); p[3] = __builtin_rintf(v[3] * inv[3]); }
;         LDS_WAIT(); asm volatile("" ::: "memory");
;         const int c = lane & 7;
; #pragma unroll
;         for (int j = 0; j < 4; ++j) { const int n = (lane >> 3) + 8 * j; const LAS float* sp = scr + (8 * c) * 33 + n;
;             u32x2 o;
;             o.x = ((unsigned)(int)sp[0 * 33] & 0xFFu) | (((unsigned)(int)sp[1 * 33] & 0xFFu) << 8) | (((unsigned)(int)sp[2 * 33] & 0xFFu) << 16) | (((unsigned)(int)sp[3 * 33] & 0xFFu) << 24);
;             o.y = ((unsigned)(int)sp[4 * 33] & 0xFFu) | (((unsigned)(int)sp[5 * 33] & 0xFFu) << 8) | (((unsigned)(int)sp[6 * 33] & 0xFFu) << 16) | (((unsigned)(int)sp[7 * 33] & 0xFFu) << 24);
;             *(GAS u32x2*)(dst + (size_t)(n0 + n) * D + 64 * kb + 8 * c) = o; }
;         LDS_WAIT(); asm volatile("" ::: "memory");
	v_pk_mul_f32 v[46:47], v[144:145], v[188:189] op_sel_hi:[1,0]
	v_pk_mul_f32 v[20:21], v[142:143], v[188:189] op_sel_hi:[1,0]
	v_pk_mul_f32 v[44:45], v[148:149], v[190:191] op_sel_hi:[1,0]
	v_pk_mul_f32 v[24:25], v[146:147], v[190:191] op_sel_hi:[1,0]
	v_pk_mul_f32 v[48:49], v[152:153], v[192:193] op_sel_hi:[1,0]
	v_pk_mul_f32 v[16:17], v[140:141], v[186:187] op_sel_hi:[1,0]
	v_pk_mul_f32 v[14:15], v[138:139], v[186:187] op_sel_hi:[1,0]
	v_pk_mul_f32 v[50:51], v[150:151], v[192:193] op_sel_hi:[1,0]
	v_pk_mul_f32 v[52:53], v[156:157], v[194:195] op_sel_hi:[1,0]
	v_pk_mul_f32 v[54:55], v[154:155], v[194:195] op_sel_hi:[1,0]
	v_pk_mul_f32 v[56:57], v[160:161], v[196:197] op_sel_hi:[1,0]
	v_pk_mul_f32 v[58:59], v[158:159], v[196:197] op_sel_hi:[1,0]
	v_pk_mul_f32 v[60:61], v[164:165], v[198:199] op_sel_hi:[1,0]
	v_pk_mul_f32 v[62:63], v[162:163], v[198:199] op_sel_hi:[1,0]
	v_pk_mul_f32 v[42:43], v[168:169], v[200:201] op_sel_hi:[1,0]
	v_pk_mul_f32 v[40:41], v[166:167], v[200:201] op_sel_hi:[1,0]
	s_add_u32 s4, s4, 0x18000
	s_addc_u32 s5, s5, 0
	global_load_dwordx4 v[138:141], v250, s[4:5] nt
	global_load_dword v186, v251, s[6:7] offset:2816
	s_add_u32 s4, s4, 0x18000
	s_addc_u32 s5, s5, 0
	global_load_dwordx4 v[142:145], v250, s[4:5] nt
	global_load_dword v188, v251, s[6:7] offset:2848
	s_add_u32 s4, s4, 0x18000
	s_addc_u32 s5, s5, 0
	global_load_dwordx4 v[146:149], v250, s[4:5] nt
	global_load_dword v190, v251, s[6:7] offset:2880
	s_add_u32 s4, s4, 0x18000
	s_addc_u32 s5, s5, 0
	global_load_dwordx4 v[150:153], v250, s[4:5] nt
	global_load_dword v192, v251, s[6:7] offset:2912
	s_add_u32 s4, s4, 0x18000
	s_addc_u32 s5, s5, 0
	global_load_dwordx4 v[154:157], v250, s[4:5] nt
	global_load_dword v194, v251, s[6:7] offset:2944
	s_add_u32 s4, s4, 0x18000
	s_addc_u32 s5, s5, 0
	global_load_dwordx4 v[158:161], v250, s[4:5] nt
	global_load_dword v196, v251, s[6:7] offset:2976
	s_add_u32 s4, s4, 0x18000
	s_addc_u32 s5, s5, 0
	global_load_dwordx4 v[162:165], v250, s[4:5] nt
	global_load_dword v198, v251, s[6:7] offset:3008
	s_add_u32 s4, s4, 0x18000
	s_addc_u32 s5, s5, 0
	global_load_dwordx4 v[166:169], v250, s[4:5] nt
	global_load_dword v200, v251, s[6:7] offset:3040
	v_mul_f32_e32 v14, v26, v14
	v_mul_f32_e32 v15, v27, v15
	v_mul_f32_e32 v16, v28, v16
	v_mul_f32_e32 v17, v29, v17
	v_mul_f32_e32 v20, v26, v20
	v_mul_f32_e32 v21, v27, v21
	v_mul_f32_e32 v46, v28, v46
	v_mul_f32_e32 v47, v29, v47
	v_mul_f32_e32 v24, v26, v24
	v_mul_f32_e32 v25, v27, v25
	v_mul_f32_e32 v44, v28, v44
	v_mul_f32_e32 v45, v29, v45
	v_mul_f32_e32 v50, v26, v50
	v_mul_f32_e32 v51, v27, v51
	v_mul_f32_e32 v48, v28, v48
	v_mul_f32_e32 v49, v29, v49
	v_mul_f32_e32 v54, v26, v54
	v_mul_f32_e32 v55, v27, v55
	v_mul_f32_e32 v52, v28, v52
	v_mul_f32_e32 v53, v29, v53
	v_mul_f32_e32 v58, v26, v58
	v_mul_f32_e32 v59, v27, v59
	v_mul_f32_e32 v56, v28, v56
	v_mul_f32_e32 v57, v29, v57
	v_mul_f32_e32 v62, v26, v62
	v_mul_f32_e32 v63, v27, v63
	v_mul_f32_e32 v60, v28, v60
	v_mul_f32_e32 v61, v29, v61
	v_mul_f32_e32 v40, v26, v40
	v_mul_f32_e32 v41, v27, v41
	v_mul_f32_e32 v42, v28, v42
	v_mul_f32_e32 v43, v29, v43
	v_rndne_f32_e32 v14, v14
	v_rndne_f32_e32 v15, v15
	v_rndne_f32_e32 v16, v16
	v_rndne_f32_e32 v17, v17
	v_rndne_f32_e32 v20, v20
	v_rndne_f32_e32 v21, v21
	v_rndne_f32_e32 v46, v46
	v_rndne_f32_e32 v47, v47
	v_rndne_f32_e32 v24, v24
	v_rndne_f32_e32 v25, v25
	v_rndne_f32_e32 v44, v44
	v_rndne_f32_e32 v45, v45
	v_rndne_f32_e32 v50, v50
	v_rndne_f32_e32 v51, v51
	v_rndne_f32_e32 v48, v48
	v_rndne_f32_e32 v49, v49
	v_rndne_f32_e32 v54, v54
	v_rndne_f32_e32 v55, v55
	v_rndne_f32_e32 v52, v52
	v_rndne_f32_e32 v53, v53
	v_rndne_f32_e32 v58, v58
	v_rndne_f32_e32 v59, v59
	v_rndne_f32_e32 v56, v56
	v_rndne_f32_e32 v57, v57
	v_rndne_f32_e32 v62, v62
	v_rndne_f32_e32 v63, v63
	v_rndne_f32_e32 v60, v60
	v_rndne_f32_e32 v61, v61
	v_rndne_f32_e32 v40, v40
	v_rndne_f32_e32 v41, v41
	v_rndne_f32_e32 v42, v42
	v_rndne_f32_e32 v43, v43
	ds_write2_b32 v31, v14, v15 offset1:1
	ds_write2_b32 v31, v16, v17 offset0:2 offset1:3
	ds_write2_b32 v32, v20, v21 offset1:1
	ds_write2_b32 v33, v46, v47 offset1:1
	ds_write2_b32 v34, v24, v25 offset1:1
	ds_write2_b32 v35, v44, v45 offset1:1
	ds_write2_b32 v36, v50, v51 offset1:1
	ds_write2_b32 v37, v48, v49 offset1:1
	ds_write2_b32 v38, v54, v55 offset1:1
	ds_write2_b32 v39, v52, v53 offset1:1
	ds_write2_b32 v87, v58, v59 offset1:1
	ds_write2_b32 v88, v56, v57 offset1:1
	ds_write2_b32 v89, v62, v63 offset1:1
	ds_write2_b32 v90, v60, v61 offset1:1
	ds_write2_b32 v91, v40, v41 offset1:1
	ds_write2_b32 v92, v42, v43 offset1:1
	s_waitcnt lgkmcnt(0)
	ds_read2_b32 v[14:15], v30 offset1:8
	ds_read2_b32 v[16:17], v30 offset0:33 offset1:41
	ds_read2_b32 v[20:21], v30 offset0:66 offset1:74
	ds_read2_b32 v[24:25], v30 offset0:99 offset1:107
	ds_read2_b32 v[40:41], v30 offset0:132 offset1:140
	ds_read2_b32 v[42:43], v30 offset0:165 offset1:173
	ds_read2_b32 v[44:45], v30 offset0:198 offset1:206
	ds_read2_b32 v[46:47], v30 offset0:231 offset1:239
	ds_read2_b32 v[48:49], v30 offset0:16 offset1:24
	ds_read2_b32 v[50:51], v30 offset0:49 offset1:57
	ds_read2_b32 v[52:53], v30 offset0:82 offset1:90
	ds_read2_b32 v[54:55], v30 offset0:115 offset1:123
	ds_read2_b32 v[56:57], v30 offset0:148 offset1:156
	ds_read2_b32 v[58:59], v30 offset0:181 offset1:189
	ds_read2_b32 v[60:61], v30 offset0:214 offset1:222
	ds_read2_b32 v[62:63], v30 offset0:247 offset1:255
	s_waitcnt lgkmcnt(14)
	v_cvt_i32_f32_e32 v16, v16
	s_waitcnt lgkmcnt(10)
	v_cvt_i32_f32_e32 v42, v42
	v_cvt_i32_f32_e32 v14, v14
	v_cvt_i32_f32_sdwa v20, v20 dst_sel:WORD_1 dst_unused:UNUSED_PAD src0_sel:DWORD
	v_cvt_i32_f32_e32 v40, v40
	s_waitcnt lgkmcnt(9)
; #define LAS __attribute__((address_space(3)))
; #define GAS __attribute__((address_space(1)))
; #define LDS_WAIT() asm volatile("s_waitcnt lgkmcnt(0)" ::: "memory")
;     ...
;         for (int i = 0; i < 8; ++i) { const int kk = 8 * i + kr; const int k = 64 * kb + kk; const f32x4 v = __builtin_nontemporal_load((const f32x4*)(W + (size_t)k * pitch)) * g[k];
;             LAS float* p = scr + kk * 33 + 4 * (lane & 7); p[0] = __builtin_rintf(v[0] * inv[0]); p[1] = __builtin_rintf(v[1] * inv[1]); p[2] = __builtin_rintf(v[2] * inv[2]); p[3] = __builtin_rintf(v[3] * inv[3]); }
;         LDS_WAIT(); asm volatile("" ::: "memory");
;         const int c = lane & 7;
; #pragma unroll
;         for (int j = 0; j < 4; ++j) { const int n = (lane >> 3) + 8 * j; const LAS float* sp = scr + (8 * c) * 33 + n;
;             u32x2 o;
;             o.x = ((unsigned)(int)sp[0 * 33] & 0xFFu) | (((unsigned)(int)sp[1 * 33] & 0xFFu) << 8) | (((unsigned)(int)sp[2 * 33] & 0xFFu) << 16) | (((unsigned)(int)sp[3 * 33] & 0xFFu) << 24);
;             o.y = ((unsigned)(int)sp[4 * 33] & 0xFFu) | (((unsigned)(int)sp[5 * 33] & 0xFFu) << 8) | (((unsigned)(int)sp[6 * 33] & 0xFFu) << 16) | (((unsigned)(int)sp[7 * 33] & 0xFFu) << 24);
;             *(GAS u32x2*)(dst + (size_t)(n0 + n) * D + 64 * kb + 8 * c) = o; }
;         LDS_WAIT(); asm volatile("" ::: "memory");
	v_cvt_i32_f32_sdwa v44, v44 dst_sel:WORD_1 dst_unused:UNUSED_PAD src0_sel:DWORD
	v_cvt_i32_f32_e32 v17, v17
	v_cvt_i32_f32_e32 v43, v43
	s_waitcnt lgkmcnt(6)
	v_cvt_i32_f32_e32 v50, v50
	s_waitcnt lgkmcnt(2)
	v_cvt_i32_f32_e32 v58, v58
	v_cvt_i32_f32_e32 v51, v51
	v_cvt_i32_f32_e32 v59, v59
	v_cvt_i32_f32_sdwa v24, v24 dst_sel:BYTE_3 dst_unused:UNUSED_PAD src0_sel:DWORD
	v_cvt_i32_f32_sdwa v46, v46 dst_sel:BYTE_3 dst_unused:UNUSED_PAD src0_sel:DWORD
	v_cvt_i32_f32_e32 v15, v15
	v_cvt_i32_f32_sdwa v21, v21 dst_sel:WORD_1 dst_unused:UNUSED_PAD src0_sel:DWORD
	v_cvt_i32_f32_e32 v41, v41
	v_cvt_i32_f32_sdwa v45, v45 dst_sel:WORD_1 dst_unused:UNUSED_PAD src0_sel:DWORD
	v_cvt_i32_f32_e32 v48, v48
	v_cvt_i32_f32_sdwa v52, v52 dst_sel:WORD_1 dst_unused:UNUSED_PAD src0_sel:DWORD
	v_cvt_i32_f32_e32 v56, v56
	s_waitcnt lgkmcnt(1)
	v_cvt_i32_f32_sdwa v60, v60 dst_sel:WORD_1 dst_unused:UNUSED_PAD src0_sel:DWORD
	v_cvt_i32_f32_e32 v49, v49
	v_cvt_i32_f32_sdwa v53, v53 dst_sel:WORD_1 dst_unused:UNUSED_PAD src0_sel:DWORD
	v_cvt_i32_f32_e32 v57, v57
	v_cvt_i32_f32_sdwa v61, v61 dst_sel:WORD_1 dst_unused:UNUSED_PAD src0_sel:DWORD
	v_cvt_i32_f32_sdwa v25, v25 dst_sel:BYTE_3 dst_unused:UNUSED_PAD src0_sel:DWORD
	v_cvt_i32_f32_sdwa v47, v47 dst_sel:BYTE_3 dst_unused:UNUSED_PAD src0_sel:DWORD
	v_cvt_i32_f32_sdwa v54, v54 dst_sel:BYTE_3 dst_unused:UNUSED_PAD src0_sel:DWORD
	s_waitcnt lgkmcnt(0)
	v_cvt_i32_f32_sdwa v62, v62 dst_sel:BYTE_3 dst_unused:UNUSED_PAD src0_sel:DWORD
	v_cvt_i32_f32_sdwa v55, v55 dst_sel:BYTE_3 dst_unused:UNUSED_PAD src0_sel:DWORD
	v_cvt_i32_f32_sdwa v63, v63 dst_sel:BYTE_3 dst_unused:UNUSED_PAD src0_sel:DWORD
	v_lshlrev_b32_e32 v16, 8, v16
	v_lshlrev_b32_e32 v42, 8, v42
	v_and_b32_e32 v20, 0xff0000, v20
	v_and_b32_e32 v44, 0xff0000, v44
	v_lshlrev_b32_e32 v17, 8, v17
	v_lshlrev_b32_e32 v43, 8, v43
	v_lshlrev_b32_e32 v50, 8, v50
	v_lshlrev_b32_e32 v58, 8, v58
	v_lshlrev_b32_e32 v51, 8, v51
	v_lshlrev_b32_e32 v59, 8, v59
	v_perm_b32 v14, v16, v14, s28
	v_perm_b32 v16, v42, v40, s28
	v_and_b32_e32 v21, 0xff0000, v21
	v_and_b32_e32 v45, 0xff0000, v45
	v_and_b32_e32 v52, 0xff0000, v52
	v_and_b32_e32 v60, 0xff0000, v60
	v_and_b32_e32 v53, 0xff0000, v53
	v_and_b32_e32 v61, 0xff0000, v61
	v_perm_b32 v17, v17, v15, s28
	v_perm_b32 v40, v43, v41, s28
	v_perm_b32 v41, v50, v48, s28
	v_perm_b32 v42, v58, v56, s28
	v_perm_b32 v43, v51, v49, s28
	v_perm_b32 v48, v59, v57, s28
	v_or3_b32 v14, v14, v20, v24
	v_or3_b32 v15, v16, v44, v46
	v_or3_b32 v16, v17, v21, v25
	v_or3_b32 v17, v40, v45, v47
	v_or3_b32 v20, v41, v52, v54
	v_or3_b32 v21, v42, v60, v62
	v_or3_b32 v24, v43, v53, v55
	v_or3_b32 v25, v48, v61, v63
	global_store_dwordx2 v[18:19], v[14:15], off
	global_store_dwordx2 v[22:23], v[16:17], off
	global_store_dwordx2 v[82:83], v[20:21], off
	global_store_dwordx2 v[84:85], v[24:25], off
	s_waitcnt lgkmcnt(0)
	v_add_u32_e32 v87, 0x14a0, v31
	v_add_u32_e32 v88, 0x14a8, v31
	v_add_u32_e32 v89, 0x18c0, v31
	v_add_u32_e32 v90, 0x18c8, v31
	v_add_u32_e32 v91, 0x1ce0, v31
	v_add_u32_e32 v92, 0x1ce8, v31
	v_lshl_add_u64 v[18:19], v[6:7], 0, v[12:13]
	v_lshl_add_u64 v[22:23], v[6:7], 0, v[10:11]
	v_lshl_add_u64 v[82:83], v[6:7], 0, v[8:9]
	v_lshl_add_u64 v[84:85], v[6:7], 0, v[4:5]
	v_lshl_add_u64 v[6:7], v[6:7], 0, 64
	s_waitcnt vmcnt(24)
	v_pk_mul_f32 v[46:47], v[112:113], v[172:173] op_sel_hi:[1,0]
	v_pk_mul_f32 v[20:21], v[110:111], v[172:173] op_sel_hi:[1,0]
	v_pk_mul_f32 v[44:45], v[116:117], v[174:175] op_sel_hi:[1,0]
	v_pk_mul_f32 v[24:25], v[114:115], v[174:175] op_sel_hi:[1,0]
	v_pk_mul_f32 v[48:49], v[120:121], v[176:177] op_sel_hi:[1,0]
	v_pk_mul_f32 v[16:17], v[108:109], v[170:171] op_sel_hi:[1,0]
	v_pk_mul_f32 v[14:15], v[106:107], v[170:171] op_sel_hi:[1,0]
	v_pk_mul_f32 v[50:51], v[118:119], v[176:177] op_sel_hi:[1,0]
	v_pk_mul_f32 v[52:53], v[124:125], v[178:179] op_sel_hi:[1,0]
	v_pk_mul_f32 v[54:55], v[122:123], v[178:179] op_sel_hi:[1,0]
	v_pk_mul_f32 v[56:57], v[128:129], v[180:181] op_sel_hi:[1,0]
	v_pk_mul_f32 v[58:59], v[126:127], v[180:181] op_sel_hi:[1,0]
	v_pk_mul_f32 v[60:61], v[132:133], v[182:183] op_sel_hi:[1,0]
	v_pk_mul_f32 v[62:63], v[130:131], v[182:183] op_sel_hi:[1,0]
	v_pk_mul_f32 v[42:43], v[136:137], v[184:185] op_sel_hi:[1,0]
	v_pk_mul_f32 v[40:41], v[134:135], v[184:185] op_sel_hi:[1,0]
	s_add_u32 s4, s4, 0x18000
	s_addc_u32 s5, s5, 0
	global_load_dwordx4 v[106:109], v250, s[4:5] nt
	global_load_dword v170, v251, s[6:7] offset:3072
	s_add_u32 s4, s4, 0x18000
	s_addc_u32 s5, s5, 0
	global_load_dwordx4 v[110:113], v250, s[4:5] nt
	global_load_dword v172, v251, s[6:7] offset:3104
	s_add_u32 s4, s4, 0x18000
	s_addc_u32 s5, s5, 0
	global_load_dwordx4 v[114:117], v250, s[4:5] nt
	global_load_dword v174, v251, s[6:7] offset:3136
	s_add_u32 s4, s4, 0x18000
	s_addc_u32 s5, s5, 0
	global_load_dwordx4 v[118:121], v250, s[4:5] nt
	global_load_dword v176, v251, s[6:7] offset:3168
	s_add_u32 s4, s4, 0x18000
	s_addc_u32 s5, s5, 0
	global_load_dwordx4 v[122:125], v250, s[4:5] nt
	global_load_dword v178, v251, s[6:7] offset:3200
	s_add_u32 s4, s4, 0x18000
	s_addc_u32 s5, s5, 0
	global_load_dwordx4 v[126:129], v250, s[4:5] nt
	global_load_dword v180, v251, s[6:7] offset:3232
	s_add_u32 s4, s4, 0x18000
	s_addc_u32 s5, s5, 0
	global_load_dwordx4 v[130:133], v250, s[4:5] nt
	global_load_dword v182, v251, s[6:7] offset:3264
	s_add_u32 s4, s4, 0x18000
	s_addc_u32 s5, s5, 0
	global_load_dwordx4 v[134:137], v250, s[4:5] nt
	global_load_dword v184, v251, s[6:7] offset:3296
	v_mul_f32_e32 v14, v26, v14
	v_mul_f32_e32 v15, v27, v15
	v_mul_f32_e32 v16, v28, v16
	v_mul_f32_e32 v17, v29, v17
	v_mul_f32_e32 v20, v26, v20
	v_mul_f32_e32 v21, v27, v21
; #define LAS __attribute__((address_space(3)))
; #define GAS __attribute__((address_space(1)))
; #define LDS_WAIT() asm volatile("s_waitcnt lgkmcnt(0)" ::: "memory")
;     ...
;         for (int i = 0; i < 8; ++i) { const int kk = 8 * i + kr; const int k = 64 * kb + kk; const f32x4 v = __builtin_nontemporal_load((const f32x4*)(W + (size_t)k * pitch)) * g[k];
;             LAS float* p = scr + kk * 33 + 4 * (lane & 7); p[0] = __builtin_rintf(v[0] * inv[0]); p[1] = __builtin_rintf(v[1] * inv[1]); p[2] = __builtin_rintf(v[2] * inv[2]); p[3] = __builtin_rintf(v[3] * inv[3]); }
;         LDS_WAIT(); asm volatile("" ::: "memory");
;         const int c = lane & 7;
; #pragma unroll
;         for (int j = 0; j < 4; ++j) { const int n = (lane >> 3) + 8 * j; const LAS float* sp = scr + (8 * c) * 33 + n;
;             u32x2 o;
;             o.x = ((unsigned)(int)sp[0 * 33] & 0xFFu) | (((unsigned)(int)sp[1 * 33] & 0xFFu) << 8) | (((unsigned)(int)sp[2 * 33] & 0xFFu) << 16) | (((unsigned)(int)sp[3 * 33] & 0xFFu) << 24);
;             o.y = ((unsigned)(int)sp[4 * 33] & 0xFFu) | (((unsigned)(int)sp[5 * 33] & 0xFFu) << 8) | (((unsigned)(int)sp[6 * 33] & 0xFFu) << 16) | (((unsigned)(int)sp[7 * 33] & 0xFFu) << 24);
;             *(GAS u32x2*)(dst + (size_t)(n0 + n) * D + 64 * kb + 8 * c) = o; }
;         LDS_WAIT(); asm volatile("" ::: "memory");
	v_mul_f32_e32 v46, v28, v46
	v_mul_f32_e32 v47, v29, v47
	v_mul_f32_e32 v24, v26, v24
	v_mul_f32_e32 v25, v27, v25
	v_mul_f32_e32 v44, v28, v44
	v_mul_f32_e32 v45, v29, v45
	v_mul_f32_e32 v50, v26, v50
	v_mul_f32_e32 v51, v27, v51
	v_mul_f32_e32 v48, v28, v48
	v_mul_f32_e32 v49, v29, v49
	v_mul_f32_e32 v54, v26, v54
	v_mul_f32_e32 v55, v27, v55
	v_mul_f32_e32 v52, v28, v52
	v_mul_f32_e32 v53, v29, v53
	v_mul_f32_e32 v58, v26, v58
	v_mul_f32_e32 v59, v27, v59
	v_mul_f32_e32 v56, v28, v56
	v_mul_f32_e32 v57, v29, v57
	v_mul_f32_e32 v62, v26, v62
	v_mul_f32_e32 v63, v27, v63
	v_mul_f32_e32 v60, v28, v60
	v_mul_f32_e32 v61, v29, v61
	v_mul_f32_e32 v40, v26, v40
	v_mul_f32_e32 v41, v27, v41
	v_mul_f32_e32 v42, v28, v42
	v_mul_f32_e32 v43, v29, v43
	v_rndne_f32_e32 v14, v14
	v_rndne_f32_e32 v15, v15
	v_rndne_f32_e32 v16, v16
	v_rndne_f32_e32 v17, v17
	v_rndne_f32_e32 v20, v20
	v_rndne_f32_e32 v21, v21
	v_rndne_f32_e32 v46, v46
	v_rndne_f32_e32 v47, v47
	v_rndne_f32_e32 v24, v24
	v_rndne_f32_e32 v25, v25
	v_rndne_f32_e32 v44, v44
	v_rndne_f32_e32 v45, v45
	v_rndne_f32_e32 v50, v50
	v_rndne_f32_e32 v51, v51
	v_rndne_f32_e32 v48, v48
	v_rndne_f32_e32 v49, v49
	v_rndne_f32_e32 v54, v54
	v_rndne_f32_e32 v55, v55
	v_rndne_f32_e32 v52, v52
	v_rndne_f32_e32 v53, v53
	v_rndne_f32_e32 v58, v58
	v_rndne_f32_e32 v59, v59
	v_rndne_f32_e32 v56, v56
	v_rndne_f32_e32 v57, v57
	v_rndne_f32_e32 v62, v62
	v_rndne_f32_e32 v63, v63
	v_rndne_f32_e32 v60, v60
	v_rndne_f32_e32 v61, v61
	v_rndne_f32_e32 v40, v40
	v_rndne_f32_e32 v41, v41
	v_rndne_f32_e32 v42, v42
	v_rndne_f32_e32 v43, v43
	ds_write2_b32 v31, v14, v15 offset1:1
	ds_write2_b32 v31, v16, v17 offset0:2 offset1:3
	ds_write2_b32 v32, v20, v21 offset1:1
	ds_write2_b32 v33, v46, v47 offset1:1
	ds_write2_b32 v34, v24, v25 offset1:1
	ds_write2_b32 v35, v44, v45 offset1:1
	ds_write2_b32 v36, v50, v51 offset1:1
	ds_write2_b32 v37, v48, v49 offset1:1
	ds_write2_b32 v38, v54, v55 offset1:1
	ds_write2_b32 v39, v52, v53 offset1:1
	ds_write2_b32 v87, v58, v59 offset1:1
	ds_write2_b32 v88, v56, v57 offset1:1
	ds_write2_b32 v89, v62, v63 offset1:1
	ds_write2_b32 v90, v60, v61 offset1:1
	ds_write2_b32 v91, v40, v41 offset1:1
	ds_write2_b32 v92, v42, v43 offset1:1
	s_waitcnt lgkmcnt(0)
	ds_read2_b32 v[14:15], v30 offset1:8
	ds_read2_b32 v[16:17], v30 offset0:33 offset1:41
	ds_read2_b32 v[20:21], v30 offset0:66 offset1:74
	ds_read2_b32 v[24:25], v30 offset0:99 offset1:107
	ds_read2_b32 v[40:41], v30 offset0:132 offset1:140
	ds_read2_b32 v[42:43], v30 offset0:165 offset1:173
	ds_read2_b32 v[44:45], v30 offset0:198 offset1:206
	ds_read2_b32 v[46:47], v30 offset0:231 offset1:239
	ds_read2_b32 v[48:49], v30 offset0:16 offset1:24
	ds_read2_b32 v[50:51], v30 offset0:49 offset1:57
	ds_read2_b32 v[52:53], v30 offset0:82 offset1:90
	ds_read2_b32 v[54:55], v30 offset0:115 offset1:123
	ds_read2_b32 v[56:57], v30 offset0:148 offset1:156
	ds_read2_b32 v[58:59], v30 offset0:181 offset1:189
	ds_read2_b32 v[60:61], v30 offset0:214 offset1:222
	ds_read2_b32 v[62:63], v30 offset0:247 offset1:255
	s_waitcnt lgkmcnt(14)
	v_cvt_i32_f32_e32 v16, v16
	s_waitcnt lgkmcnt(10)
	v_cvt_i32_f32_e32 v42, v42
	v_cvt_i32_f32_e32 v14, v14
	v_cvt_i32_f32_sdwa v20, v20 dst_sel:WORD_1 dst_unused:UNUSED_PAD src0_sel:DWORD
	v_cvt_i32_f32_e32 v40, v40
	s_waitcnt lgkmcnt(9)
	v_cvt_i32_f32_sdwa v44, v44 dst_sel:WORD_1 dst_unused:UNUSED_PAD src0_sel:DWORD
	v_cvt_i32_f32_e32 v17, v17
	v_cvt_i32_f32_e32 v43, v43
	s_waitcnt lgkmcnt(6)
	v_cvt_i32_f32_e32 v50, v50
	s_waitcnt lgkmcnt(2)
	v_cvt_i32_f32_e32 v58, v58
	v_cvt_i32_f32_e32 v51, v51
	v_cvt_i32_f32_e32 v59, v59
	v_cvt_i32_f32_sdwa v24, v24 dst_sel:BYTE_3 dst_unused:UNUSED_PAD src0_sel:DWORD
	v_cvt_i32_f32_sdwa v46, v46 dst_sel:BYTE_3 dst_unused:UNUSED_PAD src0_sel:DWORD
	v_cvt_i32_f32_e32 v15, v15
	v_cvt_i32_f32_sdwa v21, v21 dst_sel:WORD_1 dst_unused:UNUSED_PAD src0_sel:DWORD
	v_cvt_i32_f32_e32 v41, v41
	v_cvt_i32_f32_sdwa v45, v45 dst_sel:WORD_1 dst_unused:UNUSED_PAD src0_sel:DWORD
	v_cvt_i32_f32_e32 v48, v48
	v_cvt_i32_f32_sdwa v52, v52 dst_sel:WORD_1 dst_unused:UNUSED_PAD src0_sel:DWORD
	v_cvt_i32_f32_e32 v56, v56
	s_waitcnt lgkmcnt(1)
	v_cvt_i32_f32_sdwa v60, v60 dst_sel:WORD_1 dst_unused:UNUSED_PAD src0_sel:DWORD
	v_cvt_i32_f32_e32 v49, v49
	v_cvt_i32_f32_sdwa v53, v53 dst_sel:WORD_1 dst_unused:UNUSED_PAD src0_sel:DWORD
	v_cvt_i32_f32_e32 v57, v57
	v_cvt_i32_f32_sdwa v61, v61 dst_sel:WORD_1 dst_unused:UNUSED_PAD src0_sel:DWORD
	v_cvt_i32_f32_sdwa v25, v25 dst_sel:BYTE_3 dst_unused:UNUSED_PAD src0_sel:DWORD
	v_cvt_i32_f32_sdwa v47, v47 dst_sel:BYTE_3 dst_unused:UNUSED_PAD src0_sel:DWORD
	v_cvt_i32_f32_sdwa v54, v54 dst_sel:BYTE_3 dst_unused:UNUSED_PAD src0_sel:DWORD
	s_waitcnt lgkmcnt(0)
	v_cvt_i32_f32_sdwa v62, v62 dst_sel:BYTE_3 dst_unused:UNUSED_PAD src0_sel:DWORD
	v_cvt_i32_f32_sdwa v55, v55 dst_sel:BYTE_3 dst_unused:UNUSED_PAD src0_sel:DWORD
	v_cvt_i32_f32_sdwa v63, v63 dst_sel:BYTE_3 dst_unused:UNUSED_PAD src0_sel:DWORD
	v_lshlrev_b32_e32 v16, 8, v16
	v_lshlrev_b32_e32 v42, 8, v42
	v_and_b32_e32 v20, 0xff0000, v20
	v_and_b32_e32 v44, 0xff0000, v44
	v_lshlrev_b32_e32 v17, 8, v17
	v_lshlrev_b32_e32 v43, 8, v43
	v_lshlrev_b32_e32 v50, 8, v50
	v_lshlrev_b32_e32 v58, 8, v58
	v_lshlrev_b32_e32 v51, 8, v51
	v_lshlrev_b32_e32 v59, 8, v59
	v_perm_b32 v14, v16, v14, s28
	v_perm_b32 v16, v42, v40, s28
	v_and_b32_e32 v21, 0xff0000, v21
	v_and_b32_e32 v45, 0xff0000, v45
	v_and_b32_e32 v52, 0xff0000, v52
	v_and_b32_e32 v60, 0xff0000, v60
	v_and_b32_e32 v53, 0xff0000, v53
	v_and_b32_e32 v61, 0xff0000, v61
	v_perm_b32 v17, v17, v15, s28
	v_perm_b32 v40, v43, v41, s28
	v_perm_b32 v41, v50, v48, s28
	v_perm_b32 v42, v58, v56, s28
	v_perm_b32 v43, v51, v49, s28
	v_perm_b32 v48, v59, v57, s28
	v_or3_b32 v14, v14, v20, v24
	v_or3_b32 v15, v16, v44, v46
	v_or3_b32 v16, v17, v21, v25
	v_or3_b32 v17, v40, v45, v47
	v_or3_b32 v20, v41, v52, v54
	v_or3_b32 v21, v42, v60, v62
	v_or3_b32 v24, v43, v53, v55
	v_or3_b32 v25, v48, v61, v63
	global_store_dwordx2 v[18:19], v[14:15], off
	global_store_dwordx2 v[22:23], v[16:17], off
	global_store_dwordx2 v[82:83], v[20:21], off
	global_store_dwordx2 v[84:85], v[24:25], off
	s_waitcnt lgkmcnt(0)
; #define LAS __attribute__((address_space(3)))
; #define GAS __attribute__((address_space(1)))
; #define LDS_WAIT() asm volatile("s_waitcnt lgkmcnt(0)" ::: "memory")
;     ...
;         for (int i = 0; i < 8; ++i) { const int kk = 8 * i + kr; const int k = 64 * kb + kk; const f32x4 v = __builtin_nontemporal_load((const f32x4*)(W + (size_t)k * pitch)) * g[k];
;             LAS float* p = scr + kk * 33 + 4 * (lane & 7); p[0] = __builtin_rintf(v[0] * inv[0]); p[1] = __builtin_rintf(v[1] * inv[1]); p[2] = __builtin_rintf(v[2] * inv[2]); p[3] = __builtin_rintf(v[3] * inv[3]); }
;         LDS_WAIT(); asm volatile("" ::: "memory");
;         const int c = lane & 7;
; #pragma unroll
;         for (int j = 0; j < 4; ++j) { const int n = (lane >> 3) + 8 * j; const LAS float* sp = scr + (8 * c) * 33 + n;
;             u32x2 o;
;             o.x = ((unsigned)(int)sp[0 * 33] & 0xFFu) | (((unsigned)(int)sp[1 * 33] & 0xFFu) << 8) | (((unsigned)(int)sp[2 * 33] & 0xFFu) << 16) | (((unsigned)(int)sp[3 * 33] & 0xFFu) << 24);
;             o.y = ((unsigned)(int)sp[4 * 33] & 0xFFu) | (((unsigned)(int)sp[5 * 33] & 0xFFu) << 8) | (((unsigned)(int)sp[6 * 33] & 0xFFu) << 16) | (((unsigned)(int)sp[7 * 33] & 0xFFu) << 24);
;             *(GAS u32x2*)(dst + (size_t)(n0 + n) * D + 64 * kb + 8 * c) = o; }
;         LDS_WAIT(); asm volatile("" ::: "memory");
	v_add_u32_e32 v87, 0x14a0, v31
	v_add_u32_e32 v88, 0x14a8, v31
	v_add_u32_e32 v89, 0x18c0, v31
	v_add_u32_e32 v90, 0x18c8, v31
	v_add_u32_e32 v91, 0x1ce0, v31
	v_add_u32_e32 v92, 0x1ce8, v31
	v_lshl_add_u64 v[18:19], v[6:7], 0, v[12:13]
	v_lshl_add_u64 v[22:23], v[6:7], 0, v[10:11]
	v_lshl_add_u64 v[82:83], v[6:7], 0, v[8:9]
	v_lshl_add_u64 v[84:85], v[6:7], 0, v[4:5]
	v_lshl_add_u64 v[6:7], v[6:7], 0, 64
	s_waitcnt vmcnt(24)
	v_pk_mul_f32 v[46:47], v[144:145], v[188:189] op_sel_hi:[1,0]
	v_pk_mul_f32 v[20:21], v[142:143], v[188:189] op_sel_hi:[1,0]
	v_pk_mul_f32 v[44:45], v[148:149], v[190:191] op_sel_hi:[1,0]
	v_pk_mul_f32 v[24:25], v[146:147], v[190:191] op_sel_hi:[1,0]
	v_pk_mul_f32 v[48:49], v[152:153], v[192:193] op_sel_hi:[1,0]
	v_pk_mul_f32 v[16:17], v[140:141], v[186:187] op_sel_hi:[1,0]
	v_pk_mul_f32 v[14:15], v[138:139], v[186:187] op_sel_hi:[1,0]
	v_pk_mul_f32 v[50:51], v[150:151], v[192:193] op_sel_hi:[1,0]
	v_pk_mul_f32 v[52:53], v[156:157], v[194:195] op_sel_hi:[1,0]
	v_pk_mul_f32 v[54:55], v[154:155], v[194:195] op_sel_hi:[1,0]
	v_pk_mul_f32 v[56:57], v[160:161], v[196:197] op_sel_hi:[1,0]
	v_pk_mul_f32 v[58:59], v[158:159], v[196:197] op_sel_hi:[1,0]
	v_pk_mul_f32 v[60:61], v[164:165], v[198:199] op_sel_hi:[1,0]
	v_pk_mul_f32 v[62:63], v[162:163], v[198:199] op_sel_hi:[1,0]
	v_pk_mul_f32 v[42:43], v[168:169], v[200:201] op_sel_hi:[1,0]
	v_pk_mul_f32 v[40:41], v[166:167], v[200:201] op_sel_hi:[1,0]
	s_add_u32 s4, s4, 0x18000
	s_addc_u32 s5, s5, 0
	global_load_dwordx4 v[138:141], v250, s[4:5] nt
	global_load_dword v186, v251, s[6:7] offset:3328
	s_add_u32 s4, s4, 0x18000
	s_addc_u32 s5, s5, 0
	global_load_dwordx4 v[142:145], v250, s[4:5] nt
	global_load_dword v188, v251, s[6:7] offset:3360
	s_add_u32 s4, s4, 0x18000
	s_addc_u32 s5, s5, 0
	global_load_dwordx4 v[146:149], v250, s[4:5] nt
	global_load_dword v190, v251, s[6:7] offset:3392
	s_add_u32 s4, s4, 0x18000
	s_addc_u32 s5, s5, 0
	global_load_dwordx4 v[150:153], v250, s[4:5] nt
	global_load_dword v192, v251, s[6:7] offset:3424
	s_add_u32 s4, s4, 0x18000
	s_addc_u32 s5, s5, 0
	global_load_dwordx4 v[154:157], v250, s[4:5] nt
	global_load_dword v194, v251, s[6:7] offset:3456
	s_add_u32 s4, s4, 0x18000
	s_addc_u32 s5, s5, 0
	global_load_dwordx4 v[158:161], v250, s[4:5] nt
	global_load_dword v196, v251, s[6:7] offset:3488
	s_add_u32 s4, s4, 0x18000
	s_addc_u32 s5, s5, 0
	global_load_dwordx4 v[162:165], v250, s[4:5] nt
	global_load_dword v198, v251, s[6:7] offset:3520
	s_add_u32 s4, s4, 0x18000
	s_addc_u32 s5, s5, 0
	global_load_dwordx4 v[166:169], v250, s[4:5] nt
	global_load_dword v200, v251, s[6:7] offset:3552
	v_mul_f32_e32 v14, v26, v14
	v_mul_f32_e32 v15, v27, v15
	v_mul_f32_e32 v16, v28, v16
	v_mul_f32_e32 v17, v29, v17
	v_mul_f32_e32 v20, v26, v20
	v_mul_f32_e32 v21, v27, v21
	v_mul_f32_e32 v46, v28, v46
	v_mul_f32_e32 v47, v29, v47
	v_mul_f32_e32 v24, v26, v24
	v_mul_f32_e32 v25, v27, v25
	v_mul_f32_e32 v44, v28, v44
	v_mul_f32_e32 v45, v29, v45
	v_mul_f32_e32 v50, v26, v50
	v_mul_f32_e32 v51, v27, v51
	v_mul_f32_e32 v48, v28, v48
	v_mul_f32_e32 v49, v29, v49
	v_mul_f32_e32 v54, v26, v54
	v_mul_f32_e32 v55, v27, v55
	v_mul_f32_e32 v52, v28, v52
	v_mul_f32_e32 v53, v29, v53
	v_mul_f32_e32 v58, v26, v58
	v_mul_f32_e32 v59, v27, v59
	v_mul_f32_e32 v56, v28, v56
	v_mul_f32_e32 v57, v29, v57
	v_mul_f32_e32 v62, v26, v62
	v_mul_f32_e32 v63, v27, v63
	v_mul_f32_e32 v60, v28, v60
	v_mul_f32_e32 v61, v29, v61
	v_mul_f32_e32 v40, v26, v40
	v_mul_f32_e32 v41, v27, v41
	v_mul_f32_e32 v42, v28, v42
	v_mul_f32_e32 v43, v29, v43
	v_rndne_f32_e32 v14, v14
	v_rndne_f32_e32 v15, v15
	v_rndne_f32_e32 v16, v16
	v_rndne_f32_e32 v17, v17
	v_rndne_f32_e32 v20, v20
	v_rndne_f32_e32 v21, v21
	v_rndne_f32_e32 v46, v46
	v_rndne_f32_e32 v47, v47
	v_rndne_f32_e32 v24, v24
	v_rndne_f32_e32 v25, v25
	v_rndne_f32_e32 v44, v44
	v_rndne_f32_e32 v45, v45
	v_rndne_f32_e32 v50, v50
	v_rndne_f32_e32 v51, v51
	v_rndne_f32_e32 v48, v48
	v_rndne_f32_e32 v49, v49
	v_rndne_f32_e32 v54, v54
	v_rndne_f32_e32 v55, v55
	v_rndne_f32_e32 v52, v52
	v_rndne_f32_e32 v53, v53
	v_rndne_f32_e32 v58, v58
	v_rndne_f32_e32 v59, v59
	v_rndne_f32_e32 v56, v56
	v_rndne_f32_e32 v57, v57
	v_rndne_f32_e32 v62, v62
	v_rndne_f32_e32 v63, v63
	v_rndne_f32_e32 v60, v60
	v_rndne_f32_e32 v61, v61
	v_rndne_f32_e32 v40, v40
	v_rndne_f32_e32 v41, v41
	v_rndne_f32_e32 v42, v42
	v_rndne_f32_e32 v43, v43
	ds_write2_b32 v31, v14, v15 offset1:1
	ds_write2_b32 v31, v16, v17 offset0:2 offset1:3
	ds_write2_b32 v32, v20, v21 offset1:1
	ds_write2_b32 v33, v46, v47 offset1:1
	ds_write2_b32 v34, v24, v25 offset1:1
	ds_write2_b32 v35, v44, v45 offset1:1
	ds_write2_b32 v36, v50, v51 offset1:1
	ds_write2_b32 v37, v48, v49 offset1:1
	ds_write2_b32 v38, v54, v55 offset1:1
	ds_write2_b32 v39, v52, v53 offset1:1
	ds_write2_b32 v87, v58, v59 offset1:1
	ds_write2_b32 v88, v56, v57 offset1:1
	ds_write2_b32 v89, v62, v63 offset1:1
	ds_write2_b32 v90, v60, v61 offset1:1
	ds_write2_b32 v91, v40, v41 offset1:1
	ds_write2_b32 v92, v42, v43 offset1:1
	s_waitcnt lgkmcnt(0)
	ds_read2_b32 v[14:15], v30 offset1:8
	ds_read2_b32 v[16:17], v30 offset0:33 offset1:41
	ds_read2_b32 v[20:21], v30 offset0:66 offset1:74
	ds_read2_b32 v[24:25], v30 offset0:99 offset1:107
	ds_read2_b32 v[40:41], v30 offset0:132 offset1:140
	ds_read2_b32 v[42:43], v30 offset0:165 offset1:173
	ds_read2_b32 v[44:45], v30 offset0:198 offset1:206
	ds_read2_b32 v[46:47], v30 offset0:231 offset1:239
	ds_read2_b32 v[48:49], v30 offset0:16 offset1:24
	ds_read2_b32 v[50:51], v30 offset0:49 offset1:57
	ds_read2_b32 v[52:53], v30 offset0:82 offset1:90
	ds_read2_b32 v[54:55], v30 offset0:115 offset1:123
	ds_read2_b32 v[56:57], v30 offset0:148 offset1:156
	ds_read2_b32 v[58:59], v30 offset0:181 offset1:189
	ds_read2_b32 v[60:61], v30 offset0:214 offset1:222
	ds_read2_b32 v[62:63], v30 offset0:247 offset1:255
	s_waitcnt lgkmcnt(14)
; #define LAS __attribute__((address_space(3)))
; #define GAS __attribute__((address_space(1)))
; #define LDS_WAIT() asm volatile("s_waitcnt lgkmcnt(0)" ::: "memory")
;     ...
;         for (int i = 0; i < 8; ++i) { const int kk = 8 * i + kr; const int k = 64 * kb + kk; const f32x4 v = __builtin_nontemporal_load((const f32x4*)(W + (size_t)k * pitch)) * g[k];
;             LAS float* p = scr + kk * 33 + 4 * (lane & 7); p[0] = __builtin_rintf(v[0] * inv[0]); p[1] = __builtin_rintf(v[1] * inv[1]); p[2] = __builtin_rintf(v[2] * inv[2]); p[3] = __builtin_rintf(v[3] * inv[3]); }
;         LDS_WAIT(); asm volatile("" ::: "memory");
;         const int c = lane & 7;
; #pragma unroll
;         for (int j = 0; j < 4; ++j) { const int n = (lane >> 3) + 8 * j; const LAS float* sp = scr + (8 * c) * 33 + n;
;             u32x2 o;
;             o.x = ((unsigned)(int)sp[0 * 33] & 0xFFu) | (((unsigned)(int)sp[1 * 33] & 0xFFu) << 8) | (((unsigned)(int)sp[2 * 33] & 0xFFu) << 16) | (((unsigned)(int)sp[3 * 33] & 0xFFu) << 24);
;             o.y = ((unsigned)(int)sp[4 * 33] & 0xFFu) | (((unsigned)(int)sp[5 * 33] & 0xFFu) << 8) | (((unsigned)(int)sp[6 * 33] & 0xFFu) << 16) | (((unsigned)(int)sp[7 * 33] & 0xFFu) << 24);
;             *(GAS u32x2*)(dst + (size_t)(n0 + n) * D + 64 * kb + 8 * c) = o; }
;         LDS_WAIT(); asm volatile("" ::: "memory");
	v_cvt_i32_f32_e32 v16, v16
	s_waitcnt lgkmcnt(10)
	v_cvt_i32_f32_e32 v42, v42
	v_cvt_i32_f32_e32 v14, v14
	v_cvt_i32_f32_sdwa v20, v20 dst_sel:WORD_1 dst_unused:UNUSED_PAD src0_sel:DWORD
	v_cvt_i32_f32_e32 v40, v40
	s_waitcnt lgkmcnt(9)
	v_cvt_i32_f32_sdwa v44, v44 dst_sel:WORD_1 dst_unused:UNUSED_PAD src0_sel:DWORD
	v_cvt_i32_f32_e32 v17, v17
	v_cvt_i32_f32_e32 v43, v43
	s_waitcnt lgkmcnt(6)
	v_cvt_i32_f32_e32 v50, v50
	s_waitcnt lgkmcnt(2)
	v_cvt_i32_f32_e32 v58, v58
	v_cvt_i32_f32_e32 v51, v51
	v_cvt_i32_f32_e32 v59, v59
	v_cvt_i32_f32_sdwa v24, v24 dst_sel:BYTE_3 dst_unused:UNUSED_PAD src0_sel:DWORD
	v_cvt_i32_f32_sdwa v46, v46 dst_sel:BYTE_3 dst_unused:UNUSED_PAD src0_sel:DWORD
	v_cvt_i32_f32_e32 v15, v15
	v_cvt_i32_f32_sdwa v21, v21 dst_sel:WORD_1 dst_unused:UNUSED_PAD src0_sel:DWORD
	v_cvt_i32_f32_e32 v41, v41
	v_cvt_i32_f32_sdwa v45, v45 dst_sel:WORD_1 dst_unused:UNUSED_PAD src0_sel:DWORD
	v_cvt_i32_f32_e32 v48, v48
	v_cvt_i32_f32_sdwa v52, v52 dst_sel:WORD_1 dst_unused:UNUSED_PAD src0_sel:DWORD
	v_cvt_i32_f32_e32 v56, v56
	s_waitcnt lgkmcnt(1)
	v_cvt_i32_f32_sdwa v60, v60 dst_sel:WORD_1 dst_unused:UNUSED_PAD src0_sel:DWORD
	v_cvt_i32_f32_e32 v49, v49
	v_cvt_i32_f32_sdwa v53, v53 dst_sel:WORD_1 dst_unused:UNUSED_PAD src0_sel:DWORD
	v_cvt_i32_f32_e32 v57, v57
	v_cvt_i32_f32_sdwa v61, v61 dst_sel:WORD_1 dst_unused:UNUSED_PAD src0_sel:DWORD
	v_cvt_i32_f32_sdwa v25, v25 dst_sel:BYTE_3 dst_unused:UNUSED_PAD src0_sel:DWORD
	v_cvt_i32_f32_sdwa v47, v47 dst_sel:BYTE_3 dst_unused:UNUSED_PAD src0_sel:DWORD
	v_cvt_i32_f32_sdwa v54, v54 dst_sel:BYTE_3 dst_unused:UNUSED_PAD src0_sel:DWORD
	s_waitcnt lgkmcnt(0)
	v_cvt_i32_f32_sdwa v62, v62 dst_sel:BYTE_3 dst_unused:UNUSED_PAD src0_sel:DWORD
	v_cvt_i32_f32_sdwa v55, v55 dst_sel:BYTE_3 dst_unused:UNUSED_PAD src0_sel:DWORD
	v_cvt_i32_f32_sdwa v63, v63 dst_sel:BYTE_3 dst_unused:UNUSED_PAD src0_sel:DWORD
	v_lshlrev_b32_e32 v16, 8, v16
	v_lshlrev_b32_e32 v42, 8, v42
	v_and_b32_e32 v20, 0xff0000, v20
	v_and_b32_e32 v44, 0xff0000, v44
	v_lshlrev_b32_e32 v17, 8, v17
	v_lshlrev_b32_e32 v43, 8, v43
	v_lshlrev_b32_e32 v50, 8, v50
	v_lshlrev_b32_e32 v58, 8, v58
	v_lshlrev_b32_e32 v51, 8, v51
	v_lshlrev_b32_e32 v59, 8, v59
	v_perm_b32 v14, v16, v14, s28
	v_perm_b32 v16, v42, v40, s28
	v_and_b32_e32 v21, 0xff0000, v21
	v_and_b32_e32 v45, 0xff0000, v45
	v_and_b32_e32 v52, 0xff0000, v52
	v_and_b32_e32 v60, 0xff0000, v60
	v_and_b32_e32 v53, 0xff0000, v53
	v_and_b32_e32 v61, 0xff0000, v61
	v_perm_b32 v17, v17, v15, s28
	v_perm_b32 v40, v43, v41, s28
	v_perm_b32 v41, v50, v48, s28
	v_perm_b32 v42, v58, v56, s28
	v_perm_b32 v43, v51, v49, s28
	v_perm_b32 v48, v59, v57, s28
	v_or3_b32 v14, v14, v20, v24
	v_or3_b32 v15, v16, v44, v46
	v_or3_b32 v16, v17, v21, v25
	v_or3_b32 v17, v40, v45, v47
	v_or3_b32 v20, v41, v52, v54
	v_or3_b32 v21, v42, v60, v62
	v_or3_b32 v24, v43, v53, v55
	v_or3_b32 v25, v48, v61, v63
	global_store_dwordx2 v[18:19], v[14:15], off
	global_store_dwordx2 v[22:23], v[16:17], off
	global_store_dwordx2 v[82:83], v[20:21], off
	global_store_dwordx2 v[84:85], v[24:25], off
	s_waitcnt lgkmcnt(0)
	v_add_u32_e32 v87, 0x14a0, v31
	v_add_u32_e32 v88, 0x14a8, v31
	v_add_u32_e32 v89, 0x18c0, v31
	v_add_u32_e32 v90, 0x18c8, v31
	v_add_u32_e32 v91, 0x1ce0, v31
	v_add_u32_e32 v92, 0x1ce8, v31
	v_lshl_add_u64 v[18:19], v[6:7], 0, v[12:13]
	v_lshl_add_u64 v[22:23], v[6:7], 0, v[10:11]
	v_lshl_add_u64 v[82:83], v[6:7], 0, v[8:9]
	v_lshl_add_u64 v[84:85], v[6:7], 0, v[4:5]
	v_lshl_add_u64 v[6:7], v[6:7], 0, 64
	s_waitcnt vmcnt(24)
	v_pk_mul_f32 v[46:47], v[112:113], v[172:173] op_sel_hi:[1,0]
	v_pk_mul_f32 v[20:21], v[110:111], v[172:173] op_sel_hi:[1,0]
	v_pk_mul_f32 v[44:45], v[116:117], v[174:175] op_sel_hi:[1,0]
	v_pk_mul_f32 v[24:25], v[114:115], v[174:175] op_sel_hi:[1,0]
	v_pk_mul_f32 v[48:49], v[120:121], v[176:177] op_sel_hi:[1,0]
	v_pk_mul_f32 v[16:17], v[108:109], v[170:171] op_sel_hi:[1,0]
	v_pk_mul_f32 v[14:15], v[106:107], v[170:171] op_sel_hi:[1,0]
	v_pk_mul_f32 v[50:51], v[118:119], v[176:177] op_sel_hi:[1,0]
	v_pk_mul_f32 v[52:53], v[124:125], v[178:179] op_sel_hi:[1,0]
	v_pk_mul_f32 v[54:55], v[122:123], v[178:179] op_sel_hi:[1,0]
	v_pk_mul_f32 v[56:57], v[128:129], v[180:181] op_sel_hi:[1,0]
	v_pk_mul_f32 v[58:59], v[126:127], v[180:181] op_sel_hi:[1,0]
	v_pk_mul_f32 v[60:61], v[132:133], v[182:183] op_sel_hi:[1,0]
	v_pk_mul_f32 v[62:63], v[130:131], v[182:183] op_sel_hi:[1,0]
	v_pk_mul_f32 v[42:43], v[136:137], v[184:185] op_sel_hi:[1,0]
	v_pk_mul_f32 v[40:41], v[134:135], v[184:185] op_sel_hi:[1,0]
	s_add_u32 s4, s4, 0x18000
	s_addc_u32 s5, s5, 0
	global_load_dwordx4 v[106:109], v250, s[4:5] nt
	global_load_dword v170, v251, s[6:7] offset:3584
	s_add_u32 s4, s4, 0x18000
	s_addc_u32 s5, s5, 0
	global_load_dwordx4 v[110:113], v250, s[4:5] nt
	global_load_dword v172, v251, s[6:7] offset:3616
	s_add_u32 s4, s4, 0x18000
	s_addc_u32 s5, s5, 0
	global_load_dwordx4 v[114:117], v250, s[4:5] nt
	global_load_dword v174, v251, s[6:7] offset:3648
	s_add_u32 s4, s4, 0x18000
	s_addc_u32 s5, s5, 0
	global_load_dwordx4 v[118:121], v250, s[4:5] nt
	global_load_dword v176, v251, s[6:7] offset:3680
	s_add_u32 s4, s4, 0x18000
	s_addc_u32 s5, s5, 0
	global_load_dwordx4 v[122:125], v250, s[4:5] nt
	global_load_dword v178, v251, s[6:7] offset:3712
	s_add_u32 s4, s4, 0x18000
	s_addc_u32 s5, s5, 0
	global_load_dwordx4 v[126:129], v250, s[4:5] nt
	global_load_dword v180, v251, s[6:7] offset:3744
	s_add_u32 s4, s4, 0x18000
	s_addc_u32 s5, s5, 0
	global_load_dwordx4 v[130:133], v250, s[4:5] nt
	global_load_dword v182, v251, s[6:7] offset:3776
	s_add_u32 s4, s4, 0x18000
	s_addc_u32 s5, s5, 0
	global_load_dwordx4 v[134:137], v250, s[4:5] nt
; #define LAS __attribute__((address_space(3)))
; #define GAS __attribute__((address_space(1)))
; #define LDS_WAIT() asm volatile("s_waitcnt lgkmcnt(0)" ::: "memory")
;     ...
;         for (int i = 0; i < 8; ++i) { const int kk = 8 * i + kr; const int k = 64 * kb + kk; const f32x4 v = __builtin_nontemporal_load((const f32x4*)(W + (size_t)k * pitch)) * g[k];
;             LAS float* p = scr + kk * 33 + 4 * (lane & 7); p[0] = __builtin_rintf(v[0] * inv[0]); p[1] = __builtin_rintf(v[1] * inv[1]); p[2] = __builtin_rintf(v[2] * inv[2]); p[3] = __builtin_rintf(v[3] * inv[3]); }
;         LDS_WAIT(); asm volatile("" ::: "memory");
;         const int c = lane & 7;
; #pragma unroll
;         for (int j = 0; j < 4; ++j) { const int n = (lane >> 3) + 8 * j; const LAS float* sp = scr + (8 * c) * 33 + n;
;             u32x2 o;
;             o.x = ((unsigned)(int)sp[0 * 33] & 0xFFu) | (((unsigned)(int)sp[1 * 33] & 0xFFu) << 8) | (((unsigned)(int)sp[2 * 33] & 0xFFu) << 16) | (((unsigned)(int)sp[3 * 33] & 0xFFu) << 24);
;             o.y = ((unsigned)(int)sp[4 * 33] & 0xFFu) | (((unsigned)(int)sp[5 * 33] & 0xFFu) << 8) | (((unsigned)(int)sp[6 * 33] & 0xFFu) << 16) | (((unsigned)(int)sp[7 * 33] & 0xFFu) << 24);
;             *(GAS u32x2*)(dst + (size_t)(n0 + n) * D + 64 * kb + 8 * c) = o; }
;         LDS_WAIT(); asm volatile("" ::: "memory");
	global_load_dword v184, v251, s[6:7] offset:3808
	v_mul_f32_e32 v14, v26, v14
	v_mul_f32_e32 v15, v27, v15
	v_mul_f32_e32 v16, v28, v16
	v_mul_f32_e32 v17, v29, v17
	v_mul_f32_e32 v20, v26, v20
	v_mul_f32_e32 v21, v27, v21
	v_mul_f32_e32 v46, v28, v46
	v_mul_f32_e32 v47, v29, v47
	v_mul_f32_e32 v24, v26, v24
	v_mul_f32_e32 v25, v27, v25
	v_mul_f32_e32 v44, v28, v44
	v_mul_f32_e32 v45, v29, v45
	v_mul_f32_e32 v50, v26, v50
	v_mul_f32_e32 v51, v27, v51
	v_mul_f32_e32 v48, v28, v48
	v_mul_f32_e32 v49, v29, v49
	v_mul_f32_e32 v54, v26, v54
	v_mul_f32_e32 v55, v27, v55
	v_mul_f32_e32 v52, v28, v52
	v_mul_f32_e32 v53, v29, v53
	v_mul_f32_e32 v58, v26, v58
	v_mul_f32_e32 v59, v27, v59
	v_mul_f32_e32 v56, v28, v56
	v_mul_f32_e32 v57, v29, v57
	v_mul_f32_e32 v62, v26, v62
	v_mul_f32_e32 v63, v27, v63
	v_mul_f32_e32 v60, v28, v60
	v_mul_f32_e32 v61, v29, v61
	v_mul_f32_e32 v40, v26, v40
	v_mul_f32_e32 v41, v27, v41
	v_mul_f32_e32 v42, v28, v42
	v_mul_f32_e32 v43, v29, v43
	v_rndne_f32_e32 v14, v14
	v_rndne_f32_e32 v15, v15
	v_rndne_f32_e32 v16, v16
	v_rndne_f32_e32 v17, v17
	v_rndne_f32_e32 v20, v20
	v_rndne_f32_e32 v21, v21
	v_rndne_f32_e32 v46, v46
	v_rndne_f32_e32 v47, v47
	v_rndne_f32_e32 v24, v24
	v_rndne_f32_e32 v25, v25
	v_rndne_f32_e32 v44, v44
	v_rndne_f32_e32 v45, v45
	v_rndne_f32_e32 v50, v50
	v_rndne_f32_e32 v51, v51
	v_rndne_f32_e32 v48, v48
	v_rndne_f32_e32 v49, v49
	v_rndne_f32_e32 v54, v54
	v_rndne_f32_e32 v55, v55
	v_rndne_f32_e32 v52, v52
	v_rndne_f32_e32 v53, v53
	v_rndne_f32_e32 v58, v58
	v_rndne_f32_e32 v59, v59
	v_rndne_f32_e32 v56, v56
	v_rndne_f32_e32 v57, v57
	v_rndne_f32_e32 v62, v62
	v_rndne_f32_e32 v63, v63
	v_rndne_f32_e32 v60, v60
	v_rndne_f32_e32 v61, v61
	v_rndne_f32_e32 v40, v40
	v_rndne_f32_e32 v41, v41
	v_rndne_f32_e32 v42, v42
	v_rndne_f32_e32 v43, v43
	ds_write2_b32 v31, v14, v15 offset1:1
	ds_write2_b32 v31, v16, v17 offset0:2 offset1:3
	ds_write2_b32 v32, v20, v21 offset1:1
	ds_write2_b32 v33, v46, v47 offset1:1
	ds_write2_b32 v34, v24, v25 offset1:1
	ds_write2_b32 v35, v44, v45 offset1:1
	ds_write2_b32 v36, v50, v51 offset1:1
	ds_write2_b32 v37, v48, v49 offset1:1
	ds_write2_b32 v38, v54, v55 offset1:1
	ds_write2_b32 v39, v52, v53 offset1:1
	ds_write2_b32 v87, v58, v59 offset1:1
	ds_write2_b32 v88, v56, v57 offset1:1
	ds_write2_b32 v89, v62, v63 offset1:1
	ds_write2_b32 v90, v60, v61 offset1:1
	ds_write2_b32 v91, v40, v41 offset1:1
	ds_write2_b32 v92, v42, v43 offset1:1
	s_waitcnt lgkmcnt(0)
	ds_read2_b32 v[14:15], v30 offset1:8
	ds_read2_b32 v[16:17], v30 offset0:33 offset1:41
	ds_read2_b32 v[20:21], v30 offset0:66 offset1:74
	ds_read2_b32 v[24:25], v30 offset0:99 offset1:107
	ds_read2_b32 v[40:41], v30 offset0:132 offset1:140
	ds_read2_b32 v[42:43], v30 offset0:165 offset1:173
	ds_read2_b32 v[44:45], v30 offset0:198 offset1:206
	ds_read2_b32 v[46:47], v30 offset0:231 offset1:239
	ds_read2_b32 v[48:49], v30 offset0:16 offset1:24
	ds_read2_b32 v[50:51], v30 offset0:49 offset1:57
	ds_read2_b32 v[52:53], v30 offset0:82 offset1:90
	ds_read2_b32 v[54:55], v30 offset0:115 offset1:123
	ds_read2_b32 v[56:57], v30 offset0:148 offset1:156
	ds_read2_b32 v[58:59], v30 offset0:181 offset1:189
	ds_read2_b32 v[60:61], v30 offset0:214 offset1:222
	ds_read2_b32 v[62:63], v30 offset0:247 offset1:255
	s_waitcnt lgkmcnt(14)
	v_cvt_i32_f32_e32 v16, v16
	s_waitcnt lgkmcnt(10)
	v_cvt_i32_f32_e32 v42, v42
	v_cvt_i32_f32_e32 v14, v14
	v_cvt_i32_f32_sdwa v20, v20 dst_sel:WORD_1 dst_unused:UNUSED_PAD src0_sel:DWORD
	v_cvt_i32_f32_e32 v40, v40
	s_waitcnt lgkmcnt(9)
	v_cvt_i32_f32_sdwa v44, v44 dst_sel:WORD_1 dst_unused:UNUSED_PAD src0_sel:DWORD
	v_cvt_i32_f32_e32 v17, v17
	v_cvt_i32_f32_e32 v43, v43
	s_waitcnt lgkmcnt(6)
	v_cvt_i32_f32_e32 v50, v50
	s_waitcnt lgkmcnt(2)
	v_cvt_i32_f32_e32 v58, v58
	v_cvt_i32_f32_e32 v51, v51
	v_cvt_i32_f32_e32 v59, v59
	v_cvt_i32_f32_sdwa v24, v24 dst_sel:BYTE_3 dst_unused:UNUSED_PAD src0_sel:DWORD
	v_cvt_i32_f32_sdwa v46, v46 dst_sel:BYTE_3 dst_unused:UNUSED_PAD src0_sel:DWORD
	v_cvt_i32_f32_e32 v15, v15
	v_cvt_i32_f32_sdwa v21, v21 dst_sel:WORD_1 dst_unused:UNUSED_PAD src0_sel:DWORD
	v_cvt_i32_f32_e32 v41, v41
	v_cvt_i32_f32_sdwa v45, v45 dst_sel:WORD_1 dst_unused:UNUSED_PAD src0_sel:DWORD
	v_cvt_i32_f32_e32 v48, v48
	v_cvt_i32_f32_sdwa v52, v52 dst_sel:WORD_1 dst_unused:UNUSED_PAD src0_sel:DWORD
	v_cvt_i32_f32_e32 v56, v56
	s_waitcnt lgkmcnt(1)
	v_cvt_i32_f32_sdwa v60, v60 dst_sel:WORD_1 dst_unused:UNUSED_PAD src0_sel:DWORD
	v_cvt_i32_f32_e32 v49, v49
	v_cvt_i32_f32_sdwa v53, v53 dst_sel:WORD_1 dst_unused:UNUSED_PAD src0_sel:DWORD
	v_cvt_i32_f32_e32 v57, v57
	v_cvt_i32_f32_sdwa v61, v61 dst_sel:WORD_1 dst_unused:UNUSED_PAD src0_sel:DWORD
	v_cvt_i32_f32_sdwa v25, v25 dst_sel:BYTE_3 dst_unused:UNUSED_PAD src0_sel:DWORD
	v_cvt_i32_f32_sdwa v47, v47 dst_sel:BYTE_3 dst_unused:UNUSED_PAD src0_sel:DWORD
	v_cvt_i32_f32_sdwa v54, v54 dst_sel:BYTE_3 dst_unused:UNUSED_PAD src0_sel:DWORD
	s_waitcnt lgkmcnt(0)
; #define LAS __attribute__((address_space(3)))
; #define GAS __attribute__((address_space(1)))
; #define LDS_WAIT() asm volatile("s_waitcnt lgkmcnt(0)" ::: "memory")
;     ...
;     for (int kb = 0; kb < D / 64; ++kb) {
; #pragma unroll
;         for (int i = 0; i < 8; ++i) { const int kk = 8 * i + kr; const int k = 64 * kb + kk; const f32x4 v = __builtin_nontemporal_load((const f32x4*)(W + (size_t)k * pitch)) * g[k];
;             LAS float* p = scr + kk * 33 + 4 * (lane & 7); p[0] = __builtin_rintf(v[0] * inv[0]); p[1] = __builtin_rintf(v[1] * inv[1]); p[2] = __builtin_rintf(v[2] * inv[2]); p[3] = __builtin_rintf(v[3] * inv[3]); }
;         LDS_WAIT(); asm volatile("" ::: "memory");
;         const int c = lane & 7;
; #pragma unroll
;         for (int j = 0; j < 4; ++j) { const int n = (lane >> 3) + 8 * j; const LAS float* sp = scr + (8 * c) * 33 + n;
;             u32x2 o;
;             o.x = ((unsigned)(int)sp[0 * 33] & 0xFFu) | (((unsigned)(int)sp[1 * 33] & 0xFFu) << 8) | (((unsigned)(int)sp[2 * 33] & 0xFFu) << 16) | (((unsigned)(int)sp[3 * 33] & 0xFFu) << 24);
;             o.y = ((unsigned)(int)sp[4 * 33] & 0xFFu) | (((unsigned)(int)sp[5 * 33] & 0xFFu) << 8) | (((unsigned)(int)sp[6 * 33] & 0xFFu) << 16) | (((unsigned)(int)sp[7 * 33] & 0xFFu) << 24);
;             *(GAS u32x2*)(dst + (size_t)(n0 + n) * D + 64 * kb + 8 * c) = o; }
;         LDS_WAIT(); asm volatile("" ::: "memory");
	v_cvt_i32_f32_sdwa v62, v62 dst_sel:BYTE_3 dst_unused:UNUSED_PAD src0_sel:DWORD
	v_cvt_i32_f32_sdwa v55, v55 dst_sel:BYTE_3 dst_unused:UNUSED_PAD src0_sel:DWORD
	v_cvt_i32_f32_sdwa v63, v63 dst_sel:BYTE_3 dst_unused:UNUSED_PAD src0_sel:DWORD
	v_lshlrev_b32_e32 v16, 8, v16
	v_lshlrev_b32_e32 v42, 8, v42
	v_and_b32_e32 v20, 0xff0000, v20
	v_and_b32_e32 v44, 0xff0000, v44
	v_lshlrev_b32_e32 v17, 8, v17
	v_lshlrev_b32_e32 v43, 8, v43
	v_lshlrev_b32_e32 v50, 8, v50
	v_lshlrev_b32_e32 v58, 8, v58
	v_lshlrev_b32_e32 v51, 8, v51
	v_lshlrev_b32_e32 v59, 8, v59
	v_perm_b32 v14, v16, v14, s28
	v_perm_b32 v16, v42, v40, s28
	v_and_b32_e32 v21, 0xff0000, v21
	v_and_b32_e32 v45, 0xff0000, v45
	v_and_b32_e32 v52, 0xff0000, v52
	v_and_b32_e32 v60, 0xff0000, v60
	v_and_b32_e32 v53, 0xff0000, v53
	v_and_b32_e32 v61, 0xff0000, v61
	v_perm_b32 v17, v17, v15, s28
	v_perm_b32 v40, v43, v41, s28
	v_perm_b32 v41, v50, v48, s28
	v_perm_b32 v42, v58, v56, s28
	v_perm_b32 v43, v51, v49, s28
	v_perm_b32 v48, v59, v57, s28
	v_or3_b32 v14, v14, v20, v24
	v_or3_b32 v15, v16, v44, v46
	v_or3_b32 v16, v17, v21, v25
	v_or3_b32 v17, v40, v45, v47
	v_or3_b32 v20, v41, v52, v54
	v_or3_b32 v21, v42, v60, v62
	v_or3_b32 v24, v43, v53, v55
	v_or3_b32 v25, v48, v61, v63
	global_store_dwordx2 v[18:19], v[14:15], off
	global_store_dwordx2 v[22:23], v[16:17], off
	global_store_dwordx2 v[82:83], v[20:21], off
	global_store_dwordx2 v[84:85], v[24:25], off
	s_waitcnt lgkmcnt(0)
	v_add_u32_e32 v87, 0x14a0, v31
	v_add_u32_e32 v88, 0x14a8, v31
	v_add_u32_e32 v89, 0x18c0, v31
	v_add_u32_e32 v90, 0x18c8, v31
	v_add_u32_e32 v91, 0x1ce0, v31
	v_add_u32_e32 v92, 0x1ce8, v31
	v_lshl_add_u64 v[18:19], v[6:7], 0, v[12:13]
	v_lshl_add_u64 v[22:23], v[6:7], 0, v[10:11]
	v_lshl_add_u64 v[82:83], v[6:7], 0, v[8:9]
	v_lshl_add_u64 v[84:85], v[6:7], 0, v[4:5]
	v_lshl_add_u64 v[6:7], v[6:7], 0, 64
	s_waitcnt vmcnt(24)
	v_pk_mul_f32 v[46:47], v[144:145], v[188:189] op_sel_hi:[1,0]
	v_pk_mul_f32 v[20:21], v[142:143], v[188:189] op_sel_hi:[1,0]
	v_pk_mul_f32 v[44:45], v[148:149], v[190:191] op_sel_hi:[1,0]
	v_pk_mul_f32 v[24:25], v[146:147], v[190:191] op_sel_hi:[1,0]
	v_pk_mul_f32 v[48:49], v[152:153], v[192:193] op_sel_hi:[1,0]
	v_pk_mul_f32 v[16:17], v[140:141], v[186:187] op_sel_hi:[1,0]
	v_pk_mul_f32 v[14:15], v[138:139], v[186:187] op_sel_hi:[1,0]
	v_pk_mul_f32 v[50:51], v[150:151], v[192:193] op_sel_hi:[1,0]
	v_pk_mul_f32 v[52:53], v[156:157], v[194:195] op_sel_hi:[1,0]
	v_pk_mul_f32 v[54:55], v[154:155], v[194:195] op_sel_hi:[1,0]
	v_pk_mul_f32 v[56:57], v[160:161], v[196:197] op_sel_hi:[1,0]
	v_pk_mul_f32 v[58:59], v[158:159], v[196:197] op_sel_hi:[1,0]
	v_pk_mul_f32 v[60:61], v[164:165], v[198:199] op_sel_hi:[1,0]
	v_pk_mul_f32 v[62:63], v[162:163], v[198:199] op_sel_hi:[1,0]
	v_pk_mul_f32 v[42:43], v[168:169], v[200:201] op_sel_hi:[1,0]
	v_pk_mul_f32 v[40:41], v[166:167], v[200:201] op_sel_hi:[1,0]
	s_add_u32 s4, s4, 0x18000
	s_addc_u32 s5, s5, 0
	global_load_dwordx4 v[138:141], v250, s[4:5] nt
	global_load_dword v186, v251, s[6:7] offset:3840
	s_add_u32 s4, s4, 0x18000
	s_addc_u32 s5, s5, 0
	global_load_dwordx4 v[142:145], v250, s[4:5] nt
	global_load_dword v188, v251, s[6:7] offset:3872
	s_add_u32 s4, s4, 0x18000
	s_addc_u32 s5, s5, 0
	global_load_dwordx4 v[146:149], v250, s[4:5] nt
	global_load_dword v190, v251, s[6:7] offset:3904
	s_add_u32 s4, s4, 0x18000
	s_addc_u32 s5, s5, 0
	global_load_dwordx4 v[150:153], v250, s[4:5] nt
	global_load_dword v192, v251, s[6:7] offset:3936
	s_add_u32 s4, s4, 0x18000
	s_addc_u32 s5, s5, 0
	global_load_dwordx4 v[154:157], v250, s[4:5] nt
	global_load_dword v194, v251, s[6:7] offset:3968
	s_add_u32 s4, s4, 0x18000
	s_addc_u32 s5, s5, 0
	global_load_dwordx4 v[158:161], v250, s[4:5] nt
	global_load_dword v196, v251, s[6:7] offset:4000
	s_add_u32 s4, s4, 0x18000
	s_addc_u32 s5, s5, 0
	global_load_dwordx4 v[162:165], v250, s[4:5] nt
	global_load_dword v198, v251, s[6:7] offset:4032
	s_add_u32 s4, s4, 0x18000
	s_addc_u32 s5, s5, 0
	global_load_dwordx4 v[166:169], v250, s[4:5] nt
	global_load_dword v200, v251, s[6:7] offset:4064
	v_mul_f32_e32 v14, v26, v14
	v_mul_f32_e32 v15, v27, v15
	v_mul_f32_e32 v16, v28, v16
	v_mul_f32_e32 v17, v29, v17
	v_mul_f32_e32 v20, v26, v20
	v_mul_f32_e32 v21, v27, v21
	v_mul_f32_e32 v46, v28, v46
	v_mul_f32_e32 v47, v29, v47
	v_mul_f32_e32 v24, v26, v24
	v_mul_f32_e32 v25, v27, v25
	v_mul_f32_e32 v44, v28, v44
	v_mul_f32_e32 v45, v29, v45
	v_mul_f32_e32 v50, v26, v50
	v_mul_f32_e32 v51, v27, v51
	v_mul_f32_e32 v48, v28, v48
	v_mul_f32_e32 v49, v29, v49
	v_mul_f32_e32 v54, v26, v54
	v_mul_f32_e32 v55, v27, v55
	v_mul_f32_e32 v52, v28, v52
	v_mul_f32_e32 v53, v29, v53
	v_mul_f32_e32 v58, v26, v58
	v_mul_f32_e32 v59, v27, v59
	v_mul_f32_e32 v56, v28, v56
	v_mul_f32_e32 v57, v29, v57
	v_mul_f32_e32 v62, v26, v62
	v_mul_f32_e32 v63, v27, v63
	v_mul_f32_e32 v60, v28, v60
	v_mul_f32_e32 v61, v29, v61
	v_mul_f32_e32 v40, v26, v40
	v_mul_f32_e32 v41, v27, v41
	v_mul_f32_e32 v42, v28, v42
	v_mul_f32_e32 v43, v29, v43
	v_rndne_f32_e32 v14, v14
	v_rndne_f32_e32 v15, v15
	v_rndne_f32_e32 v16, v16
	v_rndne_f32_e32 v17, v17
	v_rndne_f32_e32 v20, v20
	v_rndne_f32_e32 v21, v21
	v_rndne_f32_e32 v46, v46
	v_rndne_f32_e32 v47, v47
	v_rndne_f32_e32 v24, v24
	v_rndne_f32_e32 v25, v25
	v_rndne_f32_e32 v44, v44
	v_rndne_f32_e32 v45, v45
	v_rndne_f32_e32 v50, v50
	v_rndne_f32_e32 v51, v51
	v_rndne_f32_e32 v48, v48
	v_rndne_f32_e32 v49, v49
	v_rndne_f32_e32 v54, v54
	v_rndne_f32_e32 v55, v55
	v_rndne_f32_e32 v52, v52
	v_rndne_f32_e32 v53, v53
	v_rndne_f32_e32 v58, v58
	v_rndne_f32_e32 v59, v59
	v_rndne_f32_e32 v56, v56
	v_rndne_f32_e32 v57, v57
	v_rndne_f32_e32 v62, v62
	v_rndne_f32_e32 v63, v63
	v_rndne_f32_e32 v60, v60
	v_rndne_f32_e32 v61, v61
	v_rndne_f32_e32 v40, v40
	v_rndne_f32_e32 v41, v41
	v_rndne_f32_e32 v42, v42
	v_rndne_f32_e32 v43, v43
	ds_write2_b32 v31, v14, v15 offset1:1
	ds_write2_b32 v31, v16, v17 offset0:2 offset1:3
	ds_write2_b32 v32, v20, v21 offset1:1
	ds_write2_b32 v33, v46, v47 offset1:1
	ds_write2_b32 v34, v24, v25 offset1:1
	ds_write2_b32 v35, v44, v45 offset1:1
	ds_write2_b32 v36, v50, v51 offset1:1
	ds_write2_b32 v37, v48, v49 offset1:1
	ds_write2_b32 v38, v54, v55 offset1:1
	ds_write2_b32 v39, v52, v53 offset1:1
	ds_write2_b32 v87, v58, v59 offset1:1
	ds_write2_b32 v88, v56, v57 offset1:1
	ds_write2_b32 v89, v62, v63 offset1:1
	ds_write2_b32 v90, v60, v61 offset1:1
	ds_write2_b32 v91, v40, v41 offset1:1
	ds_write2_b32 v92, v42, v43 offset1:1
	s_waitcnt lgkmcnt(0)
; #define LAS __attribute__((address_space(3)))
; #define GAS __attribute__((address_space(1)))
; #define LDS_WAIT() asm volatile("s_waitcnt lgkmcnt(0)" ::: "memory")
;     ...
;         LDS_WAIT(); asm volatile("" ::: "memory");
;         const int c = lane & 7;
; #pragma unroll
;         for (int j = 0; j < 4; ++j) { const int n = (lane >> 3) + 8 * j; const LAS float* sp = scr + (8 * c) * 33 + n;
;             u32x2 o;
;             o.x = ((unsigned)(int)sp[0 * 33] & 0xFFu) | (((unsigned)(int)sp[1 * 33] & 0xFFu) << 8) | (((unsigned)(int)sp[2 * 33] & 0xFFu) << 16) | (((unsigned)(int)sp[3 * 33] & 0xFFu) << 24);
;             o.y = ((unsigned)(int)sp[4 * 33] & 0xFFu) | (((unsigned)(int)sp[5 * 33] & 0xFFu) << 8) | (((unsigned)(int)sp[6 * 33] & 0xFFu) << 16) | (((unsigned)(int)sp[7 * 33] & 0xFFu) << 24);
;             *(GAS u32x2*)(dst + (size_t)(n0 + n) * D + 64 * kb + 8 * c) = o; }
;         LDS_WAIT(); asm volatile("" ::: "memory");
	ds_read2_b32 v[14:15], v30 offset1:8
	ds_read2_b32 v[16:17], v30 offset0:33 offset1:41
	ds_read2_b32 v[20:21], v30 offset0:66 offset1:74
	ds_read2_b32 v[24:25], v30 offset0:99 offset1:107
	ds_read2_b32 v[40:41], v30 offset0:132 offset1:140
	ds_read2_b32 v[42:43], v30 offset0:165 offset1:173
	ds_read2_b32 v[44:45], v30 offset0:198 offset1:206
	ds_read2_b32 v[46:47], v30 offset0:231 offset1:239
	ds_read2_b32 v[48:49], v30 offset0:16 offset1:24
	ds_read2_b32 v[50:51], v30 offset0:49 offset1:57
	ds_read2_b32 v[52:53], v30 offset0:82 offset1:90
	ds_read2_b32 v[54:55], v30 offset0:115 offset1:123
	ds_read2_b32 v[56:57], v30 offset0:148 offset1:156
	ds_read2_b32 v[58:59], v30 offset0:181 offset1:189
	ds_read2_b32 v[60:61], v30 offset0:214 offset1:222
	ds_read2_b32 v[62:63], v30 offset0:247 offset1:255
	s_waitcnt lgkmcnt(14)
	v_cvt_i32_f32_e32 v16, v16
	s_waitcnt lgkmcnt(10)
	v_cvt_i32_f32_e32 v42, v42
	v_cvt_i32_f32_e32 v14, v14
	v_cvt_i32_f32_sdwa v20, v20 dst_sel:WORD_1 dst_unused:UNUSED_PAD src0_sel:DWORD
	v_cvt_i32_f32_e32 v40, v40
	s_waitcnt lgkmcnt(9)
	v_cvt_i32_f32_sdwa v44, v44 dst_sel:WORD_1 dst_unused:UNUSED_PAD src0_sel:DWORD
	v_cvt_i32_f32_e32 v17, v17
	v_cvt_i32_f32_e32 v43, v43
	s_waitcnt lgkmcnt(6)
	v_cvt_i32_f32_e32 v50, v50
	s_waitcnt lgkmcnt(2)
	v_cvt_i32_f32_e32 v58, v58
	v_cvt_i32_f32_e32 v51, v51
	v_cvt_i32_f32_e32 v59, v59
	v_cvt_i32_f32_sdwa v24, v24 dst_sel:BYTE_3 dst_unused:UNUSED_PAD src0_sel:DWORD
	v_cvt_i32_f32_sdwa v46, v46 dst_sel:BYTE_3 dst_unused:UNUSED_PAD src0_sel:DWORD
	v_cvt_i32_f32_e32 v15, v15
	v_cvt_i32_f32_sdwa v21, v21 dst_sel:WORD_1 dst_unused:UNUSED_PAD src0_sel:DWORD
	v_cvt_i32_f32_e32 v41, v41
	v_cvt_i32_f32_sdwa v45, v45 dst_sel:WORD_1 dst_unused:UNUSED_PAD src0_sel:DWORD
	v_cvt_i32_f32_e32 v48, v48
	v_cvt_i32_f32_sdwa v52, v52 dst_sel:WORD_1 dst_unused:UNUSED_PAD src0_sel:DWORD
	v_cvt_i32_f32_e32 v56, v56
	s_waitcnt lgkmcnt(1)
	v_cvt_i32_f32_sdwa v60, v60 dst_sel:WORD_1 dst_unused:UNUSED_PAD src0_sel:DWORD
	v_cvt_i32_f32_e32 v49, v49
	v_cvt_i32_f32_sdwa v53, v53 dst_sel:WORD_1 dst_unused:UNUSED_PAD src0_sel:DWORD
	v_cvt_i32_f32_e32 v57, v57
	v_cvt_i32_f32_sdwa v61, v61 dst_sel:WORD_1 dst_unused:UNUSED_PAD src0_sel:DWORD
	v_cvt_i32_f32_sdwa v25, v25 dst_sel:BYTE_3 dst_unused:UNUSED_PAD src0_sel:DWORD
	v_cvt_i32_f32_sdwa v47, v47 dst_sel:BYTE_3 dst_unused:UNUSED_PAD src0_sel:DWORD
	v_cvt_i32_f32_sdwa v54, v54 dst_sel:BYTE_3 dst_unused:UNUSED_PAD src0_sel:DWORD
	s_waitcnt lgkmcnt(0)
	v_cvt_i32_f32_sdwa v62, v62 dst_sel:BYTE_3 dst_unused:UNUSED_PAD src0_sel:DWORD
	v_cvt_i32_f32_sdwa v55, v55 dst_sel:BYTE_3 dst_unused:UNUSED_PAD src0_sel:DWORD
	v_cvt_i32_f32_sdwa v63, v63 dst_sel:BYTE_3 dst_unused:UNUSED_PAD src0_sel:DWORD
	v_lshlrev_b32_e32 v16, 8, v16
	v_lshlrev_b32_e32 v42, 8, v42
	v_and_b32_e32 v20, 0xff0000, v20
	v_and_b32_e32 v44, 0xff0000, v44
	v_lshlrev_b32_e32 v17, 8, v17
	v_lshlrev_b32_e32 v43, 8, v43
	v_lshlrev_b32_e32 v50, 8, v50
	v_lshlrev_b32_e32 v58, 8, v58
	v_lshlrev_b32_e32 v51, 8, v51
	v_lshlrev_b32_e32 v59, 8, v59
	v_perm_b32 v14, v16, v14, s28
	v_perm_b32 v16, v42, v40, s28
	v_and_b32_e32 v21, 0xff0000, v21
	v_and_b32_e32 v45, 0xff0000, v45
	v_and_b32_e32 v52, 0xff0000, v52
	v_and_b32_e32 v60, 0xff0000, v60
	v_and_b32_e32 v53, 0xff0000, v53
	v_and_b32_e32 v61, 0xff0000, v61
	v_perm_b32 v17, v17, v15, s28
	v_perm_b32 v40, v43, v41, s28
	v_perm_b32 v41, v50, v48, s28
	v_perm_b32 v42, v58, v56, s28
	v_perm_b32 v43, v51, v49, s28
	v_perm_b32 v48, v59, v57, s28
	v_or3_b32 v14, v14, v20, v24
	v_or3_b32 v15, v16, v44, v46
	v_or3_b32 v16, v17, v21, v25
	v_or3_b32 v17, v40, v45, v47
	v_or3_b32 v20, v41, v52, v54
	v_or3_b32 v21, v42, v60, v62
	v_or3_b32 v24, v43, v53, v55
	v_or3_b32 v25, v48, v61, v63
	global_store_dwordx2 v[18:19], v[14:15], off
	global_store_dwordx2 v[22:23], v[16:17], off
	global_store_dwordx2 v[82:83], v[20:21], off
	global_store_dwordx2 v[84:85], v[24:25], off
	s_waitcnt lgkmcnt(0)
	v_add_u32_e32 v87, 0x14a0, v31
	v_add_u32_e32 v88, 0x14a8, v31
	v_add_u32_e32 v89, 0x18c0, v31
	v_add_u32_e32 v90, 0x18c8, v31
	v_add_u32_e32 v91, 0x1ce0, v31
	v_add_u32_e32 v92, 0x1ce8, v31
	v_lshl_add_u64 v[18:19], v[6:7], 0, v[12:13]
	v_lshl_add_u64 v[22:23], v[6:7], 0, v[10:11]
	v_lshl_add_u64 v[82:83], v[6:7], 0, v[8:9]
	v_lshl_add_u64 v[84:85], v[6:7], 0, v[4:5]
	v_lshl_add_u64 v[6:7], v[6:7], 0, 64
	s_waitcnt vmcnt(24)
; #define LAS __attribute__((address_space(3)))
; #define GAS __attribute__((address_space(1)))
; #define LDS_WAIT() asm volatile("s_waitcnt lgkmcnt(0)" ::: "memory")
;     ...
;         for (int i = 0; i < 8; ++i) { const int kk = 8 * i + kr; const int k = 64 * kb + kk; const f32x4 v = __builtin_nontemporal_load((const f32x4*)(W + (size_t)k * pitch)) * g[k];
;             LAS float* p = scr + kk * 33 + 4 * (lane & 7); p[0] = __builtin_rintf(v[0] * inv[0]); p[1] = __builtin_rintf(v[1] * inv[1]); p[2] = __builtin_rintf(v[2] * inv[2]); p[3] = __builtin_rintf(v[3] * inv[3]); }
;         LDS_WAIT(); asm volatile("" ::: "memory");
;         const int c = lane & 7;
; #pragma unroll
;         for (int j = 0; j < 4; ++j) { const int n = (lane >> 3) + 8 * j; const LAS float* sp = scr + (8 * c) * 33 + n;
;             u32x2 o;
;             o.x = ((unsigned)(int)sp[0 * 33] & 0xFFu) | (((unsigned)(int)sp[1 * 33] & 0xFFu) << 8) | (((unsigned)(int)sp[2 * 33] & 0xFFu) << 16) | (((unsigned)(int)sp[3 * 33] & 0xFFu) << 24);
;             o.y = ((unsigned)(int)sp[4 * 33] & 0xFFu) | (((unsigned)(int)sp[5 * 33] & 0xFFu) << 8) | (((unsigned)(int)sp[6 * 33] & 0xFFu) << 16) | (((unsigned)(int)sp[7 * 33] & 0xFFu) << 24);
;             *(GAS u32x2*)(dst + (size_t)(n0 + n) * D + 64 * kb + 8 * c) = o; }
;         LDS_WAIT(); asm volatile("" ::: "memory");
	v_pk_mul_f32 v[46:47], v[112:113], v[172:173] op_sel_hi:[1,0]
	v_pk_mul_f32 v[20:21], v[110:111], v[172:173] op_sel_hi:[1,0]
	v_pk_mul_f32 v[44:45], v[116:117], v[174:175] op_sel_hi:[1,0]
	v_pk_mul_f32 v[24:25], v[114:115], v[174:175] op_sel_hi:[1,0]
	v_pk_mul_f32 v[48:49], v[120:121], v[176:177] op_sel_hi:[1,0]
	v_pk_mul_f32 v[16:17], v[108:109], v[170:171] op_sel_hi:[1,0]
	v_pk_mul_f32 v[14:15], v[106:107], v[170:171] op_sel_hi:[1,0]
	v_pk_mul_f32 v[50:51], v[118:119], v[176:177] op_sel_hi:[1,0]
	v_pk_mul_f32 v[52:53], v[124:125], v[178:179] op_sel_hi:[1,0]
	v_pk_mul_f32 v[54:55], v[122:123], v[178:179] op_sel_hi:[1,0]
	v_pk_mul_f32 v[56:57], v[128:129], v[180:181] op_sel_hi:[1,0]
	v_pk_mul_f32 v[58:59], v[126:127], v[180:181] op_sel_hi:[1,0]
	v_pk_mul_f32 v[60:61], v[132:133], v[182:183] op_sel_hi:[1,0]
	v_pk_mul_f32 v[62:63], v[130:131], v[182:183] op_sel_hi:[1,0]
	v_pk_mul_f32 v[42:43], v[136:137], v[184:185] op_sel_hi:[1,0]
	v_pk_mul_f32 v[40:41], v[134:135], v[184:185] op_sel_hi:[1,0]
	v_mul_f32_e32 v14, v26, v14
	v_mul_f32_e32 v15, v27, v15
	v_mul_f32_e32 v16, v28, v16
	v_mul_f32_e32 v17, v29, v17
	v_mul_f32_e32 v20, v26, v20
	v_mul_f32_e32 v21, v27, v21
	v_mul_f32_e32 v46, v28, v46
	v_mul_f32_e32 v47, v29, v47
	v_mul_f32_e32 v24, v26, v24
	v_mul_f32_e32 v25, v27, v25
	v_mul_f32_e32 v44, v28, v44
	v_mul_f32_e32 v45, v29, v45
	v_mul_f32_e32 v50, v26, v50
	v_mul_f32_e32 v51, v27, v51
	v_mul_f32_e32 v48, v28, v48
	v_mul_f32_e32 v49, v29, v49
	v_mul_f32_e32 v54, v26, v54
	v_mul_f32_e32 v55, v27, v55
	v_mul_f32_e32 v52, v28, v52
	v_mul_f32_e32 v53, v29, v53
	v_mul_f32_e32 v58, v26, v58
	v_mul_f32_e32 v59, v27, v59
	v_mul_f32_e32 v56, v28, v56
	v_mul_f32_e32 v57, v29, v57
	v_mul_f32_e32 v62, v26, v62
	v_mul_f32_e32 v63, v27, v63
	v_mul_f32_e32 v60, v28, v60
	v_mul_f32_e32 v61, v29, v61
	v_mul_f32_e32 v40, v26, v40
	v_mul_f32_e32 v41, v27, v41
	v_mul_f32_e32 v42, v28, v42
	v_mul_f32_e32 v43, v29, v43
	v_rndne_f32_e32 v14, v14
	v_rndne_f32_e32 v15, v15
	v_rndne_f32_e32 v16, v16
	v_rndne_f32_e32 v17, v17
	v_rndne_f32_e32 v20, v20
	v_rndne_f32_e32 v21, v21
	v_rndne_f32_e32 v46, v46
	v_rndne_f32_e32 v47, v47
	v_rndne_f32_e32 v24, v24
	v_rndne_f32_e32 v25, v25
	v_rndne_f32_e32 v44, v44
	v_rndne_f32_e32 v45, v45
	v_rndne_f32_e32 v50, v50
	v_rndne_f32_e32 v51, v51
	v_rndne_f32_e32 v48, v48
	v_rndne_f32_e32 v49, v49
	v_rndne_f32_e32 v54, v54
	v_rndne_f32_e32 v55, v55
	v_rndne_f32_e32 v52, v52
	v_rndne_f32_e32 v53, v53
	v_rndne_f32_e32 v58, v58
	v_rndne_f32_e32 v59, v59
	v_rndne_f32_e32 v56, v56
	v_rndne_f32_e32 v57, v57
	v_rndne_f32_e32 v62, v62
	v_rndne_f32_e32 v63, v63
	v_rndne_f32_e32 v60, v60
	v_rndne_f32_e32 v61, v61
	v_rndne_f32_e32 v40, v40
	v_rndne_f32_e32 v41, v41
	v_rndne_f32_e32 v42, v42
	v_rndne_f32_e32 v43, v43
	ds_write2_b32 v31, v14, v15 offset1:1
	ds_write2_b32 v31, v16, v17 offset0:2 offset1:3
	ds_write2_b32 v32, v20, v21 offset1:1
	ds_write2_b32 v33, v46, v47 offset1:1
	ds_write2_b32 v34, v24, v25 offset1:1
	ds_write2_b32 v35, v44, v45 offset1:1
	ds_write2_b32 v36, v50, v51 offset1:1
	ds_write2_b32 v37, v48, v49 offset1:1
	ds_write2_b32 v38, v54, v55 offset1:1
	ds_write2_b32 v39, v52, v53 offset1:1
	ds_write2_b32 v87, v58, v59 offset1:1
	ds_write2_b32 v88, v56, v57 offset1:1
	ds_write2_b32 v89, v62, v63 offset1:1
	ds_write2_b32 v90, v60, v61 offset1:1
	ds_write2_b32 v91, v40, v41 offset1:1
	ds_write2_b32 v92, v42, v43 offset1:1
	s_waitcnt lgkmcnt(0)
	ds_read2_b32 v[14:15], v30 offset1:8
	ds_read2_b32 v[16:17], v30 offset0:33 offset1:41
	ds_read2_b32 v[20:21], v30 offset0:66 offset1:74
	ds_read2_b32 v[24:25], v30 offset0:99 offset1:107
	ds_read2_b32 v[40:41], v30 offset0:132 offset1:140
	ds_read2_b32 v[42:43], v30 offset0:165 offset1:173
	ds_read2_b32 v[44:45], v30 offset0:198 offset1:206
	ds_read2_b32 v[46:47], v30 offset0:231 offset1:239
	ds_read2_b32 v[48:49], v30 offset0:16 offset1:24
	ds_read2_b32 v[50:51], v30 offset0:49 offset1:57
	ds_read2_b32 v[52:53], v30 offset0:82 offset1:90
	ds_read2_b32 v[54:55], v30 offset0:115 offset1:123
	ds_read2_b32 v[56:57], v30 offset0:148 offset1:156
	ds_read2_b32 v[58:59], v30 offset0:181 offset1:189
	ds_read2_b32 v[60:61], v30 offset0:214 offset1:222
	ds_read2_b32 v[62:63], v30 offset0:247 offset1:255
	s_waitcnt lgkmcnt(14)
	v_cvt_i32_f32_e32 v16, v16
	s_waitcnt lgkmcnt(10)
	v_cvt_i32_f32_e32 v42, v42
	v_cvt_i32_f32_e32 v14, v14
	v_cvt_i32_f32_sdwa v20, v20 dst_sel:WORD_1 dst_unused:UNUSED_PAD src0_sel:DWORD
	v_cvt_i32_f32_e32 v40, v40
	s_waitcnt lgkmcnt(9)
	v_cvt_i32_f32_sdwa v44, v44 dst_sel:WORD_1 dst_unused:UNUSED_PAD src0_sel:DWORD
	v_cvt_i32_f32_e32 v17, v17
	v_cvt_i32_f32_e32 v43, v43
	s_waitcnt lgkmcnt(6)
	v_cvt_i32_f32_e32 v50, v50
	s_waitcnt lgkmcnt(2)
	v_cvt_i32_f32_e32 v58, v58
	v_cvt_i32_f32_e32 v51, v51
	v_cvt_i32_f32_e32 v59, v59
	v_cvt_i32_f32_sdwa v24, v24 dst_sel:BYTE_3 dst_unused:UNUSED_PAD src0_sel:DWORD
	v_cvt_i32_f32_sdwa v46, v46 dst_sel:BYTE_3 dst_unused:UNUSED_PAD src0_sel:DWORD
	v_cvt_i32_f32_e32 v15, v15
	v_cvt_i32_f32_sdwa v21, v21 dst_sel:WORD_1 dst_unused:UNUSED_PAD src0_sel:DWORD
	v_cvt_i32_f32_e32 v41, v41
	v_cvt_i32_f32_sdwa v45, v45 dst_sel:WORD_1 dst_unused:UNUSED_PAD src0_sel:DWORD
	v_cvt_i32_f32_e32 v48, v48
	v_cvt_i32_f32_sdwa v52, v52 dst_sel:WORD_1 dst_unused:UNUSED_PAD src0_sel:DWORD
	v_cvt_i32_f32_e32 v56, v56
	s_waitcnt lgkmcnt(1)
	v_cvt_i32_f32_sdwa v60, v60 dst_sel:WORD_1 dst_unused:UNUSED_PAD src0_sel:DWORD
	v_cvt_i32_f32_e32 v49, v49
	v_cvt_i32_f32_sdwa v53, v53 dst_sel:WORD_1 dst_unused:UNUSED_PAD src0_sel:DWORD
	v_cvt_i32_f32_e32 v57, v57
	v_cvt_i32_f32_sdwa v61, v61 dst_sel:WORD_1 dst_unused:UNUSED_PAD src0_sel:DWORD
	v_cvt_i32_f32_sdwa v25, v25 dst_sel:BYTE_3 dst_unused:UNUSED_PAD src0_sel:DWORD
	v_cvt_i32_f32_sdwa v47, v47 dst_sel:BYTE_3 dst_unused:UNUSED_PAD src0_sel:DWORD
	v_cvt_i32_f32_sdwa v54, v54 dst_sel:BYTE_3 dst_unused:UNUSED_PAD src0_sel:DWORD
	s_waitcnt lgkmcnt(0)
; #define LAS __attribute__((address_space(3)))
; #define GAS __attribute__((address_space(1)))
; #define LDS_WAIT() asm volatile("s_waitcnt lgkmcnt(0)" ::: "memory")
;     ...
;         for (int i = 0; i < 8; ++i) { const int kk = 8 * i + kr; const int k = 64 * kb + kk; const f32x4 v = __builtin_nontemporal_load((const f32x4*)(W + (size_t)k * pitch)) * g[k];
;             LAS float* p = scr + kk * 33 + 4 * (lane & 7); p[0] = __builtin_rintf(v[0] * inv[0]); p[1] = __builtin_rintf(v[1] * inv[1]); p[2] = __builtin_rintf(v[2] * inv[2]); p[3] = __builtin_rintf(v[3] * inv[3]); }
;         LDS_WAIT(); asm volatile("" ::: "memory");
;         const int c = lane & 7;
; #pragma unroll
;         for (int j = 0; j < 4; ++j) { const int n = (lane >> 3) + 8 * j; const LAS float* sp = scr + (8 * c) * 33 + n;
;             u32x2 o;
;             o.x = ((unsigned)(int)sp[0 * 33] & 0xFFu) | (((unsigned)(int)sp[1 * 33] & 0xFFu) << 8) | (((unsigned)(int)sp[2 * 33] & 0xFFu) << 16) | (((unsigned)(int)sp[3 * 33] & 0xFFu) << 24);
;             o.y = ((unsigned)(int)sp[4 * 33] & 0xFFu) | (((unsigned)(int)sp[5 * 33] & 0xFFu) << 8) | (((unsigned)(int)sp[6 * 33] & 0xFFu) << 16) | (((unsigned)(int)sp[7 * 33] & 0xFFu) << 24);
;             *(GAS u32x2*)(dst + (size_t)(n0 + n) * D + 64 * kb + 8 * c) = o; }
;         LDS_WAIT(); asm volatile("" ::: "memory");
	v_cvt_i32_f32_sdwa v62, v62 dst_sel:BYTE_3 dst_unused:UNUSED_PAD src0_sel:DWORD
	v_cvt_i32_f32_sdwa v55, v55 dst_sel:BYTE_3 dst_unused:UNUSED_PAD src0_sel:DWORD
	v_cvt_i32_f32_sdwa v63, v63 dst_sel:BYTE_3 dst_unused:UNUSED_PAD src0_sel:DWORD
	v_lshlrev_b32_e32 v16, 8, v16
	v_lshlrev_b32_e32 v42, 8, v42
	v_and_b32_e32 v20, 0xff0000, v20
	v_and_b32_e32 v44, 0xff0000, v44
	v_lshlrev_b32_e32 v17, 8, v17
	v_lshlrev_b32_e32 v43, 8, v43
	v_lshlrev_b32_e32 v50, 8, v50
	v_lshlrev_b32_e32 v58, 8, v58
	v_lshlrev_b32_e32 v51, 8, v51
	v_lshlrev_b32_e32 v59, 8, v59
	v_perm_b32 v14, v16, v14, s28
	v_perm_b32 v16, v42, v40, s28
	v_and_b32_e32 v21, 0xff0000, v21
	v_and_b32_e32 v45, 0xff0000, v45
	v_and_b32_e32 v52, 0xff0000, v52
	v_and_b32_e32 v60, 0xff0000, v60
	v_and_b32_e32 v53, 0xff0000, v53
	v_and_b32_e32 v61, 0xff0000, v61
	v_perm_b32 v17, v17, v15, s28
	v_perm_b32 v40, v43, v41, s28
	v_perm_b32 v41, v50, v48, s28
	v_perm_b32 v42, v58, v56, s28
	v_perm_b32 v43, v51, v49, s28
	v_perm_b32 v48, v59, v57, s28
	v_or3_b32 v14, v14, v20, v24
	v_or3_b32 v15, v16, v44, v46
	v_or3_b32 v16, v17, v21, v25
	v_or3_b32 v17, v40, v45, v47
	v_or3_b32 v20, v41, v52, v54
	v_or3_b32 v21, v42, v60, v62
	v_or3_b32 v24, v43, v53, v55
	v_or3_b32 v25, v48, v61, v63
	global_store_dwordx2 v[18:19], v[14:15], off
	global_store_dwordx2 v[22:23], v[16:17], off
	global_store_dwordx2 v[82:83], v[20:21], off
	global_store_dwordx2 v[84:85], v[24:25], off
	s_waitcnt lgkmcnt(0)
	v_add_u32_e32 v87, 0x14a0, v31
	v_add_u32_e32 v88, 0x14a8, v31
	v_add_u32_e32 v89, 0x18c0, v31
	v_add_u32_e32 v90, 0x18c8, v31
	v_add_u32_e32 v91, 0x1ce0, v31
	v_add_u32_e32 v92, 0x1ce8, v31
	v_lshl_add_u64 v[18:19], v[6:7], 0, v[12:13]
	v_lshl_add_u64 v[22:23], v[6:7], 0, v[10:11]
	v_lshl_add_u64 v[82:83], v[6:7], 0, v[8:9]
	v_lshl_add_u64 v[84:85], v[6:7], 0, v[4:5]
	v_lshl_add_u64 v[6:7], v[6:7], 0, 64
	s_waitcnt vmcnt(8)
	v_pk_mul_f32 v[46:47], v[144:145], v[188:189] op_sel_hi:[1,0]
	v_pk_mul_f32 v[20:21], v[142:143], v[188:189] op_sel_hi:[1,0]
	v_pk_mul_f32 v[44:45], v[148:149], v[190:191] op_sel_hi:[1,0]
	v_pk_mul_f32 v[24:25], v[146:147], v[190:191] op_sel_hi:[1,0]
	v_pk_mul_f32 v[48:49], v[152:153], v[192:193] op_sel_hi:[1,0]
	v_pk_mul_f32 v[16:17], v[140:141], v[186:187] op_sel_hi:[1,0]
	v_pk_mul_f32 v[14:15], v[138:139], v[186:187] op_sel_hi:[1,0]
	v_pk_mul_f32 v[50:51], v[150:151], v[192:193] op_sel_hi:[1,0]
	v_pk_mul_f32 v[52:53], v[156:157], v[194:195] op_sel_hi:[1,0]
	v_pk_mul_f32 v[54:55], v[154:155], v[194:195] op_sel_hi:[1,0]
	v_pk_mul_f32 v[56:57], v[160:161], v[196:197] op_sel_hi:[1,0]
	v_pk_mul_f32 v[58:59], v[158:159], v[196:197] op_sel_hi:[1,0]
	v_pk_mul_f32 v[60:61], v[164:165], v[198:199] op_sel_hi:[1,0]
	v_pk_mul_f32 v[62:63], v[162:163], v[198:199] op_sel_hi:[1,0]
	v_pk_mul_f32 v[42:43], v[168:169], v[200:201] op_sel_hi:[1,0]
	v_pk_mul_f32 v[40:41], v[166:167], v[200:201] op_sel_hi:[1,0]
	v_mul_f32_e32 v14, v26, v14
	v_mul_f32_e32 v15, v27, v15
	v_mul_f32_e32 v16, v28, v16
	v_mul_f32_e32 v17, v29, v17
	v_mul_f32_e32 v20, v26, v20
	v_mul_f32_e32 v21, v27, v21
	v_mul_f32_e32 v46, v28, v46
	v_mul_f32_e32 v47, v29, v47
	v_mul_f32_e32 v24, v26, v24
	v_mul_f32_e32 v25, v27, v25
	v_mul_f32_e32 v44, v28, v44
	v_mul_f32_e32 v45, v29, v45
	v_mul_f32_e32 v50, v26, v50
	v_mul_f32_e32 v51, v27, v51
	v_mul_f32_e32 v48, v28, v48
	v_mul_f32_e32 v49, v29, v49
	v_mul_f32_e32 v54, v26, v54
	v_mul_f32_e32 v55, v27, v55
	v_mul_f32_e32 v52, v28, v52
	v_mul_f32_e32 v53, v29, v53
	v_mul_f32_e32 v58, v26, v58
	v_mul_f32_e32 v59, v27, v59
	v_mul_f32_e32 v56, v28, v56
	v_mul_f32_e32 v57, v29, v57
	v_mul_f32_e32 v62, v26, v62
	v_mul_f32_e32 v63, v27, v63
	v_mul_f32_e32 v60, v28, v60
	v_mul_f32_e32 v61, v29, v61
	v_mul_f32_e32 v40, v26, v40
	v_mul_f32_e32 v41, v27, v41
	v_mul_f32_e32 v42, v28, v42
	v_mul_f32_e32 v43, v29, v43
	v_rndne_f32_e32 v14, v14
	v_rndne_f32_e32 v15, v15
	v_rndne_f32_e32 v16, v16
	v_rndne_f32_e32 v17, v17
	v_rndne_f32_e32 v20, v20
	v_rndne_f32_e32 v21, v21
	v_rndne_f32_e32 v46, v46
	v_rndne_f32_e32 v47, v47
	v_rndne_f32_e32 v24, v24
	v_rndne_f32_e32 v25, v25
	v_rndne_f32_e32 v44, v44
	v_rndne_f32_e32 v45, v45
	v_rndne_f32_e32 v50, v50
	v_rndne_f32_e32 v51, v51
	v_rndne_f32_e32 v48, v48
	v_rndne_f32_e32 v49, v49
	v_rndne_f32_e32 v54, v54
	v_rndne_f32_e32 v55, v55
	v_rndne_f32_e32 v52, v52
	v_rndne_f32_e32 v53, v53
	v_rndne_f32_e32 v58, v58
	v_rndne_f32_e32 v59, v59
	v_rndne_f32_e32 v56, v56
	v_rndne_f32_e32 v57, v57
	v_rndne_f32_e32 v62, v62
	v_rndne_f32_e32 v63, v63
	v_rndne_f32_e32 v60, v60
	v_rndne_f32_e32 v61, v61
	v_rndne_f32_e32 v40, v40
	v_rndne_f32_e32 v41, v41
	v_rndne_f32_e32 v42, v42
	v_rndne_f32_e32 v43, v43
	ds_write2_b32 v31, v14, v15 offset1:1
	ds_write2_b32 v31, v16, v17 offset0:2 offset1:3
	ds_write2_b32 v32, v20, v21 offset1:1
	ds_write2_b32 v33, v46, v47 offset1:1
	ds_write2_b32 v34, v24, v25 offset1:1
	ds_write2_b32 v35, v44, v45 offset1:1
	ds_write2_b32 v36, v50, v51 offset1:1
	ds_write2_b32 v37, v48, v49 offset1:1
	ds_write2_b32 v38, v54, v55 offset1:1
	ds_write2_b32 v39, v52, v53 offset1:1
	ds_write2_b32 v87, v58, v59 offset1:1
	ds_write2_b32 v88, v56, v57 offset1:1
	ds_write2_b32 v89, v62, v63 offset1:1
	ds_write2_b32 v90, v60, v61 offset1:1
	ds_write2_b32 v91, v40, v41 offset1:1
	ds_write2_b32 v92, v42, v43 offset1:1
	s_waitcnt lgkmcnt(0)
; #define LAS __attribute__((address_space(3)))
; #define GAS __attribute__((address_space(1)))
; #define LDS_WAIT() asm volatile("s_waitcnt lgkmcnt(0)" ::: "memory")
;     ...
;         LDS_WAIT(); asm volatile("" ::: "memory");
;         const int c = lane & 7;
; #pragma unroll
;         for (int j = 0; j < 4; ++j) { const int n = (lane >> 3) + 8 * j; const LAS float* sp = scr + (8 * c) * 33 + n;
;             u32x2 o;
;             o.x = ((unsigned)(int)sp[0 * 33] & 0xFFu) | (((unsigned)(int)sp[1 * 33] & 0xFFu) << 8) | (((unsigned)(int)sp[2 * 33] & 0xFFu) << 16) | (((unsigned)(int)sp[3 * 33] & 0xFFu) << 24);
;             o.y = ((unsigned)(int)sp[4 * 33] & 0xFFu) | (((unsigned)(int)sp[5 * 33] & 0xFFu) << 8) | (((unsigned)(int)sp[6 * 33] & 0xFFu) << 16) | (((unsigned)(int)sp[7 * 33] & 0xFFu) << 24);
;             *(GAS u32x2*)(dst + (size_t)(n0 + n) * D + 64 * kb + 8 * c) = o; }
;         LDS_WAIT(); asm volatile("" ::: "memory");
	ds_read2_b32 v[14:15], v30 offset1:8
	ds_read2_b32 v[16:17], v30 offset0:33 offset1:41
	ds_read2_b32 v[20:21], v30 offset0:66 offset1:74
	ds_read2_b32 v[24:25], v30 offset0:99 offset1:107
	ds_read2_b32 v[40:41], v30 offset0:132 offset1:140
	ds_read2_b32 v[42:43], v30 offset0:165 offset1:173
	ds_read2_b32 v[44:45], v30 offset0:198 offset1:206
	ds_read2_b32 v[46:47], v30 offset0:231 offset1:239
	ds_read2_b32 v[48:49], v30 offset0:16 offset1:24
	ds_read2_b32 v[50:51], v30 offset0:49 offset1:57
	ds_read2_b32 v[52:53], v30 offset0:82 offset1:90
	ds_read2_b32 v[54:55], v30 offset0:115 offset1:123
	ds_read2_b32 v[56:57], v30 offset0:148 offset1:156
	ds_read2_b32 v[58:59], v30 offset0:181 offset1:189
	ds_read2_b32 v[60:61], v30 offset0:214 offset1:222
	ds_read2_b32 v[62:63], v30 offset0:247 offset1:255
	s_waitcnt lgkmcnt(14)
	v_cvt_i32_f32_e32 v16, v16
	s_waitcnt lgkmcnt(10)
	v_cvt_i32_f32_e32 v42, v42
	v_cvt_i32_f32_e32 v14, v14
	v_cvt_i32_f32_sdwa v20, v20 dst_sel:WORD_1 dst_unused:UNUSED_PAD src0_sel:DWORD
	v_cvt_i32_f32_e32 v40, v40
	s_waitcnt lgkmcnt(9)
	v_cvt_i32_f32_sdwa v44, v44 dst_sel:WORD_1 dst_unused:UNUSED_PAD src0_sel:DWORD
	v_cvt_i32_f32_e32 v17, v17
	v_cvt_i32_f32_e32 v43, v43
	s_waitcnt lgkmcnt(6)
	v_cvt_i32_f32_e32 v50, v50
	s_waitcnt lgkmcnt(2)
	v_cvt_i32_f32_e32 v58, v58
	v_cvt_i32_f32_e32 v51, v51
	v_cvt_i32_f32_e32 v59, v59
	v_cvt_i32_f32_sdwa v24, v24 dst_sel:BYTE_3 dst_unused:UNUSED_PAD src0_sel:DWORD
	v_cvt_i32_f32_sdwa v46, v46 dst_sel:BYTE_3 dst_unused:UNUSED_PAD src0_sel:DWORD
	v_cvt_i32_f32_e32 v15, v15
	v_cvt_i32_f32_sdwa v21, v21 dst_sel:WORD_1 dst_unused:UNUSED_PAD src0_sel:DWORD
	v_cvt_i32_f32_e32 v41, v41
	v_cvt_i32_f32_sdwa v45, v45 dst_sel:WORD_1 dst_unused:UNUSED_PAD src0_sel:DWORD
	v_cvt_i32_f32_e32 v48, v48
	v_cvt_i32_f32_sdwa v52, v52 dst_sel:WORD_1 dst_unused:UNUSED_PAD src0_sel:DWORD
	v_cvt_i32_f32_e32 v56, v56
	s_waitcnt lgkmcnt(1)
	v_cvt_i32_f32_sdwa v60, v60 dst_sel:WORD_1 dst_unused:UNUSED_PAD src0_sel:DWORD
	v_cvt_i32_f32_e32 v49, v49
	v_cvt_i32_f32_sdwa v53, v53 dst_sel:WORD_1 dst_unused:UNUSED_PAD src0_sel:DWORD
	v_cvt_i32_f32_e32 v57, v57
	v_cvt_i32_f32_sdwa v61, v61 dst_sel:WORD_1 dst_unused:UNUSED_PAD src0_sel:DWORD
	v_cvt_i32_f32_sdwa v25, v25 dst_sel:BYTE_3 dst_unused:UNUSED_PAD src0_sel:DWORD
	v_cvt_i32_f32_sdwa v47, v47 dst_sel:BYTE_3 dst_unused:UNUSED_PAD src0_sel:DWORD
	v_cvt_i32_f32_sdwa v54, v54 dst_sel:BYTE_3 dst_unused:UNUSED_PAD src0_sel:DWORD
	s_waitcnt lgkmcnt(0)
	v_cvt_i32_f32_sdwa v62, v62 dst_sel:BYTE_3 dst_unused:UNUSED_PAD src0_sel:DWORD
	v_cvt_i32_f32_sdwa v55, v55 dst_sel:BYTE_3 dst_unused:UNUSED_PAD src0_sel:DWORD
	v_cvt_i32_f32_sdwa v63, v63 dst_sel:BYTE_3 dst_unused:UNUSED_PAD src0_sel:DWORD
	v_lshlrev_b32_e32 v16, 8, v16
	v_lshlrev_b32_e32 v42, 8, v42
	v_and_b32_e32 v20, 0xff0000, v20
	v_and_b32_e32 v44, 0xff0000, v44
	v_lshlrev_b32_e32 v17, 8, v17
	v_lshlrev_b32_e32 v43, 8, v43
	v_lshlrev_b32_e32 v50, 8, v50
	v_lshlrev_b32_e32 v58, 8, v58
	v_lshlrev_b32_e32 v51, 8, v51
	v_lshlrev_b32_e32 v59, 8, v59
	v_perm_b32 v14, v16, v14, s28
	v_perm_b32 v16, v42, v40, s28
	v_and_b32_e32 v21, 0xff0000, v21
	v_and_b32_e32 v45, 0xff0000, v45
	v_and_b32_e32 v52, 0xff0000, v52
	v_and_b32_e32 v60, 0xff0000, v60
	v_and_b32_e32 v53, 0xff0000, v53
	v_and_b32_e32 v61, 0xff0000, v61
	v_perm_b32 v17, v17, v15, s28
	v_perm_b32 v40, v43, v41, s28
	v_perm_b32 v41, v50, v48, s28
	v_perm_b32 v42, v58, v56, s28
	v_perm_b32 v43, v51, v49, s28
	v_perm_b32 v48, v59, v57, s28
	v_or3_b32 v14, v14, v20, v24
	v_or3_b32 v15, v16, v44, v46
	v_or3_b32 v16, v17, v21, v25
	v_or3_b32 v17, v40, v45, v47
	v_or3_b32 v20, v41, v52, v54
	v_or3_b32 v21, v42, v60, v62
	v_or3_b32 v24, v43, v53, v55
	v_or3_b32 v25, v48, v61, v63
	global_store_dwordx2 v[18:19], v[14:15], off
	global_store_dwordx2 v[22:23], v[16:17], off
	global_store_dwordx2 v[82:83], v[20:21], off
	global_store_dwordx2 v[84:85], v[24:25], off
	s_waitcnt lgkmcnt(0)
	s_mov_b64 s[4:5], 0

;     const int kr = lane >> 3;
;     f32x4 mx = {0.f, 0.f, 0.f, 0.f};
; #pragma unroll 2
;     for (int kb = 0; kb < D / 64; ++kb) {
; #pragma unroll
;         for (int i = 0; i < 8; ++i) { const int k = 64 * kb + 8 * i + kr; const f32x4 v = __builtin_nontemporal_load((const f32x4*)(W + (size_t)k * pitch)) * g[k];
;             mx[0] = __builtin_fmaxf(mx[0], __builtin_fabsf(v[0])); mx[1] = __builtin_fmaxf(mx[1], __builtin_fabsf(v[1])); mx[2] = __builtin_fmaxf(mx[2], __builtin_fabsf(v[2])); mx[3] = __builtin_fmaxf(mx[3], __builtin_fabsf(v[3])); } }
.LBB0_135:
	v_readfirstlane_b32 s6, v2
	v_readfirstlane_b32 s7, v3
	v_readfirstlane_b32 s8, v4
	v_readfirstlane_b32 s9, v5
	s_nop 1
	v_subrev_u32_e32 v250, s6, v2
	v_subrev_u32_e32 v251, s8, v4
	s_nop 4
	global_load_dwordx4 v[106:109], v250, s[6:7] nt
	global_load_dword v170, v251, s[8:9] offset:-480
	s_add_u32 s6, s6, 0x16000
	s_addc_u32 s7, s7, 0
	global_load_dwordx4 v[110:113], v250, s[6:7] nt
	global_load_dword v172, v251, s[8:9] offset:-448
	s_add_u32 s6, s6, 0x16000
	s_addc_u32 s7, s7, 0
	global_load_dwordx4 v[114:117], v250, s[6:7] nt
	global_load_dword v174, v251, s[8:9] offset:-416
	s_add_u32 s6, s6, 0x16000
	s_addc_u32 s7, s7, 0
	global_load_dwordx4 v[118:121], v250, s[6:7] nt
	global_load_dword v176, v251, s[8:9] offset:-384
	s_add_u32 s6, s6, 0x16000
	s_addc_u32 s7, s7, 0
	global_load_dwordx4 v[122:125], v250, s[6:7] nt
	global_load_dword v178, v251, s[8:9] offset:-352
	s_add_u32 s6, s6, 0x16000
	s_addc_u32 s7, s7, 0
	global_load_dwordx4 v[126:129], v250, s[6:7] nt
	global_load_dword v180, v251, s[8:9] offset:-320
	s_add_u32 s6, s6, 0x16000
	s_addc_u32 s7, s7, 0
	global_load_dwordx4 v[130:133], v250, s[6:7] nt
	global_load_dword v182, v251, s[8:9] offset:-288
	s_add_u32 s6, s6, 0x16000
	s_addc_u32 s7, s7, 0
	global_load_dwordx4 v[134:137], v250, s[6:7] nt
	global_load_dword v184, v251, s[8:9] offset:-256
	s_add_u32 s6, s6, 0x16000
	s_addc_u32 s7, s7, 0
	global_load_dwordx4 v[138:141], v250, s[6:7] nt
	global_load_dword v186, v251, s[8:9] offset:-224
	s_add_u32 s6, s6, 0x16000
	s_addc_u32 s7, s7, 0
	global_load_dwordx4 v[142:145], v250, s[6:7] nt
	global_load_dword v188, v251, s[8:9] offset:-192
	s_add_u32 s6, s6, 0x16000
	s_addc_u32 s7, s7, 0
	global_load_dwordx4 v[146:149], v250, s[6:7] nt
	global_load_dword v190, v251, s[8:9] offset:-160
	s_add_u32 s6, s6, 0x16000
	s_addc_u32 s7, s7, 0
	global_load_dwordx4 v[150:153], v250, s[6:7] nt
	global_load_dword v192, v251, s[8:9] offset:-128
	s_add_u32 s6, s6, 0x16000
	s_addc_u32 s7, s7, 0
	global_load_dwordx4 v[154:157], v250, s[6:7] nt
	global_load_dword v194, v251, s[8:9] offset:-96
	s_add_u32 s6, s6, 0x16000
	s_addc_u32 s7, s7, 0
	global_load_dwordx4 v[158:161], v250, s[6:7] nt
	global_load_dword v196, v251, s[8:9] offset:-64
	s_add_u32 s6, s6, 0x16000
	s_addc_u32 s7, s7, 0
	global_load_dwordx4 v[162:165], v250, s[6:7] nt
	global_load_dword v198, v251, s[8:9] offset:-32
	s_add_u32 s6, s6, 0x16000
	s_addc_u32 s7, s7, 0
	global_load_dwordx4 v[166:169], v250, s[6:7] nt
	global_load_dword v200, v251, s[8:9]
	s_waitcnt vmcnt(28)
	v_pk_mul_f32 v[16:17], v[106:107], v[170:171] op_sel_hi:[1,0]
	v_pk_mul_f32 v[18:19], v[108:109], v[170:171] op_sel_hi:[1,0]
	v_pk_mul_f32 v[20:21], v[110:111], v[172:173] op_sel_hi:[1,0]
	v_pk_mul_f32 v[22:23], v[112:113], v[172:173] op_sel_hi:[1,0]
	v_max3_f32 v15, v15, |v16|, |v20|
	v_max3_f32 v13, v13, |v17|, |v21|
	v_max3_f32 v9, v9, |v18|, |v22|
	v_max3_f32 v7, v7, |v19|, |v23|
	s_add_u32 s6, s6, 0x16000
	s_addc_u32 s7, s7, 0
	global_load_dwordx4 v[106:109], v250, s[6:7] nt
	global_load_dword v170, v251, s[8:9] offset:32
	s_add_u32 s6, s6, 0x16000
	s_addc_u32 s7, s7, 0
	global_load_dwordx4 v[110:113], v250, s[6:7] nt
	global_load_dword v172, v251, s[8:9] offset:64
	s_waitcnt vmcnt(28)
	v_pk_mul_f32 v[16:17], v[114:115], v[174:175] op_sel_hi:[1,0]
	v_pk_mul_f32 v[18:19], v[116:117], v[174:175] op_sel_hi:[1,0]
	v_pk_mul_f32 v[20:21], v[118:119], v[176:177] op_sel_hi:[1,0]
	v_pk_mul_f32 v[22:23], v[120:121], v[176:177] op_sel_hi:[1,0]
	v_max3_f32 v15, v15, |v16|, |v20|
	v_max3_f32 v13, v13, |v17|, |v21|
	v_max3_f32 v9, v9, |v18|, |v22|
	v_max3_f32 v7, v7, |v19|, |v23|
	s_add_u32 s6, s6, 0x16000
	s_addc_u32 s7, s7, 0
	global_load_dwordx4 v[114:117], v250, s[6:7] nt
	global_load_dword v174, v251, s[8:9] offset:96
	s_add_u32 s6, s6, 0x16000
	s_addc_u32 s7, s7, 0
	global_load_dwordx4 v[118:121], v250, s[6:7] nt
	global_load_dword v176, v251, s[8:9] offset:128
	s_waitcnt vmcnt(28)
	v_pk_mul_f32 v[16:17], v[122:123], v[178:179] op_sel_hi:[1,0]
	v_pk_mul_f32 v[18:19], v[124:125], v[178:179] op_sel_hi:[1,0]
	v_pk_mul_f32 v[20:21], v[126:127], v[180:181] op_sel_hi:[1,0]
	v_pk_mul_f32 v[22:23], v[128:129], v[180:181] op_sel_hi:[1,0]
	v_max3_f32 v15, v15, |v16|, |v20|
	v_max3_f32 v13, v13, |v17|, |v21|
	v_max3_f32 v9, v9, |v18|, |v22|
	v_max3_f32 v7, v7, |v19|, |v23|
	s_add_u32 s6, s6, 0x16000
	s_addc_u32 s7, s7, 0
	global_load_dwordx4 v[122:125], v250, s[6:7] nt
	global_load_dword v178, v251, s[8:9] offset:160
	s_add_u32 s6, s6, 0x16000
	s_addc_u32 s7, s7, 0
	global_load_dwordx4 v[126:129], v250, s[6:7] nt
	global_load_dword v180, v251, s[8:9] offset:192
	s_waitcnt vmcnt(28)
	v_pk_mul_f32 v[16:17], v[130:131], v[182:183] op_sel_hi:[1,0]
	v_pk_mul_f32 v[18:19], v[132:133], v[182:183] op_sel_hi:[1,0]
	v_pk_mul_f32 v[20:21], v[134:135], v[184:185] op_sel_hi:[1,0]
	v_pk_mul_f32 v[22:23], v[136:137], v[184:185] op_sel_hi:[1,0]
	v_max3_f32 v15, v15, |v16|, |v20|
	v_max3_f32 v13, v13, |v17|, |v21|
	v_max3_f32 v9, v9, |v18|, |v22|
	v_max3_f32 v7, v7, |v19|, |v23|
	s_add_u32 s6, s6, 0x16000
	s_addc_u32 s7, s7, 0
	global_load_dwordx4 v[130:133], v250, s[6:7] nt
	global_load_dword v182, v251, s[8:9] offset:224
	s_add_u32 s6, s6, 0x16000
	s_addc_u32 s7, s7, 0
	global_load_dwordx4 v[134:137], v250, s[6:7] nt
	global_load_dword v184, v251, s[8:9] offset:256
	s_waitcnt vmcnt(28)
;     ...
; #pragma unroll 2
;     for (int kb = 0; kb < D / 64; ++kb) {
; #pragma unroll
;         for (int i = 0; i < 8; ++i) { const int k = 64 * kb + 8 * i + kr; const f32x4 v = __builtin_nontemporal_load((const f32x4*)(W + (size_t)k * pitch)) * g[k];
;             mx[0] = __builtin_fmaxf(mx[0], __builtin_fabsf(v[0])); mx[1] = __builtin_fmaxf(mx[1], __builtin_fabsf(v[1])); mx[2] = __builtin_fmaxf(mx[2], __builtin_fabsf(v[2])); mx[3] = __builtin_fmaxf(mx[3], __builtin_fabsf(v[3])); } }
	v_pk_mul_f32 v[16:17], v[138:139], v[186:187] op_sel_hi:[1,0]
	v_pk_mul_f32 v[18:19], v[140:141], v[186:187] op_sel_hi:[1,0]
	v_pk_mul_f32 v[20:21], v[142:143], v[188:189] op_sel_hi:[1,0]
	v_pk_mul_f32 v[22:23], v[144:145], v[188:189] op_sel_hi:[1,0]
	v_max3_f32 v15, v15, |v16|, |v20|
	v_max3_f32 v13, v13, |v17|, |v21|
	v_max3_f32 v9, v9, |v18|, |v22|
	v_max3_f32 v7, v7, |v19|, |v23|
	s_add_u32 s6, s6, 0x16000
	s_addc_u32 s7, s7, 0
	global_load_dwordx4 v[138:141], v250, s[6:7] nt
	global_load_dword v186, v251, s[8:9] offset:288
	s_add_u32 s6, s6, 0x16000
	s_addc_u32 s7, s7, 0
	global_load_dwordx4 v[142:145], v250, s[6:7] nt
	global_load_dword v188, v251, s[8:9] offset:320
	s_waitcnt vmcnt(28)
	v_pk_mul_f32 v[16:17], v[146:147], v[190:191] op_sel_hi:[1,0]
	v_pk_mul_f32 v[18:19], v[148:149], v[190:191] op_sel_hi:[1,0]
	v_pk_mul_f32 v[20:21], v[150:151], v[192:193] op_sel_hi:[1,0]
	v_pk_mul_f32 v[22:23], v[152:153], v[192:193] op_sel_hi:[1,0]
	v_max3_f32 v15, v15, |v16|, |v20|
	v_max3_f32 v13, v13, |v17|, |v21|
	v_max3_f32 v9, v9, |v18|, |v22|
	v_max3_f32 v7, v7, |v19|, |v23|
	s_add_u32 s6, s6, 0x16000
	s_addc_u32 s7, s7, 0
	global_load_dwordx4 v[146:149], v250, s[6:7] nt
	global_load_dword v190, v251, s[8:9] offset:352
	s_add_u32 s6, s6, 0x16000
	s_addc_u32 s7, s7, 0
	global_load_dwordx4 v[150:153], v250, s[6:7] nt
	global_load_dword v192, v251, s[8:9] offset:384
	s_waitcnt vmcnt(28)
	v_pk_mul_f32 v[16:17], v[154:155], v[194:195] op_sel_hi:[1,0]
	v_pk_mul_f32 v[18:19], v[156:157], v[194:195] op_sel_hi:[1,0]
	v_pk_mul_f32 v[20:21], v[158:159], v[196:197] op_sel_hi:[1,0]
	v_pk_mul_f32 v[22:23], v[160:161], v[196:197] op_sel_hi:[1,0]
	v_max3_f32 v15, v15, |v16|, |v20|
	v_max3_f32 v13, v13, |v17|, |v21|
	v_max3_f32 v9, v9, |v18|, |v22|
	v_max3_f32 v7, v7, |v19|, |v23|
	s_add_u32 s6, s6, 0x16000
	s_addc_u32 s7, s7, 0
	global_load_dwordx4 v[154:157], v250, s[6:7] nt
	global_load_dword v194, v251, s[8:9] offset:416
	s_add_u32 s6, s6, 0x16000
	s_addc_u32 s7, s7, 0
	global_load_dwordx4 v[158:161], v250, s[6:7] nt
	global_load_dword v196, v251, s[8:9] offset:448
	s_waitcnt vmcnt(28)
	v_pk_mul_f32 v[16:17], v[162:163], v[198:199] op_sel_hi:[1,0]
	v_pk_mul_f32 v[18:19], v[164:165], v[198:199] op_sel_hi:[1,0]
	v_pk_mul_f32 v[20:21], v[166:167], v[200:201] op_sel_hi:[1,0]
	v_pk_mul_f32 v[22:23], v[168:169], v[200:201] op_sel_hi:[1,0]
	v_max3_f32 v15, v15, |v16|, |v20|
	v_max3_f32 v13, v13, |v17|, |v21|
	v_max3_f32 v9, v9, |v18|, |v22|
	v_max3_f32 v7, v7, |v19|, |v23|
	s_add_u32 s6, s6, 0x16000
	s_addc_u32 s7, s7, 0
	global_load_dwordx4 v[162:165], v250, s[6:7] nt
	global_load_dword v198, v251, s[8:9] offset:480
	s_add_u32 s6, s6, 0x16000
	s_addc_u32 s7, s7, 0
	global_load_dwordx4 v[166:169], v250, s[6:7] nt
	global_load_dword v200, v251, s[8:9] offset:512
	s_waitcnt vmcnt(28)
	v_pk_mul_f32 v[16:17], v[106:107], v[170:171] op_sel_hi:[1,0]
	v_pk_mul_f32 v[18:19], v[108:109], v[170:171] op_sel_hi:[1,0]
	v_pk_mul_f32 v[20:21], v[110:111], v[172:173] op_sel_hi:[1,0]
	v_pk_mul_f32 v[22:23], v[112:113], v[172:173] op_sel_hi:[1,0]
	v_max3_f32 v15, v15, |v16|, |v20|
	v_max3_f32 v13, v13, |v17|, |v21|
	v_max3_f32 v9, v9, |v18|, |v22|
	v_max3_f32 v7, v7, |v19|, |v23|
	s_add_u32 s6, s6, 0x16000
	s_addc_u32 s7, s7, 0
	global_load_dwordx4 v[106:109], v250, s[6:7] nt
	global_load_dword v170, v251, s[8:9] offset:544
	s_add_u32 s6, s6, 0x16000
	s_addc_u32 s7, s7, 0
	global_load_dwordx4 v[110:113], v250, s[6:7] nt
	global_load_dword v172, v251, s[8:9] offset:576
	s_waitcnt vmcnt(28)
	v_pk_mul_f32 v[16:17], v[114:115], v[174:175] op_sel_hi:[1,0]
	v_pk_mul_f32 v[18:19], v[116:117], v[174:175] op_sel_hi:[1,0]
	v_pk_mul_f32 v[20:21], v[118:119], v[176:177] op_sel_hi:[1,0]
	v_pk_mul_f32 v[22:23], v[120:121], v[176:177] op_sel_hi:[1,0]
	v_max3_f32 v15, v15, |v16|, |v20|
	v_max3_f32 v13, v13, |v17|, |v21|
	v_max3_f32 v9, v9, |v18|, |v22|
	v_max3_f32 v7, v7, |v19|, |v23|
	s_add_u32 s6, s6, 0x16000
	s_addc_u32 s7, s7, 0
	global_load_dwordx4 v[114:117], v250, s[6:7] nt
	global_load_dword v174, v251, s[8:9] offset:608
	s_add_u32 s6, s6, 0x16000
	s_addc_u32 s7, s7, 0
	global_load_dwordx4 v[118:121], v250, s[6:7] nt
	global_load_dword v176, v251, s[8:9] offset:640
	s_waitcnt vmcnt(28)
	v_pk_mul_f32 v[16:17], v[122:123], v[178:179] op_sel_hi:[1,0]
	v_pk_mul_f32 v[18:19], v[124:125], v[178:179] op_sel_hi:[1,0]
	v_pk_mul_f32 v[20:21], v[126:127], v[180:181] op_sel_hi:[1,0]
	v_pk_mul_f32 v[22:23], v[128:129], v[180:181] op_sel_hi:[1,0]
	v_max3_f32 v15, v15, |v16|, |v20|
	v_max3_f32 v13, v13, |v17|, |v21|
	v_max3_f32 v9, v9, |v18|, |v22|
	v_max3_f32 v7, v7, |v19|, |v23|
	s_add_u32 s6, s6, 0x16000
	s_addc_u32 s7, s7, 0
	global_load_dwordx4 v[122:125], v250, s[6:7] nt
	global_load_dword v178, v251, s[8:9] offset:672
	s_add_u32 s6, s6, 0x16000
	s_addc_u32 s7, s7, 0
	global_load_dwordx4 v[126:129], v250, s[6:7] nt
	global_load_dword v180, v251, s[8:9] offset:704
	s_waitcnt vmcnt(28)
	v_pk_mul_f32 v[16:17], v[130:131], v[182:183] op_sel_hi:[1,0]
	v_pk_mul_f32 v[18:19], v[132:133], v[182:183] op_sel_hi:[1,0]
	v_pk_mul_f32 v[20:21], v[134:135], v[184:185] op_sel_hi:[1,0]
	v_pk_mul_f32 v[22:23], v[136:137], v[184:185] op_sel_hi:[1,0]
	v_max3_f32 v15, v15, |v16|, |v20|
	v_max3_f32 v13, v13, |v17|, |v21|
	v_max3_f32 v9, v9, |v18|, |v22|
	v_max3_f32 v7, v7, |v19|, |v23|
	s_add_u32 s6, s6, 0x16000
	s_addc_u32 s7, s7, 0
	global_load_dwordx4 v[130:133], v250, s[6:7] nt
	global_load_dword v182, v251, s[8:9] offset:736
	s_add_u32 s6, s6, 0x16000
	s_addc_u32 s7, s7, 0
	global_load_dwordx4 v[134:137], v250, s[6:7] nt
	global_load_dword v184, v251, s[8:9] offset:768
	s_waitcnt vmcnt(28)
;     ...
; #pragma unroll 2
;     for (int kb = 0; kb < D / 64; ++kb) {
; #pragma unroll
;         for (int i = 0; i < 8; ++i) { const int k = 64 * kb + 8 * i + kr; const f32x4 v = __builtin_nontemporal_load((const f32x4*)(W + (size_t)k * pitch)) * g[k];
;             mx[0] = __builtin_fmaxf(mx[0], __builtin_fabsf(v[0])); mx[1] = __builtin_fmaxf(mx[1], __builtin_fabsf(v[1])); mx[2] = __builtin_fmaxf(mx[2], __builtin_fabsf(v[2])); mx[3] = __builtin_fmaxf(mx[3], __builtin_fabsf(v[3])); } }
	v_pk_mul_f32 v[16:17], v[138:139], v[186:187] op_sel_hi:[1,0]
	v_pk_mul_f32 v[18:19], v[140:141], v[186:187] op_sel_hi:[1,0]
	v_pk_mul_f32 v[20:21], v[142:143], v[188:189] op_sel_hi:[1,0]
	v_pk_mul_f32 v[22:23], v[144:145], v[188:189] op_sel_hi:[1,0]
	v_max3_f32 v15, v15, |v16|, |v20|
	v_max3_f32 v13, v13, |v17|, |v21|
	v_max3_f32 v9, v9, |v18|, |v22|
	v_max3_f32 v7, v7, |v19|, |v23|
	s_add_u32 s6, s6, 0x16000
	s_addc_u32 s7, s7, 0
	global_load_dwordx4 v[138:141], v250, s[6:7] nt
	global_load_dword v186, v251, s[8:9] offset:800
	s_add_u32 s6, s6, 0x16000
	s_addc_u32 s7, s7, 0
	global_load_dwordx4 v[142:145], v250, s[6:7] nt
	global_load_dword v188, v251, s[8:9] offset:832
	s_waitcnt vmcnt(28)
	v_pk_mul_f32 v[16:17], v[146:147], v[190:191] op_sel_hi:[1,0]
	v_pk_mul_f32 v[18:19], v[148:149], v[190:191] op_sel_hi:[1,0]
	v_pk_mul_f32 v[20:21], v[150:151], v[192:193] op_sel_hi:[1,0]
	v_pk_mul_f32 v[22:23], v[152:153], v[192:193] op_sel_hi:[1,0]
	v_max3_f32 v15, v15, |v16|, |v20|
	v_max3_f32 v13, v13, |v17|, |v21|
	v_max3_f32 v9, v9, |v18|, |v22|
	v_max3_f32 v7, v7, |v19|, |v23|
	s_add_u32 s6, s6, 0x16000
	s_addc_u32 s7, s7, 0
	global_load_dwordx4 v[146:149], v250, s[6:7] nt
	global_load_dword v190, v251, s[8:9] offset:864
	s_add_u32 s6, s6, 0x16000
	s_addc_u32 s7, s7, 0
	global_load_dwordx4 v[150:153], v250, s[6:7] nt
	global_load_dword v192, v251, s[8:9] offset:896
	s_waitcnt vmcnt(28)
	v_pk_mul_f32 v[16:17], v[154:155], v[194:195] op_sel_hi:[1,0]
	v_pk_mul_f32 v[18:19], v[156:157], v[194:195] op_sel_hi:[1,0]
	v_pk_mul_f32 v[20:21], v[158:159], v[196:197] op_sel_hi:[1,0]
	v_pk_mul_f32 v[22:23], v[160:161], v[196:197] op_sel_hi:[1,0]
	v_max3_f32 v15, v15, |v16|, |v20|
	v_max3_f32 v13, v13, |v17|, |v21|
	v_max3_f32 v9, v9, |v18|, |v22|
	v_max3_f32 v7, v7, |v19|, |v23|
	s_add_u32 s6, s6, 0x16000
	s_addc_u32 s7, s7, 0
	global_load_dwordx4 v[154:157], v250, s[6:7] nt
	global_load_dword v194, v251, s[8:9] offset:928
	s_add_u32 s6, s6, 0x16000
	s_addc_u32 s7, s7, 0
	global_load_dwordx4 v[158:161], v250, s[6:7] nt
	global_load_dword v196, v251, s[8:9] offset:960
	s_waitcnt vmcnt(28)
	v_pk_mul_f32 v[16:17], v[162:163], v[198:199] op_sel_hi:[1,0]
	v_pk_mul_f32 v[18:19], v[164:165], v[198:199] op_sel_hi:[1,0]
	v_pk_mul_f32 v[20:21], v[166:167], v[200:201] op_sel_hi:[1,0]
	v_pk_mul_f32 v[22:23], v[168:169], v[200:201] op_sel_hi:[1,0]
	v_max3_f32 v15, v15, |v16|, |v20|
	v_max3_f32 v13, v13, |v17|, |v21|
	v_max3_f32 v9, v9, |v18|, |v22|
	v_max3_f32 v7, v7, |v19|, |v23|
	s_add_u32 s6, s6, 0x16000
	s_addc_u32 s7, s7, 0
	global_load_dwordx4 v[162:165], v250, s[6:7] nt
	global_load_dword v198, v251, s[8:9] offset:992
	s_add_u32 s6, s6, 0x16000
	s_addc_u32 s7, s7, 0
	global_load_dwordx4 v[166:169], v250, s[6:7] nt
	global_load_dword v200, v251, s[8:9] offset:1024
	s_waitcnt vmcnt(28)
	v_pk_mul_f32 v[16:17], v[106:107], v[170:171] op_sel_hi:[1,0]
	v_pk_mul_f32 v[18:19], v[108:109], v[170:171] op_sel_hi:[1,0]
	v_pk_mul_f32 v[20:21], v[110:111], v[172:173] op_sel_hi:[1,0]
	v_pk_mul_f32 v[22:23], v[112:113], v[172:173] op_sel_hi:[1,0]
	v_max3_f32 v15, v15, |v16|, |v20|
	v_max3_f32 v13, v13, |v17|, |v21|
	v_max3_f32 v9, v9, |v18|, |v22|
	v_max3_f32 v7, v7, |v19|, |v23|
	s_add_u32 s6, s6, 0x16000
	s_addc_u32 s7, s7, 0
	global_load_dwordx4 v[106:109], v250, s[6:7] nt
	global_load_dword v170, v251, s[8:9] offset:1056
	s_add_u32 s6, s6, 0x16000
	s_addc_u32 s7, s7, 0
	global_load_dwordx4 v[110:113], v250, s[6:7] nt
	global_load_dword v172, v251, s[8:9] offset:1088
	s_waitcnt vmcnt(28)
	v_pk_mul_f32 v[16:17], v[114:115], v[174:175] op_sel_hi:[1,0]
	v_pk_mul_f32 v[18:19], v[116:117], v[174:175] op_sel_hi:[1,0]
	v_pk_mul_f32 v[20:21], v[118:119], v[176:177] op_sel_hi:[1,0]
	v_pk_mul_f32 v[22:23], v[120:121], v[176:177] op_sel_hi:[1,0]
	v_max3_f32 v15, v15, |v16|, |v20|
	v_max3_f32 v13, v13, |v17|, |v21|
	v_max3_f32 v9, v9, |v18|, |v22|
	v_max3_f32 v7, v7, |v19|, |v23|
	s_add_u32 s6, s6, 0x16000
	s_addc_u32 s7, s7, 0
	global_load_dwordx4 v[114:117], v250, s[6:7] nt
	global_load_dword v174, v251, s[8:9] offset:1120
	s_add_u32 s6, s6, 0x16000
	s_addc_u32 s7, s7, 0
	global_load_dwordx4 v[118:121], v250, s[6:7] nt
	global_load_dword v176, v251, s[8:9] offset:1152
	s_waitcnt vmcnt(28)
	v_pk_mul_f32 v[16:17], v[122:123], v[178:179] op_sel_hi:[1,0]
	v_pk_mul_f32 v[18:19], v[124:125], v[178:179] op_sel_hi:[1,0]
	v_pk_mul_f32 v[20:21], v[126:127], v[180:181] op_sel_hi:[1,0]
	v_pk_mul_f32 v[22:23], v[128:129], v[180:181] op_sel_hi:[1,0]
	v_max3_f32 v15, v15, |v16|, |v20|
	v_max3_f32 v13, v13, |v17|, |v21|
	v_max3_f32 v9, v9, |v18|, |v22|
	v_max3_f32 v7, v7, |v19|, |v23|
	s_add_u32 s6, s6, 0x16000
	s_addc_u32 s7, s7, 0
	global_load_dwordx4 v[122:125], v250, s[6:7] nt
	global_load_dword v178, v251, s[8:9] offset:1184
	s_add_u32 s6, s6, 0x16000
	s_addc_u32 s7, s7, 0
	global_load_dwordx4 v[126:129], v250, s[6:7] nt
	global_load_dword v180, v251, s[8:9] offset:1216
	s_waitcnt vmcnt(28)
	v_pk_mul_f32 v[16:17], v[130:131], v[182:183] op_sel_hi:[1,0]
	v_pk_mul_f32 v[18:19], v[132:133], v[182:183] op_sel_hi:[1,0]
	v_pk_mul_f32 v[20:21], v[134:135], v[184:185] op_sel_hi:[1,0]
	v_pk_mul_f32 v[22:23], v[136:137], v[184:185] op_sel_hi:[1,0]
	v_max3_f32 v15, v15, |v16|, |v20|
	v_max3_f32 v13, v13, |v17|, |v21|
	v_max3_f32 v9, v9, |v18|, |v22|
	v_max3_f32 v7, v7, |v19|, |v23|
	s_add_u32 s6, s6, 0x16000
	s_addc_u32 s7, s7, 0
	global_load_dwordx4 v[130:133], v250, s[6:7] nt
	global_load_dword v182, v251, s[8:9] offset:1248
	s_add_u32 s6, s6, 0x16000
	s_addc_u32 s7, s7, 0
	global_load_dwordx4 v[134:137], v250, s[6:7] nt
	global_load_dword v184, v251, s[8:9] offset:1280
	s_waitcnt vmcnt(28)
;     ...
; #pragma unroll 2
;     for (int kb = 0; kb < D / 64; ++kb) {
; #pragma unroll
;         for (int i = 0; i < 8; ++i) { const int k = 64 * kb + 8 * i + kr; const f32x4 v = __builtin_nontemporal_load((const f32x4*)(W + (size_t)k * pitch)) * g[k];
;             mx[0] = __builtin_fmaxf(mx[0], __builtin_fabsf(v[0])); mx[1] = __builtin_fmaxf(mx[1], __builtin_fabsf(v[1])); mx[2] = __builtin_fmaxf(mx[2], __builtin_fabsf(v[2])); mx[3] = __builtin_fmaxf(mx[3], __builtin_fabsf(v[3])); } }
	v_pk_mul_f32 v[16:17], v[138:139], v[186:187] op_sel_hi:[1,0]
	v_pk_mul_f32 v[18:19], v[140:141], v[186:187] op_sel_hi:[1,0]
	v_pk_mul_f32 v[20:21], v[142:143], v[188:189] op_sel_hi:[1,0]
	v_pk_mul_f32 v[22:23], v[144:145], v[188:189] op_sel_hi:[1,0]
	v_max3_f32 v15, v15, |v16|, |v20|
	v_max3_f32 v13, v13, |v17|, |v21|
	v_max3_f32 v9, v9, |v18|, |v22|
	v_max3_f32 v7, v7, |v19|, |v23|
	s_add_u32 s6, s6, 0x16000
	s_addc_u32 s7, s7, 0
	global_load_dwordx4 v[138:141], v250, s[6:7] nt
	global_load_dword v186, v251, s[8:9] offset:1312
	s_add_u32 s6, s6, 0x16000
	s_addc_u32 s7, s7, 0
	global_load_dwordx4 v[142:145], v250, s[6:7] nt
	global_load_dword v188, v251, s[8:9] offset:1344
	s_waitcnt vmcnt(28)
	v_pk_mul_f32 v[16:17], v[146:147], v[190:191] op_sel_hi:[1,0]
	v_pk_mul_f32 v[18:19], v[148:149], v[190:191] op_sel_hi:[1,0]
	v_pk_mul_f32 v[20:21], v[150:151], v[192:193] op_sel_hi:[1,0]
	v_pk_mul_f32 v[22:23], v[152:153], v[192:193] op_sel_hi:[1,0]
	v_max3_f32 v15, v15, |v16|, |v20|
	v_max3_f32 v13, v13, |v17|, |v21|
	v_max3_f32 v9, v9, |v18|, |v22|
	v_max3_f32 v7, v7, |v19|, |v23|
	s_add_u32 s6, s6, 0x16000
	s_addc_u32 s7, s7, 0
	global_load_dwordx4 v[146:149], v250, s[6:7] nt
	global_load_dword v190, v251, s[8:9] offset:1376
	s_add_u32 s6, s6, 0x16000
	s_addc_u32 s7, s7, 0
	global_load_dwordx4 v[150:153], v250, s[6:7] nt
	global_load_dword v192, v251, s[8:9] offset:1408
	s_waitcnt vmcnt(28)
	v_pk_mul_f32 v[16:17], v[154:155], v[194:195] op_sel_hi:[1,0]
	v_pk_mul_f32 v[18:19], v[156:157], v[194:195] op_sel_hi:[1,0]
	v_pk_mul_f32 v[20:21], v[158:159], v[196:197] op_sel_hi:[1,0]
	v_pk_mul_f32 v[22:23], v[160:161], v[196:197] op_sel_hi:[1,0]
	v_max3_f32 v15, v15, |v16|, |v20|
	v_max3_f32 v13, v13, |v17|, |v21|
	v_max3_f32 v9, v9, |v18|, |v22|
	v_max3_f32 v7, v7, |v19|, |v23|
	s_add_u32 s6, s6, 0x16000
	s_addc_u32 s7, s7, 0
	global_load_dwordx4 v[154:157], v250, s[6:7] nt
	global_load_dword v194, v251, s[8:9] offset:1440
	s_add_u32 s6, s6, 0x16000
	s_addc_u32 s7, s7, 0
	global_load_dwordx4 v[158:161], v250, s[6:7] nt
	global_load_dword v196, v251, s[8:9] offset:1472
	s_waitcnt vmcnt(28)
	v_pk_mul_f32 v[16:17], v[162:163], v[198:199] op_sel_hi:[1,0]
	v_pk_mul_f32 v[18:19], v[164:165], v[198:199] op_sel_hi:[1,0]
	v_pk_mul_f32 v[20:21], v[166:167], v[200:201] op_sel_hi:[1,0]
	v_pk_mul_f32 v[22:23], v[168:169], v[200:201] op_sel_hi:[1,0]
	v_max3_f32 v15, v15, |v16|, |v20|
	v_max3_f32 v13, v13, |v17|, |v21|
	v_max3_f32 v9, v9, |v18|, |v22|
	v_max3_f32 v7, v7, |v19|, |v23|
	s_add_u32 s6, s6, 0x16000
	s_addc_u32 s7, s7, 0
	global_load_dwordx4 v[162:165], v250, s[6:7] nt
	global_load_dword v198, v251, s[8:9] offset:1504
	s_add_u32 s6, s6, 0x16000
	s_addc_u32 s7, s7, 0
	global_load_dwordx4 v[166:169], v250, s[6:7] nt
	global_load_dword v200, v251, s[8:9] offset:1536
	s_waitcnt vmcnt(28)
	v_pk_mul_f32 v[16:17], v[106:107], v[170:171] op_sel_hi:[1,0]
	v_pk_mul_f32 v[18:19], v[108:109], v[170:171] op_sel_hi:[1,0]
	v_pk_mul_f32 v[20:21], v[110:111], v[172:173] op_sel_hi:[1,0]
	v_pk_mul_f32 v[22:23], v[112:113], v[172:173] op_sel_hi:[1,0]
	v_max3_f32 v15, v15, |v16|, |v20|
	v_max3_f32 v13, v13, |v17|, |v21|
	v_max3_f32 v9, v9, |v18|, |v22|
	v_max3_f32 v7, v7, |v19|, |v23|
	s_add_u32 s6, s6, 0x16000
	s_addc_u32 s7, s7, 0
	global_load_dwordx4 v[106:109], v250, s[6:7] nt
	global_load_dword v170, v251, s[8:9] offset:1568
	s_add_u32 s6, s6, 0x16000
	s_addc_u32 s7, s7, 0
	global_load_dwordx4 v[110:113], v250, s[6:7] nt
	global_load_dword v172, v251, s[8:9] offset:1600
	s_waitcnt vmcnt(28)
	v_pk_mul_f32 v[16:17], v[114:115], v[174:175] op_sel_hi:[1,0]
	v_pk_mul_f32 v[18:19], v[116:117], v[174:175] op_sel_hi:[1,0]
	v_pk_mul_f32 v[20:21], v[118:119], v[176:177] op_sel_hi:[1,0]
	v_pk_mul_f32 v[22:23], v[120:121], v[176:177] op_sel_hi:[1,0]
	v_max3_f32 v15, v15, |v16|, |v20|
	v_max3_f32 v13, v13, |v17|, |v21|
	v_max3_f32 v9, v9, |v18|, |v22|
	v_max3_f32 v7, v7, |v19|, |v23|
	s_add_u32 s6, s6, 0x16000
	s_addc_u32 s7, s7, 0
	global_load_dwordx4 v[114:117], v250, s[6:7] nt
	global_load_dword v174, v251, s[8:9] offset:1632
	s_add_u32 s6, s6, 0x16000
	s_addc_u32 s7, s7, 0
	global_load_dwordx4 v[118:121], v250, s[6:7] nt
	global_load_dword v176, v251, s[8:9] offset:1664
	s_waitcnt vmcnt(28)
	v_pk_mul_f32 v[16:17], v[122:123], v[178:179] op_sel_hi:[1,0]
	v_pk_mul_f32 v[18:19], v[124:125], v[178:179] op_sel_hi:[1,0]
	v_pk_mul_f32 v[20:21], v[126:127], v[180:181] op_sel_hi:[1,0]
	v_pk_mul_f32 v[22:23], v[128:129], v[180:181] op_sel_hi:[1,0]
	v_max3_f32 v15, v15, |v16|, |v20|
	v_max3_f32 v13, v13, |v17|, |v21|
	v_max3_f32 v9, v9, |v18|, |v22|
	v_max3_f32 v7, v7, |v19|, |v23|
	s_add_u32 s6, s6, 0x16000
	s_addc_u32 s7, s7, 0
	global_load_dwordx4 v[122:125], v250, s[6:7] nt
	global_load_dword v178, v251, s[8:9] offset:1696
	s_add_u32 s6, s6, 0x16000
	s_addc_u32 s7, s7, 0
	global_load_dwordx4 v[126:129], v250, s[6:7] nt
	global_load_dword v180, v251, s[8:9] offset:1728
	s_waitcnt vmcnt(28)
	v_pk_mul_f32 v[16:17], v[130:131], v[182:183] op_sel_hi:[1,0]
	v_pk_mul_f32 v[18:19], v[132:133], v[182:183] op_sel_hi:[1,0]
	v_pk_mul_f32 v[20:21], v[134:135], v[184:185] op_sel_hi:[1,0]
	v_pk_mul_f32 v[22:23], v[136:137], v[184:185] op_sel_hi:[1,0]
	v_max3_f32 v15, v15, |v16|, |v20|
	v_max3_f32 v13, v13, |v17|, |v21|
	v_max3_f32 v9, v9, |v18|, |v22|
	v_max3_f32 v7, v7, |v19|, |v23|
	s_add_u32 s6, s6, 0x16000
	s_addc_u32 s7, s7, 0
	global_load_dwordx4 v[130:133], v250, s[6:7] nt
	global_load_dword v182, v251, s[8:9] offset:1760
	s_add_u32 s6, s6, 0x16000
	s_addc_u32 s7, s7, 0
	global_load_dwordx4 v[134:137], v250, s[6:7] nt
	global_load_dword v184, v251, s[8:9] offset:1792
	s_waitcnt vmcnt(28)
;     ...
; #pragma unroll 2
;     for (int kb = 0; kb < D / 64; ++kb) {
; #pragma unroll
;         for (int i = 0; i < 8; ++i) { const int k = 64 * kb + 8 * i + kr; const f32x4 v = __builtin_nontemporal_load((const f32x4*)(W + (size_t)k * pitch)) * g[k];
;             mx[0] = __builtin_fmaxf(mx[0], __builtin_fabsf(v[0])); mx[1] = __builtin_fmaxf(mx[1], __builtin_fabsf(v[1])); mx[2] = __builtin_fmaxf(mx[2], __builtin_fabsf(v[2])); mx[3] = __builtin_fmaxf(mx[3], __builtin_fabsf(v[3])); } }
	v_pk_mul_f32 v[16:17], v[138:139], v[186:187] op_sel_hi:[1,0]
	v_pk_mul_f32 v[18:19], v[140:141], v[186:187] op_sel_hi:[1,0]
	v_pk_mul_f32 v[20:21], v[142:143], v[188:189] op_sel_hi:[1,0]
	v_pk_mul_f32 v[22:23], v[144:145], v[188:189] op_sel_hi:[1,0]
	v_max3_f32 v15, v15, |v16|, |v20|
	v_max3_f32 v13, v13, |v17|, |v21|
	v_max3_f32 v9, v9, |v18|, |v22|
	v_max3_f32 v7, v7, |v19|, |v23|
	s_add_u32 s6, s6, 0x16000
	s_addc_u32 s7, s7, 0
	global_load_dwordx4 v[138:141], v250, s[6:7] nt
	global_load_dword v186, v251, s[8:9] offset:1824
	s_add_u32 s6, s6, 0x16000
	s_addc_u32 s7, s7, 0
	global_load_dwordx4 v[142:145], v250, s[6:7] nt
	global_load_dword v188, v251, s[8:9] offset:1856
	s_waitcnt vmcnt(28)
	v_pk_mul_f32 v[16:17], v[146:147], v[190:191] op_sel_hi:[1,0]
	v_pk_mul_f32 v[18:19], v[148:149], v[190:191] op_sel_hi:[1,0]
	v_pk_mul_f32 v[20:21], v[150:151], v[192:193] op_sel_hi:[1,0]
	v_pk_mul_f32 v[22:23], v[152:153], v[192:193] op_sel_hi:[1,0]
	v_max3_f32 v15, v15, |v16|, |v20|
	v_max3_f32 v13, v13, |v17|, |v21|
	v_max3_f32 v9, v9, |v18|, |v22|
	v_max3_f32 v7, v7, |v19|, |v23|
	s_add_u32 s6, s6, 0x16000
	s_addc_u32 s7, s7, 0
	global_load_dwordx4 v[146:149], v250, s[6:7] nt
	global_load_dword v190, v251, s[8:9] offset:1888
	s_add_u32 s6, s6, 0x16000
	s_addc_u32 s7, s7, 0
	global_load_dwordx4 v[150:153], v250, s[6:7] nt
	global_load_dword v192, v251, s[8:9] offset:1920
	s_waitcnt vmcnt(28)
	v_pk_mul_f32 v[16:17], v[154:155], v[194:195] op_sel_hi:[1,0]
	v_pk_mul_f32 v[18:19], v[156:157], v[194:195] op_sel_hi:[1,0]
	v_pk_mul_f32 v[20:21], v[158:159], v[196:197] op_sel_hi:[1,0]
	v_pk_mul_f32 v[22:23], v[160:161], v[196:197] op_sel_hi:[1,0]
	v_max3_f32 v15, v15, |v16|, |v20|
	v_max3_f32 v13, v13, |v17|, |v21|
	v_max3_f32 v9, v9, |v18|, |v22|
	v_max3_f32 v7, v7, |v19|, |v23|
	s_add_u32 s6, s6, 0x16000
	s_addc_u32 s7, s7, 0
	global_load_dwordx4 v[154:157], v250, s[6:7] nt
	global_load_dword v194, v251, s[8:9] offset:1952
	s_add_u32 s6, s6, 0x16000
	s_addc_u32 s7, s7, 0
	global_load_dwordx4 v[158:161], v250, s[6:7] nt
	global_load_dword v196, v251, s[8:9] offset:1984
	s_waitcnt vmcnt(28)
	v_pk_mul_f32 v[16:17], v[162:163], v[198:199] op_sel_hi:[1,0]
	v_pk_mul_f32 v[18:19], v[164:165], v[198:199] op_sel_hi:[1,0]
	v_pk_mul_f32 v[20:21], v[166:167], v[200:201] op_sel_hi:[1,0]
	v_pk_mul_f32 v[22:23], v[168:169], v[200:201] op_sel_hi:[1,0]
	v_max3_f32 v15, v15, |v16|, |v20|
	v_max3_f32 v13, v13, |v17|, |v21|
	v_max3_f32 v9, v9, |v18|, |v22|
	v_max3_f32 v7, v7, |v19|, |v23|
	s_add_u32 s6, s6, 0x16000
	s_addc_u32 s7, s7, 0
	global_load_dwordx4 v[162:165], v250, s[6:7] nt
	global_load_dword v198, v251, s[8:9] offset:2016
	s_add_u32 s6, s6, 0x16000
	s_addc_u32 s7, s7, 0
	global_load_dwordx4 v[166:169], v250, s[6:7] nt
	global_load_dword v200, v251, s[8:9] offset:2048
	s_waitcnt vmcnt(28)
	v_pk_mul_f32 v[16:17], v[106:107], v[170:171] op_sel_hi:[1,0]
	v_pk_mul_f32 v[18:19], v[108:109], v[170:171] op_sel_hi:[1,0]
	v_pk_mul_f32 v[20:21], v[110:111], v[172:173] op_sel_hi:[1,0]
	v_pk_mul_f32 v[22:23], v[112:113], v[172:173] op_sel_hi:[1,0]
	v_max3_f32 v15, v15, |v16|, |v20|
	v_max3_f32 v13, v13, |v17|, |v21|
	v_max3_f32 v9, v9, |v18|, |v22|
	v_max3_f32 v7, v7, |v19|, |v23|
	s_add_u32 s6, s6, 0x16000
	s_addc_u32 s7, s7, 0
	global_load_dwordx4 v[106:109], v250, s[6:7] nt
	global_load_dword v170, v251, s[8:9] offset:2080
	s_add_u32 s6, s6, 0x16000
	s_addc_u32 s7, s7, 0
	global_load_dwordx4 v[110:113], v250, s[6:7] nt
	global_load_dword v172, v251, s[8:9] offset:2112
	s_waitcnt vmcnt(28)
	v_pk_mul_f32 v[16:17], v[114:115], v[174:175] op_sel_hi:[1,0]
	v_pk_mul_f32 v[18:19], v[116:117], v[174:175] op_sel_hi:[1,0]
	v_pk_mul_f32 v[20:21], v[118:119], v[176:177] op_sel_hi:[1,0]
	v_pk_mul_f32 v[22:23], v[120:121], v[176:177] op_sel_hi:[1,0]
	v_max3_f32 v15, v15, |v16|, |v20|
	v_max3_f32 v13, v13, |v17|, |v21|
	v_max3_f32 v9, v9, |v18|, |v22|
	v_max3_f32 v7, v7, |v19|, |v23|
	s_add_u32 s6, s6, 0x16000
	s_addc_u32 s7, s7, 0
	global_load_dwordx4 v[114:117], v250, s[6:7] nt
	global_load_dword v174, v251, s[8:9] offset:2144
	s_add_u32 s6, s6, 0x16000
	s_addc_u32 s7, s7, 0
	global_load_dwordx4 v[118:121], v250, s[6:7] nt
	global_load_dword v176, v251, s[8:9] offset:2176
	s_waitcnt vmcnt(28)
	v_pk_mul_f32 v[16:17], v[122:123], v[178:179] op_sel_hi:[1,0]
	v_pk_mul_f32 v[18:19], v[124:125], v[178:179] op_sel_hi:[1,0]
	v_pk_mul_f32 v[20:21], v[126:127], v[180:181] op_sel_hi:[1,0]
	v_pk_mul_f32 v[22:23], v[128:129], v[180:181] op_sel_hi:[1,0]
	v_max3_f32 v15, v15, |v16|, |v20|
	v_max3_f32 v13, v13, |v17|, |v21|
	v_max3_f32 v9, v9, |v18|, |v22|
	v_max3_f32 v7, v7, |v19|, |v23|
	s_add_u32 s6, s6, 0x16000
	s_addc_u32 s7, s7, 0
	global_load_dwordx4 v[122:125], v250, s[6:7] nt
	global_load_dword v178, v251, s[8:9] offset:2208
	s_add_u32 s6, s6, 0x16000
	s_addc_u32 s7, s7, 0
	global_load_dwordx4 v[126:129], v250, s[6:7] nt
	global_load_dword v180, v251, s[8:9] offset:2240
	s_waitcnt vmcnt(28)
	v_pk_mul_f32 v[16:17], v[130:131], v[182:183] op_sel_hi:[1,0]
	v_pk_mul_f32 v[18:19], v[132:133], v[182:183] op_sel_hi:[1,0]
	v_pk_mul_f32 v[20:21], v[134:135], v[184:185] op_sel_hi:[1,0]
	v_pk_mul_f32 v[22:23], v[136:137], v[184:185] op_sel_hi:[1,0]
	v_max3_f32 v15, v15, |v16|, |v20|
	v_max3_f32 v13, v13, |v17|, |v21|
	v_max3_f32 v9, v9, |v18|, |v22|
	v_max3_f32 v7, v7, |v19|, |v23|
	s_add_u32 s6, s6, 0x16000
	s_addc_u32 s7, s7, 0
	global_load_dwordx4 v[130:133], v250, s[6:7] nt
	global_load_dword v182, v251, s[8:9] offset:2272
	s_add_u32 s6, s6, 0x16000
	s_addc_u32 s7, s7, 0
	global_load_dwordx4 v[134:137], v250, s[6:7] nt
	global_load_dword v184, v251, s[8:9] offset:2304
	s_waitcnt vmcnt(28)
;     ...
; #pragma unroll 2
;     for (int kb = 0; kb < D / 64; ++kb) {
; #pragma unroll
;         for (int i = 0; i < 8; ++i) { const int k = 64 * kb + 8 * i + kr; const f32x4 v = __builtin_nontemporal_load((const f32x4*)(W + (size_t)k * pitch)) * g[k];
;             mx[0] = __builtin_fmaxf(mx[0], __builtin_fabsf(v[0])); mx[1] = __builtin_fmaxf(mx[1], __builtin_fabsf(v[1])); mx[2] = __builtin_fmaxf(mx[2], __builtin_fabsf(v[2])); mx[3] = __builtin_fmaxf(mx[3], __builtin_fabsf(v[3])); } }
	v_pk_mul_f32 v[16:17], v[138:139], v[186:187] op_sel_hi:[1,0]
	v_pk_mul_f32 v[18:19], v[140:141], v[186:187] op_sel_hi:[1,0]
	v_pk_mul_f32 v[20:21], v[142:143], v[188:189] op_sel_hi:[1,0]
	v_pk_mul_f32 v[22:23], v[144:145], v[188:189] op_sel_hi:[1,0]
	v_max3_f32 v15, v15, |v16|, |v20|
	v_max3_f32 v13, v13, |v17|, |v21|
	v_max3_f32 v9, v9, |v18|, |v22|
	v_max3_f32 v7, v7, |v19|, |v23|
	s_add_u32 s6, s6, 0x16000
	s_addc_u32 s7, s7, 0
	global_load_dwordx4 v[138:141], v250, s[6:7] nt
	global_load_dword v186, v251, s[8:9] offset:2336
	s_add_u32 s6, s6, 0x16000
	s_addc_u32 s7, s7, 0
	global_load_dwordx4 v[142:145], v250, s[6:7] nt
	global_load_dword v188, v251, s[8:9] offset:2368
	s_waitcnt vmcnt(28)
	v_pk_mul_f32 v[16:17], v[146:147], v[190:191] op_sel_hi:[1,0]
	v_pk_mul_f32 v[18:19], v[148:149], v[190:191] op_sel_hi:[1,0]
	v_pk_mul_f32 v[20:21], v[150:151], v[192:193] op_sel_hi:[1,0]
	v_pk_mul_f32 v[22:23], v[152:153], v[192:193] op_sel_hi:[1,0]
	v_max3_f32 v15, v15, |v16|, |v20|
	v_max3_f32 v13, v13, |v17|, |v21|
	v_max3_f32 v9, v9, |v18|, |v22|
	v_max3_f32 v7, v7, |v19|, |v23|
	s_add_u32 s6, s6, 0x16000
	s_addc_u32 s7, s7, 0
	global_load_dwordx4 v[146:149], v250, s[6:7] nt
	global_load_dword v190, v251, s[8:9] offset:2400
	s_add_u32 s6, s6, 0x16000
	s_addc_u32 s7, s7, 0
	global_load_dwordx4 v[150:153], v250, s[6:7] nt
	global_load_dword v192, v251, s[8:9] offset:2432
	s_waitcnt vmcnt(28)
	v_pk_mul_f32 v[16:17], v[154:155], v[194:195] op_sel_hi:[1,0]
	v_pk_mul_f32 v[18:19], v[156:157], v[194:195] op_sel_hi:[1,0]
	v_pk_mul_f32 v[20:21], v[158:159], v[196:197] op_sel_hi:[1,0]
	v_pk_mul_f32 v[22:23], v[160:161], v[196:197] op_sel_hi:[1,0]
	v_max3_f32 v15, v15, |v16|, |v20|
	v_max3_f32 v13, v13, |v17|, |v21|
	v_max3_f32 v9, v9, |v18|, |v22|
	v_max3_f32 v7, v7, |v19|, |v23|
	s_add_u32 s6, s6, 0x16000
	s_addc_u32 s7, s7, 0
	global_load_dwordx4 v[154:157], v250, s[6:7] nt
	global_load_dword v194, v251, s[8:9] offset:2464
	s_add_u32 s6, s6, 0x16000
	s_addc_u32 s7, s7, 0
	global_load_dwordx4 v[158:161], v250, s[6:7] nt
	global_load_dword v196, v251, s[8:9] offset:2496
	s_waitcnt vmcnt(28)
	v_pk_mul_f32 v[16:17], v[162:163], v[198:199] op_sel_hi:[1,0]
	v_pk_mul_f32 v[18:19], v[164:165], v[198:199] op_sel_hi:[1,0]
	v_pk_mul_f32 v[20:21], v[166:167], v[200:201] op_sel_hi:[1,0]
	v_pk_mul_f32 v[22:23], v[168:169], v[200:201] op_sel_hi:[1,0]
	v_max3_f32 v15, v15, |v16|, |v20|
	v_max3_f32 v13, v13, |v17|, |v21|
	v_max3_f32 v9, v9, |v18|, |v22|
	v_max3_f32 v7, v7, |v19|, |v23|
	s_add_u32 s6, s6, 0x16000
	s_addc_u32 s7, s7, 0
	global_load_dwordx4 v[162:165], v250, s[6:7] nt
	global_load_dword v198, v251, s[8:9] offset:2528
	s_add_u32 s6, s6, 0x16000
	s_addc_u32 s7, s7, 0
	global_load_dwordx4 v[166:169], v250, s[6:7] nt
	global_load_dword v200, v251, s[8:9] offset:2560
	s_waitcnt vmcnt(28)
	v_pk_mul_f32 v[16:17], v[106:107], v[170:171] op_sel_hi:[1,0]
	v_pk_mul_f32 v[18:19], v[108:109], v[170:171] op_sel_hi:[1,0]
	v_pk_mul_f32 v[20:21], v[110:111], v[172:173] op_sel_hi:[1,0]
	v_pk_mul_f32 v[22:23], v[112:113], v[172:173] op_sel_hi:[1,0]
	v_max3_f32 v15, v15, |v16|, |v20|
	v_max3_f32 v13, v13, |v17|, |v21|
	v_max3_f32 v9, v9, |v18|, |v22|
	v_max3_f32 v7, v7, |v19|, |v23|
	s_add_u32 s6, s6, 0x16000
	s_addc_u32 s7, s7, 0
	global_load_dwordx4 v[106:109], v250, s[6:7] nt
	global_load_dword v170, v251, s[8:9] offset:2592
	s_add_u32 s6, s6, 0x16000
	s_addc_u32 s7, s7, 0
	global_load_dwordx4 v[110:113], v250, s[6:7] nt
	global_load_dword v172, v251, s[8:9] offset:2624
	s_waitcnt vmcnt(28)
	v_pk_mul_f32 v[16:17], v[114:115], v[174:175] op_sel_hi:[1,0]
	v_pk_mul_f32 v[18:19], v[116:117], v[174:175] op_sel_hi:[1,0]
	v_pk_mul_f32 v[20:21], v[118:119], v[176:177] op_sel_hi:[1,0]
	v_pk_mul_f32 v[22:23], v[120:121], v[176:177] op_sel_hi:[1,0]
	v_max3_f32 v15, v15, |v16|, |v20|
	v_max3_f32 v13, v13, |v17|, |v21|
	v_max3_f32 v9, v9, |v18|, |v22|
	v_max3_f32 v7, v7, |v19|, |v23|
	s_add_u32 s6, s6, 0x16000
	s_addc_u32 s7, s7, 0
	global_load_dwordx4 v[114:117], v250, s[6:7] nt
	global_load_dword v174, v251, s[8:9] offset:2656
	s_add_u32 s6, s6, 0x16000
	s_addc_u32 s7, s7, 0
	global_load_dwordx4 v[118:121], v250, s[6:7] nt
	global_load_dword v176, v251, s[8:9] offset:2688
	s_waitcnt vmcnt(28)
	v_pk_mul_f32 v[16:17], v[122:123], v[178:179] op_sel_hi:[1,0]
	v_pk_mul_f32 v[18:19], v[124:125], v[178:179] op_sel_hi:[1,0]
	v_pk_mul_f32 v[20:21], v[126:127], v[180:181] op_sel_hi:[1,0]
	v_pk_mul_f32 v[22:23], v[128:129], v[180:181] op_sel_hi:[1,0]
	v_max3_f32 v15, v15, |v16|, |v20|
	v_max3_f32 v13, v13, |v17|, |v21|
	v_max3_f32 v9, v9, |v18|, |v22|
	v_max3_f32 v7, v7, |v19|, |v23|
	s_add_u32 s6, s6, 0x16000
	s_addc_u32 s7, s7, 0
	global_load_dwordx4 v[122:125], v250, s[6:7] nt
	global_load_dword v178, v251, s[8:9] offset:2720
	s_add_u32 s6, s6, 0x16000
	s_addc_u32 s7, s7, 0
	global_load_dwordx4 v[126:129], v250, s[6:7] nt
	global_load_dword v180, v251, s[8:9] offset:2752
	s_waitcnt vmcnt(28)
	v_pk_mul_f32 v[16:17], v[130:131], v[182:183] op_sel_hi:[1,0]
	v_pk_mul_f32 v[18:19], v[132:133], v[182:183] op_sel_hi:[1,0]
	v_pk_mul_f32 v[20:21], v[134:135], v[184:185] op_sel_hi:[1,0]
	v_pk_mul_f32 v[22:23], v[136:137], v[184:185] op_sel_hi:[1,0]
	v_max3_f32 v15, v15, |v16|, |v20|
	v_max3_f32 v13, v13, |v17|, |v21|
	v_max3_f32 v9, v9, |v18|, |v22|
	v_max3_f32 v7, v7, |v19|, |v23|
	s_add_u32 s6, s6, 0x16000
	s_addc_u32 s7, s7, 0
	global_load_dwordx4 v[130:133], v250, s[6:7] nt
	global_load_dword v182, v251, s[8:9] offset:2784
	s_add_u32 s6, s6, 0x16000
	s_addc_u32 s7, s7, 0
	global_load_dwordx4 v[134:137], v250, s[6:7] nt
	global_load_dword v184, v251, s[8:9] offset:2816
	s_waitcnt vmcnt(28)
;     ...
; #pragma unroll 2
;     for (int kb = 0; kb < D / 64; ++kb) {
; #pragma unroll
;         for (int i = 0; i < 8; ++i) { const int k = 64 * kb + 8 * i + kr; const f32x4 v = __builtin_nontemporal_load((const f32x4*)(W + (size_t)k * pitch)) * g[k];
;             mx[0] = __builtin_fmaxf(mx[0], __builtin_fabsf(v[0])); mx[1] = __builtin_fmaxf(mx[1], __builtin_fabsf(v[1])); mx[2] = __builtin_fmaxf(mx[2], __builtin_fabsf(v[2])); mx[3] = __builtin_fmaxf(mx[3], __builtin_fabsf(v[3])); } }
	v_pk_mul_f32 v[16:17], v[138:139], v[186:187] op_sel_hi:[1,0]
	v_pk_mul_f32 v[18:19], v[140:141], v[186:187] op_sel_hi:[1,0]
	v_pk_mul_f32 v[20:21], v[142:143], v[188:189] op_sel_hi:[1,0]
	v_pk_mul_f32 v[22:23], v[144:145], v[188:189] op_sel_hi:[1,0]
	v_max3_f32 v15, v15, |v16|, |v20|
	v_max3_f32 v13, v13, |v17|, |v21|
	v_max3_f32 v9, v9, |v18|, |v22|
	v_max3_f32 v7, v7, |v19|, |v23|
	s_add_u32 s6, s6, 0x16000
	s_addc_u32 s7, s7, 0
	global_load_dwordx4 v[138:141], v250, s[6:7] nt
	global_load_dword v186, v251, s[8:9] offset:2848
	s_add_u32 s6, s6, 0x16000
	s_addc_u32 s7, s7, 0
	global_load_dwordx4 v[142:145], v250, s[6:7] nt
	global_load_dword v188, v251, s[8:9] offset:2880
	s_waitcnt vmcnt(28)
	v_pk_mul_f32 v[16:17], v[146:147], v[190:191] op_sel_hi:[1,0]
	v_pk_mul_f32 v[18:19], v[148:149], v[190:191] op_sel_hi:[1,0]
	v_pk_mul_f32 v[20:21], v[150:151], v[192:193] op_sel_hi:[1,0]
	v_pk_mul_f32 v[22:23], v[152:153], v[192:193] op_sel_hi:[1,0]
	v_max3_f32 v15, v15, |v16|, |v20|
	v_max3_f32 v13, v13, |v17|, |v21|
	v_max3_f32 v9, v9, |v18|, |v22|
	v_max3_f32 v7, v7, |v19|, |v23|
	s_add_u32 s6, s6, 0x16000
	s_addc_u32 s7, s7, 0
	global_load_dwordx4 v[146:149], v250, s[6:7] nt
	global_load_dword v190, v251, s[8:9] offset:2912
	s_add_u32 s6, s6, 0x16000
	s_addc_u32 s7, s7, 0
	global_load_dwordx4 v[150:153], v250, s[6:7] nt
	global_load_dword v192, v251, s[8:9] offset:2944
	s_waitcnt vmcnt(28)
	v_pk_mul_f32 v[16:17], v[154:155], v[194:195] op_sel_hi:[1,0]
	v_pk_mul_f32 v[18:19], v[156:157], v[194:195] op_sel_hi:[1,0]
	v_pk_mul_f32 v[20:21], v[158:159], v[196:197] op_sel_hi:[1,0]
	v_pk_mul_f32 v[22:23], v[160:161], v[196:197] op_sel_hi:[1,0]
	v_max3_f32 v15, v15, |v16|, |v20|
	v_max3_f32 v13, v13, |v17|, |v21|
	v_max3_f32 v9, v9, |v18|, |v22|
	v_max3_f32 v7, v7, |v19|, |v23|
	s_add_u32 s6, s6, 0x16000
	s_addc_u32 s7, s7, 0
	global_load_dwordx4 v[154:157], v250, s[6:7] nt
	global_load_dword v194, v251, s[8:9] offset:2976
	s_add_u32 s6, s6, 0x16000
	s_addc_u32 s7, s7, 0
	global_load_dwordx4 v[158:161], v250, s[6:7] nt
	global_load_dword v196, v251, s[8:9] offset:3008
	s_waitcnt vmcnt(28)
	v_pk_mul_f32 v[16:17], v[162:163], v[198:199] op_sel_hi:[1,0]
	v_pk_mul_f32 v[18:19], v[164:165], v[198:199] op_sel_hi:[1,0]
	v_pk_mul_f32 v[20:21], v[166:167], v[200:201] op_sel_hi:[1,0]
	v_pk_mul_f32 v[22:23], v[168:169], v[200:201] op_sel_hi:[1,0]
	v_max3_f32 v15, v15, |v16|, |v20|
	v_max3_f32 v13, v13, |v17|, |v21|
	v_max3_f32 v9, v9, |v18|, |v22|
	v_max3_f32 v7, v7, |v19|, |v23|
	s_add_u32 s6, s6, 0x16000
	s_addc_u32 s7, s7, 0
	global_load_dwordx4 v[162:165], v250, s[6:7] nt
	global_load_dword v198, v251, s[8:9] offset:3040
	s_add_u32 s6, s6, 0x16000
	s_addc_u32 s7, s7, 0
	global_load_dwordx4 v[166:169], v250, s[6:7] nt
	global_load_dword v200, v251, s[8:9] offset:3072
	s_waitcnt vmcnt(28)
	v_pk_mul_f32 v[16:17], v[106:107], v[170:171] op_sel_hi:[1,0]
	v_pk_mul_f32 v[18:19], v[108:109], v[170:171] op_sel_hi:[1,0]
	v_pk_mul_f32 v[20:21], v[110:111], v[172:173] op_sel_hi:[1,0]
	v_pk_mul_f32 v[22:23], v[112:113], v[172:173] op_sel_hi:[1,0]
	v_max3_f32 v15, v15, |v16|, |v20|
	v_max3_f32 v13, v13, |v17|, |v21|
	v_max3_f32 v9, v9, |v18|, |v22|
	v_max3_f32 v7, v7, |v19|, |v23|
	s_add_u32 s6, s6, 0x16000
	s_addc_u32 s7, s7, 0
	global_load_dwordx4 v[106:109], v250, s[6:7] nt
	global_load_dword v170, v251, s[8:9] offset:3104
	s_add_u32 s6, s6, 0x16000
	s_addc_u32 s7, s7, 0
	global_load_dwordx4 v[110:113], v250, s[6:7] nt
	global_load_dword v172, v251, s[8:9] offset:3136
	s_waitcnt vmcnt(28)
	v_pk_mul_f32 v[16:17], v[114:115], v[174:175] op_sel_hi:[1,0]
	v_pk_mul_f32 v[18:19], v[116:117], v[174:175] op_sel_hi:[1,0]
	v_pk_mul_f32 v[20:21], v[118:119], v[176:177] op_sel_hi:[1,0]
	v_pk_mul_f32 v[22:23], v[120:121], v[176:177] op_sel_hi:[1,0]
	v_max3_f32 v15, v15, |v16|, |v20|
	v_max3_f32 v13, v13, |v17|, |v21|
	v_max3_f32 v9, v9, |v18|, |v22|
	v_max3_f32 v7, v7, |v19|, |v23|
	s_add_u32 s6, s6, 0x16000
	s_addc_u32 s7, s7, 0
	global_load_dwordx4 v[114:117], v250, s[6:7] nt
	global_load_dword v174, v251, s[8:9] offset:3168
	s_add_u32 s6, s6, 0x16000
	s_addc_u32 s7, s7, 0
	global_load_dwordx4 v[118:121], v250, s[6:7] nt
	global_load_dword v176, v251, s[8:9] offset:3200
	s_waitcnt vmcnt(28)
	v_pk_mul_f32 v[16:17], v[122:123], v[178:179] op_sel_hi:[1,0]
	v_pk_mul_f32 v[18:19], v[124:125], v[178:179] op_sel_hi:[1,0]
	v_pk_mul_f32 v[20:21], v[126:127], v[180:181] op_sel_hi:[1,0]
	v_pk_mul_f32 v[22:23], v[128:129], v[180:181] op_sel_hi:[1,0]
	v_max3_f32 v15, v15, |v16|, |v20|
	v_max3_f32 v13, v13, |v17|, |v21|
	v_max3_f32 v9, v9, |v18|, |v22|
	v_max3_f32 v7, v7, |v19|, |v23|
	s_add_u32 s6, s6, 0x16000
	s_addc_u32 s7, s7, 0
	global_load_dwordx4 v[122:125], v250, s[6:7] nt
	global_load_dword v178, v251, s[8:9] offset:3232
	s_add_u32 s6, s6, 0x16000
	s_addc_u32 s7, s7, 0
	global_load_dwordx4 v[126:129], v250, s[6:7] nt
	global_load_dword v180, v251, s[8:9] offset:3264
	s_waitcnt vmcnt(28)
	v_pk_mul_f32 v[16:17], v[130:131], v[182:183] op_sel_hi:[1,0]
	v_pk_mul_f32 v[18:19], v[132:133], v[182:183] op_sel_hi:[1,0]
	v_pk_mul_f32 v[20:21], v[134:135], v[184:185] op_sel_hi:[1,0]
	v_pk_mul_f32 v[22:23], v[136:137], v[184:185] op_sel_hi:[1,0]
	v_max3_f32 v15, v15, |v16|, |v20|
	v_max3_f32 v13, v13, |v17|, |v21|
	v_max3_f32 v9, v9, |v18|, |v22|
	v_max3_f32 v7, v7, |v19|, |v23|
	s_add_u32 s6, s6, 0x16000
	s_addc_u32 s7, s7, 0
	global_load_dwordx4 v[130:133], v250, s[6:7] nt
	global_load_dword v182, v251, s[8:9] offset:3296
	s_add_u32 s6, s6, 0x16000
	s_addc_u32 s7, s7, 0
	global_load_dwordx4 v[134:137], v250, s[6:7] nt
	global_load_dword v184, v251, s[8:9] offset:3328
	s_waitcnt vmcnt(28)
;     ...
; #pragma unroll 2
;     for (int kb = 0; kb < D / 64; ++kb) {
; #pragma unroll
;         for (int i = 0; i < 8; ++i) { const int k = 64 * kb + 8 * i + kr; const f32x4 v = __builtin_nontemporal_load((const f32x4*)(W + (size_t)k * pitch)) * g[k];
;             mx[0] = __builtin_fmaxf(mx[0], __builtin_fabsf(v[0])); mx[1] = __builtin_fmaxf(mx[1], __builtin_fabsf(v[1])); mx[2] = __builtin_fmaxf(mx[2], __builtin_fabsf(v[2])); mx[3] = __builtin_fmaxf(mx[3], __builtin_fabsf(v[3])); } }
	v_pk_mul_f32 v[16:17], v[138:139], v[186:187] op_sel_hi:[1,0]
	v_pk_mul_f32 v[18:19], v[140:141], v[186:187] op_sel_hi:[1,0]
	v_pk_mul_f32 v[20:21], v[142:143], v[188:189] op_sel_hi:[1,0]
	v_pk_mul_f32 v[22:23], v[144:145], v[188:189] op_sel_hi:[1,0]
	v_max3_f32 v15, v15, |v16|, |v20|
	v_max3_f32 v13, v13, |v17|, |v21|
	v_max3_f32 v9, v9, |v18|, |v22|
	v_max3_f32 v7, v7, |v19|, |v23|
	s_add_u32 s6, s6, 0x16000
	s_addc_u32 s7, s7, 0
	global_load_dwordx4 v[138:141], v250, s[6:7] nt
	global_load_dword v186, v251, s[8:9] offset:3360
	s_add_u32 s6, s6, 0x16000
	s_addc_u32 s7, s7, 0
	global_load_dwordx4 v[142:145], v250, s[6:7] nt
	global_load_dword v188, v251, s[8:9] offset:3392
	s_waitcnt vmcnt(28)
	v_pk_mul_f32 v[16:17], v[146:147], v[190:191] op_sel_hi:[1,0]
	v_pk_mul_f32 v[18:19], v[148:149], v[190:191] op_sel_hi:[1,0]
	v_pk_mul_f32 v[20:21], v[150:151], v[192:193] op_sel_hi:[1,0]
	v_pk_mul_f32 v[22:23], v[152:153], v[192:193] op_sel_hi:[1,0]
	v_max3_f32 v15, v15, |v16|, |v20|
	v_max3_f32 v13, v13, |v17|, |v21|
	v_max3_f32 v9, v9, |v18|, |v22|
	v_max3_f32 v7, v7, |v19|, |v23|
	s_add_u32 s6, s6, 0x16000
	s_addc_u32 s7, s7, 0
	global_load_dwordx4 v[146:149], v250, s[6:7] nt
	global_load_dword v190, v251, s[8:9] offset:3424
	s_add_u32 s6, s6, 0x16000
	s_addc_u32 s7, s7, 0
	global_load_dwordx4 v[150:153], v250, s[6:7] nt
	global_load_dword v192, v251, s[8:9] offset:3456
	s_waitcnt vmcnt(28)
	v_pk_mul_f32 v[16:17], v[154:155], v[194:195] op_sel_hi:[1,0]
	v_pk_mul_f32 v[18:19], v[156:157], v[194:195] op_sel_hi:[1,0]
	v_pk_mul_f32 v[20:21], v[158:159], v[196:197] op_sel_hi:[1,0]
	v_pk_mul_f32 v[22:23], v[160:161], v[196:197] op_sel_hi:[1,0]
	v_max3_f32 v15, v15, |v16|, |v20|
	v_max3_f32 v13, v13, |v17|, |v21|
	v_max3_f32 v9, v9, |v18|, |v22|
	v_max3_f32 v7, v7, |v19|, |v23|
	s_add_u32 s6, s6, 0x16000
	s_addc_u32 s7, s7, 0
	global_load_dwordx4 v[154:157], v250, s[6:7] nt
	global_load_dword v194, v251, s[8:9] offset:3488
	s_add_u32 s6, s6, 0x16000
	s_addc_u32 s7, s7, 0
	global_load_dwordx4 v[158:161], v250, s[6:7] nt
	global_load_dword v196, v251, s[8:9] offset:3520
	s_waitcnt vmcnt(28)
	v_pk_mul_f32 v[16:17], v[162:163], v[198:199] op_sel_hi:[1,0]
	v_pk_mul_f32 v[18:19], v[164:165], v[198:199] op_sel_hi:[1,0]
	v_pk_mul_f32 v[20:21], v[166:167], v[200:201] op_sel_hi:[1,0]
	v_pk_mul_f32 v[22:23], v[168:169], v[200:201] op_sel_hi:[1,0]
	v_max3_f32 v15, v15, |v16|, |v20|
	v_max3_f32 v13, v13, |v17|, |v21|
	v_max3_f32 v9, v9, |v18|, |v22|
	v_max3_f32 v7, v7, |v19|, |v23|
	s_add_u32 s6, s6, 0x16000
	s_addc_u32 s7, s7, 0
	global_load_dwordx4 v[162:165], v250, s[6:7] nt
	global_load_dword v198, v251, s[8:9] offset:3552
	s_add_u32 s6, s6, 0x16000
	s_addc_u32 s7, s7, 0
	global_load_dwordx4 v[166:169], v250, s[6:7] nt
	global_load_dword v200, v251, s[8:9] offset:3584
	s_waitcnt vmcnt(28)
	v_pk_mul_f32 v[16:17], v[106:107], v[170:171] op_sel_hi:[1,0]
	v_pk_mul_f32 v[18:19], v[108:109], v[170:171] op_sel_hi:[1,0]
	v_pk_mul_f32 v[20:21], v[110:111], v[172:173] op_sel_hi:[1,0]
	v_pk_mul_f32 v[22:23], v[112:113], v[172:173] op_sel_hi:[1,0]
	v_max3_f32 v15, v15, |v16|, |v20|
	v_max3_f32 v13, v13, |v17|, |v21|
	v_max3_f32 v9, v9, |v18|, |v22|
	v_max3_f32 v7, v7, |v19|, |v23|
	s_waitcnt vmcnt(24)
	v_pk_mul_f32 v[16:17], v[114:115], v[174:175] op_sel_hi:[1,0]
	v_pk_mul_f32 v[18:19], v[116:117], v[174:175] op_sel_hi:[1,0]
	v_pk_mul_f32 v[20:21], v[118:119], v[176:177] op_sel_hi:[1,0]
	v_pk_mul_f32 v[22:23], v[120:121], v[176:177] op_sel_hi:[1,0]
	v_max3_f32 v15, v15, |v16|, |v20|
	v_max3_f32 v13, v13, |v17|, |v21|
	v_max3_f32 v9, v9, |v18|, |v22|
	v_max3_f32 v7, v7, |v19|, |v23|
	s_waitcnt vmcnt(20)
	v_pk_mul_f32 v[16:17], v[122:123], v[178:179] op_sel_hi:[1,0]
	v_pk_mul_f32 v[18:19], v[124:125], v[178:179] op_sel_hi:[1,0]
	v_pk_mul_f32 v[20:21], v[126:127], v[180:181] op_sel_hi:[1,0]
	v_pk_mul_f32 v[22:23], v[128:129], v[180:181] op_sel_hi:[1,0]
	v_max3_f32 v15, v15, |v16|, |v20|
	v_max3_f32 v13, v13, |v17|, |v21|
	v_max3_f32 v9, v9, |v18|, |v22|
	v_max3_f32 v7, v7, |v19|, |v23|
	s_waitcnt vmcnt(16)
	v_pk_mul_f32 v[16:17], v[130:131], v[182:183] op_sel_hi:[1,0]
	v_pk_mul_f32 v[18:19], v[132:133], v[182:183] op_sel_hi:[1,0]
	v_pk_mul_f32 v[20:21], v[134:135], v[184:185] op_sel_hi:[1,0]
	v_pk_mul_f32 v[22:23], v[136:137], v[184:185] op_sel_hi:[1,0]
	v_max3_f32 v15, v15, |v16|, |v20|
	v_max3_f32 v13, v13, |v17|, |v21|
	v_max3_f32 v9, v9, |v18|, |v22|
	v_max3_f32 v7, v7, |v19|, |v23|
	s_waitcnt vmcnt(12)
; __device__ __forceinline__ float shfl_xor_f(float v, int mask, int lane) { return __int_as_float(__builtin_amdgcn_ds_bpermute((lane ^ mask) << 2, __float_as_int(v))); }
;     ...
;         for (int i = 0; i < 8; ++i) { const int k = 64 * kb + 8 * i + kr; const f32x4 v = __builtin_nontemporal_load((const f32x4*)(W + (size_t)k * pitch)) * g[k];
;             mx[0] = __builtin_fmaxf(mx[0], __builtin_fabsf(v[0])); mx[1] = __builtin_fmaxf(mx[1], __builtin_fabsf(v[1])); mx[2] = __builtin_fmaxf(mx[2], __builtin_fabsf(v[2])); mx[3] = __builtin_fmaxf(mx[3], __builtin_fabsf(v[3])); } }
; #pragma unroll
;     for (int c = 0; c < 4; ++c) { float m = mx[c]; m = __builtin_fmaxf(m, shfl_xor_f(m, 8, lane)); m = __builtin_fmaxf(m, shfl_xor_f(m, 16, lane)); m = __builtin_fmaxf(m, shfl_xor_f(m, 32, lane)); mx[c] = m; }
;     f32x4 inv, step;
; #pragma unroll
;     for (int c = 0; c < 4; ++c) { step[c] = mx[c] > 0.f ? mx[c] * (1.0f / 127.0f) : 1.0f; inv[c] = mx[c] > 0.f ? 127.0f / mx[c] : 0.f; }
;     if (lane < 8) *(f32x4*)(sw + n0 + 4 * lane) = step * swm;
	v_pk_mul_f32 v[16:17], v[138:139], v[186:187] op_sel_hi:[1,0]
	v_pk_mul_f32 v[18:19], v[140:141], v[186:187] op_sel_hi:[1,0]
	v_pk_mul_f32 v[20:21], v[142:143], v[188:189] op_sel_hi:[1,0]
	v_pk_mul_f32 v[22:23], v[144:145], v[188:189] op_sel_hi:[1,0]
	v_max3_f32 v15, v15, |v16|, |v20|
	v_max3_f32 v13, v13, |v17|, |v21|
	v_max3_f32 v9, v9, |v18|, |v22|
	v_max3_f32 v7, v7, |v19|, |v23|
	s_waitcnt vmcnt(8)
	v_pk_mul_f32 v[16:17], v[146:147], v[190:191] op_sel_hi:[1,0]
	v_pk_mul_f32 v[18:19], v[148:149], v[190:191] op_sel_hi:[1,0]
	v_pk_mul_f32 v[20:21], v[150:151], v[192:193] op_sel_hi:[1,0]
	v_pk_mul_f32 v[22:23], v[152:153], v[192:193] op_sel_hi:[1,0]
	v_max3_f32 v15, v15, |v16|, |v20|
	v_max3_f32 v13, v13, |v17|, |v21|
	v_max3_f32 v9, v9, |v18|, |v22|
	v_max3_f32 v7, v7, |v19|, |v23|
	s_waitcnt vmcnt(4)
	v_pk_mul_f32 v[16:17], v[154:155], v[194:195] op_sel_hi:[1,0]
	v_pk_mul_f32 v[18:19], v[156:157], v[194:195] op_sel_hi:[1,0]
	v_pk_mul_f32 v[20:21], v[158:159], v[196:197] op_sel_hi:[1,0]
	v_pk_mul_f32 v[22:23], v[160:161], v[196:197] op_sel_hi:[1,0]
	v_max3_f32 v15, v15, |v16|, |v20|
	v_max3_f32 v13, v13, |v17|, |v21|
	v_max3_f32 v9, v9, |v18|, |v22|
	v_max3_f32 v7, v7, |v19|, |v23|
	s_waitcnt vmcnt(0)
	v_pk_mul_f32 v[16:17], v[162:163], v[198:199] op_sel_hi:[1,0]
	v_pk_mul_f32 v[18:19], v[164:165], v[198:199] op_sel_hi:[1,0]
	v_pk_mul_f32 v[20:21], v[166:167], v[200:201] op_sel_hi:[1,0]
	v_pk_mul_f32 v[22:23], v[168:169], v[200:201] op_sel_hi:[1,0]
	v_max3_f32 v15, v15, |v16|, |v20|
	v_max3_f32 v13, v13, |v17|, |v21|
	v_max3_f32 v9, v9, |v18|, |v22|
	v_max3_f32 v7, v7, |v19|, |v23|
	v_lshlrev_b32_e32 v2, 2, v68
	v_xor_b32_e32 v3, 32, v2
	ds_bpermute_b32 v4, v3, v15
	v_max_f32_e32 v5, v15, v15
	v_xor_b32_e32 v8, 64, v2
	ds_bpermute_b32 v10, v3, v13
	v_max_f32_e32 v6, v13, v13
	s_waitcnt lgkmcnt(1)
	v_max_f32_e32 v4, v4, v4
	v_max_f32_e32 v4, v5, v4
	ds_bpermute_b32 v5, v8, v4
	s_waitcnt lgkmcnt(1)
	v_max_f32_e32 v10, v10, v10
	v_xor_b32_e32 v11, 0x80, v2
	v_max_f32_e32 v6, v6, v10
	ds_bpermute_b32 v10, v8, v6
	s_waitcnt lgkmcnt(1)
	v_max_f32_e32 v5, v5, v5
	v_max_f32_e32 v4, v4, v5
	ds_bpermute_b32 v5, v11, v4
	ds_bpermute_b32 v12, v3, v9
	ds_bpermute_b32 v3, v3, v7
	s_waitcnt lgkmcnt(3)
	v_max_f32_e32 v10, v10, v10
	v_max_f32_e32 v10, v6, v10
	s_waitcnt lgkmcnt(2)
	v_max_f32_e32 v5, v5, v5
	v_max_f32_e32 v6, v4, v5
	s_waitcnt lgkmcnt(1)
	v_max_f32_e32 v4, v12, v12
	v_max_f32_e32 v5, v9, v9
	v_max_f32_e32 v4, v5, v4
	s_waitcnt lgkmcnt(0)
	v_max_f32_e32 v3, v3, v3
	v_max_f32_e32 v7, v7, v7
	ds_bpermute_b32 v5, v8, v4
	v_max_f32_e32 v3, v7, v3
	ds_bpermute_b32 v7, v8, v3
	ds_bpermute_b32 v8, v11, v10
	v_cmp_lt_f32_e64 s[12:13], 0, v6
	s_waitcnt lgkmcnt(2)
	v_max_f32_e32 v5, v5, v5
	v_max_f32_e32 v4, v4, v5
	s_waitcnt lgkmcnt(1)
	v_max_f32_e32 v5, v7, v7
	v_max_f32_e32 v3, v3, v5
	ds_bpermute_b32 v9, v11, v4
	ds_bpermute_b32 v7, v11, v3
	s_waitcnt lgkmcnt(2)
	v_max_f32_e32 v5, v8, v8
	v_max_f32_e32 v5, v10, v5
	v_cmp_lt_f32_e64 s[10:11], 0, v5
	s_waitcnt lgkmcnt(1)
	v_max_f32_e32 v8, v9, v9
	s_waitcnt lgkmcnt(0)
	v_max_f32_e32 v7, v7, v7
	v_max_f32_e32 v4, v4, v8
	v_max_f32_e32 v3, v3, v7
	v_cmp_lt_f32_e64 s[8:9], 0, v4
	v_cmp_lt_f32_e64 s[6:7], 0, v3
	v_cmp_gt_u32_e32 vcc, 8, v68
	s_and_saveexec_b64 s[40:41], vcc
	s_cbranch_execz .LBB0_138
	s_mul_i32 s43, s28, 0x5800
	s_mul_hi_i32 s39, s28, 0x5800
	s_add_u32 s43, s14, s43
	v_mov_b32_e32 v7, 0x3f317218
	v_mov_b32_e32 v8, 0x3fb8aa3b
	s_addc_u32 s44, s15, s39
	v_cndmask_b32_e64 v8, v7, v8, s[4:5]
	v_mul_f32_e32 v7, 0x3c010204, v6
	s_ashr_i32 s39, s38, 31
	v_cndmask_b32_e64 v12, 1.0, v7, s[12:13]
	v_mul_f32_e32 v7, 0x3c010204, v5
	s_lshl_b64 s[4:5], s[38:39], 2
	v_cndmask_b32_e64 v13, 1.0, v7, s[10:11]
	v_mul_f32_e32 v7, 0x3c010204, v4
	s_add_u32 s4, s43, s4
	v_cndmask_b32_e64 v10, 1.0, v7, s[8:9]
	v_mul_f32_e32 v7, 0x3c010204, v3
	s_addc_u32 s5, s44, s5
	v_lshlrev_b32_e32 v14, 2, v2
	v_mov_b32_e32 v15, 0
	v_cndmask_b32_e64 v11, 1.0, v7, s[6:7]
	v_lshl_add_u64 v[14:15], s[4:5], 0, v[14:15]
	v_pk_mul_f32 v[10:11], v[8:9], v[10:11] op_sel_hi:[0,1]
	v_pk_mul_f32 v[8:9], v[8:9], v[12:13] op_sel_hi:[0,1]
	v_add_co_u32_e32 v12, vcc, 0x40000, v14
	s_nop 1
	v_addc_co_u32_e32 v13, vcc, 0, v15, vcc
	global_store_dwordx4 v[12:13], v[8:11], off

; #define LAS __attribute__((address_space(3)))
; #define LDS_WAIT() asm volatile("s_waitcnt lgkmcnt(0)" ::: "memory")
;     ...
;     for (int kb = 0; kb < D / 64; ++kb) {
; #pragma unroll
;         for (int i = 0; i < 8; ++i) { const int kk = 8 * i + kr; const int k = 64 * kb + kk; const f32x4 v = __builtin_nontemporal_load((const f32x4*)(W + (size_t)k * pitch)) * g[k];
;             LAS float* p = scr + kk * 33 + 4 * (lane & 7); p[0] = __builtin_rintf(v[0] * inv[0]); p[1] = __builtin_rintf(v[1] * inv[1]); p[2] = __builtin_rintf(v[2] * inv[2]); p[3] = __builtin_rintf(v[3] * inv[3]); }
;         LDS_WAIT(); asm volatile("" ::: "memory");
.LBB0_139:
	v_readfirstlane_b32 s4, v0
	v_readfirstlane_b32 s5, v1
	v_readfirstlane_b32 s6, v2
	v_readfirstlane_b32 s7, v3
	s_nop 1
	v_subrev_u32_e32 v250, s4, v0
	v_subrev_u32_e32 v251, s6, v2
	s_add_u32 s4, s4, s26
	s_addc_u32 s5, s5, s27
	s_nop 4
	global_load_dwordx4 v[106:109], v250, s[4:5] nt
	global_load_dword v170, v251, s[6:7]
	s_add_u32 s4, s4, 0x16000
	s_addc_u32 s5, s5, 0
	global_load_dwordx4 v[110:113], v250, s[4:5] nt
	global_load_dword v172, v251, s[6:7] offset:32
	s_add_u32 s4, s4, 0x16000
	s_addc_u32 s5, s5, 0
	global_load_dwordx4 v[114:117], v250, s[4:5] nt
	global_load_dword v174, v251, s[6:7] offset:64
	s_add_u32 s4, s4, 0x16000
	s_addc_u32 s5, s5, 0
	global_load_dwordx4 v[118:121], v250, s[4:5] nt
	global_load_dword v176, v251, s[6:7] offset:96
	s_add_u32 s4, s4, 0x16000
	s_addc_u32 s5, s5, 0
	global_load_dwordx4 v[122:125], v250, s[4:5] nt
	global_load_dword v178, v251, s[6:7] offset:128
	s_add_u32 s4, s4, 0x16000
	s_addc_u32 s5, s5, 0
	global_load_dwordx4 v[126:129], v250, s[4:5] nt
	global_load_dword v180, v251, s[6:7] offset:160
	s_add_u32 s4, s4, 0x16000
	s_addc_u32 s5, s5, 0
	global_load_dwordx4 v[130:133], v250, s[4:5] nt
	global_load_dword v182, v251, s[6:7] offset:192
	s_add_u32 s4, s4, 0x16000
	s_addc_u32 s5, s5, 0
	global_load_dwordx4 v[134:137], v250, s[4:5] nt
	global_load_dword v184, v251, s[6:7] offset:224
	s_add_u32 s4, s4, 0x16000
	s_addc_u32 s5, s5, 0
	global_load_dwordx4 v[138:141], v250, s[4:5] nt
	global_load_dword v186, v251, s[6:7] offset:256
	s_add_u32 s4, s4, 0x16000
	s_addc_u32 s5, s5, 0
	global_load_dwordx4 v[142:145], v250, s[4:5] nt
	global_load_dword v188, v251, s[6:7] offset:288
	s_add_u32 s4, s4, 0x16000
	s_addc_u32 s5, s5, 0
	global_load_dwordx4 v[146:149], v250, s[4:5] nt
	global_load_dword v190, v251, s[6:7] offset:320
	s_add_u32 s4, s4, 0x16000
	s_addc_u32 s5, s5, 0
	global_load_dwordx4 v[150:153], v250, s[4:5] nt
	global_load_dword v192, v251, s[6:7] offset:352
	s_add_u32 s4, s4, 0x16000
	s_addc_u32 s5, s5, 0
	global_load_dwordx4 v[154:157], v250, s[4:5] nt
	global_load_dword v194, v251, s[6:7] offset:384
	s_add_u32 s4, s4, 0x16000
	s_addc_u32 s5, s5, 0
	global_load_dwordx4 v[158:161], v250, s[4:5] nt
	global_load_dword v196, v251, s[6:7] offset:416
	s_add_u32 s4, s4, 0x16000
	s_addc_u32 s5, s5, 0
	global_load_dwordx4 v[162:165], v250, s[4:5] nt
	global_load_dword v198, v251, s[6:7] offset:448
	s_add_u32 s4, s4, 0x16000
	s_addc_u32 s5, s5, 0
	global_load_dwordx4 v[166:169], v250, s[4:5] nt
	global_load_dword v200, v251, s[6:7] offset:480
	v_add_u32_e32 v77, 0x420, v25
	v_add_u32_e32 v79, 0x428, v25
	v_add_u32_e32 v81, 0x840, v25
	v_add_u32_e32 v83, 0x848, v25
	v_add_u32_e32 v85, 0xc60, v25
	v_add_u32_e32 v87, 0xc68, v25
	v_add_u32_e32 v89, 0x1080, v25
	v_add_u32_e32 v91, 0x1088, v25
	v_add_u32_e32 v92, 0x14a0, v25
	v_add_u32_e32 v93, 0x14a8, v25
	v_add_u32_e32 v94, 0x18c0, v25
	v_add_u32_e32 v95, 0x18c8, v25
	v_add_u32_e32 v96, 0x1ce0, v25
	v_add_u32_e32 v97, 0x1ce8, v25
	v_lshl_add_u64 v[16:17], v[10:11], 0, s[26:27]
	v_lshl_add_u64 v[18:19], v[8:9], 0, s[26:27]
	v_lshl_add_u64 v[58:59], v[6:7], 0, s[26:27]
	v_lshl_add_u64 v[60:61], v[4:5], 0, s[26:27]
	v_lshl_add_u64 v[4:5], v[4:5], 0, 64
	v_lshl_add_u64 v[6:7], v[6:7], 0, 64
	v_lshl_add_u64 v[8:9], v[8:9], 0, 64
	v_lshl_add_u64 v[10:11], v[10:11], 0, 64
	s_waitcnt vmcnt(16)
	v_pk_mul_f32 v[14:15], v[106:107], v[170:171] op_sel_hi:[1,0]
	v_pk_mul_f32 v[12:13], v[108:109], v[170:171] op_sel_hi:[1,0]
	v_mul_f32_e32 v62, v20, v14
	v_mul_f32_e32 v63, v21, v15
	v_mul_f32_e32 v64, v22, v12
	v_mul_f32_e32 v65, v23, v13
	v_pk_mul_f32 v[14:15], v[110:111], v[172:173] op_sel_hi:[1,0]
	v_pk_mul_f32 v[12:13], v[112:113], v[172:173] op_sel_hi:[1,0]
	v_pk_mul_f32 v[26:27], v[116:117], v[174:175] op_sel_hi:[1,0]
	v_pk_mul_f32 v[28:29], v[114:115], v[174:175] op_sel_hi:[1,0]
	v_pk_mul_f32 v[30:31], v[120:121], v[176:177] op_sel_hi:[1,0]
	v_pk_mul_f32 v[32:33], v[118:119], v[176:177] op_sel_hi:[1,0]
	v_pk_mul_f32 v[34:35], v[124:125], v[178:179] op_sel_hi:[1,0]
	v_pk_mul_f32 v[36:37], v[122:123], v[178:179] op_sel_hi:[1,0]
	v_pk_mul_f32 v[38:39], v[128:129], v[180:181] op_sel_hi:[1,0]
	v_pk_mul_f32 v[40:41], v[126:127], v[180:181] op_sel_hi:[1,0]
	v_pk_mul_f32 v[42:43], v[132:133], v[182:183] op_sel_hi:[1,0]
	v_pk_mul_f32 v[44:45], v[130:131], v[182:183] op_sel_hi:[1,0]
	v_pk_mul_f32 v[46:47], v[136:137], v[184:185] op_sel_hi:[1,0]
	v_pk_mul_f32 v[48:49], v[134:135], v[184:185] op_sel_hi:[1,0]
	s_add_u32 s4, s4, 0x16000
	s_addc_u32 s5, s5, 0
	global_load_dwordx4 v[106:109], v250, s[4:5] nt
	global_load_dword v170, v251, s[6:7] offset:512
	s_add_u32 s4, s4, 0x16000
	s_addc_u32 s5, s5, 0
	global_load_dwordx4 v[110:113], v250, s[4:5] nt
	global_load_dword v172, v251, s[6:7] offset:544
	s_add_u32 s4, s4, 0x16000
	s_addc_u32 s5, s5, 0
	global_load_dwordx4 v[114:117], v250, s[4:5] nt
	global_load_dword v174, v251, s[6:7] offset:576
	s_add_u32 s4, s4, 0x16000
	s_addc_u32 s5, s5, 0
	global_load_dwordx4 v[118:121], v250, s[4:5] nt
	global_load_dword v176, v251, s[6:7] offset:608
	s_add_u32 s4, s4, 0x16000
	s_addc_u32 s5, s5, 0
	global_load_dwordx4 v[122:125], v250, s[4:5] nt
	global_load_dword v178, v251, s[6:7] offset:640
	s_add_u32 s4, s4, 0x16000
	s_addc_u32 s5, s5, 0
	global_load_dwordx4 v[126:129], v250, s[4:5] nt
	global_load_dword v180, v251, s[6:7] offset:672
	s_add_u32 s4, s4, 0x16000
	s_addc_u32 s5, s5, 0
	global_load_dwordx4 v[130:133], v250, s[4:5] nt
	global_load_dword v182, v251, s[6:7] offset:704
	s_add_u32 s4, s4, 0x16000
	s_addc_u32 s5, s5, 0
	global_load_dwordx4 v[134:137], v250, s[4:5] nt
	global_load_dword v184, v251, s[6:7] offset:736
; #define LAS __attribute__((address_space(3)))
; #define GAS __attribute__((address_space(1)))
; #define LDS_WAIT() asm volatile("s_waitcnt lgkmcnt(0)" ::: "memory")
;     ...
;         for (int i = 0; i < 8; ++i) { const int kk = 8 * i + kr; const int k = 64 * kb + kk; const f32x4 v = __builtin_nontemporal_load((const f32x4*)(W + (size_t)k * pitch)) * g[k];
;             LAS float* p = scr + kk * 33 + 4 * (lane & 7); p[0] = __builtin_rintf(v[0] * inv[0]); p[1] = __builtin_rintf(v[1] * inv[1]); p[2] = __builtin_rintf(v[2] * inv[2]); p[3] = __builtin_rintf(v[3] * inv[3]); }
;         LDS_WAIT(); asm volatile("" ::: "memory");
;         const int c = lane & 7;
; #pragma unroll
;         for (int j = 0; j < 4; ++j) { const int n = (lane >> 3) + 8 * j; const LAS float* sp = scr + (8 * c) * 33 + n;
;             u32x2 o;
;             o.x = ((unsigned)(int)sp[0 * 33] & 0xFFu) | (((unsigned)(int)sp[1 * 33] & 0xFFu) << 8) | (((unsigned)(int)sp[2 * 33] & 0xFFu) << 16) | (((unsigned)(int)sp[3 * 33] & 0xFFu) << 24);
;             o.y = ((unsigned)(int)sp[4 * 33] & 0xFFu) | (((unsigned)(int)sp[5 * 33] & 0xFFu) << 8) | (((unsigned)(int)sp[6 * 33] & 0xFFu) << 16) | (((unsigned)(int)sp[7 * 33] & 0xFFu) << 24);
;             *(GAS u32x2*)(dst + (size_t)(n0 + n) * D + 64 * kb + 8 * c) = o; }
;         LDS_WAIT(); asm volatile("" ::: "memory");
	v_mul_f32_e32 v14, v20, v14
	v_mul_f32_e32 v15, v21, v15
	v_rndne_f32_e32 v50, v62
	v_rndne_f32_e32 v51, v63
	v_mul_f32_e32 v12, v22, v12
	v_mul_f32_e32 v13, v23, v13
	v_mul_f32_e32 v28, v20, v28
	v_mul_f32_e32 v29, v21, v29
	v_mul_f32_e32 v26, v22, v26
	v_mul_f32_e32 v27, v23, v27
	v_mul_f32_e32 v32, v20, v32
	v_mul_f32_e32 v33, v21, v33
	v_mul_f32_e32 v30, v22, v30
	v_mul_f32_e32 v31, v23, v31
	v_mul_f32_e32 v36, v20, v36
	v_mul_f32_e32 v37, v21, v37
	v_mul_f32_e32 v34, v22, v34
	v_mul_f32_e32 v35, v23, v35
	v_mul_f32_e32 v40, v20, v40
	v_mul_f32_e32 v41, v21, v41
	v_mul_f32_e32 v38, v22, v38
	v_mul_f32_e32 v39, v23, v39
	v_mul_f32_e32 v44, v20, v44
	v_mul_f32_e32 v45, v21, v45
	v_mul_f32_e32 v42, v22, v42
	v_mul_f32_e32 v43, v23, v43
	v_mul_f32_e32 v48, v20, v48
	v_mul_f32_e32 v49, v21, v49
	v_mul_f32_e32 v46, v22, v46
	v_mul_f32_e32 v47, v23, v47
	v_rndne_f32_e32 v14, v14
	v_rndne_f32_e32 v15, v15
	v_rndne_f32_e32 v52, v64
	v_rndne_f32_e32 v53, v65
	ds_write2_b32 v25, v50, v51 offset1:1
	ds_write2_b32 v25, v52, v53 offset0:2 offset1:3
	v_rndne_f32_e32 v12, v12
	v_rndne_f32_e32 v13, v13
	v_rndne_f32_e32 v28, v28
	v_rndne_f32_e32 v29, v29
	v_rndne_f32_e32 v26, v26
	v_rndne_f32_e32 v27, v27
	v_rndne_f32_e32 v32, v32
	v_rndne_f32_e32 v33, v33
	v_rndne_f32_e32 v30, v30
	v_rndne_f32_e32 v31, v31
	v_rndne_f32_e32 v36, v36
	v_rndne_f32_e32 v37, v37
	v_rndne_f32_e32 v34, v34
	v_rndne_f32_e32 v35, v35
	v_rndne_f32_e32 v40, v40
	v_rndne_f32_e32 v41, v41
	v_rndne_f32_e32 v38, v38
	v_rndne_f32_e32 v39, v39
	v_rndne_f32_e32 v44, v44
	v_rndne_f32_e32 v45, v45
	v_rndne_f32_e32 v42, v42
	v_rndne_f32_e32 v43, v43
	v_rndne_f32_e32 v48, v48
	v_rndne_f32_e32 v49, v49
	v_rndne_f32_e32 v46, v46
	v_rndne_f32_e32 v47, v47
	ds_write2_b32 v77, v14, v15 offset1:1
	ds_write2_b32 v79, v12, v13 offset1:1
	ds_write2_b32 v81, v28, v29 offset1:1
	ds_write2_b32 v83, v26, v27 offset1:1
	ds_write2_b32 v85, v32, v33 offset1:1
	ds_write2_b32 v87, v30, v31 offset1:1
	ds_write2_b32 v89, v36, v37 offset1:1
	ds_write2_b32 v91, v34, v35 offset1:1
	ds_write2_b32 v92, v40, v41 offset1:1
	ds_write2_b32 v93, v38, v39 offset1:1
	ds_write2_b32 v94, v44, v45 offset1:1
	ds_write2_b32 v95, v42, v43 offset1:1
	ds_write2_b32 v96, v48, v49 offset1:1
	ds_write2_b32 v97, v46, v47 offset1:1
	s_waitcnt lgkmcnt(0)
	ds_read2_b32 v[12:13], v24 offset1:8
	ds_read2_b32 v[14:15], v24 offset0:33 offset1:41
	ds_read2_b32 v[26:27], v24 offset0:66 offset1:74
	ds_read2_b32 v[28:29], v24 offset0:99 offset1:107
	ds_read2_b32 v[30:31], v24 offset0:132 offset1:140
	ds_read2_b32 v[32:33], v24 offset0:165 offset1:173
	ds_read2_b32 v[34:35], v24 offset0:198 offset1:206
	ds_read2_b32 v[36:37], v24 offset0:231 offset1:239
	ds_read2_b32 v[38:39], v24 offset0:16 offset1:24
	ds_read2_b32 v[40:41], v24 offset0:49 offset1:57
	ds_read2_b32 v[42:43], v24 offset0:82 offset1:90
	ds_read2_b32 v[44:45], v24 offset0:115 offset1:123
	ds_read2_b32 v[46:47], v24 offset0:148 offset1:156
	ds_read2_b32 v[48:49], v24 offset0:181 offset1:189
	ds_read2_b32 v[50:51], v24 offset0:214 offset1:222
	ds_read2_b32 v[52:53], v24 offset0:247 offset1:255
	s_waitcnt lgkmcnt(14)
	v_cvt_i32_f32_e32 v14, v14
	s_waitcnt lgkmcnt(10)
	v_cvt_i32_f32_e32 v32, v32
	v_cvt_i32_f32_e32 v12, v12
	v_cvt_i32_f32_sdwa v26, v26 dst_sel:WORD_1 dst_unused:UNUSED_PAD src0_sel:DWORD
	v_cvt_i32_f32_e32 v30, v30
	s_waitcnt lgkmcnt(9)
	v_cvt_i32_f32_sdwa v34, v34 dst_sel:WORD_1 dst_unused:UNUSED_PAD src0_sel:DWORD
	v_cvt_i32_f32_e32 v15, v15
	v_cvt_i32_f32_e32 v33, v33
	s_waitcnt lgkmcnt(6)
	v_cvt_i32_f32_e32 v40, v40
	s_waitcnt lgkmcnt(2)
	v_cvt_i32_f32_e32 v48, v48
	v_cvt_i32_f32_e32 v41, v41
	v_cvt_i32_f32_e32 v49, v49
	v_cvt_i32_f32_sdwa v28, v28 dst_sel:BYTE_3 dst_unused:UNUSED_PAD src0_sel:DWORD
	v_cvt_i32_f32_sdwa v36, v36 dst_sel:BYTE_3 dst_unused:UNUSED_PAD src0_sel:DWORD
	v_cvt_i32_f32_e32 v13, v13
	v_cvt_i32_f32_sdwa v27, v27 dst_sel:WORD_1 dst_unused:UNUSED_PAD src0_sel:DWORD
	v_cvt_i32_f32_e32 v31, v31
	v_cvt_i32_f32_sdwa v35, v35 dst_sel:WORD_1 dst_unused:UNUSED_PAD src0_sel:DWORD
	v_cvt_i32_f32_e32 v38, v38
	v_cvt_i32_f32_sdwa v42, v42 dst_sel:WORD_1 dst_unused:UNUSED_PAD src0_sel:DWORD
	v_cvt_i32_f32_e32 v46, v46
	s_waitcnt lgkmcnt(1)
	v_cvt_i32_f32_sdwa v50, v50 dst_sel:WORD_1 dst_unused:UNUSED_PAD src0_sel:DWORD
	v_cvt_i32_f32_e32 v39, v39
	v_cvt_i32_f32_sdwa v43, v43 dst_sel:WORD_1 dst_unused:UNUSED_PAD src0_sel:DWORD
	v_cvt_i32_f32_e32 v47, v47
	v_cvt_i32_f32_sdwa v51, v51 dst_sel:WORD_1 dst_unused:UNUSED_PAD src0_sel:DWORD
	v_cvt_i32_f32_sdwa v29, v29 dst_sel:BYTE_3 dst_unused:UNUSED_PAD src0_sel:DWORD
	v_cvt_i32_f32_sdwa v37, v37 dst_sel:BYTE_3 dst_unused:UNUSED_PAD src0_sel:DWORD
	v_cvt_i32_f32_sdwa v44, v44 dst_sel:BYTE_3 dst_unused:UNUSED_PAD src0_sel:DWORD
	s_waitcnt lgkmcnt(0)
	v_cvt_i32_f32_sdwa v52, v52 dst_sel:BYTE_3 dst_unused:UNUSED_PAD src0_sel:DWORD
	v_cvt_i32_f32_sdwa v45, v45 dst_sel:BYTE_3 dst_unused:UNUSED_PAD src0_sel:DWORD
	v_cvt_i32_f32_sdwa v53, v53 dst_sel:BYTE_3 dst_unused:UNUSED_PAD src0_sel:DWORD
	v_lshlrev_b32_e32 v14, 8, v14
	v_lshlrev_b32_e32 v32, 8, v32
	v_and_b32_e32 v26, 0xff0000, v26
	v_and_b32_e32 v34, 0xff0000, v34
	v_lshlrev_b32_e32 v15, 8, v15
	v_lshlrev_b32_e32 v33, 8, v33
	v_lshlrev_b32_e32 v40, 8, v40
	v_lshlrev_b32_e32 v48, 8, v48
	v_lshlrev_b32_e32 v41, 8, v41
	v_lshlrev_b32_e32 v49, 8, v49
	v_perm_b32 v12, v14, v12, s28
	v_perm_b32 v14, v32, v30, s28
	v_and_b32_e32 v27, 0xff0000, v27
	v_and_b32_e32 v35, 0xff0000, v35
	v_and_b32_e32 v42, 0xff0000, v42
	v_and_b32_e32 v50, 0xff0000, v50
	v_and_b32_e32 v43, 0xff0000, v43
	v_and_b32_e32 v51, 0xff0000, v51
	v_perm_b32 v15, v15, v13, s28
	v_perm_b32 v30, v33, v31, s28
	v_perm_b32 v31, v40, v38, s28
	v_perm_b32 v32, v48, v46, s28
	v_perm_b32 v33, v41, v39, s28
	v_perm_b32 v38, v49, v47, s28
	v_or3_b32 v12, v12, v26, v28
	v_or3_b32 v13, v14, v34, v36
	v_or3_b32 v14, v15, v27, v29
	v_or3_b32 v15, v30, v35, v37
	v_or3_b32 v26, v31, v42, v44
	v_or3_b32 v27, v32, v50, v52
	v_or3_b32 v28, v33, v43, v45
	v_or3_b32 v29, v38, v51, v53
	global_store_dwordx2 v[16:17], v[12:13], off
	global_store_dwordx2 v[18:19], v[14:15], off
	global_store_dwordx2 v[58:59], v[26:27], off
	global_store_dwordx2 v[60:61], v[28:29], off
	s_waitcnt lgkmcnt(0)
; #define LAS __attribute__((address_space(3)))
; #define LDS_WAIT() asm volatile("s_waitcnt lgkmcnt(0)" ::: "memory")
;     ...
;     for (int kb = 0; kb < D / 64; ++kb) {
; #pragma unroll
;         for (int i = 0; i < 8; ++i) { const int kk = 8 * i + kr; const int k = 64 * kb + kk; const f32x4 v = __builtin_nontemporal_load((const f32x4*)(W + (size_t)k * pitch)) * g[k];
;             LAS float* p = scr + kk * 33 + 4 * (lane & 7); p[0] = __builtin_rintf(v[0] * inv[0]); p[1] = __builtin_rintf(v[1] * inv[1]); p[2] = __builtin_rintf(v[2] * inv[2]); p[3] = __builtin_rintf(v[3] * inv[3]); }
;         LDS_WAIT(); asm volatile("" ::: "memory");
	v_add_u32_e32 v77, 0x420, v25
	v_add_u32_e32 v79, 0x428, v25
	v_add_u32_e32 v81, 0x840, v25
	v_add_u32_e32 v83, 0x848, v25
	v_add_u32_e32 v85, 0xc60, v25
	v_add_u32_e32 v87, 0xc68, v25
	v_add_u32_e32 v89, 0x1080, v25
	v_add_u32_e32 v91, 0x1088, v25
	v_add_u32_e32 v92, 0x14a0, v25
	v_add_u32_e32 v93, 0x14a8, v25
	v_add_u32_e32 v94, 0x18c0, v25
	v_add_u32_e32 v95, 0x18c8, v25
	v_add_u32_e32 v96, 0x1ce0, v25
	v_add_u32_e32 v97, 0x1ce8, v25
	v_lshl_add_u64 v[16:17], v[10:11], 0, s[26:27]
	v_lshl_add_u64 v[18:19], v[8:9], 0, s[26:27]
	v_lshl_add_u64 v[58:59], v[6:7], 0, s[26:27]
	v_lshl_add_u64 v[60:61], v[4:5], 0, s[26:27]
	v_lshl_add_u64 v[4:5], v[4:5], 0, 64
	v_lshl_add_u64 v[6:7], v[6:7], 0, 64
	v_lshl_add_u64 v[8:9], v[8:9], 0, 64
	v_lshl_add_u64 v[10:11], v[10:11], 0, 64
	s_waitcnt vmcnt(20)
	v_pk_mul_f32 v[14:15], v[138:139], v[186:187] op_sel_hi:[1,0]
	v_pk_mul_f32 v[12:13], v[140:141], v[186:187] op_sel_hi:[1,0]
	v_mul_f32_e32 v62, v20, v14
	v_mul_f32_e32 v63, v21, v15
	v_mul_f32_e32 v64, v22, v12
	v_mul_f32_e32 v65, v23, v13
	v_pk_mul_f32 v[14:15], v[142:143], v[188:189] op_sel_hi:[1,0]
	v_pk_mul_f32 v[12:13], v[144:145], v[188:189] op_sel_hi:[1,0]
	v_pk_mul_f32 v[26:27], v[148:149], v[190:191] op_sel_hi:[1,0]
	v_pk_mul_f32 v[28:29], v[146:147], v[190:191] op_sel_hi:[1,0]
	v_pk_mul_f32 v[30:31], v[152:153], v[192:193] op_sel_hi:[1,0]
	v_pk_mul_f32 v[32:33], v[150:151], v[192:193] op_sel_hi:[1,0]
	v_pk_mul_f32 v[34:35], v[156:157], v[194:195] op_sel_hi:[1,0]
	v_pk_mul_f32 v[36:37], v[154:155], v[194:195] op_sel_hi:[1,0]
	v_pk_mul_f32 v[38:39], v[160:161], v[196:197] op_sel_hi:[1,0]
	v_pk_mul_f32 v[40:41], v[158:159], v[196:197] op_sel_hi:[1,0]
	v_pk_mul_f32 v[42:43], v[164:165], v[198:199] op_sel_hi:[1,0]
	v_pk_mul_f32 v[44:45], v[162:163], v[198:199] op_sel_hi:[1,0]
	v_pk_mul_f32 v[46:47], v[168:169], v[200:201] op_sel_hi:[1,0]
	v_pk_mul_f32 v[48:49], v[166:167], v[200:201] op_sel_hi:[1,0]
	s_add_u32 s4, s4, 0x16000
	s_addc_u32 s5, s5, 0
	global_load_dwordx4 v[138:141], v250, s[4:5] nt
	global_load_dword v186, v251, s[6:7] offset:768
	s_add_u32 s4, s4, 0x16000
	s_addc_u32 s5, s5, 0
	global_load_dwordx4 v[142:145], v250, s[4:5] nt
	global_load_dword v188, v251, s[6:7] offset:800
	s_add_u32 s4, s4, 0x16000
	s_addc_u32 s5, s5, 0
	global_load_dwordx4 v[146:149], v250, s[4:5] nt
	global_load_dword v190, v251, s[6:7] offset:832
	s_add_u32 s4, s4, 0x16000
	s_addc_u32 s5, s5, 0
	global_load_dwordx4 v[150:153], v250, s[4:5] nt
	global_load_dword v192, v251, s[6:7] offset:864
	s_add_u32 s4, s4, 0x16000
	s_addc_u32 s5, s5, 0
	global_load_dwordx4 v[154:157], v250, s[4:5] nt
	global_load_dword v194, v251, s[6:7] offset:896
	s_add_u32 s4, s4, 0x16000
	s_addc_u32 s5, s5, 0
	global_load_dwordx4 v[158:161], v250, s[4:5] nt
	global_load_dword v196, v251, s[6:7] offset:928
	s_add_u32 s4, s4, 0x16000
	s_addc_u32 s5, s5, 0
	global_load_dwordx4 v[162:165], v250, s[4:5] nt
	global_load_dword v198, v251, s[6:7] offset:960
	s_add_u32 s4, s4, 0x16000
	s_addc_u32 s5, s5, 0
	global_load_dwordx4 v[166:169], v250, s[4:5] nt
	global_load_dword v200, v251, s[6:7] offset:992
	v_mul_f32_e32 v14, v20, v14
	v_mul_f32_e32 v15, v21, v15
	v_rndne_f32_e32 v50, v62
	v_rndne_f32_e32 v51, v63
	v_mul_f32_e32 v12, v22, v12
	v_mul_f32_e32 v13, v23, v13
	v_mul_f32_e32 v28, v20, v28
	v_mul_f32_e32 v29, v21, v29
	v_mul_f32_e32 v26, v22, v26
	v_mul_f32_e32 v27, v23, v27
	v_mul_f32_e32 v32, v20, v32
	v_mul_f32_e32 v33, v21, v33
	v_mul_f32_e32 v30, v22, v30
	v_mul_f32_e32 v31, v23, v31
	v_mul_f32_e32 v36, v20, v36
	v_mul_f32_e32 v37, v21, v37
	v_mul_f32_e32 v34, v22, v34
	v_mul_f32_e32 v35, v23, v35
	v_mul_f32_e32 v40, v20, v40
	v_mul_f32_e32 v41, v21, v41
	v_mul_f32_e32 v38, v22, v38
	v_mul_f32_e32 v39, v23, v39
	v_mul_f32_e32 v44, v20, v44
	v_mul_f32_e32 v45, v21, v45
	v_mul_f32_e32 v42, v22, v42
	v_mul_f32_e32 v43, v23, v43
	v_mul_f32_e32 v48, v20, v48
	v_mul_f32_e32 v49, v21, v49
	v_mul_f32_e32 v46, v22, v46
	v_mul_f32_e32 v47, v23, v47
	v_rndne_f32_e32 v14, v14
	v_rndne_f32_e32 v15, v15
	v_rndne_f32_e32 v52, v64
	v_rndne_f32_e32 v53, v65
	ds_write2_b32 v25, v50, v51 offset1:1
	ds_write2_b32 v25, v52, v53 offset0:2 offset1:3
	v_rndne_f32_e32 v12, v12
	v_rndne_f32_e32 v13, v13
	v_rndne_f32_e32 v28, v28
	v_rndne_f32_e32 v29, v29
	v_rndne_f32_e32 v26, v26
	v_rndne_f32_e32 v27, v27
	v_rndne_f32_e32 v32, v32
	v_rndne_f32_e32 v33, v33
	v_rndne_f32_e32 v30, v30
	v_rndne_f32_e32 v31, v31
	v_rndne_f32_e32 v36, v36
	v_rndne_f32_e32 v37, v37
	v_rndne_f32_e32 v34, v34
	v_rndne_f32_e32 v35, v35
	v_rndne_f32_e32 v40, v40
	v_rndne_f32_e32 v41, v41
	v_rndne_f32_e32 v38, v38
	v_rndne_f32_e32 v39, v39
	v_rndne_f32_e32 v44, v44
	v_rndne_f32_e32 v45, v45
	v_rndne_f32_e32 v42, v42
	v_rndne_f32_e32 v43, v43
	v_rndne_f32_e32 v48, v48
	v_rndne_f32_e32 v49, v49
	v_rndne_f32_e32 v46, v46
	v_rndne_f32_e32 v47, v47
	ds_write2_b32 v77, v14, v15 offset1:1
	ds_write2_b32 v79, v12, v13 offset1:1
	ds_write2_b32 v81, v28, v29 offset1:1
	ds_write2_b32 v83, v26, v27 offset1:1
	ds_write2_b32 v85, v32, v33 offset1:1
	ds_write2_b32 v87, v30, v31 offset1:1
	ds_write2_b32 v89, v36, v37 offset1:1
	ds_write2_b32 v91, v34, v35 offset1:1
	ds_write2_b32 v92, v40, v41 offset1:1
	ds_write2_b32 v93, v38, v39 offset1:1
	ds_write2_b32 v94, v44, v45 offset1:1
	ds_write2_b32 v95, v42, v43 offset1:1
	ds_write2_b32 v96, v48, v49 offset1:1
	ds_write2_b32 v97, v46, v47 offset1:1
	s_waitcnt lgkmcnt(0)
; #define LAS __attribute__((address_space(3)))
; #define GAS __attribute__((address_space(1)))
; #define LDS_WAIT() asm volatile("s_waitcnt lgkmcnt(0)" ::: "memory")
;     ...
;     for (int kb = 0; kb < D / 64; ++kb) {
; #pragma unroll
;         for (int i = 0; i < 8; ++i) { const int kk = 8 * i + kr; const int k = 64 * kb + kk; const f32x4 v = __builtin_nontemporal_load((const f32x4*)(W + (size_t)k * pitch)) * g[k];
;             LAS float* p = scr + kk * 33 + 4 * (lane & 7); p[0] = __builtin_rintf(v[0] * inv[0]); p[1] = __builtin_rintf(v[1] * inv[1]); p[2] = __builtin_rintf(v[2] * inv[2]); p[3] = __builtin_rintf(v[3] * inv[3]); }
;         LDS_WAIT(); asm volatile("" ::: "memory");
;         const int c = lane & 7;
; #pragma unroll
;         for (int j = 0; j < 4; ++j) { const int n = (lane >> 3) + 8 * j; const LAS float* sp = scr + (8 * c) * 33 + n;
;             u32x2 o;
;             o.x = ((unsigned)(int)sp[0 * 33] & 0xFFu) | (((unsigned)(int)sp[1 * 33] & 0xFFu) << 8) | (((unsigned)(int)sp[2 * 33] & 0xFFu) << 16) | (((unsigned)(int)sp[3 * 33] & 0xFFu) << 24);
;             o.y = ((unsigned)(int)sp[4 * 33] & 0xFFu) | (((unsigned)(int)sp[5 * 33] & 0xFFu) << 8) | (((unsigned)(int)sp[6 * 33] & 0xFFu) << 16) | (((unsigned)(int)sp[7 * 33] & 0xFFu) << 24);
;             *(GAS u32x2*)(dst + (size_t)(n0 + n) * D + 64 * kb + 8 * c) = o; }
;         LDS_WAIT(); asm volatile("" ::: "memory");
;     }
	ds_read2_b32 v[12:13], v24 offset1:8
	ds_read2_b32 v[14:15], v24 offset0:33 offset1:41
	ds_read2_b32 v[26:27], v24 offset0:66 offset1:74
	ds_read2_b32 v[28:29], v24 offset0:99 offset1:107
	ds_read2_b32 v[30:31], v24 offset0:132 offset1:140
	ds_read2_b32 v[32:33], v24 offset0:165 offset1:173
	ds_read2_b32 v[34:35], v24 offset0:198 offset1:206
	ds_read2_b32 v[36:37], v24 offset0:231 offset1:239
	ds_read2_b32 v[38:39], v24 offset0:16 offset1:24
	ds_read2_b32 v[40:41], v24 offset0:49 offset1:57
	ds_read2_b32 v[42:43], v24 offset0:82 offset1:90
	ds_read2_b32 v[44:45], v24 offset0:115 offset1:123
	ds_read2_b32 v[46:47], v24 offset0:148 offset1:156
	ds_read2_b32 v[48:49], v24 offset0:181 offset1:189
	ds_read2_b32 v[50:51], v24 offset0:214 offset1:222
	ds_read2_b32 v[52:53], v24 offset0:247 offset1:255
	s_waitcnt lgkmcnt(14)
	v_cvt_i32_f32_e32 v14, v14
	s_waitcnt lgkmcnt(10)
	v_cvt_i32_f32_e32 v32, v32
	v_cvt_i32_f32_e32 v12, v12
	v_cvt_i32_f32_sdwa v26, v26 dst_sel:WORD_1 dst_unused:UNUSED_PAD src0_sel:DWORD
	v_cvt_i32_f32_e32 v30, v30
	s_waitcnt lgkmcnt(9)
	v_cvt_i32_f32_sdwa v34, v34 dst_sel:WORD_1 dst_unused:UNUSED_PAD src0_sel:DWORD
	v_cvt_i32_f32_e32 v15, v15
	v_cvt_i32_f32_e32 v33, v33
	s_waitcnt lgkmcnt(6)
	v_cvt_i32_f32_e32 v40, v40
	s_waitcnt lgkmcnt(2)
	v_cvt_i32_f32_e32 v48, v48
	v_cvt_i32_f32_e32 v41, v41
	v_cvt_i32_f32_e32 v49, v49
	v_cvt_i32_f32_sdwa v28, v28 dst_sel:BYTE_3 dst_unused:UNUSED_PAD src0_sel:DWORD
	v_cvt_i32_f32_sdwa v36, v36 dst_sel:BYTE_3 dst_unused:UNUSED_PAD src0_sel:DWORD
	v_cvt_i32_f32_e32 v13, v13
	v_cvt_i32_f32_sdwa v27, v27 dst_sel:WORD_1 dst_unused:UNUSED_PAD src0_sel:DWORD
	v_cvt_i32_f32_e32 v31, v31
	v_cvt_i32_f32_sdwa v35, v35 dst_sel:WORD_1 dst_unused:UNUSED_PAD src0_sel:DWORD
	v_cvt_i32_f32_e32 v38, v38
	v_cvt_i32_f32_sdwa v42, v42 dst_sel:WORD_1 dst_unused:UNUSED_PAD src0_sel:DWORD
	v_cvt_i32_f32_e32 v46, v46
	s_waitcnt lgkmcnt(1)
	v_cvt_i32_f32_sdwa v50, v50 dst_sel:WORD_1 dst_unused:UNUSED_PAD src0_sel:DWORD
	v_cvt_i32_f32_e32 v39, v39
	v_cvt_i32_f32_sdwa v43, v43 dst_sel:WORD_1 dst_unused:UNUSED_PAD src0_sel:DWORD
	v_cvt_i32_f32_e32 v47, v47
	v_cvt_i32_f32_sdwa v51, v51 dst_sel:WORD_1 dst_unused:UNUSED_PAD src0_sel:DWORD
	v_cvt_i32_f32_sdwa v29, v29 dst_sel:BYTE_3 dst_unused:UNUSED_PAD src0_sel:DWORD
	v_cvt_i32_f32_sdwa v37, v37 dst_sel:BYTE_3 dst_unused:UNUSED_PAD src0_sel:DWORD
	v_cvt_i32_f32_sdwa v44, v44 dst_sel:BYTE_3 dst_unused:UNUSED_PAD src0_sel:DWORD
	s_waitcnt lgkmcnt(0)
	v_cvt_i32_f32_sdwa v52, v52 dst_sel:BYTE_3 dst_unused:UNUSED_PAD src0_sel:DWORD
	v_cvt_i32_f32_sdwa v45, v45 dst_sel:BYTE_3 dst_unused:UNUSED_PAD src0_sel:DWORD
	v_cvt_i32_f32_sdwa v53, v53 dst_sel:BYTE_3 dst_unused:UNUSED_PAD src0_sel:DWORD
	v_lshlrev_b32_e32 v14, 8, v14
	v_lshlrev_b32_e32 v32, 8, v32
	v_and_b32_e32 v26, 0xff0000, v26
	v_and_b32_e32 v34, 0xff0000, v34
	v_lshlrev_b32_e32 v15, 8, v15
	v_lshlrev_b32_e32 v33, 8, v33
	v_lshlrev_b32_e32 v40, 8, v40
	v_lshlrev_b32_e32 v48, 8, v48
	v_lshlrev_b32_e32 v41, 8, v41
	v_lshlrev_b32_e32 v49, 8, v49
	v_perm_b32 v12, v14, v12, s28
	v_perm_b32 v14, v32, v30, s28
	v_and_b32_e32 v27, 0xff0000, v27
	v_and_b32_e32 v35, 0xff0000, v35
	v_and_b32_e32 v42, 0xff0000, v42
	v_and_b32_e32 v50, 0xff0000, v50
	v_and_b32_e32 v43, 0xff0000, v43
	v_and_b32_e32 v51, 0xff0000, v51
	v_perm_b32 v15, v15, v13, s28
	v_perm_b32 v30, v33, v31, s28
	v_perm_b32 v31, v40, v38, s28
	v_perm_b32 v32, v48, v46, s28
	v_perm_b32 v33, v41, v39, s28
	v_perm_b32 v38, v49, v47, s28
	v_or3_b32 v12, v12, v26, v28
	v_or3_b32 v13, v14, v34, v36
	v_or3_b32 v14, v15, v27, v29
	v_or3_b32 v15, v30, v35, v37
	v_or3_b32 v26, v31, v42, v44
	v_or3_b32 v27, v32, v50, v52
	v_or3_b32 v28, v33, v43, v45
	v_or3_b32 v29, v38, v51, v53
	global_store_dwordx2 v[16:17], v[12:13], off
	global_store_dwordx2 v[18:19], v[14:15], off
	global_store_dwordx2 v[58:59], v[26:27], off
	global_store_dwordx2 v[60:61], v[28:29], off
	s_waitcnt lgkmcnt(0)
	v_add_u32_e32 v77, 0x420, v25
	v_add_u32_e32 v79, 0x428, v25
	v_add_u32_e32 v81, 0x840, v25
	v_add_u32_e32 v83, 0x848, v25
	v_add_u32_e32 v85, 0xc60, v25
	v_add_u32_e32 v87, 0xc68, v25
	v_add_u32_e32 v89, 0x1080, v25
	v_add_u32_e32 v91, 0x1088, v25
	v_add_u32_e32 v92, 0x14a0, v25
	v_add_u32_e32 v93, 0x14a8, v25
	v_add_u32_e32 v94, 0x18c0, v25
	v_add_u32_e32 v95, 0x18c8, v25
	v_add_u32_e32 v96, 0x1ce0, v25
	v_add_u32_e32 v97, 0x1ce8, v25
	v_lshl_add_u64 v[16:17], v[10:11], 0, s[26:27]
	v_lshl_add_u64 v[18:19], v[8:9], 0, s[26:27]
	v_lshl_add_u64 v[58:59], v[6:7], 0, s[26:27]
	v_lshl_add_u64 v[60:61], v[4:5], 0, s[26:27]
	v_lshl_add_u64 v[4:5], v[4:5], 0, 64
	v_lshl_add_u64 v[6:7], v[6:7], 0, 64
	v_lshl_add_u64 v[8:9], v[8:9], 0, 64
	v_lshl_add_u64 v[10:11], v[10:11], 0, 64
	s_waitcnt vmcnt(24)
; #define LAS __attribute__((address_space(3)))
;     ...
;         for (int i = 0; i < 8; ++i) { const int kk = 8 * i + kr; const int k = 64 * kb + kk; const f32x4 v = __builtin_nontemporal_load((const f32x4*)(W + (size_t)k * pitch)) * g[k];
;             LAS float* p = scr + kk * 33 + 4 * (lane & 7); p[0] = __builtin_rintf(v[0] * inv[0]); p[1] = __builtin_rintf(v[1] * inv[1]); p[2] = __builtin_rintf(v[2] * inv[2]); p[3] = __builtin_rintf(v[3] * inv[3]); }
	v_pk_mul_f32 v[14:15], v[106:107], v[170:171] op_sel_hi:[1,0]
	v_pk_mul_f32 v[12:13], v[108:109], v[170:171] op_sel_hi:[1,0]
	v_mul_f32_e32 v62, v20, v14
	v_mul_f32_e32 v63, v21, v15
	v_mul_f32_e32 v64, v22, v12
	v_mul_f32_e32 v65, v23, v13
	v_pk_mul_f32 v[14:15], v[110:111], v[172:173] op_sel_hi:[1,0]
	v_pk_mul_f32 v[12:13], v[112:113], v[172:173] op_sel_hi:[1,0]
	v_pk_mul_f32 v[26:27], v[116:117], v[174:175] op_sel_hi:[1,0]
	v_pk_mul_f32 v[28:29], v[114:115], v[174:175] op_sel_hi:[1,0]
	v_pk_mul_f32 v[30:31], v[120:121], v[176:177] op_sel_hi:[1,0]
	v_pk_mul_f32 v[32:33], v[118:119], v[176:177] op_sel_hi:[1,0]
	v_pk_mul_f32 v[34:35], v[124:125], v[178:179] op_sel_hi:[1,0]
	v_pk_mul_f32 v[36:37], v[122:123], v[178:179] op_sel_hi:[1,0]
	v_pk_mul_f32 v[38:39], v[128:129], v[180:181] op_sel_hi:[1,0]
	v_pk_mul_f32 v[40:41], v[126:127], v[180:181] op_sel_hi:[1,0]
	v_pk_mul_f32 v[42:43], v[132:133], v[182:183] op_sel_hi:[1,0]
	v_pk_mul_f32 v[44:45], v[130:131], v[182:183] op_sel_hi:[1,0]
	v_pk_mul_f32 v[46:47], v[136:137], v[184:185] op_sel_hi:[1,0]
	v_pk_mul_f32 v[48:49], v[134:135], v[184:185] op_sel_hi:[1,0]
	s_add_u32 s4, s4, 0x16000
	s_addc_u32 s5, s5, 0
	global_load_dwordx4 v[106:109], v250, s[4:5] nt
	global_load_dword v170, v251, s[6:7] offset:1024
	s_add_u32 s4, s4, 0x16000
	s_addc_u32 s5, s5, 0
	global_load_dwordx4 v[110:113], v250, s[4:5] nt
	global_load_dword v172, v251, s[6:7] offset:1056
	s_add_u32 s4, s4, 0x16000
	s_addc_u32 s5, s5, 0
	global_load_dwordx4 v[114:117], v250, s[4:5] nt
	global_load_dword v174, v251, s[6:7] offset:1088
	s_add_u32 s4, s4, 0x16000
	s_addc_u32 s5, s5, 0
	global_load_dwordx4 v[118:121], v250, s[4:5] nt
	global_load_dword v176, v251, s[6:7] offset:1120
	s_add_u32 s4, s4, 0x16000
	s_addc_u32 s5, s5, 0
	global_load_dwordx4 v[122:125], v250, s[4:5] nt
	global_load_dword v178, v251, s[6:7] offset:1152
	s_add_u32 s4, s4, 0x16000
	s_addc_u32 s5, s5, 0
	global_load_dwordx4 v[126:129], v250, s[4:5] nt
	global_load_dword v180, v251, s[6:7] offset:1184
	s_add_u32 s4, s4, 0x16000
	s_addc_u32 s5, s5, 0
	global_load_dwordx4 v[130:133], v250, s[4:5] nt
	global_load_dword v182, v251, s[6:7] offset:1216
	s_add_u32 s4, s4, 0x16000
	s_addc_u32 s5, s5, 0
	global_load_dwordx4 v[134:137], v250, s[4:5] nt
	global_load_dword v184, v251, s[6:7] offset:1248
	v_mul_f32_e32 v14, v20, v14
	v_mul_f32_e32 v15, v21, v15
	v_rndne_f32_e32 v50, v62
	v_rndne_f32_e32 v51, v63
	v_mul_f32_e32 v12, v22, v12
	v_mul_f32_e32 v13, v23, v13
	v_mul_f32_e32 v28, v20, v28
	v_mul_f32_e32 v29, v21, v29
	v_mul_f32_e32 v26, v22, v26
	v_mul_f32_e32 v27, v23, v27
	v_mul_f32_e32 v32, v20, v32
	v_mul_f32_e32 v33, v21, v33
	v_mul_f32_e32 v30, v22, v30
	v_mul_f32_e32 v31, v23, v31
	v_mul_f32_e32 v36, v20, v36
	v_mul_f32_e32 v37, v21, v37
	v_mul_f32_e32 v34, v22, v34
	v_mul_f32_e32 v35, v23, v35
	v_mul_f32_e32 v40, v20, v40
	v_mul_f32_e32 v41, v21, v41
	v_mul_f32_e32 v38, v22, v38
	v_mul_f32_e32 v39, v23, v39
	v_mul_f32_e32 v44, v20, v44
	v_mul_f32_e32 v45, v21, v45
	v_mul_f32_e32 v42, v22, v42
	v_mul_f32_e32 v43, v23, v43
	v_mul_f32_e32 v48, v20, v48
	v_mul_f32_e32 v49, v21, v49
	v_mul_f32_e32 v46, v22, v46
	v_mul_f32_e32 v47, v23, v47
	v_rndne_f32_e32 v14, v14
	v_rndne_f32_e32 v15, v15
	v_rndne_f32_e32 v52, v64
	v_rndne_f32_e32 v53, v65
	ds_write2_b32 v25, v50, v51 offset1:1
	ds_write2_b32 v25, v52, v53 offset0:2 offset1:3
	v_rndne_f32_e32 v12, v12
	v_rndne_f32_e32 v13, v13
	v_rndne_f32_e32 v28, v28
	v_rndne_f32_e32 v29, v29
	v_rndne_f32_e32 v26, v26
	v_rndne_f32_e32 v27, v27
	v_rndne_f32_e32 v32, v32
	v_rndne_f32_e32 v33, v33
	v_rndne_f32_e32 v30, v30
	v_rndne_f32_e32 v31, v31
	v_rndne_f32_e32 v36, v36
	v_rndne_f32_e32 v37, v37
	v_rndne_f32_e32 v34, v34
	v_rndne_f32_e32 v35, v35
	v_rndne_f32_e32 v40, v40
	v_rndne_f32_e32 v41, v41
	v_rndne_f32_e32 v38, v38
	v_rndne_f32_e32 v39, v39
	v_rndne_f32_e32 v44, v44
	v_rndne_f32_e32 v45, v45
	v_rndne_f32_e32 v42, v42
	v_rndne_f32_e32 v43, v43
	v_rndne_f32_e32 v48, v48
	v_rndne_f32_e32 v49, v49
	v_rndne_f32_e32 v46, v46
	v_rndne_f32_e32 v47, v47
	ds_write2_b32 v77, v14, v15 offset1:1
	ds_write2_b32 v79, v12, v13 offset1:1
	ds_write2_b32 v81, v28, v29 offset1:1
	ds_write2_b32 v83, v26, v27 offset1:1
	ds_write2_b32 v85, v32, v33 offset1:1
	ds_write2_b32 v87, v30, v31 offset1:1
	ds_write2_b32 v89, v36, v37 offset1:1
	ds_write2_b32 v91, v34, v35 offset1:1
	ds_write2_b32 v92, v40, v41 offset1:1
	ds_write2_b32 v93, v38, v39 offset1:1
	ds_write2_b32 v94, v44, v45 offset1:1
	ds_write2_b32 v95, v42, v43 offset1:1
	ds_write2_b32 v96, v48, v49 offset1:1
	ds_write2_b32 v97, v46, v47 offset1:1
	s_waitcnt lgkmcnt(0)
	ds_read2_b32 v[12:13], v24 offset1:8
	ds_read2_b32 v[14:15], v24 offset0:33 offset1:41
	ds_read2_b32 v[26:27], v24 offset0:66 offset1:74
	ds_read2_b32 v[28:29], v24 offset0:99 offset1:107
	ds_read2_b32 v[30:31], v24 offset0:132 offset1:140
	ds_read2_b32 v[32:33], v24 offset0:165 offset1:173
	ds_read2_b32 v[34:35], v24 offset0:198 offset1:206
	ds_read2_b32 v[36:37], v24 offset0:231 offset1:239
	ds_read2_b32 v[38:39], v24 offset0:16 offset1:24
	ds_read2_b32 v[40:41], v24 offset0:49 offset1:57
	ds_read2_b32 v[42:43], v24 offset0:82 offset1:90
	ds_read2_b32 v[44:45], v24 offset0:115 offset1:123
	ds_read2_b32 v[46:47], v24 offset0:148 offset1:156
	ds_read2_b32 v[48:49], v24 offset0:181 offset1:189
	ds_read2_b32 v[50:51], v24 offset0:214 offset1:222
	ds_read2_b32 v[52:53], v24 offset0:247 offset1:255
	s_waitcnt lgkmcnt(14)
	v_cvt_i32_f32_e32 v14, v14
	s_waitcnt lgkmcnt(10)
	v_cvt_i32_f32_e32 v32, v32
	v_cvt_i32_f32_e32 v12, v12
	v_cvt_i32_f32_sdwa v26, v26 dst_sel:WORD_1 dst_unused:UNUSED_PAD src0_sel:DWORD
	v_cvt_i32_f32_e32 v30, v30
	s_waitcnt lgkmcnt(9)
; #define LAS __attribute__((address_space(3)))
; #define GAS __attribute__((address_space(1)))
; #define LDS_WAIT() asm volatile("s_waitcnt lgkmcnt(0)" ::: "memory")
;     ...
;         for (int i = 0; i < 8; ++i) { const int kk = 8 * i + kr; const int k = 64 * kb + kk; const f32x4 v = __builtin_nontemporal_load((const f32x4*)(W + (size_t)k * pitch)) * g[k];
;             LAS float* p = scr + kk * 33 + 4 * (lane & 7); p[0] = __builtin_rintf(v[0] * inv[0]); p[1] = __builtin_rintf(v[1] * inv[1]); p[2] = __builtin_rintf(v[2] * inv[2]); p[3] = __builtin_rintf(v[3] * inv[3]); }
;         LDS_WAIT(); asm volatile("" ::: "memory");
;         const int c = lane & 7;
; #pragma unroll
;         for (int j = 0; j < 4; ++j) { const int n = (lane >> 3) + 8 * j; const LAS float* sp = scr + (8 * c) * 33 + n;
;             u32x2 o;
;             o.x = ((unsigned)(int)sp[0 * 33] & 0xFFu) | (((unsigned)(int)sp[1 * 33] & 0xFFu) << 8) | (((unsigned)(int)sp[2 * 33] & 0xFFu) << 16) | (((unsigned)(int)sp[3 * 33] & 0xFFu) << 24);
;             o.y = ((unsigned)(int)sp[4 * 33] & 0xFFu) | (((unsigned)(int)sp[5 * 33] & 0xFFu) << 8) | (((unsigned)(int)sp[6 * 33] & 0xFFu) << 16) | (((unsigned)(int)sp[7 * 33] & 0xFFu) << 24);
;             *(GAS u32x2*)(dst + (size_t)(n0 + n) * D + 64 * kb + 8 * c) = o; }
	v_cvt_i32_f32_sdwa v34, v34 dst_sel:WORD_1 dst_unused:UNUSED_PAD src0_sel:DWORD
	v_cvt_i32_f32_e32 v15, v15
	v_cvt_i32_f32_e32 v33, v33
	s_waitcnt lgkmcnt(6)
	v_cvt_i32_f32_e32 v40, v40
	s_waitcnt lgkmcnt(2)
	v_cvt_i32_f32_e32 v48, v48
	v_cvt_i32_f32_e32 v41, v41
	v_cvt_i32_f32_e32 v49, v49
	v_cvt_i32_f32_sdwa v28, v28 dst_sel:BYTE_3 dst_unused:UNUSED_PAD src0_sel:DWORD
	v_cvt_i32_f32_sdwa v36, v36 dst_sel:BYTE_3 dst_unused:UNUSED_PAD src0_sel:DWORD
	v_cvt_i32_f32_e32 v13, v13
	v_cvt_i32_f32_sdwa v27, v27 dst_sel:WORD_1 dst_unused:UNUSED_PAD src0_sel:DWORD
	v_cvt_i32_f32_e32 v31, v31
	v_cvt_i32_f32_sdwa v35, v35 dst_sel:WORD_1 dst_unused:UNUSED_PAD src0_sel:DWORD
	v_cvt_i32_f32_e32 v38, v38
	v_cvt_i32_f32_sdwa v42, v42 dst_sel:WORD_1 dst_unused:UNUSED_PAD src0_sel:DWORD
	v_cvt_i32_f32_e32 v46, v46
	s_waitcnt lgkmcnt(1)
	v_cvt_i32_f32_sdwa v50, v50 dst_sel:WORD_1 dst_unused:UNUSED_PAD src0_sel:DWORD
	v_cvt_i32_f32_e32 v39, v39
	v_cvt_i32_f32_sdwa v43, v43 dst_sel:WORD_1 dst_unused:UNUSED_PAD src0_sel:DWORD
	v_cvt_i32_f32_e32 v47, v47
	v_cvt_i32_f32_sdwa v51, v51 dst_sel:WORD_1 dst_unused:UNUSED_PAD src0_sel:DWORD
	v_cvt_i32_f32_sdwa v29, v29 dst_sel:BYTE_3 dst_unused:UNUSED_PAD src0_sel:DWORD
	v_cvt_i32_f32_sdwa v37, v37 dst_sel:BYTE_3 dst_unused:UNUSED_PAD src0_sel:DWORD
	v_cvt_i32_f32_sdwa v44, v44 dst_sel:BYTE_3 dst_unused:UNUSED_PAD src0_sel:DWORD
	s_waitcnt lgkmcnt(0)
	v_cvt_i32_f32_sdwa v52, v52 dst_sel:BYTE_3 dst_unused:UNUSED_PAD src0_sel:DWORD
	v_cvt_i32_f32_sdwa v45, v45 dst_sel:BYTE_3 dst_unused:UNUSED_PAD src0_sel:DWORD
	v_cvt_i32_f32_sdwa v53, v53 dst_sel:BYTE_3 dst_unused:UNUSED_PAD src0_sel:DWORD
	v_lshlrev_b32_e32 v14, 8, v14
	v_lshlrev_b32_e32 v32, 8, v32
	v_and_b32_e32 v26, 0xff0000, v26
	v_and_b32_e32 v34, 0xff0000, v34
	v_lshlrev_b32_e32 v15, 8, v15
	v_lshlrev_b32_e32 v33, 8, v33
	v_lshlrev_b32_e32 v40, 8, v40
	v_lshlrev_b32_e32 v48, 8, v48
	v_lshlrev_b32_e32 v41, 8, v41
	v_lshlrev_b32_e32 v49, 8, v49
	v_perm_b32 v12, v14, v12, s28
	v_perm_b32 v14, v32, v30, s28
	v_and_b32_e32 v27, 0xff0000, v27
	v_and_b32_e32 v35, 0xff0000, v35
	v_and_b32_e32 v42, 0xff0000, v42
	v_and_b32_e32 v50, 0xff0000, v50
	v_and_b32_e32 v43, 0xff0000, v43
	v_and_b32_e32 v51, 0xff0000, v51
	v_perm_b32 v15, v15, v13, s28
	v_perm_b32 v30, v33, v31, s28
	v_perm_b32 v31, v40, v38, s28
	v_perm_b32 v32, v48, v46, s28
	v_perm_b32 v33, v41, v39, s28
	v_perm_b32 v38, v49, v47, s28
	v_or3_b32 v12, v12, v26, v28
	v_or3_b32 v13, v14, v34, v36
	v_or3_b32 v14, v15, v27, v29
	v_or3_b32 v15, v30, v35, v37
	v_or3_b32 v26, v31, v42, v44
	v_or3_b32 v27, v32, v50, v52
	v_or3_b32 v28, v33, v43, v45
	v_or3_b32 v29, v38, v51, v53
	global_store_dwordx2 v[16:17], v[12:13], off
	global_store_dwordx2 v[18:19], v[14:15], off
	global_store_dwordx2 v[58:59], v[26:27], off
	global_store_dwordx2 v[60:61], v[28:29], off
	s_waitcnt lgkmcnt(0)
	v_add_u32_e32 v77, 0x420, v25
	v_add_u32_e32 v79, 0x428, v25
	v_add_u32_e32 v81, 0x840, v25
	v_add_u32_e32 v83, 0x848, v25
	v_add_u32_e32 v85, 0xc60, v25
	v_add_u32_e32 v87, 0xc68, v25
	v_add_u32_e32 v89, 0x1080, v25
	v_add_u32_e32 v91, 0x1088, v25
	v_add_u32_e32 v92, 0x14a0, v25
	v_add_u32_e32 v93, 0x14a8, v25
	v_add_u32_e32 v94, 0x18c0, v25
	v_add_u32_e32 v95, 0x18c8, v25
	v_add_u32_e32 v96, 0x1ce0, v25
	v_add_u32_e32 v97, 0x1ce8, v25
	v_lshl_add_u64 v[16:17], v[10:11], 0, s[26:27]
	v_lshl_add_u64 v[18:19], v[8:9], 0, s[26:27]
	v_lshl_add_u64 v[58:59], v[6:7], 0, s[26:27]
	v_lshl_add_u64 v[60:61], v[4:5], 0, s[26:27]
	v_lshl_add_u64 v[4:5], v[4:5], 0, 64
	v_lshl_add_u64 v[6:7], v[6:7], 0, 64
	v_lshl_add_u64 v[8:9], v[8:9], 0, 64
	v_lshl_add_u64 v[10:11], v[10:11], 0, 64
	s_waitcnt vmcnt(24)
	v_pk_mul_f32 v[14:15], v[138:139], v[186:187] op_sel_hi:[1,0]
	v_pk_mul_f32 v[12:13], v[140:141], v[186:187] op_sel_hi:[1,0]
	v_mul_f32_e32 v62, v20, v14
	v_mul_f32_e32 v63, v21, v15
	v_mul_f32_e32 v64, v22, v12
	v_mul_f32_e32 v65, v23, v13
	v_pk_mul_f32 v[14:15], v[142:143], v[188:189] op_sel_hi:[1,0]
	v_pk_mul_f32 v[12:13], v[144:145], v[188:189] op_sel_hi:[1,0]
	v_pk_mul_f32 v[26:27], v[148:149], v[190:191] op_sel_hi:[1,0]
	v_pk_mul_f32 v[28:29], v[146:147], v[190:191] op_sel_hi:[1,0]
	v_pk_mul_f32 v[30:31], v[152:153], v[192:193] op_sel_hi:[1,0]
	v_pk_mul_f32 v[32:33], v[150:151], v[192:193] op_sel_hi:[1,0]
	v_pk_mul_f32 v[34:35], v[156:157], v[194:195] op_sel_hi:[1,0]
	v_pk_mul_f32 v[36:37], v[154:155], v[194:195] op_sel_hi:[1,0]
	v_pk_mul_f32 v[38:39], v[160:161], v[196:197] op_sel_hi:[1,0]
	v_pk_mul_f32 v[40:41], v[158:159], v[196:197] op_sel_hi:[1,0]
	v_pk_mul_f32 v[42:43], v[164:165], v[198:199] op_sel_hi:[1,0]
	v_pk_mul_f32 v[44:45], v[162:163], v[198:199] op_sel_hi:[1,0]
	v_pk_mul_f32 v[46:47], v[168:169], v[200:201] op_sel_hi:[1,0]
	v_pk_mul_f32 v[48:49], v[166:167], v[200:201] op_sel_hi:[1,0]
	s_add_u32 s4, s4, 0x16000
	s_addc_u32 s5, s5, 0
	global_load_dwordx4 v[138:141], v250, s[4:5] nt
	global_load_dword v186, v251, s[6:7] offset:1280
	s_add_u32 s4, s4, 0x16000
	s_addc_u32 s5, s5, 0
	global_load_dwordx4 v[142:145], v250, s[4:5] nt
	global_load_dword v188, v251, s[6:7] offset:1312
	s_add_u32 s4, s4, 0x16000
	s_addc_u32 s5, s5, 0
	global_load_dwordx4 v[146:149], v250, s[4:5] nt
	global_load_dword v190, v251, s[6:7] offset:1344
	s_add_u32 s4, s4, 0x16000
	s_addc_u32 s5, s5, 0
	global_load_dwordx4 v[150:153], v250, s[4:5] nt
	global_load_dword v192, v251, s[6:7] offset:1376
	s_add_u32 s4, s4, 0x16000
	s_addc_u32 s5, s5, 0
	global_load_dwordx4 v[154:157], v250, s[4:5] nt
	global_load_dword v194, v251, s[6:7] offset:1408
	s_add_u32 s4, s4, 0x16000
	s_addc_u32 s5, s5, 0
	global_load_dwordx4 v[158:161], v250, s[4:5] nt
; #define LAS __attribute__((address_space(3)))
; #define GAS __attribute__((address_space(1)))
; #define LDS_WAIT() asm volatile("s_waitcnt lgkmcnt(0)" ::: "memory")
;     ...
;         for (int i = 0; i < 8; ++i) { const int kk = 8 * i + kr; const int k = 64 * kb + kk; const f32x4 v = __builtin_nontemporal_load((const f32x4*)(W + (size_t)k * pitch)) * g[k];
;             LAS float* p = scr + kk * 33 + 4 * (lane & 7); p[0] = __builtin_rintf(v[0] * inv[0]); p[1] = __builtin_rintf(v[1] * inv[1]); p[2] = __builtin_rintf(v[2] * inv[2]); p[3] = __builtin_rintf(v[3] * inv[3]); }
;         LDS_WAIT(); asm volatile("" ::: "memory");
;         const int c = lane & 7;
; #pragma unroll
;         for (int j = 0; j < 4; ++j) { const int n = (lane >> 3) + 8 * j; const LAS float* sp = scr + (8 * c) * 33 + n;
;             u32x2 o;
;             o.x = ((unsigned)(int)sp[0 * 33] & 0xFFu) | (((unsigned)(int)sp[1 * 33] & 0xFFu) << 8) | (((unsigned)(int)sp[2 * 33] & 0xFFu) << 16) | (((unsigned)(int)sp[3 * 33] & 0xFFu) << 24);
;             o.y = ((unsigned)(int)sp[4 * 33] & 0xFFu) | (((unsigned)(int)sp[5 * 33] & 0xFFu) << 8) | (((unsigned)(int)sp[6 * 33] & 0xFFu) << 16) | (((unsigned)(int)sp[7 * 33] & 0xFFu) << 24);
;             *(GAS u32x2*)(dst + (size_t)(n0 + n) * D + 64 * kb + 8 * c) = o; }
	global_load_dword v196, v251, s[6:7] offset:1440
	s_add_u32 s4, s4, 0x16000
	s_addc_u32 s5, s5, 0
	global_load_dwordx4 v[162:165], v250, s[4:5] nt
	global_load_dword v198, v251, s[6:7] offset:1472
	s_add_u32 s4, s4, 0x16000
	s_addc_u32 s5, s5, 0
	global_load_dwordx4 v[166:169], v250, s[4:5] nt
	global_load_dword v200, v251, s[6:7] offset:1504
	v_mul_f32_e32 v14, v20, v14
	v_mul_f32_e32 v15, v21, v15
	v_rndne_f32_e32 v50, v62
	v_rndne_f32_e32 v51, v63
	v_mul_f32_e32 v12, v22, v12
	v_mul_f32_e32 v13, v23, v13
	v_mul_f32_e32 v28, v20, v28
	v_mul_f32_e32 v29, v21, v29
	v_mul_f32_e32 v26, v22, v26
	v_mul_f32_e32 v27, v23, v27
	v_mul_f32_e32 v32, v20, v32
	v_mul_f32_e32 v33, v21, v33
	v_mul_f32_e32 v30, v22, v30
	v_mul_f32_e32 v31, v23, v31
	v_mul_f32_e32 v36, v20, v36
	v_mul_f32_e32 v37, v21, v37
	v_mul_f32_e32 v34, v22, v34
	v_mul_f32_e32 v35, v23, v35
	v_mul_f32_e32 v40, v20, v40
	v_mul_f32_e32 v41, v21, v41
	v_mul_f32_e32 v38, v22, v38
	v_mul_f32_e32 v39, v23, v39
	v_mul_f32_e32 v44, v20, v44
	v_mul_f32_e32 v45, v21, v45
	v_mul_f32_e32 v42, v22, v42
	v_mul_f32_e32 v43, v23, v43
	v_mul_f32_e32 v48, v20, v48
	v_mul_f32_e32 v49, v21, v49
	v_mul_f32_e32 v46, v22, v46
	v_mul_f32_e32 v47, v23, v47
	v_rndne_f32_e32 v14, v14
	v_rndne_f32_e32 v15, v15
	v_rndne_f32_e32 v52, v64
	v_rndne_f32_e32 v53, v65
	ds_write2_b32 v25, v50, v51 offset1:1
	ds_write2_b32 v25, v52, v53 offset0:2 offset1:3
	v_rndne_f32_e32 v12, v12
	v_rndne_f32_e32 v13, v13
	v_rndne_f32_e32 v28, v28
	v_rndne_f32_e32 v29, v29
	v_rndne_f32_e32 v26, v26
	v_rndne_f32_e32 v27, v27
	v_rndne_f32_e32 v32, v32
	v_rndne_f32_e32 v33, v33
	v_rndne_f32_e32 v30, v30
	v_rndne_f32_e32 v31, v31
	v_rndne_f32_e32 v36, v36
	v_rndne_f32_e32 v37, v37
	v_rndne_f32_e32 v34, v34
	v_rndne_f32_e32 v35, v35
	v_rndne_f32_e32 v40, v40
	v_rndne_f32_e32 v41, v41
	v_rndne_f32_e32 v38, v38
	v_rndne_f32_e32 v39, v39
	v_rndne_f32_e32 v44, v44
	v_rndne_f32_e32 v45, v45
	v_rndne_f32_e32 v42, v42
	v_rndne_f32_e32 v43, v43
	v_rndne_f32_e32 v48, v48
	v_rndne_f32_e32 v49, v49
	v_rndne_f32_e32 v46, v46
	v_rndne_f32_e32 v47, v47
	ds_write2_b32 v77, v14, v15 offset1:1
	ds_write2_b32 v79, v12, v13 offset1:1
	ds_write2_b32 v81, v28, v29 offset1:1
	ds_write2_b32 v83, v26, v27 offset1:1
	ds_write2_b32 v85, v32, v33 offset1:1
	ds_write2_b32 v87, v30, v31 offset1:1
	ds_write2_b32 v89, v36, v37 offset1:1
	ds_write2_b32 v91, v34, v35 offset1:1
	ds_write2_b32 v92, v40, v41 offset1:1
	ds_write2_b32 v93, v38, v39 offset1:1
	ds_write2_b32 v94, v44, v45 offset1:1
	ds_write2_b32 v95, v42, v43 offset1:1
	ds_write2_b32 v96, v48, v49 offset1:1
	ds_write2_b32 v97, v46, v47 offset1:1
	s_waitcnt lgkmcnt(0)
	ds_read2_b32 v[12:13], v24 offset1:8
	ds_read2_b32 v[14:15], v24 offset0:33 offset1:41
	ds_read2_b32 v[26:27], v24 offset0:66 offset1:74
	ds_read2_b32 v[28:29], v24 offset0:99 offset1:107
	ds_read2_b32 v[30:31], v24 offset0:132 offset1:140
	ds_read2_b32 v[32:33], v24 offset0:165 offset1:173
	ds_read2_b32 v[34:35], v24 offset0:198 offset1:206
	ds_read2_b32 v[36:37], v24 offset0:231 offset1:239
	ds_read2_b32 v[38:39], v24 offset0:16 offset1:24
	ds_read2_b32 v[40:41], v24 offset0:49 offset1:57
	ds_read2_b32 v[42:43], v24 offset0:82 offset1:90
	ds_read2_b32 v[44:45], v24 offset0:115 offset1:123
	ds_read2_b32 v[46:47], v24 offset0:148 offset1:156
	ds_read2_b32 v[48:49], v24 offset0:181 offset1:189
	ds_read2_b32 v[50:51], v24 offset0:214 offset1:222
	ds_read2_b32 v[52:53], v24 offset0:247 offset1:255
	s_waitcnt lgkmcnt(14)
	v_cvt_i32_f32_e32 v14, v14
	s_waitcnt lgkmcnt(10)
	v_cvt_i32_f32_e32 v32, v32
	v_cvt_i32_f32_e32 v12, v12
	v_cvt_i32_f32_sdwa v26, v26 dst_sel:WORD_1 dst_unused:UNUSED_PAD src0_sel:DWORD
	v_cvt_i32_f32_e32 v30, v30
	s_waitcnt lgkmcnt(9)
	v_cvt_i32_f32_sdwa v34, v34 dst_sel:WORD_1 dst_unused:UNUSED_PAD src0_sel:DWORD
	v_cvt_i32_f32_e32 v15, v15
	v_cvt_i32_f32_e32 v33, v33
	s_waitcnt lgkmcnt(6)
	v_cvt_i32_f32_e32 v40, v40
	s_waitcnt lgkmcnt(2)
	v_cvt_i32_f32_e32 v48, v48
	v_cvt_i32_f32_e32 v41, v41
	v_cvt_i32_f32_e32 v49, v49
	v_cvt_i32_f32_sdwa v28, v28 dst_sel:BYTE_3 dst_unused:UNUSED_PAD src0_sel:DWORD
	v_cvt_i32_f32_sdwa v36, v36 dst_sel:BYTE_3 dst_unused:UNUSED_PAD src0_sel:DWORD
	v_cvt_i32_f32_e32 v13, v13
	v_cvt_i32_f32_sdwa v27, v27 dst_sel:WORD_1 dst_unused:UNUSED_PAD src0_sel:DWORD
	v_cvt_i32_f32_e32 v31, v31
	v_cvt_i32_f32_sdwa v35, v35 dst_sel:WORD_1 dst_unused:UNUSED_PAD src0_sel:DWORD
	v_cvt_i32_f32_e32 v38, v38
	v_cvt_i32_f32_sdwa v42, v42 dst_sel:WORD_1 dst_unused:UNUSED_PAD src0_sel:DWORD
	v_cvt_i32_f32_e32 v46, v46
	s_waitcnt lgkmcnt(1)
	v_cvt_i32_f32_sdwa v50, v50 dst_sel:WORD_1 dst_unused:UNUSED_PAD src0_sel:DWORD
	v_cvt_i32_f32_e32 v39, v39
	v_cvt_i32_f32_sdwa v43, v43 dst_sel:WORD_1 dst_unused:UNUSED_PAD src0_sel:DWORD
	v_cvt_i32_f32_e32 v47, v47
	v_cvt_i32_f32_sdwa v51, v51 dst_sel:WORD_1 dst_unused:UNUSED_PAD src0_sel:DWORD
	v_cvt_i32_f32_sdwa v29, v29 dst_sel:BYTE_3 dst_unused:UNUSED_PAD src0_sel:DWORD
	v_cvt_i32_f32_sdwa v37, v37 dst_sel:BYTE_3 dst_unused:UNUSED_PAD src0_sel:DWORD
	v_cvt_i32_f32_sdwa v44, v44 dst_sel:BYTE_3 dst_unused:UNUSED_PAD src0_sel:DWORD
	s_waitcnt lgkmcnt(0)
; #define LAS __attribute__((address_space(3)))
; #define GAS __attribute__((address_space(1)))
; #define LDS_WAIT() asm volatile("s_waitcnt lgkmcnt(0)" ::: "memory")
;     ...
;         for (int i = 0; i < 8; ++i) { const int kk = 8 * i + kr; const int k = 64 * kb + kk; const f32x4 v = __builtin_nontemporal_load((const f32x4*)(W + (size_t)k * pitch)) * g[k];
;             LAS float* p = scr + kk * 33 + 4 * (lane & 7); p[0] = __builtin_rintf(v[0] * inv[0]); p[1] = __builtin_rintf(v[1] * inv[1]); p[2] = __builtin_rintf(v[2] * inv[2]); p[3] = __builtin_rintf(v[3] * inv[3]); }
;         LDS_WAIT(); asm volatile("" ::: "memory");
;         const int c = lane & 7;
; #pragma unroll
;         for (int j = 0; j < 4; ++j) { const int n = (lane >> 3) + 8 * j; const LAS float* sp = scr + (8 * c) * 33 + n;
;             u32x2 o;
;             o.x = ((unsigned)(int)sp[0 * 33] & 0xFFu) | (((unsigned)(int)sp[1 * 33] & 0xFFu) << 8) | (((unsigned)(int)sp[2 * 33] & 0xFFu) << 16) | (((unsigned)(int)sp[3 * 33] & 0xFFu) << 24);
;             o.y = ((unsigned)(int)sp[4 * 33] & 0xFFu) | (((unsigned)(int)sp[5 * 33] & 0xFFu) << 8) | (((unsigned)(int)sp[6 * 33] & 0xFFu) << 16) | (((unsigned)(int)sp[7 * 33] & 0xFFu) << 24);
;             *(GAS u32x2*)(dst + (size_t)(n0 + n) * D + 64 * kb + 8 * c) = o; }
	v_cvt_i32_f32_sdwa v52, v52 dst_sel:BYTE_3 dst_unused:UNUSED_PAD src0_sel:DWORD
	v_cvt_i32_f32_sdwa v45, v45 dst_sel:BYTE_3 dst_unused:UNUSED_PAD src0_sel:DWORD
	v_cvt_i32_f32_sdwa v53, v53 dst_sel:BYTE_3 dst_unused:UNUSED_PAD src0_sel:DWORD
	v_lshlrev_b32_e32 v14, 8, v14
	v_lshlrev_b32_e32 v32, 8, v32
	v_and_b32_e32 v26, 0xff0000, v26
	v_and_b32_e32 v34, 0xff0000, v34
	v_lshlrev_b32_e32 v15, 8, v15
	v_lshlrev_b32_e32 v33, 8, v33
	v_lshlrev_b32_e32 v40, 8, v40
	v_lshlrev_b32_e32 v48, 8, v48
	v_lshlrev_b32_e32 v41, 8, v41
	v_lshlrev_b32_e32 v49, 8, v49
	v_perm_b32 v12, v14, v12, s28
	v_perm_b32 v14, v32, v30, s28
	v_and_b32_e32 v27, 0xff0000, v27
	v_and_b32_e32 v35, 0xff0000, v35
	v_and_b32_e32 v42, 0xff0000, v42
	v_and_b32_e32 v50, 0xff0000, v50
	v_and_b32_e32 v43, 0xff0000, v43
	v_and_b32_e32 v51, 0xff0000, v51
	v_perm_b32 v15, v15, v13, s28
	v_perm_b32 v30, v33, v31, s28
	v_perm_b32 v31, v40, v38, s28
	v_perm_b32 v32, v48, v46, s28
	v_perm_b32 v33, v41, v39, s28
	v_perm_b32 v38, v49, v47, s28
	v_or3_b32 v12, v12, v26, v28
	v_or3_b32 v13, v14, v34, v36
	v_or3_b32 v14, v15, v27, v29
	v_or3_b32 v15, v30, v35, v37
	v_or3_b32 v26, v31, v42, v44
	v_or3_b32 v27, v32, v50, v52
	v_or3_b32 v28, v33, v43, v45
	v_or3_b32 v29, v38, v51, v53
	global_store_dwordx2 v[16:17], v[12:13], off
	global_store_dwordx2 v[18:19], v[14:15], off
	global_store_dwordx2 v[58:59], v[26:27], off
	global_store_dwordx2 v[60:61], v[28:29], off
	s_waitcnt lgkmcnt(0)
	v_add_u32_e32 v77, 0x420, v25
	v_add_u32_e32 v79, 0x428, v25
	v_add_u32_e32 v81, 0x840, v25
	v_add_u32_e32 v83, 0x848, v25
	v_add_u32_e32 v85, 0xc60, v25
	v_add_u32_e32 v87, 0xc68, v25
	v_add_u32_e32 v89, 0x1080, v25
	v_add_u32_e32 v91, 0x1088, v25
	v_add_u32_e32 v92, 0x14a0, v25
	v_add_u32_e32 v93, 0x14a8, v25
	v_add_u32_e32 v94, 0x18c0, v25
	v_add_u32_e32 v95, 0x18c8, v25
	v_add_u32_e32 v96, 0x1ce0, v25
	v_add_u32_e32 v97, 0x1ce8, v25
	v_lshl_add_u64 v[16:17], v[10:11], 0, s[26:27]
	v_lshl_add_u64 v[18:19], v[8:9], 0, s[26:27]
	v_lshl_add_u64 v[58:59], v[6:7], 0, s[26:27]
	v_lshl_add_u64 v[60:61], v[4:5], 0, s[26:27]
	v_lshl_add_u64 v[4:5], v[4:5], 0, 64
	v_lshl_add_u64 v[6:7], v[6:7], 0, 64
	v_lshl_add_u64 v[8:9], v[8:9], 0, 64
	v_lshl_add_u64 v[10:11], v[10:11], 0, 64
	s_waitcnt vmcnt(24)
	v_pk_mul_f32 v[14:15], v[106:107], v[170:171] op_sel_hi:[1,0]
	v_pk_mul_f32 v[12:13], v[108:109], v[170:171] op_sel_hi:[1,0]
	v_mul_f32_e32 v62, v20, v14
	v_mul_f32_e32 v63, v21, v15
	v_mul_f32_e32 v64, v22, v12
	v_mul_f32_e32 v65, v23, v13
	v_pk_mul_f32 v[14:15], v[110:111], v[172:173] op_sel_hi:[1,0]
	v_pk_mul_f32 v[12:13], v[112:113], v[172:173] op_sel_hi:[1,0]
	v_pk_mul_f32 v[26:27], v[116:117], v[174:175] op_sel_hi:[1,0]
	v_pk_mul_f32 v[28:29], v[114:115], v[174:175] op_sel_hi:[1,0]
	v_pk_mul_f32 v[30:31], v[120:121], v[176:177] op_sel_hi:[1,0]
	v_pk_mul_f32 v[32:33], v[118:119], v[176:177] op_sel_hi:[1,0]
	v_pk_mul_f32 v[34:35], v[124:125], v[178:179] op_sel_hi:[1,0]
	v_pk_mul_f32 v[36:37], v[122:123], v[178:179] op_sel_hi:[1,0]
	v_pk_mul_f32 v[38:39], v[128:129], v[180:181] op_sel_hi:[1,0]
	v_pk_mul_f32 v[40:41], v[126:127], v[180:181] op_sel_hi:[1,0]
	v_pk_mul_f32 v[42:43], v[132:133], v[182:183] op_sel_hi:[1,0]
	v_pk_mul_f32 v[44:45], v[130:131], v[182:183] op_sel_hi:[1,0]
	v_pk_mul_f32 v[46:47], v[136:137], v[184:185] op_sel_hi:[1,0]
	v_pk_mul_f32 v[48:49], v[134:135], v[184:185] op_sel_hi:[1,0]
	s_add_u32 s4, s4, 0x16000
	s_addc_u32 s5, s5, 0
	global_load_dwordx4 v[106:109], v250, s[4:5] nt
	global_load_dword v170, v251, s[6:7] offset:1536
	s_add_u32 s4, s4, 0x16000
	s_addc_u32 s5, s5, 0
	global_load_dwordx4 v[110:113], v250, s[4:5] nt
	global_load_dword v172, v251, s[6:7] offset:1568
	s_add_u32 s4, s4, 0x16000
	s_addc_u32 s5, s5, 0
	global_load_dwordx4 v[114:117], v250, s[4:5] nt
	global_load_dword v174, v251, s[6:7] offset:1600
	s_add_u32 s4, s4, 0x16000
	s_addc_u32 s5, s5, 0
	global_load_dwordx4 v[118:121], v250, s[4:5] nt
	global_load_dword v176, v251, s[6:7] offset:1632
	s_add_u32 s4, s4, 0x16000
	s_addc_u32 s5, s5, 0
	global_load_dwordx4 v[122:125], v250, s[4:5] nt
	global_load_dword v178, v251, s[6:7] offset:1664
	s_add_u32 s4, s4, 0x16000
	s_addc_u32 s5, s5, 0
	global_load_dwordx4 v[126:129], v250, s[4:5] nt
	global_load_dword v180, v251, s[6:7] offset:1696
	s_add_u32 s4, s4, 0x16000
	s_addc_u32 s5, s5, 0
	global_load_dwordx4 v[130:133], v250, s[4:5] nt
	global_load_dword v182, v251, s[6:7] offset:1728
	s_add_u32 s4, s4, 0x16000
	s_addc_u32 s5, s5, 0
	global_load_dwordx4 v[134:137], v250, s[4:5] nt
	global_load_dword v184, v251, s[6:7] offset:1760
	v_mul_f32_e32 v14, v20, v14
	v_mul_f32_e32 v15, v21, v15
	v_rndne_f32_e32 v50, v62
	v_rndne_f32_e32 v51, v63
	v_mul_f32_e32 v12, v22, v12
	v_mul_f32_e32 v13, v23, v13
	v_mul_f32_e32 v28, v20, v28
	v_mul_f32_e32 v29, v21, v29
	v_mul_f32_e32 v26, v22, v26
	v_mul_f32_e32 v27, v23, v27
	v_mul_f32_e32 v32, v20, v32
	v_mul_f32_e32 v33, v21, v33
	v_mul_f32_e32 v30, v22, v30
	v_mul_f32_e32 v31, v23, v31
	v_mul_f32_e32 v36, v20, v36
	v_mul_f32_e32 v37, v21, v37
	v_mul_f32_e32 v34, v22, v34
	v_mul_f32_e32 v35, v23, v35
	v_mul_f32_e32 v40, v20, v40
	v_mul_f32_e32 v41, v21, v41
	v_mul_f32_e32 v38, v22, v38
	v_mul_f32_e32 v39, v23, v39
	v_mul_f32_e32 v44, v20, v44
	v_mul_f32_e32 v45, v21, v45
	v_mul_f32_e32 v42, v22, v42
	v_mul_f32_e32 v43, v23, v43
	v_mul_f32_e32 v48, v20, v48
	v_mul_f32_e32 v49, v21, v49
	v_mul_f32_e32 v46, v22, v46
	v_mul_f32_e32 v47, v23, v47
	v_rndne_f32_e32 v14, v14
	v_rndne_f32_e32 v15, v15
	v_rndne_f32_e32 v52, v64
	v_rndne_f32_e32 v53, v65
	ds_write2_b32 v25, v50, v51 offset1:1
	ds_write2_b32 v25, v52, v53 offset0:2 offset1:3
	v_rndne_f32_e32 v12, v12
	v_rndne_f32_e32 v13, v13
	v_rndne_f32_e32 v28, v28
	v_rndne_f32_e32 v29, v29
	v_rndne_f32_e32 v26, v26
	v_rndne_f32_e32 v27, v27
	v_rndne_f32_e32 v32, v32
	v_rndne_f32_e32 v33, v33
	v_rndne_f32_e32 v30, v30
	v_rndne_f32_e32 v31, v31
	v_rndne_f32_e32 v36, v36
	v_rndne_f32_e32 v37, v37
	v_rndne_f32_e32 v34, v34
	v_rndne_f32_e32 v35, v35
	v_rndne_f32_e32 v40, v40
	v_rndne_f32_e32 v41, v41
	v_rndne_f32_e32 v38, v38
	v_rndne_f32_e32 v39, v39
	v_rndne_f32_e32 v44, v44
	v_rndne_f32_e32 v45, v45
	v_rndne_f32_e32 v42, v42
	v_rndne_f32_e32 v43, v43
	v_rndne_f32_e32 v48, v48
	v_rndne_f32_e32 v49, v49
	v_rndne_f32_e32 v46, v46
	v_rndne_f32_e32 v47, v47
	ds_write2_b32 v77, v14, v15 offset1:1
	ds_write2_b32 v79, v12, v13 offset1:1
	ds_write2_b32 v81, v28, v29 offset1:1
	ds_write2_b32 v83, v26, v27 offset1:1
	ds_write2_b32 v85, v32, v33 offset1:1
	ds_write2_b32 v87, v30, v31 offset1:1
	ds_write2_b32 v89, v36, v37 offset1:1
	ds_write2_b32 v91, v34, v35 offset1:1
	ds_write2_b32 v92, v40, v41 offset1:1
	ds_write2_b32 v93, v38, v39 offset1:1
	ds_write2_b32 v94, v44, v45 offset1:1
	ds_write2_b32 v95, v42, v43 offset1:1
	ds_write2_b32 v96, v48, v49 offset1:1
	ds_write2_b32 v97, v46, v47 offset1:1
	s_waitcnt lgkmcnt(0)
; #define LAS __attribute__((address_space(3)))
; #define GAS __attribute__((address_space(1)))
; #define LDS_WAIT() asm volatile("s_waitcnt lgkmcnt(0)" ::: "memory")
;     ...
;         LDS_WAIT(); asm volatile("" ::: "memory");
;         const int c = lane & 7;
; #pragma unroll
;         for (int j = 0; j < 4; ++j) { const int n = (lane >> 3) + 8 * j; const LAS float* sp = scr + (8 * c) * 33 + n;
;             u32x2 o;
;             o.x = ((unsigned)(int)sp[0 * 33] & 0xFFu) | (((unsigned)(int)sp[1 * 33] & 0xFFu) << 8) | (((unsigned)(int)sp[2 * 33] & 0xFFu) << 16) | (((unsigned)(int)sp[3 * 33] & 0xFFu) << 24);
;             o.y = ((unsigned)(int)sp[4 * 33] & 0xFFu) | (((unsigned)(int)sp[5 * 33] & 0xFFu) << 8) | (((unsigned)(int)sp[6 * 33] & 0xFFu) << 16) | (((unsigned)(int)sp[7 * 33] & 0xFFu) << 24);
;             *(GAS u32x2*)(dst + (size_t)(n0 + n) * D + 64 * kb + 8 * c) = o; }
	ds_read2_b32 v[12:13], v24 offset1:8
	ds_read2_b32 v[14:15], v24 offset0:33 offset1:41
	ds_read2_b32 v[26:27], v24 offset0:66 offset1:74
	ds_read2_b32 v[28:29], v24 offset0:99 offset1:107
	ds_read2_b32 v[30:31], v24 offset0:132 offset1:140
	ds_read2_b32 v[32:33], v24 offset0:165 offset1:173
	ds_read2_b32 v[34:35], v24 offset0:198 offset1:206
	ds_read2_b32 v[36:37], v24 offset0:231 offset1:239
	ds_read2_b32 v[38:39], v24 offset0:16 offset1:24
	ds_read2_b32 v[40:41], v24 offset0:49 offset1:57
	ds_read2_b32 v[42:43], v24 offset0:82 offset1:90
	ds_read2_b32 v[44:45], v24 offset0:115 offset1:123
	ds_read2_b32 v[46:47], v24 offset0:148 offset1:156
	ds_read2_b32 v[48:49], v24 offset0:181 offset1:189
	ds_read2_b32 v[50:51], v24 offset0:214 offset1:222
	ds_read2_b32 v[52:53], v24 offset0:247 offset1:255
	s_waitcnt lgkmcnt(14)
	v_cvt_i32_f32_e32 v14, v14
	s_waitcnt lgkmcnt(10)
	v_cvt_i32_f32_e32 v32, v32
	v_cvt_i32_f32_e32 v12, v12
	v_cvt_i32_f32_sdwa v26, v26 dst_sel:WORD_1 dst_unused:UNUSED_PAD src0_sel:DWORD
	v_cvt_i32_f32_e32 v30, v30
	s_waitcnt lgkmcnt(9)
	v_cvt_i32_f32_sdwa v34, v34 dst_sel:WORD_1 dst_unused:UNUSED_PAD src0_sel:DWORD
	v_cvt_i32_f32_e32 v15, v15
	v_cvt_i32_f32_e32 v33, v33
	s_waitcnt lgkmcnt(6)
	v_cvt_i32_f32_e32 v40, v40
	s_waitcnt lgkmcnt(2)
	v_cvt_i32_f32_e32 v48, v48
	v_cvt_i32_f32_e32 v41, v41
	v_cvt_i32_f32_e32 v49, v49
	v_cvt_i32_f32_sdwa v28, v28 dst_sel:BYTE_3 dst_unused:UNUSED_PAD src0_sel:DWORD
	v_cvt_i32_f32_sdwa v36, v36 dst_sel:BYTE_3 dst_unused:UNUSED_PAD src0_sel:DWORD
	v_cvt_i32_f32_e32 v13, v13
	v_cvt_i32_f32_sdwa v27, v27 dst_sel:WORD_1 dst_unused:UNUSED_PAD src0_sel:DWORD
	v_cvt_i32_f32_e32 v31, v31
	v_cvt_i32_f32_sdwa v35, v35 dst_sel:WORD_1 dst_unused:UNUSED_PAD src0_sel:DWORD
	v_cvt_i32_f32_e32 v38, v38
	v_cvt_i32_f32_sdwa v42, v42 dst_sel:WORD_1 dst_unused:UNUSED_PAD src0_sel:DWORD
	v_cvt_i32_f32_e32 v46, v46
	s_waitcnt lgkmcnt(1)
	v_cvt_i32_f32_sdwa v50, v50 dst_sel:WORD_1 dst_unused:UNUSED_PAD src0_sel:DWORD
	v_cvt_i32_f32_e32 v39, v39
	v_cvt_i32_f32_sdwa v43, v43 dst_sel:WORD_1 dst_unused:UNUSED_PAD src0_sel:DWORD
	v_cvt_i32_f32_e32 v47, v47
	v_cvt_i32_f32_sdwa v51, v51 dst_sel:WORD_1 dst_unused:UNUSED_PAD src0_sel:DWORD
	v_cvt_i32_f32_sdwa v29, v29 dst_sel:BYTE_3 dst_unused:UNUSED_PAD src0_sel:DWORD
	v_cvt_i32_f32_sdwa v37, v37 dst_sel:BYTE_3 dst_unused:UNUSED_PAD src0_sel:DWORD
	v_cvt_i32_f32_sdwa v44, v44 dst_sel:BYTE_3 dst_unused:UNUSED_PAD src0_sel:DWORD
	s_waitcnt lgkmcnt(0)
	v_cvt_i32_f32_sdwa v52, v52 dst_sel:BYTE_3 dst_unused:UNUSED_PAD src0_sel:DWORD
	v_cvt_i32_f32_sdwa v45, v45 dst_sel:BYTE_3 dst_unused:UNUSED_PAD src0_sel:DWORD
	v_cvt_i32_f32_sdwa v53, v53 dst_sel:BYTE_3 dst_unused:UNUSED_PAD src0_sel:DWORD
	v_lshlrev_b32_e32 v14, 8, v14
	v_lshlrev_b32_e32 v32, 8, v32
	v_and_b32_e32 v26, 0xff0000, v26
	v_and_b32_e32 v34, 0xff0000, v34
	v_lshlrev_b32_e32 v15, 8, v15
	v_lshlrev_b32_e32 v33, 8, v33
	v_lshlrev_b32_e32 v40, 8, v40
	v_lshlrev_b32_e32 v48, 8, v48
	v_lshlrev_b32_e32 v41, 8, v41
	v_lshlrev_b32_e32 v49, 8, v49
	v_perm_b32 v12, v14, v12, s28
	v_perm_b32 v14, v32, v30, s28
	v_and_b32_e32 v27, 0xff0000, v27
	v_and_b32_e32 v35, 0xff0000, v35
	v_and_b32_e32 v42, 0xff0000, v42
	v_and_b32_e32 v50, 0xff0000, v50
	v_and_b32_e32 v43, 0xff0000, v43
	v_and_b32_e32 v51, 0xff0000, v51
	v_perm_b32 v15, v15, v13, s28
	v_perm_b32 v30, v33, v31, s28
	v_perm_b32 v31, v40, v38, s28
	v_perm_b32 v32, v48, v46, s28
	v_perm_b32 v33, v41, v39, s28
	v_perm_b32 v38, v49, v47, s28
	v_or3_b32 v12, v12, v26, v28
	v_or3_b32 v13, v14, v34, v36
	v_or3_b32 v14, v15, v27, v29
	v_or3_b32 v15, v30, v35, v37
	v_or3_b32 v26, v31, v42, v44
	v_or3_b32 v27, v32, v50, v52
	v_or3_b32 v28, v33, v43, v45
	v_or3_b32 v29, v38, v51, v53
	global_store_dwordx2 v[16:17], v[12:13], off
	global_store_dwordx2 v[18:19], v[14:15], off
	global_store_dwordx2 v[58:59], v[26:27], off
	global_store_dwordx2 v[60:61], v[28:29], off
	s_waitcnt lgkmcnt(0)
	v_add_u32_e32 v77, 0x420, v25
	v_add_u32_e32 v79, 0x428, v25
	v_add_u32_e32 v81, 0x840, v25
	v_add_u32_e32 v83, 0x848, v25
	v_add_u32_e32 v85, 0xc60, v25
	v_add_u32_e32 v87, 0xc68, v25
	v_add_u32_e32 v89, 0x1080, v25
	v_add_u32_e32 v91, 0x1088, v25
	v_add_u32_e32 v92, 0x14a0, v25
	v_add_u32_e32 v93, 0x14a8, v25
	v_add_u32_e32 v94, 0x18c0, v25
	v_add_u32_e32 v95, 0x18c8, v25
	v_add_u32_e32 v96, 0x1ce0, v25
	v_add_u32_e32 v97, 0x1ce8, v25
	v_lshl_add_u64 v[16:17], v[10:11], 0, s[26:27]
	v_lshl_add_u64 v[18:19], v[8:9], 0, s[26:27]
	v_lshl_add_u64 v[58:59], v[6:7], 0, s[26:27]
	v_lshl_add_u64 v[60:61], v[4:5], 0, s[26:27]
	v_lshl_add_u64 v[4:5], v[4:5], 0, 64
	v_lshl_add_u64 v[6:7], v[6:7], 0, 64
	v_lshl_add_u64 v[8:9], v[8:9], 0, 64
	v_lshl_add_u64 v[10:11], v[10:11], 0, 64
	s_waitcnt vmcnt(24)
; #define LAS __attribute__((address_space(3)))
;     ...
;         for (int i = 0; i < 8; ++i) { const int kk = 8 * i + kr; const int k = 64 * kb + kk; const f32x4 v = __builtin_nontemporal_load((const f32x4*)(W + (size_t)k * pitch)) * g[k];
;             LAS float* p = scr + kk * 33 + 4 * (lane & 7); p[0] = __builtin_rintf(v[0] * inv[0]); p[1] = __builtin_rintf(v[1] * inv[1]); p[2] = __builtin_rintf(v[2] * inv[2]); p[3] = __builtin_rintf(v[3] * inv[3]); }
	v_pk_mul_f32 v[14:15], v[138:139], v[186:187] op_sel_hi:[1,0]
	v_pk_mul_f32 v[12:13], v[140:141], v[186:187] op_sel_hi:[1,0]
	v_mul_f32_e32 v62, v20, v14
	v_mul_f32_e32 v63, v21, v15
	v_mul_f32_e32 v64, v22, v12
	v_mul_f32_e32 v65, v23, v13
	v_pk_mul_f32 v[14:15], v[142:143], v[188:189] op_sel_hi:[1,0]
	v_pk_mul_f32 v[12:13], v[144:145], v[188:189] op_sel_hi:[1,0]
	v_pk_mul_f32 v[26:27], v[148:149], v[190:191] op_sel_hi:[1,0]
	v_pk_mul_f32 v[28:29], v[146:147], v[190:191] op_sel_hi:[1,0]
	v_pk_mul_f32 v[30:31], v[152:153], v[192:193] op_sel_hi:[1,0]
	v_pk_mul_f32 v[32:33], v[150:151], v[192:193] op_sel_hi:[1,0]
	v_pk_mul_f32 v[34:35], v[156:157], v[194:195] op_sel_hi:[1,0]
	v_pk_mul_f32 v[36:37], v[154:155], v[194:195] op_sel_hi:[1,0]
	v_pk_mul_f32 v[38:39], v[160:161], v[196:197] op_sel_hi:[1,0]
	v_pk_mul_f32 v[40:41], v[158:159], v[196:197] op_sel_hi:[1,0]
	v_pk_mul_f32 v[42:43], v[164:165], v[198:199] op_sel_hi:[1,0]
	v_pk_mul_f32 v[44:45], v[162:163], v[198:199] op_sel_hi:[1,0]
	v_pk_mul_f32 v[46:47], v[168:169], v[200:201] op_sel_hi:[1,0]
	v_pk_mul_f32 v[48:49], v[166:167], v[200:201] op_sel_hi:[1,0]
	s_add_u32 s4, s4, 0x16000
	s_addc_u32 s5, s5, 0
	global_load_dwordx4 v[138:141], v250, s[4:5] nt
	global_load_dword v186, v251, s[6:7] offset:1792
	s_add_u32 s4, s4, 0x16000
	s_addc_u32 s5, s5, 0
	global_load_dwordx4 v[142:145], v250, s[4:5] nt
	global_load_dword v188, v251, s[6:7] offset:1824
	s_add_u32 s4, s4, 0x16000
	s_addc_u32 s5, s5, 0
	global_load_dwordx4 v[146:149], v250, s[4:5] nt
	global_load_dword v190, v251, s[6:7] offset:1856
	s_add_u32 s4, s4, 0x16000
	s_addc_u32 s5, s5, 0
	global_load_dwordx4 v[150:153], v250, s[4:5] nt
	global_load_dword v192, v251, s[6:7] offset:1888
	s_add_u32 s4, s4, 0x16000
	s_addc_u32 s5, s5, 0
	global_load_dwordx4 v[154:157], v250, s[4:5] nt
	global_load_dword v194, v251, s[6:7] offset:1920
	s_add_u32 s4, s4, 0x16000
	s_addc_u32 s5, s5, 0
	global_load_dwordx4 v[158:161], v250, s[4:5] nt
	global_load_dword v196, v251, s[6:7] offset:1952
	s_add_u32 s4, s4, 0x16000
	s_addc_u32 s5, s5, 0
	global_load_dwordx4 v[162:165], v250, s[4:5] nt
	global_load_dword v198, v251, s[6:7] offset:1984
	s_add_u32 s4, s4, 0x16000
	s_addc_u32 s5, s5, 0
	global_load_dwordx4 v[166:169], v250, s[4:5] nt
	global_load_dword v200, v251, s[6:7] offset:2016
	v_mul_f32_e32 v14, v20, v14
	v_mul_f32_e32 v15, v21, v15
	v_rndne_f32_e32 v50, v62
	v_rndne_f32_e32 v51, v63
	v_mul_f32_e32 v12, v22, v12
	v_mul_f32_e32 v13, v23, v13
	v_mul_f32_e32 v28, v20, v28
	v_mul_f32_e32 v29, v21, v29
	v_mul_f32_e32 v26, v22, v26
	v_mul_f32_e32 v27, v23, v27
	v_mul_f32_e32 v32, v20, v32
	v_mul_f32_e32 v33, v21, v33
	v_mul_f32_e32 v30, v22, v30
	v_mul_f32_e32 v31, v23, v31
	v_mul_f32_e32 v36, v20, v36
	v_mul_f32_e32 v37, v21, v37
	v_mul_f32_e32 v34, v22, v34
	v_mul_f32_e32 v35, v23, v35
	v_mul_f32_e32 v40, v20, v40
	v_mul_f32_e32 v41, v21, v41
	v_mul_f32_e32 v38, v22, v38
	v_mul_f32_e32 v39, v23, v39
	v_mul_f32_e32 v44, v20, v44
	v_mul_f32_e32 v45, v21, v45
	v_mul_f32_e32 v42, v22, v42
	v_mul_f32_e32 v43, v23, v43
	v_mul_f32_e32 v48, v20, v48
	v_mul_f32_e32 v49, v21, v49
	v_mul_f32_e32 v46, v22, v46
	v_mul_f32_e32 v47, v23, v47
	v_rndne_f32_e32 v14, v14
	v_rndne_f32_e32 v15, v15
	v_rndne_f32_e32 v52, v64
	v_rndne_f32_e32 v53, v65
	ds_write2_b32 v25, v50, v51 offset1:1
	ds_write2_b32 v25, v52, v53 offset0:2 offset1:3
	v_rndne_f32_e32 v12, v12
	v_rndne_f32_e32 v13, v13
	v_rndne_f32_e32 v28, v28
	v_rndne_f32_e32 v29, v29
	v_rndne_f32_e32 v26, v26
	v_rndne_f32_e32 v27, v27
	v_rndne_f32_e32 v32, v32
	v_rndne_f32_e32 v33, v33
	v_rndne_f32_e32 v30, v30
	v_rndne_f32_e32 v31, v31
	v_rndne_f32_e32 v36, v36
	v_rndne_f32_e32 v37, v37
	v_rndne_f32_e32 v34, v34
	v_rndne_f32_e32 v35, v35
	v_rndne_f32_e32 v40, v40
	v_rndne_f32_e32 v41, v41
	v_rndne_f32_e32 v38, v38
	v_rndne_f32_e32 v39, v39
	v_rndne_f32_e32 v44, v44
	v_rndne_f32_e32 v45, v45
	v_rndne_f32_e32 v42, v42
	v_rndne_f32_e32 v43, v43
	v_rndne_f32_e32 v48, v48
	v_rndne_f32_e32 v49, v49
	v_rndne_f32_e32 v46, v46
	v_rndne_f32_e32 v47, v47
	ds_write2_b32 v77, v14, v15 offset1:1
	ds_write2_b32 v79, v12, v13 offset1:1
	ds_write2_b32 v81, v28, v29 offset1:1
	ds_write2_b32 v83, v26, v27 offset1:1
	ds_write2_b32 v85, v32, v33 offset1:1
	ds_write2_b32 v87, v30, v31 offset1:1
	ds_write2_b32 v89, v36, v37 offset1:1
	ds_write2_b32 v91, v34, v35 offset1:1
	ds_write2_b32 v92, v40, v41 offset1:1
	ds_write2_b32 v93, v38, v39 offset1:1
	ds_write2_b32 v94, v44, v45 offset1:1
	ds_write2_b32 v95, v42, v43 offset1:1
	ds_write2_b32 v96, v48, v49 offset1:1
	ds_write2_b32 v97, v46, v47 offset1:1
	s_waitcnt lgkmcnt(0)
	ds_read2_b32 v[12:13], v24 offset1:8
	ds_read2_b32 v[14:15], v24 offset0:33 offset1:41
	ds_read2_b32 v[26:27], v24 offset0:66 offset1:74
	ds_read2_b32 v[28:29], v24 offset0:99 offset1:107
	ds_read2_b32 v[30:31], v24 offset0:132 offset1:140
	ds_read2_b32 v[32:33], v24 offset0:165 offset1:173
	ds_read2_b32 v[34:35], v24 offset0:198 offset1:206
	ds_read2_b32 v[36:37], v24 offset0:231 offset1:239
	ds_read2_b32 v[38:39], v24 offset0:16 offset1:24
	ds_read2_b32 v[40:41], v24 offset0:49 offset1:57
	ds_read2_b32 v[42:43], v24 offset0:82 offset1:90
	ds_read2_b32 v[44:45], v24 offset0:115 offset1:123
	ds_read2_b32 v[46:47], v24 offset0:148 offset1:156
	ds_read2_b32 v[48:49], v24 offset0:181 offset1:189
	ds_read2_b32 v[50:51], v24 offset0:214 offset1:222
	ds_read2_b32 v[52:53], v24 offset0:247 offset1:255
	s_waitcnt lgkmcnt(14)
	v_cvt_i32_f32_e32 v14, v14
	s_waitcnt lgkmcnt(10)
	v_cvt_i32_f32_e32 v32, v32
	v_cvt_i32_f32_e32 v12, v12
	v_cvt_i32_f32_sdwa v26, v26 dst_sel:WORD_1 dst_unused:UNUSED_PAD src0_sel:DWORD
	v_cvt_i32_f32_e32 v30, v30
	s_waitcnt lgkmcnt(9)
; #define LAS __attribute__((address_space(3)))
; #define GAS __attribute__((address_space(1)))
; #define LDS_WAIT() asm volatile("s_waitcnt lgkmcnt(0)" ::: "memory")
;     ...
;         for (int i = 0; i < 8; ++i) { const int kk = 8 * i + kr; const int k = 64 * kb + kk; const f32x4 v = __builtin_nontemporal_load((const f32x4*)(W + (size_t)k * pitch)) * g[k];
;             LAS float* p = scr + kk * 33 + 4 * (lane & 7); p[0] = __builtin_rintf(v[0] * inv[0]); p[1] = __builtin_rintf(v[1] * inv[1]); p[2] = __builtin_rintf(v[2] * inv[2]); p[3] = __builtin_rintf(v[3] * inv[3]); }
;         LDS_WAIT(); asm volatile("" ::: "memory");
;         const int c = lane & 7;
; #pragma unroll
;         for (int j = 0; j < 4; ++j) { const int n = (lane >> 3) + 8 * j; const LAS float* sp = scr + (8 * c) * 33 + n;
;             u32x2 o;
;             o.x = ((unsigned)(int)sp[0 * 33] & 0xFFu) | (((unsigned)(int)sp[1 * 33] & 0xFFu) << 8) | (((unsigned)(int)sp[2 * 33] & 0xFFu) << 16) | (((unsigned)(int)sp[3 * 33] & 0xFFu) << 24);
;             o.y = ((unsigned)(int)sp[4 * 33] & 0xFFu) | (((unsigned)(int)sp[5 * 33] & 0xFFu) << 8) | (((unsigned)(int)sp[6 * 33] & 0xFFu) << 16) | (((unsigned)(int)sp[7 * 33] & 0xFFu) << 24);
;             *(GAS u32x2*)(dst + (size_t)(n0 + n) * D + 64 * kb + 8 * c) = o; }
	v_cvt_i32_f32_sdwa v34, v34 dst_sel:WORD_1 dst_unused:UNUSED_PAD src0_sel:DWORD
	v_cvt_i32_f32_e32 v15, v15
	v_cvt_i32_f32_e32 v33, v33
	s_waitcnt lgkmcnt(6)
	v_cvt_i32_f32_e32 v40, v40
	s_waitcnt lgkmcnt(2)
	v_cvt_i32_f32_e32 v48, v48
	v_cvt_i32_f32_e32 v41, v41
	v_cvt_i32_f32_e32 v49, v49
	v_cvt_i32_f32_sdwa v28, v28 dst_sel:BYTE_3 dst_unused:UNUSED_PAD src0_sel:DWORD
	v_cvt_i32_f32_sdwa v36, v36 dst_sel:BYTE_3 dst_unused:UNUSED_PAD src0_sel:DWORD
	v_cvt_i32_f32_e32 v13, v13
	v_cvt_i32_f32_sdwa v27, v27 dst_sel:WORD_1 dst_unused:UNUSED_PAD src0_sel:DWORD
	v_cvt_i32_f32_e32 v31, v31
	v_cvt_i32_f32_sdwa v35, v35 dst_sel:WORD_1 dst_unused:UNUSED_PAD src0_sel:DWORD
	v_cvt_i32_f32_e32 v38, v38
	v_cvt_i32_f32_sdwa v42, v42 dst_sel:WORD_1 dst_unused:UNUSED_PAD src0_sel:DWORD
	v_cvt_i32_f32_e32 v46, v46
	s_waitcnt lgkmcnt(1)
	v_cvt_i32_f32_sdwa v50, v50 dst_sel:WORD_1 dst_unused:UNUSED_PAD src0_sel:DWORD
	v_cvt_i32_f32_e32 v39, v39
	v_cvt_i32_f32_sdwa v43, v43 dst_sel:WORD_1 dst_unused:UNUSED_PAD src0_sel:DWORD
	v_cvt_i32_f32_e32 v47, v47
	v_cvt_i32_f32_sdwa v51, v51 dst_sel:WORD_1 dst_unused:UNUSED_PAD src0_sel:DWORD
	v_cvt_i32_f32_sdwa v29, v29 dst_sel:BYTE_3 dst_unused:UNUSED_PAD src0_sel:DWORD
	v_cvt_i32_f32_sdwa v37, v37 dst_sel:BYTE_3 dst_unused:UNUSED_PAD src0_sel:DWORD
	v_cvt_i32_f32_sdwa v44, v44 dst_sel:BYTE_3 dst_unused:UNUSED_PAD src0_sel:DWORD
	s_waitcnt lgkmcnt(0)
	v_cvt_i32_f32_sdwa v52, v52 dst_sel:BYTE_3 dst_unused:UNUSED_PAD src0_sel:DWORD
	v_cvt_i32_f32_sdwa v45, v45 dst_sel:BYTE_3 dst_unused:UNUSED_PAD src0_sel:DWORD
	v_cvt_i32_f32_sdwa v53, v53 dst_sel:BYTE_3 dst_unused:UNUSED_PAD src0_sel:DWORD
	v_lshlrev_b32_e32 v14, 8, v14
	v_lshlrev_b32_e32 v32, 8, v32
	v_and_b32_e32 v26, 0xff0000, v26
	v_and_b32_e32 v34, 0xff0000, v34
	v_lshlrev_b32_e32 v15, 8, v15
	v_lshlrev_b32_e32 v33, 8, v33
	v_lshlrev_b32_e32 v40, 8, v40
	v_lshlrev_b32_e32 v48, 8, v48
	v_lshlrev_b32_e32 v41, 8, v41
	v_lshlrev_b32_e32 v49, 8, v49
	v_perm_b32 v12, v14, v12, s28
	v_perm_b32 v14, v32, v30, s28
	v_and_b32_e32 v27, 0xff0000, v27
	v_and_b32_e32 v35, 0xff0000, v35
	v_and_b32_e32 v42, 0xff0000, v42
	v_and_b32_e32 v50, 0xff0000, v50
	v_and_b32_e32 v43, 0xff0000, v43
	v_and_b32_e32 v51, 0xff0000, v51
	v_perm_b32 v15, v15, v13, s28
	v_perm_b32 v30, v33, v31, s28
	v_perm_b32 v31, v40, v38, s28
	v_perm_b32 v32, v48, v46, s28
	v_perm_b32 v33, v41, v39, s28
	v_perm_b32 v38, v49, v47, s28
	v_or3_b32 v12, v12, v26, v28
	v_or3_b32 v13, v14, v34, v36
	v_or3_b32 v14, v15, v27, v29
	v_or3_b32 v15, v30, v35, v37
	v_or3_b32 v26, v31, v42, v44
	v_or3_b32 v27, v32, v50, v52
	v_or3_b32 v28, v33, v43, v45
	v_or3_b32 v29, v38, v51, v53
	global_store_dwordx2 v[16:17], v[12:13], off
	global_store_dwordx2 v[18:19], v[14:15], off
	global_store_dwordx2 v[58:59], v[26:27], off
	global_store_dwordx2 v[60:61], v[28:29], off
	s_waitcnt lgkmcnt(0)
	v_add_u32_e32 v77, 0x420, v25
	v_add_u32_e32 v79, 0x428, v25
	v_add_u32_e32 v81, 0x840, v25
	v_add_u32_e32 v83, 0x848, v25
	v_add_u32_e32 v85, 0xc60, v25
	v_add_u32_e32 v87, 0xc68, v25
	v_add_u32_e32 v89, 0x1080, v25
	v_add_u32_e32 v91, 0x1088, v25
	v_add_u32_e32 v92, 0x14a0, v25
	v_add_u32_e32 v93, 0x14a8, v25
	v_add_u32_e32 v94, 0x18c0, v25
	v_add_u32_e32 v95, 0x18c8, v25
	v_add_u32_e32 v96, 0x1ce0, v25
	v_add_u32_e32 v97, 0x1ce8, v25
	v_lshl_add_u64 v[16:17], v[10:11], 0, s[26:27]
	v_lshl_add_u64 v[18:19], v[8:9], 0, s[26:27]
	v_lshl_add_u64 v[58:59], v[6:7], 0, s[26:27]
	v_lshl_add_u64 v[60:61], v[4:5], 0, s[26:27]
	v_lshl_add_u64 v[4:5], v[4:5], 0, 64
	v_lshl_add_u64 v[6:7], v[6:7], 0, 64
	v_lshl_add_u64 v[8:9], v[8:9], 0, 64
	v_lshl_add_u64 v[10:11], v[10:11], 0, 64
	s_waitcnt vmcnt(24)
	v_pk_mul_f32 v[14:15], v[106:107], v[170:171] op_sel_hi:[1,0]
	v_pk_mul_f32 v[12:13], v[108:109], v[170:171] op_sel_hi:[1,0]
	v_mul_f32_e32 v62, v20, v14
	v_mul_f32_e32 v63, v21, v15
	v_mul_f32_e32 v64, v22, v12
	v_mul_f32_e32 v65, v23, v13
	v_pk_mul_f32 v[14:15], v[110:111], v[172:173] op_sel_hi:[1,0]
	v_pk_mul_f32 v[12:13], v[112:113], v[172:173] op_sel_hi:[1,0]
	v_pk_mul_f32 v[26:27], v[116:117], v[174:175] op_sel_hi:[1,0]
	v_pk_mul_f32 v[28:29], v[114:115], v[174:175] op_sel_hi:[1,0]
	v_pk_mul_f32 v[30:31], v[120:121], v[176:177] op_sel_hi:[1,0]
	v_pk_mul_f32 v[32:33], v[118:119], v[176:177] op_sel_hi:[1,0]
	v_pk_mul_f32 v[34:35], v[124:125], v[178:179] op_sel_hi:[1,0]
	v_pk_mul_f32 v[36:37], v[122:123], v[178:179] op_sel_hi:[1,0]
	v_pk_mul_f32 v[38:39], v[128:129], v[180:181] op_sel_hi:[1,0]
	v_pk_mul_f32 v[40:41], v[126:127], v[180:181] op_sel_hi:[1,0]
	v_pk_mul_f32 v[42:43], v[132:133], v[182:183] op_sel_hi:[1,0]
	v_pk_mul_f32 v[44:45], v[130:131], v[182:183] op_sel_hi:[1,0]
	v_pk_mul_f32 v[46:47], v[136:137], v[184:185] op_sel_hi:[1,0]
	v_pk_mul_f32 v[48:49], v[134:135], v[184:185] op_sel_hi:[1,0]
	s_add_u32 s4, s4, 0x16000
	s_addc_u32 s5, s5, 0
	global_load_dwordx4 v[106:109], v250, s[4:5] nt
	global_load_dword v170, v251, s[6:7] offset:2048
	s_add_u32 s4, s4, 0x16000
	s_addc_u32 s5, s5, 0
	global_load_dwordx4 v[110:113], v250, s[4:5] nt
	global_load_dword v172, v251, s[6:7] offset:2080
	s_add_u32 s4, s4, 0x16000
	s_addc_u32 s5, s5, 0
	global_load_dwordx4 v[114:117], v250, s[4:5] nt
	global_load_dword v174, v251, s[6:7] offset:2112
	s_add_u32 s4, s4, 0x16000
	s_addc_u32 s5, s5, 0
	global_load_dwordx4 v[118:121], v250, s[4:5] nt
	global_load_dword v176, v251, s[6:7] offset:2144
	s_add_u32 s4, s4, 0x16000
	s_addc_u32 s5, s5, 0
	global_load_dwordx4 v[122:125], v250, s[4:5] nt
	global_load_dword v178, v251, s[6:7] offset:2176
	s_add_u32 s4, s4, 0x16000
	s_addc_u32 s5, s5, 0
	global_load_dwordx4 v[126:129], v250, s[4:5] nt
; #define LAS __attribute__((address_space(3)))
; #define GAS __attribute__((address_space(1)))
; #define LDS_WAIT() asm volatile("s_waitcnt lgkmcnt(0)" ::: "memory")
;     ...
;         for (int i = 0; i < 8; ++i) { const int kk = 8 * i + kr; const int k = 64 * kb + kk; const f32x4 v = __builtin_nontemporal_load((const f32x4*)(W + (size_t)k * pitch)) * g[k];
;             LAS float* p = scr + kk * 33 + 4 * (lane & 7); p[0] = __builtin_rintf(v[0] * inv[0]); p[1] = __builtin_rintf(v[1] * inv[1]); p[2] = __builtin_rintf(v[2] * inv[2]); p[3] = __builtin_rintf(v[3] * inv[3]); }
;         LDS_WAIT(); asm volatile("" ::: "memory");
;         const int c = lane & 7;
; #pragma unroll
;         for (int j = 0; j < 4; ++j) { const int n = (lane >> 3) + 8 * j; const LAS float* sp = scr + (8 * c) * 33 + n;
;             u32x2 o;
;             o.x = ((unsigned)(int)sp[0 * 33] & 0xFFu) | (((unsigned)(int)sp[1 * 33] & 0xFFu) << 8) | (((unsigned)(int)sp[2 * 33] & 0xFFu) << 16) | (((unsigned)(int)sp[3 * 33] & 0xFFu) << 24);
;             o.y = ((unsigned)(int)sp[4 * 33] & 0xFFu) | (((unsigned)(int)sp[5 * 33] & 0xFFu) << 8) | (((unsigned)(int)sp[6 * 33] & 0xFFu) << 16) | (((unsigned)(int)sp[7 * 33] & 0xFFu) << 24);
;             *(GAS u32x2*)(dst + (size_t)(n0 + n) * D + 64 * kb + 8 * c) = o; }
	global_load_dword v180, v251, s[6:7] offset:2208
	s_add_u32 s4, s4, 0x16000
	s_addc_u32 s5, s5, 0
	global_load_dwordx4 v[130:133], v250, s[4:5] nt
	global_load_dword v182, v251, s[6:7] offset:2240
	s_add_u32 s4, s4, 0x16000
	s_addc_u32 s5, s5, 0
	global_load_dwordx4 v[134:137], v250, s[4:5] nt
	global_load_dword v184, v251, s[6:7] offset:2272
	v_mul_f32_e32 v14, v20, v14
	v_mul_f32_e32 v15, v21, v15
	v_rndne_f32_e32 v50, v62
	v_rndne_f32_e32 v51, v63
	v_mul_f32_e32 v12, v22, v12
	v_mul_f32_e32 v13, v23, v13
	v_mul_f32_e32 v28, v20, v28
	v_mul_f32_e32 v29, v21, v29
	v_mul_f32_e32 v26, v22, v26
	v_mul_f32_e32 v27, v23, v27
	v_mul_f32_e32 v32, v20, v32
	v_mul_f32_e32 v33, v21, v33
	v_mul_f32_e32 v30, v22, v30
	v_mul_f32_e32 v31, v23, v31
	v_mul_f32_e32 v36, v20, v36
	v_mul_f32_e32 v37, v21, v37
	v_mul_f32_e32 v34, v22, v34
	v_mul_f32_e32 v35, v23, v35
	v_mul_f32_e32 v40, v20, v40
	v_mul_f32_e32 v41, v21, v41
	v_mul_f32_e32 v38, v22, v38
	v_mul_f32_e32 v39, v23, v39
	v_mul_f32_e32 v44, v20, v44
	v_mul_f32_e32 v45, v21, v45
	v_mul_f32_e32 v42, v22, v42
	v_mul_f32_e32 v43, v23, v43
	v_mul_f32_e32 v48, v20, v48
	v_mul_f32_e32 v49, v21, v49
	v_mul_f32_e32 v46, v22, v46
	v_mul_f32_e32 v47, v23, v47
	v_rndne_f32_e32 v14, v14
	v_rndne_f32_e32 v15, v15
	v_rndne_f32_e32 v52, v64
	v_rndne_f32_e32 v53, v65
	ds_write2_b32 v25, v50, v51 offset1:1
	ds_write2_b32 v25, v52, v53 offset0:2 offset1:3
	v_rndne_f32_e32 v12, v12
	v_rndne_f32_e32 v13, v13
	v_rndne_f32_e32 v28, v28
	v_rndne_f32_e32 v29, v29
	v_rndne_f32_e32 v26, v26
	v_rndne_f32_e32 v27, v27
	v_rndne_f32_e32 v32, v32
	v_rndne_f32_e32 v33, v33
	v_rndne_f32_e32 v30, v30
	v_rndne_f32_e32 v31, v31
	v_rndne_f32_e32 v36, v36
	v_rndne_f32_e32 v37, v37
	v_rndne_f32_e32 v34, v34
	v_rndne_f32_e32 v35, v35
	v_rndne_f32_e32 v40, v40
	v_rndne_f32_e32 v41, v41
	v_rndne_f32_e32 v38, v38
	v_rndne_f32_e32 v39, v39
	v_rndne_f32_e32 v44, v44
	v_rndne_f32_e32 v45, v45
	v_rndne_f32_e32 v42, v42
	v_rndne_f32_e32 v43, v43
	v_rndne_f32_e32 v48, v48
	v_rndne_f32_e32 v49, v49
	v_rndne_f32_e32 v46, v46
	v_rndne_f32_e32 v47, v47
	ds_write2_b32 v77, v14, v15 offset1:1
	ds_write2_b32 v79, v12, v13 offset1:1
	ds_write2_b32 v81, v28, v29 offset1:1
	ds_write2_b32 v83, v26, v27 offset1:1
	ds_write2_b32 v85, v32, v33 offset1:1
	ds_write2_b32 v87, v30, v31 offset1:1
	ds_write2_b32 v89, v36, v37 offset1:1
	ds_write2_b32 v91, v34, v35 offset1:1
	ds_write2_b32 v92, v40, v41 offset1:1
	ds_write2_b32 v93, v38, v39 offset1:1
	ds_write2_b32 v94, v44, v45 offset1:1
	ds_write2_b32 v95, v42, v43 offset1:1
	ds_write2_b32 v96, v48, v49 offset1:1
	ds_write2_b32 v97, v46, v47 offset1:1
	s_waitcnt lgkmcnt(0)
	ds_read2_b32 v[12:13], v24 offset1:8
	ds_read2_b32 v[14:15], v24 offset0:33 offset1:41
	ds_read2_b32 v[26:27], v24 offset0:66 offset1:74
	ds_read2_b32 v[28:29], v24 offset0:99 offset1:107
	ds_read2_b32 v[30:31], v24 offset0:132 offset1:140
	ds_read2_b32 v[32:33], v24 offset0:165 offset1:173
	ds_read2_b32 v[34:35], v24 offset0:198 offset1:206
	ds_read2_b32 v[36:37], v24 offset0:231 offset1:239
	ds_read2_b32 v[38:39], v24 offset0:16 offset1:24
	ds_read2_b32 v[40:41], v24 offset0:49 offset1:57
	ds_read2_b32 v[42:43], v24 offset0:82 offset1:90
	ds_read2_b32 v[44:45], v24 offset0:115 offset1:123
	ds_read2_b32 v[46:47], v24 offset0:148 offset1:156
	ds_read2_b32 v[48:49], v24 offset0:181 offset1:189
	ds_read2_b32 v[50:51], v24 offset0:214 offset1:222
	ds_read2_b32 v[52:53], v24 offset0:247 offset1:255
	s_waitcnt lgkmcnt(14)
	v_cvt_i32_f32_e32 v14, v14
	s_waitcnt lgkmcnt(10)
	v_cvt_i32_f32_e32 v32, v32
	v_cvt_i32_f32_e32 v12, v12
	v_cvt_i32_f32_sdwa v26, v26 dst_sel:WORD_1 dst_unused:UNUSED_PAD src0_sel:DWORD
	v_cvt_i32_f32_e32 v30, v30
	s_waitcnt lgkmcnt(9)
	v_cvt_i32_f32_sdwa v34, v34 dst_sel:WORD_1 dst_unused:UNUSED_PAD src0_sel:DWORD
	v_cvt_i32_f32_e32 v15, v15
	v_cvt_i32_f32_e32 v33, v33
	s_waitcnt lgkmcnt(6)
	v_cvt_i32_f32_e32 v40, v40
	s_waitcnt lgkmcnt(2)
	v_cvt_i32_f32_e32 v48, v48
	v_cvt_i32_f32_e32 v41, v41
	v_cvt_i32_f32_e32 v49, v49
	v_cvt_i32_f32_sdwa v28, v28 dst_sel:BYTE_3 dst_unused:UNUSED_PAD src0_sel:DWORD
	v_cvt_i32_f32_sdwa v36, v36 dst_sel:BYTE_3 dst_unused:UNUSED_PAD src0_sel:DWORD
	v_cvt_i32_f32_e32 v13, v13
	v_cvt_i32_f32_sdwa v27, v27 dst_sel:WORD_1 dst_unused:UNUSED_PAD src0_sel:DWORD
	v_cvt_i32_f32_e32 v31, v31
	v_cvt_i32_f32_sdwa v35, v35 dst_sel:WORD_1 dst_unused:UNUSED_PAD src0_sel:DWORD
	v_cvt_i32_f32_e32 v38, v38
	v_cvt_i32_f32_sdwa v42, v42 dst_sel:WORD_1 dst_unused:UNUSED_PAD src0_sel:DWORD
	v_cvt_i32_f32_e32 v46, v46
	s_waitcnt lgkmcnt(1)
	v_cvt_i32_f32_sdwa v50, v50 dst_sel:WORD_1 dst_unused:UNUSED_PAD src0_sel:DWORD
	v_cvt_i32_f32_e32 v39, v39
	v_cvt_i32_f32_sdwa v43, v43 dst_sel:WORD_1 dst_unused:UNUSED_PAD src0_sel:DWORD
	v_cvt_i32_f32_e32 v47, v47
	v_cvt_i32_f32_sdwa v51, v51 dst_sel:WORD_1 dst_unused:UNUSED_PAD src0_sel:DWORD
	v_cvt_i32_f32_sdwa v29, v29 dst_sel:BYTE_3 dst_unused:UNUSED_PAD src0_sel:DWORD
	v_cvt_i32_f32_sdwa v37, v37 dst_sel:BYTE_3 dst_unused:UNUSED_PAD src0_sel:DWORD
	v_cvt_i32_f32_sdwa v44, v44 dst_sel:BYTE_3 dst_unused:UNUSED_PAD src0_sel:DWORD
	s_waitcnt lgkmcnt(0)
; #define LAS __attribute__((address_space(3)))
; #define GAS __attribute__((address_space(1)))
; #define LDS_WAIT() asm volatile("s_waitcnt lgkmcnt(0)" ::: "memory")
;     ...
;         for (int i = 0; i < 8; ++i) { const int kk = 8 * i + kr; const int k = 64 * kb + kk; const f32x4 v = __builtin_nontemporal_load((const f32x4*)(W + (size_t)k * pitch)) * g[k];
;             LAS float* p = scr + kk * 33 + 4 * (lane & 7); p[0] = __builtin_rintf(v[0] * inv[0]); p[1] = __builtin_rintf(v[1] * inv[1]); p[2] = __builtin_rintf(v[2] * inv[2]); p[3] = __builtin_rintf(v[3] * inv[3]); }
;         LDS_WAIT(); asm volatile("" ::: "memory");
;         const int c = lane & 7;
; #pragma unroll
;         for (int j = 0; j < 4; ++j) { const int n = (lane >> 3) + 8 * j; const LAS float* sp = scr + (8 * c) * 33 + n;
;             u32x2 o;
;             o.x = ((unsigned)(int)sp[0 * 33] & 0xFFu) | (((unsigned)(int)sp[1 * 33] & 0xFFu) << 8) | (((unsigned)(int)sp[2 * 33] & 0xFFu) << 16) | (((unsigned)(int)sp[3 * 33] & 0xFFu) << 24);
;             o.y = ((unsigned)(int)sp[4 * 33] & 0xFFu) | (((unsigned)(int)sp[5 * 33] & 0xFFu) << 8) | (((unsigned)(int)sp[6 * 33] & 0xFFu) << 16) | (((unsigned)(int)sp[7 * 33] & 0xFFu) << 24);
;             *(GAS u32x2*)(dst + (size_t)(n0 + n) * D + 64 * kb + 8 * c) = o; }
	v_cvt_i32_f32_sdwa v52, v52 dst_sel:BYTE_3 dst_unused:UNUSED_PAD src0_sel:DWORD
	v_cvt_i32_f32_sdwa v45, v45 dst_sel:BYTE_3 dst_unused:UNUSED_PAD src0_sel:DWORD
	v_cvt_i32_f32_sdwa v53, v53 dst_sel:BYTE_3 dst_unused:UNUSED_PAD src0_sel:DWORD
	v_lshlrev_b32_e32 v14, 8, v14
	v_lshlrev_b32_e32 v32, 8, v32
	v_and_b32_e32 v26, 0xff0000, v26
	v_and_b32_e32 v34, 0xff0000, v34
	v_lshlrev_b32_e32 v15, 8, v15
	v_lshlrev_b32_e32 v33, 8, v33
	v_lshlrev_b32_e32 v40, 8, v40
	v_lshlrev_b32_e32 v48, 8, v48
	v_lshlrev_b32_e32 v41, 8, v41
	v_lshlrev_b32_e32 v49, 8, v49
	v_perm_b32 v12, v14, v12, s28
	v_perm_b32 v14, v32, v30, s28
	v_and_b32_e32 v27, 0xff0000, v27
	v_and_b32_e32 v35, 0xff0000, v35
	v_and_b32_e32 v42, 0xff0000, v42
	v_and_b32_e32 v50, 0xff0000, v50
	v_and_b32_e32 v43, 0xff0000, v43
	v_and_b32_e32 v51, 0xff0000, v51
	v_perm_b32 v15, v15, v13, s28
	v_perm_b32 v30, v33, v31, s28
	v_perm_b32 v31, v40, v38, s28
	v_perm_b32 v32, v48, v46, s28
	v_perm_b32 v33, v41, v39, s28
	v_perm_b32 v38, v49, v47, s28
	v_or3_b32 v12, v12, v26, v28
	v_or3_b32 v13, v14, v34, v36
	v_or3_b32 v14, v15, v27, v29
	v_or3_b32 v15, v30, v35, v37
	v_or3_b32 v26, v31, v42, v44
	v_or3_b32 v27, v32, v50, v52
	v_or3_b32 v28, v33, v43, v45
	v_or3_b32 v29, v38, v51, v53
	global_store_dwordx2 v[16:17], v[12:13], off
	global_store_dwordx2 v[18:19], v[14:15], off
	global_store_dwordx2 v[58:59], v[26:27], off
	global_store_dwordx2 v[60:61], v[28:29], off
	s_waitcnt lgkmcnt(0)
	v_add_u32_e32 v77, 0x420, v25
	v_add_u32_e32 v79, 0x428, v25
	v_add_u32_e32 v81, 0x840, v25
	v_add_u32_e32 v83, 0x848, v25
	v_add_u32_e32 v85, 0xc60, v25
	v_add_u32_e32 v87, 0xc68, v25
	v_add_u32_e32 v89, 0x1080, v25
	v_add_u32_e32 v91, 0x1088, v25
	v_add_u32_e32 v92, 0x14a0, v25
	v_add_u32_e32 v93, 0x14a8, v25
	v_add_u32_e32 v94, 0x18c0, v25
	v_add_u32_e32 v95, 0x18c8, v25
	v_add_u32_e32 v96, 0x1ce0, v25
	v_add_u32_e32 v97, 0x1ce8, v25
	v_lshl_add_u64 v[16:17], v[10:11], 0, s[26:27]
	v_lshl_add_u64 v[18:19], v[8:9], 0, s[26:27]
	v_lshl_add_u64 v[58:59], v[6:7], 0, s[26:27]
	v_lshl_add_u64 v[60:61], v[4:5], 0, s[26:27]
	v_lshl_add_u64 v[4:5], v[4:5], 0, 64
	v_lshl_add_u64 v[6:7], v[6:7], 0, 64
	v_lshl_add_u64 v[8:9], v[8:9], 0, 64
	v_lshl_add_u64 v[10:11], v[10:11], 0, 64
	s_waitcnt vmcnt(24)
	v_pk_mul_f32 v[14:15], v[138:139], v[186:187] op_sel_hi:[1,0]
	v_pk_mul_f32 v[12:13], v[140:141], v[186:187] op_sel_hi:[1,0]
	v_mul_f32_e32 v62, v20, v14
	v_mul_f32_e32 v63, v21, v15
	v_mul_f32_e32 v64, v22, v12
	v_mul_f32_e32 v65, v23, v13
	v_pk_mul_f32 v[14:15], v[142:143], v[188:189] op_sel_hi:[1,0]
	v_pk_mul_f32 v[12:13], v[144:145], v[188:189] op_sel_hi:[1,0]
	v_pk_mul_f32 v[26:27], v[148:149], v[190:191] op_sel_hi:[1,0]
	v_pk_mul_f32 v[28:29], v[146:147], v[190:191] op_sel_hi:[1,0]
	v_pk_mul_f32 v[30:31], v[152:153], v[192:193] op_sel_hi:[1,0]
	v_pk_mul_f32 v[32:33], v[150:151], v[192:193] op_sel_hi:[1,0]
	v_pk_mul_f32 v[34:35], v[156:157], v[194:195] op_sel_hi:[1,0]
	v_pk_mul_f32 v[36:37], v[154:155], v[194:195] op_sel_hi:[1,0]
	v_pk_mul_f32 v[38:39], v[160:161], v[196:197] op_sel_hi:[1,0]
	v_pk_mul_f32 v[40:41], v[158:159], v[196:197] op_sel_hi:[1,0]
	v_pk_mul_f32 v[42:43], v[164:165], v[198:199] op_sel_hi:[1,0]
	v_pk_mul_f32 v[44:45], v[162:163], v[198:199] op_sel_hi:[1,0]
	v_pk_mul_f32 v[46:47], v[168:169], v[200:201] op_sel_hi:[1,0]
	v_pk_mul_f32 v[48:49], v[166:167], v[200:201] op_sel_hi:[1,0]
	s_add_u32 s4, s4, 0x16000
	s_addc_u32 s5, s5, 0
	global_load_dwordx4 v[138:141], v250, s[4:5] nt
	global_load_dword v186, v251, s[6:7] offset:2304
	s_add_u32 s4, s4, 0x16000
	s_addc_u32 s5, s5, 0
	global_load_dwordx4 v[142:145], v250, s[4:5] nt
	global_load_dword v188, v251, s[6:7] offset:2336
	s_add_u32 s4, s4, 0x16000
	s_addc_u32 s5, s5, 0
	global_load_dwordx4 v[146:149], v250, s[4:5] nt
	global_load_dword v190, v251, s[6:7] offset:2368
	s_add_u32 s4, s4, 0x16000
	s_addc_u32 s5, s5, 0
	global_load_dwordx4 v[150:153], v250, s[4:5] nt
	global_load_dword v192, v251, s[6:7] offset:2400
	s_add_u32 s4, s4, 0x16000
	s_addc_u32 s5, s5, 0
	global_load_dwordx4 v[154:157], v250, s[4:5] nt
	global_load_dword v194, v251, s[6:7] offset:2432
	s_add_u32 s4, s4, 0x16000
	s_addc_u32 s5, s5, 0
	global_load_dwordx4 v[158:161], v250, s[4:5] nt
	global_load_dword v196, v251, s[6:7] offset:2464
	s_add_u32 s4, s4, 0x16000
	s_addc_u32 s5, s5, 0
	global_load_dwordx4 v[162:165], v250, s[4:5] nt
	global_load_dword v198, v251, s[6:7] offset:2496
	s_add_u32 s4, s4, 0x16000
	s_addc_u32 s5, s5, 0
	global_load_dwordx4 v[166:169], v250, s[4:5] nt
	global_load_dword v200, v251, s[6:7] offset:2528
	v_mul_f32_e32 v14, v20, v14
	v_mul_f32_e32 v15, v21, v15
	v_rndne_f32_e32 v50, v62
	v_rndne_f32_e32 v51, v63
	v_mul_f32_e32 v12, v22, v12
	v_mul_f32_e32 v13, v23, v13
	v_mul_f32_e32 v28, v20, v28
	v_mul_f32_e32 v29, v21, v29
	v_mul_f32_e32 v26, v22, v26
	v_mul_f32_e32 v27, v23, v27
	v_mul_f32_e32 v32, v20, v32
	v_mul_f32_e32 v33, v21, v33
	v_mul_f32_e32 v30, v22, v30
	v_mul_f32_e32 v31, v23, v31
	v_mul_f32_e32 v36, v20, v36
	v_mul_f32_e32 v37, v21, v37
	v_mul_f32_e32 v34, v22, v34
	v_mul_f32_e32 v35, v23, v35
	v_mul_f32_e32 v40, v20, v40
	v_mul_f32_e32 v41, v21, v41
	v_mul_f32_e32 v38, v22, v38
	v_mul_f32_e32 v39, v23, v39
	v_mul_f32_e32 v44, v20, v44
	v_mul_f32_e32 v45, v21, v45
	v_mul_f32_e32 v42, v22, v42
	v_mul_f32_e32 v43, v23, v43
	v_mul_f32_e32 v48, v20, v48
	v_mul_f32_e32 v49, v21, v49
	v_mul_f32_e32 v46, v22, v46
	v_mul_f32_e32 v47, v23, v47
	v_rndne_f32_e32 v14, v14
	v_rndne_f32_e32 v15, v15
	v_rndne_f32_e32 v52, v64
	v_rndne_f32_e32 v53, v65
	ds_write2_b32 v25, v50, v51 offset1:1
	ds_write2_b32 v25, v52, v53 offset0:2 offset1:3
	v_rndne_f32_e32 v12, v12
	v_rndne_f32_e32 v13, v13
	v_rndne_f32_e32 v28, v28
	v_rndne_f32_e32 v29, v29
	v_rndne_f32_e32 v26, v26
	v_rndne_f32_e32 v27, v27
	v_rndne_f32_e32 v32, v32
	v_rndne_f32_e32 v33, v33
	v_rndne_f32_e32 v30, v30
	v_rndne_f32_e32 v31, v31
	v_rndne_f32_e32 v36, v36
	v_rndne_f32_e32 v37, v37
	v_rndne_f32_e32 v34, v34
	v_rndne_f32_e32 v35, v35
	v_rndne_f32_e32 v40, v40
	v_rndne_f32_e32 v41, v41
	v_rndne_f32_e32 v38, v38
	v_rndne_f32_e32 v39, v39
	v_rndne_f32_e32 v44, v44
	v_rndne_f32_e32 v45, v45
	v_rndne_f32_e32 v42, v42
	v_rndne_f32_e32 v43, v43
	v_rndne_f32_e32 v48, v48
	v_rndne_f32_e32 v49, v49
	v_rndne_f32_e32 v46, v46
	v_rndne_f32_e32 v47, v47
	ds_write2_b32 v77, v14, v15 offset1:1
	ds_write2_b32 v79, v12, v13 offset1:1
	ds_write2_b32 v81, v28, v29 offset1:1
	ds_write2_b32 v83, v26, v27 offset1:1
	ds_write2_b32 v85, v32, v33 offset1:1
	ds_write2_b32 v87, v30, v31 offset1:1
	ds_write2_b32 v89, v36, v37 offset1:1
	ds_write2_b32 v91, v34, v35 offset1:1
	ds_write2_b32 v92, v40, v41 offset1:1
	ds_write2_b32 v93, v38, v39 offset1:1
	ds_write2_b32 v94, v44, v45 offset1:1
	ds_write2_b32 v95, v42, v43 offset1:1
	ds_write2_b32 v96, v48, v49 offset1:1
	ds_write2_b32 v97, v46, v47 offset1:1
	s_waitcnt lgkmcnt(0)
; #define LAS __attribute__((address_space(3)))
; #define GAS __attribute__((address_space(1)))
; #define LDS_WAIT() asm volatile("s_waitcnt lgkmcnt(0)" ::: "memory")
;     ...
;         LDS_WAIT(); asm volatile("" ::: "memory");
;         const int c = lane & 7;
; #pragma unroll
;         for (int j = 0; j < 4; ++j) { const int n = (lane >> 3) + 8 * j; const LAS float* sp = scr + (8 * c) * 33 + n;
;             u32x2 o;
;             o.x = ((unsigned)(int)sp[0 * 33] & 0xFFu) | (((unsigned)(int)sp[1 * 33] & 0xFFu) << 8) | (((unsigned)(int)sp[2 * 33] & 0xFFu) << 16) | (((unsigned)(int)sp[3 * 33] & 0xFFu) << 24);
;             o.y = ((unsigned)(int)sp[4 * 33] & 0xFFu) | (((unsigned)(int)sp[5 * 33] & 0xFFu) << 8) | (((unsigned)(int)sp[6 * 33] & 0xFFu) << 16) | (((unsigned)(int)sp[7 * 33] & 0xFFu) << 24);
;             *(GAS u32x2*)(dst + (size_t)(n0 + n) * D + 64 * kb + 8 * c) = o; }
	ds_read2_b32 v[12:13], v24 offset1:8
	ds_read2_b32 v[14:15], v24 offset0:33 offset1:41
	ds_read2_b32 v[26:27], v24 offset0:66 offset1:74
	ds_read2_b32 v[28:29], v24 offset0:99 offset1:107
	ds_read2_b32 v[30:31], v24 offset0:132 offset1:140
	ds_read2_b32 v[32:33], v24 offset0:165 offset1:173
	ds_read2_b32 v[34:35], v24 offset0:198 offset1:206
	ds_read2_b32 v[36:37], v24 offset0:231 offset1:239
	ds_read2_b32 v[38:39], v24 offset0:16 offset1:24
	ds_read2_b32 v[40:41], v24 offset0:49 offset1:57
	ds_read2_b32 v[42:43], v24 offset0:82 offset1:90
	ds_read2_b32 v[44:45], v24 offset0:115 offset1:123
	ds_read2_b32 v[46:47], v24 offset0:148 offset1:156
	ds_read2_b32 v[48:49], v24 offset0:181 offset1:189
	ds_read2_b32 v[50:51], v24 offset0:214 offset1:222
	ds_read2_b32 v[52:53], v24 offset0:247 offset1:255
	s_waitcnt lgkmcnt(14)
	v_cvt_i32_f32_e32 v14, v14
	s_waitcnt lgkmcnt(10)
	v_cvt_i32_f32_e32 v32, v32
	v_cvt_i32_f32_e32 v12, v12
	v_cvt_i32_f32_sdwa v26, v26 dst_sel:WORD_1 dst_unused:UNUSED_PAD src0_sel:DWORD
	v_cvt_i32_f32_e32 v30, v30
	s_waitcnt lgkmcnt(9)
	v_cvt_i32_f32_sdwa v34, v34 dst_sel:WORD_1 dst_unused:UNUSED_PAD src0_sel:DWORD
	v_cvt_i32_f32_e32 v15, v15
	v_cvt_i32_f32_e32 v33, v33
	s_waitcnt lgkmcnt(6)
	v_cvt_i32_f32_e32 v40, v40
	s_waitcnt lgkmcnt(2)
	v_cvt_i32_f32_e32 v48, v48
	v_cvt_i32_f32_e32 v41, v41
	v_cvt_i32_f32_e32 v49, v49
	v_cvt_i32_f32_sdwa v28, v28 dst_sel:BYTE_3 dst_unused:UNUSED_PAD src0_sel:DWORD
	v_cvt_i32_f32_sdwa v36, v36 dst_sel:BYTE_3 dst_unused:UNUSED_PAD src0_sel:DWORD
	v_cvt_i32_f32_e32 v13, v13
	v_cvt_i32_f32_sdwa v27, v27 dst_sel:WORD_1 dst_unused:UNUSED_PAD src0_sel:DWORD
	v_cvt_i32_f32_e32 v31, v31
	v_cvt_i32_f32_sdwa v35, v35 dst_sel:WORD_1 dst_unused:UNUSED_PAD src0_sel:DWORD
	v_cvt_i32_f32_e32 v38, v38
	v_cvt_i32_f32_sdwa v42, v42 dst_sel:WORD_1 dst_unused:UNUSED_PAD src0_sel:DWORD
	v_cvt_i32_f32_e32 v46, v46
	s_waitcnt lgkmcnt(1)
	v_cvt_i32_f32_sdwa v50, v50 dst_sel:WORD_1 dst_unused:UNUSED_PAD src0_sel:DWORD
	v_cvt_i32_f32_e32 v39, v39
	v_cvt_i32_f32_sdwa v43, v43 dst_sel:WORD_1 dst_unused:UNUSED_PAD src0_sel:DWORD
	v_cvt_i32_f32_e32 v47, v47
	v_cvt_i32_f32_sdwa v51, v51 dst_sel:WORD_1 dst_unused:UNUSED_PAD src0_sel:DWORD
	v_cvt_i32_f32_sdwa v29, v29 dst_sel:BYTE_3 dst_unused:UNUSED_PAD src0_sel:DWORD
	v_cvt_i32_f32_sdwa v37, v37 dst_sel:BYTE_3 dst_unused:UNUSED_PAD src0_sel:DWORD
	v_cvt_i32_f32_sdwa v44, v44 dst_sel:BYTE_3 dst_unused:UNUSED_PAD src0_sel:DWORD
	s_waitcnt lgkmcnt(0)
	v_cvt_i32_f32_sdwa v52, v52 dst_sel:BYTE_3 dst_unused:UNUSED_PAD src0_sel:DWORD
	v_cvt_i32_f32_sdwa v45, v45 dst_sel:BYTE_3 dst_unused:UNUSED_PAD src0_sel:DWORD
	v_cvt_i32_f32_sdwa v53, v53 dst_sel:BYTE_3 dst_unused:UNUSED_PAD src0_sel:DWORD
	v_lshlrev_b32_e32 v14, 8, v14
	v_lshlrev_b32_e32 v32, 8, v32
	v_and_b32_e32 v26, 0xff0000, v26
	v_and_b32_e32 v34, 0xff0000, v34
	v_lshlrev_b32_e32 v15, 8, v15
	v_lshlrev_b32_e32 v33, 8, v33
	v_lshlrev_b32_e32 v40, 8, v40
	v_lshlrev_b32_e32 v48, 8, v48
	v_lshlrev_b32_e32 v41, 8, v41
	v_lshlrev_b32_e32 v49, 8, v49
	v_perm_b32 v12, v14, v12, s28
	v_perm_b32 v14, v32, v30, s28
	v_and_b32_e32 v27, 0xff0000, v27
	v_and_b32_e32 v35, 0xff0000, v35
	v_and_b32_e32 v42, 0xff0000, v42
	v_and_b32_e32 v50, 0xff0000, v50
	v_and_b32_e32 v43, 0xff0000, v43
	v_and_b32_e32 v51, 0xff0000, v51
	v_perm_b32 v15, v15, v13, s28
	v_perm_b32 v30, v33, v31, s28
	v_perm_b32 v31, v40, v38, s28
	v_perm_b32 v32, v48, v46, s28
	v_perm_b32 v33, v41, v39, s28
	v_perm_b32 v38, v49, v47, s28
	v_or3_b32 v12, v12, v26, v28
	v_or3_b32 v13, v14, v34, v36
	v_or3_b32 v14, v15, v27, v29
	v_or3_b32 v15, v30, v35, v37
	v_or3_b32 v26, v31, v42, v44
	v_or3_b32 v27, v32, v50, v52
	v_or3_b32 v28, v33, v43, v45
	v_or3_b32 v29, v38, v51, v53
	global_store_dwordx2 v[16:17], v[12:13], off
	global_store_dwordx2 v[18:19], v[14:15], off
	global_store_dwordx2 v[58:59], v[26:27], off
	global_store_dwordx2 v[60:61], v[28:29], off
	s_waitcnt lgkmcnt(0)
	v_add_u32_e32 v77, 0x420, v25
	v_add_u32_e32 v79, 0x428, v25
	v_add_u32_e32 v81, 0x840, v25
	v_add_u32_e32 v83, 0x848, v25
	v_add_u32_e32 v85, 0xc60, v25
	v_add_u32_e32 v87, 0xc68, v25
	v_add_u32_e32 v89, 0x1080, v25
	v_add_u32_e32 v91, 0x1088, v25
	v_add_u32_e32 v92, 0x14a0, v25
	v_add_u32_e32 v93, 0x14a8, v25
	v_add_u32_e32 v94, 0x18c0, v25
	v_add_u32_e32 v95, 0x18c8, v25
	v_add_u32_e32 v96, 0x1ce0, v25
	v_add_u32_e32 v97, 0x1ce8, v25
	v_lshl_add_u64 v[16:17], v[10:11], 0, s[26:27]
	v_lshl_add_u64 v[18:19], v[8:9], 0, s[26:27]
	v_lshl_add_u64 v[58:59], v[6:7], 0, s[26:27]
	v_lshl_add_u64 v[60:61], v[4:5], 0, s[26:27]
	v_lshl_add_u64 v[4:5], v[4:5], 0, 64
	v_lshl_add_u64 v[6:7], v[6:7], 0, 64
	v_lshl_add_u64 v[8:9], v[8:9], 0, 64
	v_lshl_add_u64 v[10:11], v[10:11], 0, 64
	s_waitcnt vmcnt(24)
; #define LAS __attribute__((address_space(3)))
;     ...
;         for (int i = 0; i < 8; ++i) { const int kk = 8 * i + kr; const int k = 64 * kb + kk; const f32x4 v = __builtin_nontemporal_load((const f32x4*)(W + (size_t)k * pitch)) * g[k];
;             LAS float* p = scr + kk * 33 + 4 * (lane & 7); p[0] = __builtin_rintf(v[0] * inv[0]); p[1] = __builtin_rintf(v[1] * inv[1]); p[2] = __builtin_rintf(v[2] * inv[2]); p[3] = __builtin_rintf(v[3] * inv[3]); }
	v_pk_mul_f32 v[14:15], v[106:107], v[170:171] op_sel_hi:[1,0]
	v_pk_mul_f32 v[12:13], v[108:109], v[170:171] op_sel_hi:[1,0]
	v_mul_f32_e32 v62, v20, v14
	v_mul_f32_e32 v63, v21, v15
	v_mul_f32_e32 v64, v22, v12
	v_mul_f32_e32 v65, v23, v13
	v_pk_mul_f32 v[14:15], v[110:111], v[172:173] op_sel_hi:[1,0]
	v_pk_mul_f32 v[12:13], v[112:113], v[172:173] op_sel_hi:[1,0]
	v_pk_mul_f32 v[26:27], v[116:117], v[174:175] op_sel_hi:[1,0]
	v_pk_mul_f32 v[28:29], v[114:115], v[174:175] op_sel_hi:[1,0]
	v_pk_mul_f32 v[30:31], v[120:121], v[176:177] op_sel_hi:[1,0]
	v_pk_mul_f32 v[32:33], v[118:119], v[176:177] op_sel_hi:[1,0]
	v_pk_mul_f32 v[34:35], v[124:125], v[178:179] op_sel_hi:[1,0]
	v_pk_mul_f32 v[36:37], v[122:123], v[178:179] op_sel_hi:[1,0]
	v_pk_mul_f32 v[38:39], v[128:129], v[180:181] op_sel_hi:[1,0]
	v_pk_mul_f32 v[40:41], v[126:127], v[180:181] op_sel_hi:[1,0]
	v_pk_mul_f32 v[42:43], v[132:133], v[182:183] op_sel_hi:[1,0]
	v_pk_mul_f32 v[44:45], v[130:131], v[182:183] op_sel_hi:[1,0]
	v_pk_mul_f32 v[46:47], v[136:137], v[184:185] op_sel_hi:[1,0]
	v_pk_mul_f32 v[48:49], v[134:135], v[184:185] op_sel_hi:[1,0]
	s_add_u32 s4, s4, 0x16000
	s_addc_u32 s5, s5, 0
	global_load_dwordx4 v[106:109], v250, s[4:5] nt
	global_load_dword v170, v251, s[6:7] offset:2560
	s_add_u32 s4, s4, 0x16000
	s_addc_u32 s5, s5, 0
	global_load_dwordx4 v[110:113], v250, s[4:5] nt
	global_load_dword v172, v251, s[6:7] offset:2592
	s_add_u32 s4, s4, 0x16000
	s_addc_u32 s5, s5, 0
	global_load_dwordx4 v[114:117], v250, s[4:5] nt
	global_load_dword v174, v251, s[6:7] offset:2624
	s_add_u32 s4, s4, 0x16000
	s_addc_u32 s5, s5, 0
	global_load_dwordx4 v[118:121], v250, s[4:5] nt
	global_load_dword v176, v251, s[6:7] offset:2656
	s_add_u32 s4, s4, 0x16000
	s_addc_u32 s5, s5, 0
	global_load_dwordx4 v[122:125], v250, s[4:5] nt
	global_load_dword v178, v251, s[6:7] offset:2688
	s_add_u32 s4, s4, 0x16000
	s_addc_u32 s5, s5, 0
	global_load_dwordx4 v[126:129], v250, s[4:5] nt
	global_load_dword v180, v251, s[6:7] offset:2720
	s_add_u32 s4, s4, 0x16000
	s_addc_u32 s5, s5, 0
	global_load_dwordx4 v[130:133], v250, s[4:5] nt
	global_load_dword v182, v251, s[6:7] offset:2752
	s_add_u32 s4, s4, 0x16000
	s_addc_u32 s5, s5, 0
	global_load_dwordx4 v[134:137], v250, s[4:5] nt
	global_load_dword v184, v251, s[6:7] offset:2784
	v_mul_f32_e32 v14, v20, v14
	v_mul_f32_e32 v15, v21, v15
	v_rndne_f32_e32 v50, v62
	v_rndne_f32_e32 v51, v63
	v_mul_f32_e32 v12, v22, v12
	v_mul_f32_e32 v13, v23, v13
	v_mul_f32_e32 v28, v20, v28
	v_mul_f32_e32 v29, v21, v29
	v_mul_f32_e32 v26, v22, v26
	v_mul_f32_e32 v27, v23, v27
	v_mul_f32_e32 v32, v20, v32
	v_mul_f32_e32 v33, v21, v33
	v_mul_f32_e32 v30, v22, v30
	v_mul_f32_e32 v31, v23, v31
	v_mul_f32_e32 v36, v20, v36
	v_mul_f32_e32 v37, v21, v37
	v_mul_f32_e32 v34, v22, v34
	v_mul_f32_e32 v35, v23, v35
	v_mul_f32_e32 v40, v20, v40
	v_mul_f32_e32 v41, v21, v41
	v_mul_f32_e32 v38, v22, v38
	v_mul_f32_e32 v39, v23, v39
	v_mul_f32_e32 v44, v20, v44
	v_mul_f32_e32 v45, v21, v45
	v_mul_f32_e32 v42, v22, v42
	v_mul_f32_e32 v43, v23, v43
	v_mul_f32_e32 v48, v20, v48
	v_mul_f32_e32 v49, v21, v49
	v_mul_f32_e32 v46, v22, v46
	v_mul_f32_e32 v47, v23, v47
	v_rndne_f32_e32 v14, v14
	v_rndne_f32_e32 v15, v15
	v_rndne_f32_e32 v52, v64
	v_rndne_f32_e32 v53, v65
	ds_write2_b32 v25, v50, v51 offset1:1
	ds_write2_b32 v25, v52, v53 offset0:2 offset1:3
	v_rndne_f32_e32 v12, v12
	v_rndne_f32_e32 v13, v13
	v_rndne_f32_e32 v28, v28
	v_rndne_f32_e32 v29, v29
	v_rndne_f32_e32 v26, v26
	v_rndne_f32_e32 v27, v27
	v_rndne_f32_e32 v32, v32
	v_rndne_f32_e32 v33, v33
	v_rndne_f32_e32 v30, v30
	v_rndne_f32_e32 v31, v31
	v_rndne_f32_e32 v36, v36
	v_rndne_f32_e32 v37, v37
	v_rndne_f32_e32 v34, v34
	v_rndne_f32_e32 v35, v35
	v_rndne_f32_e32 v40, v40
	v_rndne_f32_e32 v41, v41
	v_rndne_f32_e32 v38, v38
	v_rndne_f32_e32 v39, v39
	v_rndne_f32_e32 v44, v44
	v_rndne_f32_e32 v45, v45
	v_rndne_f32_e32 v42, v42
	v_rndne_f32_e32 v43, v43
	v_rndne_f32_e32 v48, v48
	v_rndne_f32_e32 v49, v49
	v_rndne_f32_e32 v46, v46
	v_rndne_f32_e32 v47, v47
	ds_write2_b32 v77, v14, v15 offset1:1
	ds_write2_b32 v79, v12, v13 offset1:1
	ds_write2_b32 v81, v28, v29 offset1:1
	ds_write2_b32 v83, v26, v27 offset1:1
	ds_write2_b32 v85, v32, v33 offset1:1
	ds_write2_b32 v87, v30, v31 offset1:1
	ds_write2_b32 v89, v36, v37 offset1:1
	ds_write2_b32 v91, v34, v35 offset1:1
	ds_write2_b32 v92, v40, v41 offset1:1
	ds_write2_b32 v93, v38, v39 offset1:1
	ds_write2_b32 v94, v44, v45 offset1:1
	ds_write2_b32 v95, v42, v43 offset1:1
	ds_write2_b32 v96, v48, v49 offset1:1
	ds_write2_b32 v97, v46, v47 offset1:1
	s_waitcnt lgkmcnt(0)
	ds_read2_b32 v[12:13], v24 offset1:8
	ds_read2_b32 v[14:15], v24 offset0:33 offset1:41
	ds_read2_b32 v[26:27], v24 offset0:66 offset1:74
	ds_read2_b32 v[28:29], v24 offset0:99 offset1:107
	ds_read2_b32 v[30:31], v24 offset0:132 offset1:140
	ds_read2_b32 v[32:33], v24 offset0:165 offset1:173
	ds_read2_b32 v[34:35], v24 offset0:198 offset1:206
	ds_read2_b32 v[36:37], v24 offset0:231 offset1:239
	ds_read2_b32 v[38:39], v24 offset0:16 offset1:24
	ds_read2_b32 v[40:41], v24 offset0:49 offset1:57
	ds_read2_b32 v[42:43], v24 offset0:82 offset1:90
	ds_read2_b32 v[44:45], v24 offset0:115 offset1:123
	ds_read2_b32 v[46:47], v24 offset0:148 offset1:156
	ds_read2_b32 v[48:49], v24 offset0:181 offset1:189
	ds_read2_b32 v[50:51], v24 offset0:214 offset1:222
	ds_read2_b32 v[52:53], v24 offset0:247 offset1:255
	s_waitcnt lgkmcnt(14)
	v_cvt_i32_f32_e32 v14, v14
	s_waitcnt lgkmcnt(10)
	v_cvt_i32_f32_e32 v32, v32
	v_cvt_i32_f32_e32 v12, v12
	v_cvt_i32_f32_sdwa v26, v26 dst_sel:WORD_1 dst_unused:UNUSED_PAD src0_sel:DWORD
	v_cvt_i32_f32_e32 v30, v30
	s_waitcnt lgkmcnt(9)
; #define LAS __attribute__((address_space(3)))
; #define GAS __attribute__((address_space(1)))
; #define LDS_WAIT() asm volatile("s_waitcnt lgkmcnt(0)" ::: "memory")
;     ...
;         for (int i = 0; i < 8; ++i) { const int kk = 8 * i + kr; const int k = 64 * kb + kk; const f32x4 v = __builtin_nontemporal_load((const f32x4*)(W + (size_t)k * pitch)) * g[k];
;             LAS float* p = scr + kk * 33 + 4 * (lane & 7); p[0] = __builtin_rintf(v[0] * inv[0]); p[1] = __builtin_rintf(v[1] * inv[1]); p[2] = __builtin_rintf(v[2] * inv[2]); p[3] = __builtin_rintf(v[3] * inv[3]); }
;         LDS_WAIT(); asm volatile("" ::: "memory");
;         const int c = lane & 7;
; #pragma unroll
;         for (int j = 0; j < 4; ++j) { const int n = (lane >> 3) + 8 * j; const LAS float* sp = scr + (8 * c) * 33 + n;
;             u32x2 o;
;             o.x = ((unsigned)(int)sp[0 * 33] & 0xFFu) | (((unsigned)(int)sp[1 * 33] & 0xFFu) << 8) | (((unsigned)(int)sp[2 * 33] & 0xFFu) << 16) | (((unsigned)(int)sp[3 * 33] & 0xFFu) << 24);
;             o.y = ((unsigned)(int)sp[4 * 33] & 0xFFu) | (((unsigned)(int)sp[5 * 33] & 0xFFu) << 8) | (((unsigned)(int)sp[6 * 33] & 0xFFu) << 16) | (((unsigned)(int)sp[7 * 33] & 0xFFu) << 24);
;             *(GAS u32x2*)(dst + (size_t)(n0 + n) * D + 64 * kb + 8 * c) = o; }
	v_cvt_i32_f32_sdwa v34, v34 dst_sel:WORD_1 dst_unused:UNUSED_PAD src0_sel:DWORD
	v_cvt_i32_f32_e32 v15, v15
	v_cvt_i32_f32_e32 v33, v33
	s_waitcnt lgkmcnt(6)
	v_cvt_i32_f32_e32 v40, v40
	s_waitcnt lgkmcnt(2)
	v_cvt_i32_f32_e32 v48, v48
	v_cvt_i32_f32_e32 v41, v41
	v_cvt_i32_f32_e32 v49, v49
	v_cvt_i32_f32_sdwa v28, v28 dst_sel:BYTE_3 dst_unused:UNUSED_PAD src0_sel:DWORD
	v_cvt_i32_f32_sdwa v36, v36 dst_sel:BYTE_3 dst_unused:UNUSED_PAD src0_sel:DWORD
	v_cvt_i32_f32_e32 v13, v13
	v_cvt_i32_f32_sdwa v27, v27 dst_sel:WORD_1 dst_unused:UNUSED_PAD src0_sel:DWORD
	v_cvt_i32_f32_e32 v31, v31
	v_cvt_i32_f32_sdwa v35, v35 dst_sel:WORD_1 dst_unused:UNUSED_PAD src0_sel:DWORD
	v_cvt_i32_f32_e32 v38, v38
	v_cvt_i32_f32_sdwa v42, v42 dst_sel:WORD_1 dst_unused:UNUSED_PAD src0_sel:DWORD
	v_cvt_i32_f32_e32 v46, v46
	s_waitcnt lgkmcnt(1)
	v_cvt_i32_f32_sdwa v50, v50 dst_sel:WORD_1 dst_unused:UNUSED_PAD src0_sel:DWORD
	v_cvt_i32_f32_e32 v39, v39
	v_cvt_i32_f32_sdwa v43, v43 dst_sel:WORD_1 dst_unused:UNUSED_PAD src0_sel:DWORD
	v_cvt_i32_f32_e32 v47, v47
	v_cvt_i32_f32_sdwa v51, v51 dst_sel:WORD_1 dst_unused:UNUSED_PAD src0_sel:DWORD
	v_cvt_i32_f32_sdwa v29, v29 dst_sel:BYTE_3 dst_unused:UNUSED_PAD src0_sel:DWORD
	v_cvt_i32_f32_sdwa v37, v37 dst_sel:BYTE_3 dst_unused:UNUSED_PAD src0_sel:DWORD
	v_cvt_i32_f32_sdwa v44, v44 dst_sel:BYTE_3 dst_unused:UNUSED_PAD src0_sel:DWORD
	s_waitcnt lgkmcnt(0)
	v_cvt_i32_f32_sdwa v52, v52 dst_sel:BYTE_3 dst_unused:UNUSED_PAD src0_sel:DWORD
	v_cvt_i32_f32_sdwa v45, v45 dst_sel:BYTE_3 dst_unused:UNUSED_PAD src0_sel:DWORD
	v_cvt_i32_f32_sdwa v53, v53 dst_sel:BYTE_3 dst_unused:UNUSED_PAD src0_sel:DWORD
	v_lshlrev_b32_e32 v14, 8, v14
	v_lshlrev_b32_e32 v32, 8, v32
	v_and_b32_e32 v26, 0xff0000, v26
	v_and_b32_e32 v34, 0xff0000, v34
	v_lshlrev_b32_e32 v15, 8, v15
	v_lshlrev_b32_e32 v33, 8, v33
	v_lshlrev_b32_e32 v40, 8, v40
	v_lshlrev_b32_e32 v48, 8, v48
	v_lshlrev_b32_e32 v41, 8, v41
	v_lshlrev_b32_e32 v49, 8, v49
	v_perm_b32 v12, v14, v12, s28
	v_perm_b32 v14, v32, v30, s28
	v_and_b32_e32 v27, 0xff0000, v27
	v_and_b32_e32 v35, 0xff0000, v35
	v_and_b32_e32 v42, 0xff0000, v42
	v_and_b32_e32 v50, 0xff0000, v50
	v_and_b32_e32 v43, 0xff0000, v43
	v_and_b32_e32 v51, 0xff0000, v51
	v_perm_b32 v15, v15, v13, s28
	v_perm_b32 v30, v33, v31, s28
	v_perm_b32 v31, v40, v38, s28
	v_perm_b32 v32, v48, v46, s28
	v_perm_b32 v33, v41, v39, s28
	v_perm_b32 v38, v49, v47, s28
	v_or3_b32 v12, v12, v26, v28
	v_or3_b32 v13, v14, v34, v36
	v_or3_b32 v14, v15, v27, v29
	v_or3_b32 v15, v30, v35, v37
	v_or3_b32 v26, v31, v42, v44
	v_or3_b32 v27, v32, v50, v52
	v_or3_b32 v28, v33, v43, v45
	v_or3_b32 v29, v38, v51, v53
	global_store_dwordx2 v[16:17], v[12:13], off
	global_store_dwordx2 v[18:19], v[14:15], off
	global_store_dwordx2 v[58:59], v[26:27], off
	global_store_dwordx2 v[60:61], v[28:29], off
	s_waitcnt lgkmcnt(0)
	v_add_u32_e32 v77, 0x420, v25
	v_add_u32_e32 v79, 0x428, v25
	v_add_u32_e32 v81, 0x840, v25
	v_add_u32_e32 v83, 0x848, v25
	v_add_u32_e32 v85, 0xc60, v25
	v_add_u32_e32 v87, 0xc68, v25
	v_add_u32_e32 v89, 0x1080, v25
	v_add_u32_e32 v91, 0x1088, v25
	v_add_u32_e32 v92, 0x14a0, v25
	v_add_u32_e32 v93, 0x14a8, v25
	v_add_u32_e32 v94, 0x18c0, v25
	v_add_u32_e32 v95, 0x18c8, v25
	v_add_u32_e32 v96, 0x1ce0, v25
	v_add_u32_e32 v97, 0x1ce8, v25
	v_lshl_add_u64 v[16:17], v[10:11], 0, s[26:27]
	v_lshl_add_u64 v[18:19], v[8:9], 0, s[26:27]
	v_lshl_add_u64 v[58:59], v[6:7], 0, s[26:27]
	v_lshl_add_u64 v[60:61], v[4:5], 0, s[26:27]
	v_lshl_add_u64 v[4:5], v[4:5], 0, 64
	v_lshl_add_u64 v[6:7], v[6:7], 0, 64
	v_lshl_add_u64 v[8:9], v[8:9], 0, 64
	v_lshl_add_u64 v[10:11], v[10:11], 0, 64
	s_waitcnt vmcnt(24)
	v_pk_mul_f32 v[14:15], v[138:139], v[186:187] op_sel_hi:[1,0]
	v_pk_mul_f32 v[12:13], v[140:141], v[186:187] op_sel_hi:[1,0]
	v_mul_f32_e32 v62, v20, v14
	v_mul_f32_e32 v63, v21, v15
	v_mul_f32_e32 v64, v22, v12
	v_mul_f32_e32 v65, v23, v13
	v_pk_mul_f32 v[14:15], v[142:143], v[188:189] op_sel_hi:[1,0]
	v_pk_mul_f32 v[12:13], v[144:145], v[188:189] op_sel_hi:[1,0]
	v_pk_mul_f32 v[26:27], v[148:149], v[190:191] op_sel_hi:[1,0]
	v_pk_mul_f32 v[28:29], v[146:147], v[190:191] op_sel_hi:[1,0]
	v_pk_mul_f32 v[30:31], v[152:153], v[192:193] op_sel_hi:[1,0]
	v_pk_mul_f32 v[32:33], v[150:151], v[192:193] op_sel_hi:[1,0]
	v_pk_mul_f32 v[34:35], v[156:157], v[194:195] op_sel_hi:[1,0]
	v_pk_mul_f32 v[36:37], v[154:155], v[194:195] op_sel_hi:[1,0]
	v_pk_mul_f32 v[38:39], v[160:161], v[196:197] op_sel_hi:[1,0]
	v_pk_mul_f32 v[40:41], v[158:159], v[196:197] op_sel_hi:[1,0]
	v_pk_mul_f32 v[42:43], v[164:165], v[198:199] op_sel_hi:[1,0]
	v_pk_mul_f32 v[44:45], v[162:163], v[198:199] op_sel_hi:[1,0]
	v_pk_mul_f32 v[46:47], v[168:169], v[200:201] op_sel_hi:[1,0]
	v_pk_mul_f32 v[48:49], v[166:167], v[200:201] op_sel_hi:[1,0]
	s_add_u32 s4, s4, 0x16000
	s_addc_u32 s5, s5, 0
	global_load_dwordx4 v[138:141], v250, s[4:5] nt
	global_load_dword v186, v251, s[6:7] offset:2816
	s_add_u32 s4, s4, 0x16000
	s_addc_u32 s5, s5, 0
	global_load_dwordx4 v[142:145], v250, s[4:5] nt
	global_load_dword v188, v251, s[6:7] offset:2848
	s_add_u32 s4, s4, 0x16000
	s_addc_u32 s5, s5, 0
	global_load_dwordx4 v[146:149], v250, s[4:5] nt
	global_load_dword v190, v251, s[6:7] offset:2880
	s_add_u32 s4, s4, 0x16000
	s_addc_u32 s5, s5, 0
	global_load_dwordx4 v[150:153], v250, s[4:5] nt
	global_load_dword v192, v251, s[6:7] offset:2912
	s_add_u32 s4, s4, 0x16000
	s_addc_u32 s5, s5, 0
	global_load_dwordx4 v[154:157], v250, s[4:5] nt
	global_load_dword v194, v251, s[6:7] offset:2944
	s_add_u32 s4, s4, 0x16000
	s_addc_u32 s5, s5, 0
	global_load_dwordx4 v[158:161], v250, s[4:5] nt
; #define LAS __attribute__((address_space(3)))
; #define GAS __attribute__((address_space(1)))
; #define LDS_WAIT() asm volatile("s_waitcnt lgkmcnt(0)" ::: "memory")
;     ...
;         for (int i = 0; i < 8; ++i) { const int kk = 8 * i + kr; const int k = 64 * kb + kk; const f32x4 v = __builtin_nontemporal_load((const f32x4*)(W + (size_t)k * pitch)) * g[k];
;             LAS float* p = scr + kk * 33 + 4 * (lane & 7); p[0] = __builtin_rintf(v[0] * inv[0]); p[1] = __builtin_rintf(v[1] * inv[1]); p[2] = __builtin_rintf(v[2] * inv[2]); p[3] = __builtin_rintf(v[3] * inv[3]); }
;         LDS_WAIT(); asm volatile("" ::: "memory");
;         const int c = lane & 7;
; #pragma unroll
;         for (int j = 0; j < 4; ++j) { const int n = (lane >> 3) + 8 * j; const LAS float* sp = scr + (8 * c) * 33 + n;
;             u32x2 o;
;             o.x = ((unsigned)(int)sp[0 * 33] & 0xFFu) | (((unsigned)(int)sp[1 * 33] & 0xFFu) << 8) | (((unsigned)(int)sp[2 * 33] & 0xFFu) << 16) | (((unsigned)(int)sp[3 * 33] & 0xFFu) << 24);
;             o.y = ((unsigned)(int)sp[4 * 33] & 0xFFu) | (((unsigned)(int)sp[5 * 33] & 0xFFu) << 8) | (((unsigned)(int)sp[6 * 33] & 0xFFu) << 16) | (((unsigned)(int)sp[7 * 33] & 0xFFu) << 24);
;             *(GAS u32x2*)(dst + (size_t)(n0 + n) * D + 64 * kb + 8 * c) = o; }
	global_load_dword v196, v251, s[6:7] offset:2976
	s_add_u32 s4, s4, 0x16000
	s_addc_u32 s5, s5, 0
	global_load_dwordx4 v[162:165], v250, s[4:5] nt
	global_load_dword v198, v251, s[6:7] offset:3008
	s_add_u32 s4, s4, 0x16000
	s_addc_u32 s5, s5, 0
	global_load_dwordx4 v[166:169], v250, s[4:5] nt
	global_load_dword v200, v251, s[6:7] offset:3040
	v_mul_f32_e32 v14, v20, v14
	v_mul_f32_e32 v15, v21, v15
	v_rndne_f32_e32 v50, v62
	v_rndne_f32_e32 v51, v63
	v_mul_f32_e32 v12, v22, v12
	v_mul_f32_e32 v13, v23, v13
	v_mul_f32_e32 v28, v20, v28
	v_mul_f32_e32 v29, v21, v29
	v_mul_f32_e32 v26, v22, v26
	v_mul_f32_e32 v27, v23, v27
	v_mul_f32_e32 v32, v20, v32
	v_mul_f32_e32 v33, v21, v33
	v_mul_f32_e32 v30, v22, v30
	v_mul_f32_e32 v31, v23, v31
	v_mul_f32_e32 v36, v20, v36
	v_mul_f32_e32 v37, v21, v37
	v_mul_f32_e32 v34, v22, v34
	v_mul_f32_e32 v35, v23, v35
	v_mul_f32_e32 v40, v20, v40
	v_mul_f32_e32 v41, v21, v41
	v_mul_f32_e32 v38, v22, v38
	v_mul_f32_e32 v39, v23, v39
	v_mul_f32_e32 v44, v20, v44
	v_mul_f32_e32 v45, v21, v45
	v_mul_f32_e32 v42, v22, v42
	v_mul_f32_e32 v43, v23, v43
	v_mul_f32_e32 v48, v20, v48
	v_mul_f32_e32 v49, v21, v49
	v_mul_f32_e32 v46, v22, v46
	v_mul_f32_e32 v47, v23, v47
	v_rndne_f32_e32 v14, v14
	v_rndne_f32_e32 v15, v15
	v_rndne_f32_e32 v52, v64
	v_rndne_f32_e32 v53, v65
	ds_write2_b32 v25, v50, v51 offset1:1
	ds_write2_b32 v25, v52, v53 offset0:2 offset1:3
	v_rndne_f32_e32 v12, v12
	v_rndne_f32_e32 v13, v13
	v_rndne_f32_e32 v28, v28
	v_rndne_f32_e32 v29, v29
	v_rndne_f32_e32 v26, v26
	v_rndne_f32_e32 v27, v27
	v_rndne_f32_e32 v32, v32
	v_rndne_f32_e32 v33, v33
	v_rndne_f32_e32 v30, v30
	v_rndne_f32_e32 v31, v31
	v_rndne_f32_e32 v36, v36
	v_rndne_f32_e32 v37, v37
	v_rndne_f32_e32 v34, v34
	v_rndne_f32_e32 v35, v35
	v_rndne_f32_e32 v40, v40
	v_rndne_f32_e32 v41, v41
	v_rndne_f32_e32 v38, v38
	v_rndne_f32_e32 v39, v39
	v_rndne_f32_e32 v44, v44
	v_rndne_f32_e32 v45, v45
	v_rndne_f32_e32 v42, v42
	v_rndne_f32_e32 v43, v43
	v_rndne_f32_e32 v48, v48
	v_rndne_f32_e32 v49, v49
	v_rndne_f32_e32 v46, v46
	v_rndne_f32_e32 v47, v47
	ds_write2_b32 v77, v14, v15 offset1:1
	ds_write2_b32 v79, v12, v13 offset1:1
	ds_write2_b32 v81, v28, v29 offset1:1
	ds_write2_b32 v83, v26, v27 offset1:1
	ds_write2_b32 v85, v32, v33 offset1:1
	ds_write2_b32 v87, v30, v31 offset1:1
	ds_write2_b32 v89, v36, v37 offset1:1
	ds_write2_b32 v91, v34, v35 offset1:1
	ds_write2_b32 v92, v40, v41 offset1:1
	ds_write2_b32 v93, v38, v39 offset1:1
	ds_write2_b32 v94, v44, v45 offset1:1
	ds_write2_b32 v95, v42, v43 offset1:1
	ds_write2_b32 v96, v48, v49 offset1:1
	ds_write2_b32 v97, v46, v47 offset1:1
	s_waitcnt lgkmcnt(0)
	ds_read2_b32 v[12:13], v24 offset1:8
	ds_read2_b32 v[14:15], v24 offset0:33 offset1:41
	ds_read2_b32 v[26:27], v24 offset0:66 offset1:74
	ds_read2_b32 v[28:29], v24 offset0:99 offset1:107
	ds_read2_b32 v[30:31], v24 offset0:132 offset1:140
	ds_read2_b32 v[32:33], v24 offset0:165 offset1:173
	ds_read2_b32 v[34:35], v24 offset0:198 offset1:206
	ds_read2_b32 v[36:37], v24 offset0:231 offset1:239
	ds_read2_b32 v[38:39], v24 offset0:16 offset1:24
	ds_read2_b32 v[40:41], v24 offset0:49 offset1:57
	ds_read2_b32 v[42:43], v24 offset0:82 offset1:90
	ds_read2_b32 v[44:45], v24 offset0:115 offset1:123
	ds_read2_b32 v[46:47], v24 offset0:148 offset1:156
	ds_read2_b32 v[48:49], v24 offset0:181 offset1:189
	ds_read2_b32 v[50:51], v24 offset0:214 offset1:222
	ds_read2_b32 v[52:53], v24 offset0:247 offset1:255
	s_waitcnt lgkmcnt(14)
	v_cvt_i32_f32_e32 v14, v14
	s_waitcnt lgkmcnt(10)
	v_cvt_i32_f32_e32 v32, v32
	v_cvt_i32_f32_e32 v12, v12
	v_cvt_i32_f32_sdwa v26, v26 dst_sel:WORD_1 dst_unused:UNUSED_PAD src0_sel:DWORD
	v_cvt_i32_f32_e32 v30, v30
	s_waitcnt lgkmcnt(9)
	v_cvt_i32_f32_sdwa v34, v34 dst_sel:WORD_1 dst_unused:UNUSED_PAD src0_sel:DWORD
	v_cvt_i32_f32_e32 v15, v15
	v_cvt_i32_f32_e32 v33, v33
	s_waitcnt lgkmcnt(6)
	v_cvt_i32_f32_e32 v40, v40
	s_waitcnt lgkmcnt(2)
	v_cvt_i32_f32_e32 v48, v48
	v_cvt_i32_f32_e32 v41, v41
	v_cvt_i32_f32_e32 v49, v49
	v_cvt_i32_f32_sdwa v28, v28 dst_sel:BYTE_3 dst_unused:UNUSED_PAD src0_sel:DWORD
	v_cvt_i32_f32_sdwa v36, v36 dst_sel:BYTE_3 dst_unused:UNUSED_PAD src0_sel:DWORD
	v_cvt_i32_f32_e32 v13, v13
	v_cvt_i32_f32_sdwa v27, v27 dst_sel:WORD_1 dst_unused:UNUSED_PAD src0_sel:DWORD
	v_cvt_i32_f32_e32 v31, v31
	v_cvt_i32_f32_sdwa v35, v35 dst_sel:WORD_1 dst_unused:UNUSED_PAD src0_sel:DWORD
	v_cvt_i32_f32_e32 v38, v38
	v_cvt_i32_f32_sdwa v42, v42 dst_sel:WORD_1 dst_unused:UNUSED_PAD src0_sel:DWORD
	v_cvt_i32_f32_e32 v46, v46
	s_waitcnt lgkmcnt(1)
	v_cvt_i32_f32_sdwa v50, v50 dst_sel:WORD_1 dst_unused:UNUSED_PAD src0_sel:DWORD
	v_cvt_i32_f32_e32 v39, v39
	v_cvt_i32_f32_sdwa v43, v43 dst_sel:WORD_1 dst_unused:UNUSED_PAD src0_sel:DWORD
	v_cvt_i32_f32_e32 v47, v47
	v_cvt_i32_f32_sdwa v51, v51 dst_sel:WORD_1 dst_unused:UNUSED_PAD src0_sel:DWORD
	v_cvt_i32_f32_sdwa v29, v29 dst_sel:BYTE_3 dst_unused:UNUSED_PAD src0_sel:DWORD
	v_cvt_i32_f32_sdwa v37, v37 dst_sel:BYTE_3 dst_unused:UNUSED_PAD src0_sel:DWORD
	v_cvt_i32_f32_sdwa v44, v44 dst_sel:BYTE_3 dst_unused:UNUSED_PAD src0_sel:DWORD
	s_waitcnt lgkmcnt(0)
; #define LAS __attribute__((address_space(3)))
; #define GAS __attribute__((address_space(1)))
; #define LDS_WAIT() asm volatile("s_waitcnt lgkmcnt(0)" ::: "memory")
;     ...
;         for (int i = 0; i < 8; ++i) { const int kk = 8 * i + kr; const int k = 64 * kb + kk; const f32x4 v = __builtin_nontemporal_load((const f32x4*)(W + (size_t)k * pitch)) * g[k];
;             LAS float* p = scr + kk * 33 + 4 * (lane & 7); p[0] = __builtin_rintf(v[0] * inv[0]); p[1] = __builtin_rintf(v[1] * inv[1]); p[2] = __builtin_rintf(v[2] * inv[2]); p[3] = __builtin_rintf(v[3] * inv[3]); }
;         LDS_WAIT(); asm volatile("" ::: "memory");
;         const int c = lane & 7;
; #pragma unroll
;         for (int j = 0; j < 4; ++j) { const int n = (lane >> 3) + 8 * j; const LAS float* sp = scr + (8 * c) * 33 + n;
;             u32x2 o;
;             o.x = ((unsigned)(int)sp[0 * 33] & 0xFFu) | (((unsigned)(int)sp[1 * 33] & 0xFFu) << 8) | (((unsigned)(int)sp[2 * 33] & 0xFFu) << 16) | (((unsigned)(int)sp[3 * 33] & 0xFFu) << 24);
;             o.y = ((unsigned)(int)sp[4 * 33] & 0xFFu) | (((unsigned)(int)sp[5 * 33] & 0xFFu) << 8) | (((unsigned)(int)sp[6 * 33] & 0xFFu) << 16) | (((unsigned)(int)sp[7 * 33] & 0xFFu) << 24);
;             *(GAS u32x2*)(dst + (size_t)(n0 + n) * D + 64 * kb + 8 * c) = o; }
	v_cvt_i32_f32_sdwa v52, v52 dst_sel:BYTE_3 dst_unused:UNUSED_PAD src0_sel:DWORD
	v_cvt_i32_f32_sdwa v45, v45 dst_sel:BYTE_3 dst_unused:UNUSED_PAD src0_sel:DWORD
	v_cvt_i32_f32_sdwa v53, v53 dst_sel:BYTE_3 dst_unused:UNUSED_PAD src0_sel:DWORD
	v_lshlrev_b32_e32 v14, 8, v14
	v_lshlrev_b32_e32 v32, 8, v32
	v_and_b32_e32 v26, 0xff0000, v26
	v_and_b32_e32 v34, 0xff0000, v34
	v_lshlrev_b32_e32 v15, 8, v15
	v_lshlrev_b32_e32 v33, 8, v33
	v_lshlrev_b32_e32 v40, 8, v40
	v_lshlrev_b32_e32 v48, 8, v48
	v_lshlrev_b32_e32 v41, 8, v41
	v_lshlrev_b32_e32 v49, 8, v49
	v_perm_b32 v12, v14, v12, s28
	v_perm_b32 v14, v32, v30, s28
	v_and_b32_e32 v27, 0xff0000, v27
	v_and_b32_e32 v35, 0xff0000, v35
	v_and_b32_e32 v42, 0xff0000, v42
	v_and_b32_e32 v50, 0xff0000, v50
	v_and_b32_e32 v43, 0xff0000, v43
	v_and_b32_e32 v51, 0xff0000, v51
	v_perm_b32 v15, v15, v13, s28
	v_perm_b32 v30, v33, v31, s28
	v_perm_b32 v31, v40, v38, s28
	v_perm_b32 v32, v48, v46, s28
	v_perm_b32 v33, v41, v39, s28
	v_perm_b32 v38, v49, v47, s28
	v_or3_b32 v12, v12, v26, v28
	v_or3_b32 v13, v14, v34, v36
	v_or3_b32 v14, v15, v27, v29
	v_or3_b32 v15, v30, v35, v37
	v_or3_b32 v26, v31, v42, v44
	v_or3_b32 v27, v32, v50, v52
	v_or3_b32 v28, v33, v43, v45
	v_or3_b32 v29, v38, v51, v53
	global_store_dwordx2 v[16:17], v[12:13], off
	global_store_dwordx2 v[18:19], v[14:15], off
	global_store_dwordx2 v[58:59], v[26:27], off
	global_store_dwordx2 v[60:61], v[28:29], off
	s_waitcnt lgkmcnt(0)
	v_add_u32_e32 v77, 0x420, v25
	v_add_u32_e32 v79, 0x428, v25
	v_add_u32_e32 v81, 0x840, v25
	v_add_u32_e32 v83, 0x848, v25
	v_add_u32_e32 v85, 0xc60, v25
	v_add_u32_e32 v87, 0xc68, v25
	v_add_u32_e32 v89, 0x1080, v25
	v_add_u32_e32 v91, 0x1088, v25
	v_add_u32_e32 v92, 0x14a0, v25
	v_add_u32_e32 v93, 0x14a8, v25
	v_add_u32_e32 v94, 0x18c0, v25
	v_add_u32_e32 v95, 0x18c8, v25
	v_add_u32_e32 v96, 0x1ce0, v25
	v_add_u32_e32 v97, 0x1ce8, v25
	v_lshl_add_u64 v[16:17], v[10:11], 0, s[26:27]
	v_lshl_add_u64 v[18:19], v[8:9], 0, s[26:27]
	v_lshl_add_u64 v[58:59], v[6:7], 0, s[26:27]
	v_lshl_add_u64 v[60:61], v[4:5], 0, s[26:27]
	v_lshl_add_u64 v[4:5], v[4:5], 0, 64
	v_lshl_add_u64 v[6:7], v[6:7], 0, 64
	v_lshl_add_u64 v[8:9], v[8:9], 0, 64
	v_lshl_add_u64 v[10:11], v[10:11], 0, 64
	s_waitcnt vmcnt(24)
	v_pk_mul_f32 v[14:15], v[106:107], v[170:171] op_sel_hi:[1,0]
	v_pk_mul_f32 v[12:13], v[108:109], v[170:171] op_sel_hi:[1,0]
	v_mul_f32_e32 v62, v20, v14
	v_mul_f32_e32 v63, v21, v15
	v_mul_f32_e32 v64, v22, v12
	v_mul_f32_e32 v65, v23, v13
	v_pk_mul_f32 v[14:15], v[110:111], v[172:173] op_sel_hi:[1,0]
	v_pk_mul_f32 v[12:13], v[112:113], v[172:173] op_sel_hi:[1,0]
	v_pk_mul_f32 v[26:27], v[116:117], v[174:175] op_sel_hi:[1,0]
	v_pk_mul_f32 v[28:29], v[114:115], v[174:175] op_sel_hi:[1,0]
	v_pk_mul_f32 v[30:31], v[120:121], v[176:177] op_sel_hi:[1,0]
	v_pk_mul_f32 v[32:33], v[118:119], v[176:177] op_sel_hi:[1,0]
	v_pk_mul_f32 v[34:35], v[124:125], v[178:179] op_sel_hi:[1,0]
	v_pk_mul_f32 v[36:37], v[122:123], v[178:179] op_sel_hi:[1,0]
	v_pk_mul_f32 v[38:39], v[128:129], v[180:181] op_sel_hi:[1,0]
	v_pk_mul_f32 v[40:41], v[126:127], v[180:181] op_sel_hi:[1,0]
	v_pk_mul_f32 v[42:43], v[132:133], v[182:183] op_sel_hi:[1,0]
	v_pk_mul_f32 v[44:45], v[130:131], v[182:183] op_sel_hi:[1,0]
	v_pk_mul_f32 v[46:47], v[136:137], v[184:185] op_sel_hi:[1,0]
	v_pk_mul_f32 v[48:49], v[134:135], v[184:185] op_sel_hi:[1,0]
	s_add_u32 s4, s4, 0x16000
	s_addc_u32 s5, s5, 0
	global_load_dwordx4 v[106:109], v250, s[4:5] nt
	global_load_dword v170, v251, s[6:7] offset:3072
	s_add_u32 s4, s4, 0x16000
	s_addc_u32 s5, s5, 0
	global_load_dwordx4 v[110:113], v250, s[4:5] nt
	global_load_dword v172, v251, s[6:7] offset:3104
	s_add_u32 s4, s4, 0x16000
	s_addc_u32 s5, s5, 0
	global_load_dwordx4 v[114:117], v250, s[4:5] nt
	global_load_dword v174, v251, s[6:7] offset:3136
	s_add_u32 s4, s4, 0x16000
	s_addc_u32 s5, s5, 0
	global_load_dwordx4 v[118:121], v250, s[4:5] nt
	global_load_dword v176, v251, s[6:7] offset:3168
	s_add_u32 s4, s4, 0x16000
	s_addc_u32 s5, s5, 0
	global_load_dwordx4 v[122:125], v250, s[4:5] nt
	global_load_dword v178, v251, s[6:7] offset:3200
	s_add_u32 s4, s4, 0x16000
	s_addc_u32 s5, s5, 0
	global_load_dwordx4 v[126:129], v250, s[4:5] nt
	global_load_dword v180, v251, s[6:7] offset:3232
	s_add_u32 s4, s4, 0x16000
	s_addc_u32 s5, s5, 0
	global_load_dwordx4 v[130:133], v250, s[4:5] nt
	global_load_dword v182, v251, s[6:7] offset:3264
	s_add_u32 s4, s4, 0x16000
	s_addc_u32 s5, s5, 0
	global_load_dwordx4 v[134:137], v250, s[4:5] nt
	global_load_dword v184, v251, s[6:7] offset:3296
	v_mul_f32_e32 v14, v20, v14
	v_mul_f32_e32 v15, v21, v15
	v_rndne_f32_e32 v50, v62
	v_rndne_f32_e32 v51, v63
	v_mul_f32_e32 v12, v22, v12
	v_mul_f32_e32 v13, v23, v13
	v_mul_f32_e32 v28, v20, v28
	v_mul_f32_e32 v29, v21, v29
	v_mul_f32_e32 v26, v22, v26
	v_mul_f32_e32 v27, v23, v27
	v_mul_f32_e32 v32, v20, v32
	v_mul_f32_e32 v33, v21, v33
	v_mul_f32_e32 v30, v22, v30
	v_mul_f32_e32 v31, v23, v31
	v_mul_f32_e32 v36, v20, v36
	v_mul_f32_e32 v37, v21, v37
	v_mul_f32_e32 v34, v22, v34
	v_mul_f32_e32 v35, v23, v35
	v_mul_f32_e32 v40, v20, v40
	v_mul_f32_e32 v41, v21, v41
	v_mul_f32_e32 v38, v22, v38
	v_mul_f32_e32 v39, v23, v39
	v_mul_f32_e32 v44, v20, v44
	v_mul_f32_e32 v45, v21, v45
	v_mul_f32_e32 v42, v22, v42
	v_mul_f32_e32 v43, v23, v43
	v_mul_f32_e32 v48, v20, v48
	v_mul_f32_e32 v49, v21, v49
	v_mul_f32_e32 v46, v22, v46
	v_mul_f32_e32 v47, v23, v47
	v_rndne_f32_e32 v14, v14
	v_rndne_f32_e32 v15, v15
	v_rndne_f32_e32 v52, v64
	v_rndne_f32_e32 v53, v65
	ds_write2_b32 v25, v50, v51 offset1:1
	ds_write2_b32 v25, v52, v53 offset0:2 offset1:3
	v_rndne_f32_e32 v12, v12
	v_rndne_f32_e32 v13, v13
	v_rndne_f32_e32 v28, v28
	v_rndne_f32_e32 v29, v29
	v_rndne_f32_e32 v26, v26
	v_rndne_f32_e32 v27, v27
	v_rndne_f32_e32 v32, v32
	v_rndne_f32_e32 v33, v33
	v_rndne_f32_e32 v30, v30
	v_rndne_f32_e32 v31, v31
	v_rndne_f32_e32 v36, v36
	v_rndne_f32_e32 v37, v37
	v_rndne_f32_e32 v34, v34
	v_rndne_f32_e32 v35, v35
	v_rndne_f32_e32 v40, v40
	v_rndne_f32_e32 v41, v41
	v_rndne_f32_e32 v38, v38
	v_rndne_f32_e32 v39, v39
	v_rndne_f32_e32 v44, v44
	v_rndne_f32_e32 v45, v45
	v_rndne_f32_e32 v42, v42
	v_rndne_f32_e32 v43, v43
	v_rndne_f32_e32 v48, v48
	v_rndne_f32_e32 v49, v49
	v_rndne_f32_e32 v46, v46
	v_rndne_f32_e32 v47, v47
	ds_write2_b32 v77, v14, v15 offset1:1
	ds_write2_b32 v79, v12, v13 offset1:1
	ds_write2_b32 v81, v28, v29 offset1:1
	ds_write2_b32 v83, v26, v27 offset1:1
	ds_write2_b32 v85, v32, v33 offset1:1
	ds_write2_b32 v87, v30, v31 offset1:1
	ds_write2_b32 v89, v36, v37 offset1:1
	ds_write2_b32 v91, v34, v35 offset1:1
	ds_write2_b32 v92, v40, v41 offset1:1
	ds_write2_b32 v93, v38, v39 offset1:1
	ds_write2_b32 v94, v44, v45 offset1:1
	ds_write2_b32 v95, v42, v43 offset1:1
	ds_write2_b32 v96, v48, v49 offset1:1
	ds_write2_b32 v97, v46, v47 offset1:1
	s_waitcnt lgkmcnt(0)
; #define LAS __attribute__((address_space(3)))
; #define GAS __attribute__((address_space(1)))
; #define LDS_WAIT() asm volatile("s_waitcnt lgkmcnt(0)" ::: "memory")
;     ...
;         LDS_WAIT(); asm volatile("" ::: "memory");
;         const int c = lane & 7;
; #pragma unroll
;         for (int j = 0; j < 4; ++j) { const int n = (lane >> 3) + 8 * j; const LAS float* sp = scr + (8 * c) * 33 + n;
;             u32x2 o;
;             o.x = ((unsigned)(int)sp[0 * 33] & 0xFFu) | (((unsigned)(int)sp[1 * 33] & 0xFFu) << 8) | (((unsigned)(int)sp[2 * 33] & 0xFFu) << 16) | (((unsigned)(int)sp[3 * 33] & 0xFFu) << 24);
;             o.y = ((unsigned)(int)sp[4 * 33] & 0xFFu) | (((unsigned)(int)sp[5 * 33] & 0xFFu) << 8) | (((unsigned)(int)sp[6 * 33] & 0xFFu) << 16) | (((unsigned)(int)sp[7 * 33] & 0xFFu) << 24);
;             *(GAS u32x2*)(dst + (size_t)(n0 + n) * D + 64 * kb + 8 * c) = o; }
	ds_read2_b32 v[12:13], v24 offset1:8
	ds_read2_b32 v[14:15], v24 offset0:33 offset1:41
	ds_read2_b32 v[26:27], v24 offset0:66 offset1:74
	ds_read2_b32 v[28:29], v24 offset0:99 offset1:107
	ds_read2_b32 v[30:31], v24 offset0:132 offset1:140
	ds_read2_b32 v[32:33], v24 offset0:165 offset1:173
	ds_read2_b32 v[34:35], v24 offset0:198 offset1:206
	ds_read2_b32 v[36:37], v24 offset0:231 offset1:239
	ds_read2_b32 v[38:39], v24 offset0:16 offset1:24
	ds_read2_b32 v[40:41], v24 offset0:49 offset1:57
	ds_read2_b32 v[42:43], v24 offset0:82 offset1:90
	ds_read2_b32 v[44:45], v24 offset0:115 offset1:123
	ds_read2_b32 v[46:47], v24 offset0:148 offset1:156
	ds_read2_b32 v[48:49], v24 offset0:181 offset1:189
	ds_read2_b32 v[50:51], v24 offset0:214 offset1:222
	ds_read2_b32 v[52:53], v24 offset0:247 offset1:255
	s_waitcnt lgkmcnt(14)
	v_cvt_i32_f32_e32 v14, v14
	s_waitcnt lgkmcnt(10)
	v_cvt_i32_f32_e32 v32, v32
	v_cvt_i32_f32_e32 v12, v12
	v_cvt_i32_f32_sdwa v26, v26 dst_sel:WORD_1 dst_unused:UNUSED_PAD src0_sel:DWORD
	v_cvt_i32_f32_e32 v30, v30
	s_waitcnt lgkmcnt(9)
	v_cvt_i32_f32_sdwa v34, v34 dst_sel:WORD_1 dst_unused:UNUSED_PAD src0_sel:DWORD
	v_cvt_i32_f32_e32 v15, v15
	v_cvt_i32_f32_e32 v33, v33
	s_waitcnt lgkmcnt(6)
	v_cvt_i32_f32_e32 v40, v40
	s_waitcnt lgkmcnt(2)
	v_cvt_i32_f32_e32 v48, v48
	v_cvt_i32_f32_e32 v41, v41
	v_cvt_i32_f32_e32 v49, v49
	v_cvt_i32_f32_sdwa v28, v28 dst_sel:BYTE_3 dst_unused:UNUSED_PAD src0_sel:DWORD
	v_cvt_i32_f32_sdwa v36, v36 dst_sel:BYTE_3 dst_unused:UNUSED_PAD src0_sel:DWORD
	v_cvt_i32_f32_e32 v13, v13
	v_cvt_i32_f32_sdwa v27, v27 dst_sel:WORD_1 dst_unused:UNUSED_PAD src0_sel:DWORD
	v_cvt_i32_f32_e32 v31, v31
	v_cvt_i32_f32_sdwa v35, v35 dst_sel:WORD_1 dst_unused:UNUSED_PAD src0_sel:DWORD
	v_cvt_i32_f32_e32 v38, v38
	v_cvt_i32_f32_sdwa v42, v42 dst_sel:WORD_1 dst_unused:UNUSED_PAD src0_sel:DWORD
	v_cvt_i32_f32_e32 v46, v46
	s_waitcnt lgkmcnt(1)
	v_cvt_i32_f32_sdwa v50, v50 dst_sel:WORD_1 dst_unused:UNUSED_PAD src0_sel:DWORD
	v_cvt_i32_f32_e32 v39, v39
	v_cvt_i32_f32_sdwa v43, v43 dst_sel:WORD_1 dst_unused:UNUSED_PAD src0_sel:DWORD
	v_cvt_i32_f32_e32 v47, v47
	v_cvt_i32_f32_sdwa v51, v51 dst_sel:WORD_1 dst_unused:UNUSED_PAD src0_sel:DWORD
	v_cvt_i32_f32_sdwa v29, v29 dst_sel:BYTE_3 dst_unused:UNUSED_PAD src0_sel:DWORD
	v_cvt_i32_f32_sdwa v37, v37 dst_sel:BYTE_3 dst_unused:UNUSED_PAD src0_sel:DWORD
	v_cvt_i32_f32_sdwa v44, v44 dst_sel:BYTE_3 dst_unused:UNUSED_PAD src0_sel:DWORD
	s_waitcnt lgkmcnt(0)
	v_cvt_i32_f32_sdwa v52, v52 dst_sel:BYTE_3 dst_unused:UNUSED_PAD src0_sel:DWORD
	v_cvt_i32_f32_sdwa v45, v45 dst_sel:BYTE_3 dst_unused:UNUSED_PAD src0_sel:DWORD
	v_cvt_i32_f32_sdwa v53, v53 dst_sel:BYTE_3 dst_unused:UNUSED_PAD src0_sel:DWORD
	v_lshlrev_b32_e32 v14, 8, v14
	v_lshlrev_b32_e32 v32, 8, v32
	v_and_b32_e32 v26, 0xff0000, v26
	v_and_b32_e32 v34, 0xff0000, v34
	v_lshlrev_b32_e32 v15, 8, v15
	v_lshlrev_b32_e32 v33, 8, v33
	v_lshlrev_b32_e32 v40, 8, v40
	v_lshlrev_b32_e32 v48, 8, v48
	v_lshlrev_b32_e32 v41, 8, v41
	v_lshlrev_b32_e32 v49, 8, v49
	v_perm_b32 v12, v14, v12, s28
	v_perm_b32 v14, v32, v30, s28
	v_and_b32_e32 v27, 0xff0000, v27
	v_and_b32_e32 v35, 0xff0000, v35
	v_and_b32_e32 v42, 0xff0000, v42
	v_and_b32_e32 v50, 0xff0000, v50
	v_and_b32_e32 v43, 0xff0000, v43
	v_and_b32_e32 v51, 0xff0000, v51
	v_perm_b32 v15, v15, v13, s28
	v_perm_b32 v30, v33, v31, s28
	v_perm_b32 v31, v40, v38, s28
	v_perm_b32 v32, v48, v46, s28
	v_perm_b32 v33, v41, v39, s28
	v_perm_b32 v38, v49, v47, s28
	v_or3_b32 v12, v12, v26, v28
	v_or3_b32 v13, v14, v34, v36
	v_or3_b32 v14, v15, v27, v29
	v_or3_b32 v15, v30, v35, v37
	v_or3_b32 v26, v31, v42, v44
	v_or3_b32 v27, v32, v50, v52
	v_or3_b32 v28, v33, v43, v45
	v_or3_b32 v29, v38, v51, v53
	global_store_dwordx2 v[16:17], v[12:13], off
	global_store_dwordx2 v[18:19], v[14:15], off
	global_store_dwordx2 v[58:59], v[26:27], off
	global_store_dwordx2 v[60:61], v[28:29], off
	s_waitcnt lgkmcnt(0)
	v_add_u32_e32 v77, 0x420, v25
	v_add_u32_e32 v79, 0x428, v25
	v_add_u32_e32 v81, 0x840, v25
	v_add_u32_e32 v83, 0x848, v25
	v_add_u32_e32 v85, 0xc60, v25
	v_add_u32_e32 v87, 0xc68, v25
	v_add_u32_e32 v89, 0x1080, v25
	v_add_u32_e32 v91, 0x1088, v25
	v_add_u32_e32 v92, 0x14a0, v25
	v_add_u32_e32 v93, 0x14a8, v25
	v_add_u32_e32 v94, 0x18c0, v25
	v_add_u32_e32 v95, 0x18c8, v25
	v_add_u32_e32 v96, 0x1ce0, v25
	v_add_u32_e32 v97, 0x1ce8, v25
	v_lshl_add_u64 v[16:17], v[10:11], 0, s[26:27]
	v_lshl_add_u64 v[18:19], v[8:9], 0, s[26:27]
	v_lshl_add_u64 v[58:59], v[6:7], 0, s[26:27]
	v_lshl_add_u64 v[60:61], v[4:5], 0, s[26:27]
	v_lshl_add_u64 v[4:5], v[4:5], 0, 64
	v_lshl_add_u64 v[6:7], v[6:7], 0, 64
	v_lshl_add_u64 v[8:9], v[8:9], 0, 64
	v_lshl_add_u64 v[10:11], v[10:11], 0, 64
	s_waitcnt vmcnt(24)
; #define LAS __attribute__((address_space(3)))
;     ...
;         for (int i = 0; i < 8; ++i) { const int kk = 8 * i + kr; const int k = 64 * kb + kk; const f32x4 v = __builtin_nontemporal_load((const f32x4*)(W + (size_t)k * pitch)) * g[k];
;             LAS float* p = scr + kk * 33 + 4 * (lane & 7); p[0] = __builtin_rintf(v[0] * inv[0]); p[1] = __builtin_rintf(v[1] * inv[1]); p[2] = __builtin_rintf(v[2] * inv[2]); p[3] = __builtin_rintf(v[3] * inv[3]); }
	v_pk_mul_f32 v[14:15], v[138:139], v[186:187] op_sel_hi:[1,0]
	v_pk_mul_f32 v[12:13], v[140:141], v[186:187] op_sel_hi:[1,0]
	v_mul_f32_e32 v62, v20, v14
	v_mul_f32_e32 v63, v21, v15
	v_mul_f32_e32 v64, v22, v12
	v_mul_f32_e32 v65, v23, v13
	v_pk_mul_f32 v[14:15], v[142:143], v[188:189] op_sel_hi:[1,0]
	v_pk_mul_f32 v[12:13], v[144:145], v[188:189] op_sel_hi:[1,0]
	v_pk_mul_f32 v[26:27], v[148:149], v[190:191] op_sel_hi:[1,0]
	v_pk_mul_f32 v[28:29], v[146:147], v[190:191] op_sel_hi:[1,0]
	v_pk_mul_f32 v[30:31], v[152:153], v[192:193] op_sel_hi:[1,0]
	v_pk_mul_f32 v[32:33], v[150:151], v[192:193] op_sel_hi:[1,0]
	v_pk_mul_f32 v[34:35], v[156:157], v[194:195] op_sel_hi:[1,0]
	v_pk_mul_f32 v[36:37], v[154:155], v[194:195] op_sel_hi:[1,0]
	v_pk_mul_f32 v[38:39], v[160:161], v[196:197] op_sel_hi:[1,0]
	v_pk_mul_f32 v[40:41], v[158:159], v[196:197] op_sel_hi:[1,0]
	v_pk_mul_f32 v[42:43], v[164:165], v[198:199] op_sel_hi:[1,0]
	v_pk_mul_f32 v[44:45], v[162:163], v[198:199] op_sel_hi:[1,0]
	v_pk_mul_f32 v[46:47], v[168:169], v[200:201] op_sel_hi:[1,0]
	v_pk_mul_f32 v[48:49], v[166:167], v[200:201] op_sel_hi:[1,0]
	s_add_u32 s4, s4, 0x16000
	s_addc_u32 s5, s5, 0
	global_load_dwordx4 v[138:141], v250, s[4:5] nt
	global_load_dword v186, v251, s[6:7] offset:3328
	s_add_u32 s4, s4, 0x16000
	s_addc_u32 s5, s5, 0
	global_load_dwordx4 v[142:145], v250, s[4:5] nt
	global_load_dword v188, v251, s[6:7] offset:3360
	s_add_u32 s4, s4, 0x16000
	s_addc_u32 s5, s5, 0
	global_load_dwordx4 v[146:149], v250, s[4:5] nt
	global_load_dword v190, v251, s[6:7] offset:3392
	s_add_u32 s4, s4, 0x16000
	s_addc_u32 s5, s5, 0
	global_load_dwordx4 v[150:153], v250, s[4:5] nt
	global_load_dword v192, v251, s[6:7] offset:3424
	s_add_u32 s4, s4, 0x16000
	s_addc_u32 s5, s5, 0
	global_load_dwordx4 v[154:157], v250, s[4:5] nt
	global_load_dword v194, v251, s[6:7] offset:3456
	s_add_u32 s4, s4, 0x16000
	s_addc_u32 s5, s5, 0
	global_load_dwordx4 v[158:161], v250, s[4:5] nt
	global_load_dword v196, v251, s[6:7] offset:3488
	s_add_u32 s4, s4, 0x16000
	s_addc_u32 s5, s5, 0
	global_load_dwordx4 v[162:165], v250, s[4:5] nt
	global_load_dword v198, v251, s[6:7] offset:3520
	s_add_u32 s4, s4, 0x16000
	s_addc_u32 s5, s5, 0
	global_load_dwordx4 v[166:169], v250, s[4:5] nt
	global_load_dword v200, v251, s[6:7] offset:3552
	v_mul_f32_e32 v14, v20, v14
	v_mul_f32_e32 v15, v21, v15
	v_rndne_f32_e32 v50, v62
	v_rndne_f32_e32 v51, v63
	v_mul_f32_e32 v12, v22, v12
	v_mul_f32_e32 v13, v23, v13
	v_mul_f32_e32 v28, v20, v28
	v_mul_f32_e32 v29, v21, v29
	v_mul_f32_e32 v26, v22, v26
	v_mul_f32_e32 v27, v23, v27
	v_mul_f32_e32 v32, v20, v32
	v_mul_f32_e32 v33, v21, v33
	v_mul_f32_e32 v30, v22, v30
	v_mul_f32_e32 v31, v23, v31
	v_mul_f32_e32 v36, v20, v36
	v_mul_f32_e32 v37, v21, v37
	v_mul_f32_e32 v34, v22, v34
	v_mul_f32_e32 v35, v23, v35
	v_mul_f32_e32 v40, v20, v40
	v_mul_f32_e32 v41, v21, v41
	v_mul_f32_e32 v38, v22, v38
	v_mul_f32_e32 v39, v23, v39
	v_mul_f32_e32 v44, v20, v44
	v_mul_f32_e32 v45, v21, v45
	v_mul_f32_e32 v42, v22, v42
	v_mul_f32_e32 v43, v23, v43
	v_mul_f32_e32 v48, v20, v48
	v_mul_f32_e32 v49, v21, v49
	v_mul_f32_e32 v46, v22, v46
	v_mul_f32_e32 v47, v23, v47
	v_rndne_f32_e32 v14, v14
	v_rndne_f32_e32 v15, v15
	v_rndne_f32_e32 v52, v64
	v_rndne_f32_e32 v53, v65
	ds_write2_b32 v25, v50, v51 offset1:1
	ds_write2_b32 v25, v52, v53 offset0:2 offset1:3
	v_rndne_f32_e32 v12, v12
	v_rndne_f32_e32 v13, v13
	v_rndne_f32_e32 v28, v28
	v_rndne_f32_e32 v29, v29
	v_rndne_f32_e32 v26, v26
	v_rndne_f32_e32 v27, v27
	v_rndne_f32_e32 v32, v32
	v_rndne_f32_e32 v33, v33
	v_rndne_f32_e32 v30, v30
	v_rndne_f32_e32 v31, v31
	v_rndne_f32_e32 v36, v36
	v_rndne_f32_e32 v37, v37
	v_rndne_f32_e32 v34, v34
	v_rndne_f32_e32 v35, v35
	v_rndne_f32_e32 v40, v40
	v_rndne_f32_e32 v41, v41
	v_rndne_f32_e32 v38, v38
	v_rndne_f32_e32 v39, v39
	v_rndne_f32_e32 v44, v44
	v_rndne_f32_e32 v45, v45
	v_rndne_f32_e32 v42, v42
	v_rndne_f32_e32 v43, v43
	v_rndne_f32_e32 v48, v48
	v_rndne_f32_e32 v49, v49
	v_rndne_f32_e32 v46, v46
	v_rndne_f32_e32 v47, v47
	ds_write2_b32 v77, v14, v15 offset1:1
	ds_write2_b32 v79, v12, v13 offset1:1
	ds_write2_b32 v81, v28, v29 offset1:1
	ds_write2_b32 v83, v26, v27 offset1:1
	ds_write2_b32 v85, v32, v33 offset1:1
	ds_write2_b32 v87, v30, v31 offset1:1
	ds_write2_b32 v89, v36, v37 offset1:1
	ds_write2_b32 v91, v34, v35 offset1:1
	ds_write2_b32 v92, v40, v41 offset1:1
	ds_write2_b32 v93, v38, v39 offset1:1
	ds_write2_b32 v94, v44, v45 offset1:1
	ds_write2_b32 v95, v42, v43 offset1:1
	ds_write2_b32 v96, v48, v49 offset1:1
	ds_write2_b32 v97, v46, v47 offset1:1
	s_waitcnt lgkmcnt(0)
	ds_read2_b32 v[12:13], v24 offset1:8
	ds_read2_b32 v[14:15], v24 offset0:33 offset1:41
	ds_read2_b32 v[26:27], v24 offset0:66 offset1:74
	ds_read2_b32 v[28:29], v24 offset0:99 offset1:107
	ds_read2_b32 v[30:31], v24 offset0:132 offset1:140
	ds_read2_b32 v[32:33], v24 offset0:165 offset1:173
	ds_read2_b32 v[34:35], v24 offset0:198 offset1:206
	ds_read2_b32 v[36:37], v24 offset0:231 offset1:239
	ds_read2_b32 v[38:39], v24 offset0:16 offset1:24
	ds_read2_b32 v[40:41], v24 offset0:49 offset1:57
	ds_read2_b32 v[42:43], v24 offset0:82 offset1:90
	ds_read2_b32 v[44:45], v24 offset0:115 offset1:123
	ds_read2_b32 v[46:47], v24 offset0:148 offset1:156
	ds_read2_b32 v[48:49], v24 offset0:181 offset1:189
	ds_read2_b32 v[50:51], v24 offset0:214 offset1:222
	ds_read2_b32 v[52:53], v24 offset0:247 offset1:255
	s_waitcnt lgkmcnt(14)
	v_cvt_i32_f32_e32 v14, v14
	s_waitcnt lgkmcnt(10)
	v_cvt_i32_f32_e32 v32, v32
	v_cvt_i32_f32_e32 v12, v12
	v_cvt_i32_f32_sdwa v26, v26 dst_sel:WORD_1 dst_unused:UNUSED_PAD src0_sel:DWORD
	v_cvt_i32_f32_e32 v30, v30
	s_waitcnt lgkmcnt(9)
; #define LAS __attribute__((address_space(3)))
; #define GAS __attribute__((address_space(1)))
; #define LDS_WAIT() asm volatile("s_waitcnt lgkmcnt(0)" ::: "memory")
;     ...
;         for (int i = 0; i < 8; ++i) { const int kk = 8 * i + kr; const int k = 64 * kb + kk; const f32x4 v = __builtin_nontemporal_load((const f32x4*)(W + (size_t)k * pitch)) * g[k];
;             LAS float* p = scr + kk * 33 + 4 * (lane & 7); p[0] = __builtin_rintf(v[0] * inv[0]); p[1] = __builtin_rintf(v[1] * inv[1]); p[2] = __builtin_rintf(v[2] * inv[2]); p[3] = __builtin_rintf(v[3] * inv[3]); }
;         LDS_WAIT(); asm volatile("" ::: "memory");
;         const int c = lane & 7;
; #pragma unroll
;         for (int j = 0; j < 4; ++j) { const int n = (lane >> 3) + 8 * j; const LAS float* sp = scr + (8 * c) * 33 + n;
;             u32x2 o;
;             o.x = ((unsigned)(int)sp[0 * 33] & 0xFFu) | (((unsigned)(int)sp[1 * 33] & 0xFFu) << 8) | (((unsigned)(int)sp[2 * 33] & 0xFFu) << 16) | (((unsigned)(int)sp[3 * 33] & 0xFFu) << 24);
;             o.y = ((unsigned)(int)sp[4 * 33] & 0xFFu) | (((unsigned)(int)sp[5 * 33] & 0xFFu) << 8) | (((unsigned)(int)sp[6 * 33] & 0xFFu) << 16) | (((unsigned)(int)sp[7 * 33] & 0xFFu) << 24);
;             *(GAS u32x2*)(dst + (size_t)(n0 + n) * D + 64 * kb + 8 * c) = o; }
	v_cvt_i32_f32_sdwa v34, v34 dst_sel:WORD_1 dst_unused:UNUSED_PAD src0_sel:DWORD
	v_cvt_i32_f32_e32 v15, v15
	v_cvt_i32_f32_e32 v33, v33
	s_waitcnt lgkmcnt(6)
	v_cvt_i32_f32_e32 v40, v40
	s_waitcnt lgkmcnt(2)
	v_cvt_i32_f32_e32 v48, v48
	v_cvt_i32_f32_e32 v41, v41
	v_cvt_i32_f32_e32 v49, v49
	v_cvt_i32_f32_sdwa v28, v28 dst_sel:BYTE_3 dst_unused:UNUSED_PAD src0_sel:DWORD
	v_cvt_i32_f32_sdwa v36, v36 dst_sel:BYTE_3 dst_unused:UNUSED_PAD src0_sel:DWORD
	v_cvt_i32_f32_e32 v13, v13
	v_cvt_i32_f32_sdwa v27, v27 dst_sel:WORD_1 dst_unused:UNUSED_PAD src0_sel:DWORD
	v_cvt_i32_f32_e32 v31, v31
	v_cvt_i32_f32_sdwa v35, v35 dst_sel:WORD_1 dst_unused:UNUSED_PAD src0_sel:DWORD
	v_cvt_i32_f32_e32 v38, v38
	v_cvt_i32_f32_sdwa v42, v42 dst_sel:WORD_1 dst_unused:UNUSED_PAD src0_sel:DWORD
	v_cvt_i32_f32_e32 v46, v46
	s_waitcnt lgkmcnt(1)
	v_cvt_i32_f32_sdwa v50, v50 dst_sel:WORD_1 dst_unused:UNUSED_PAD src0_sel:DWORD
	v_cvt_i32_f32_e32 v39, v39
	v_cvt_i32_f32_sdwa v43, v43 dst_sel:WORD_1 dst_unused:UNUSED_PAD src0_sel:DWORD
	v_cvt_i32_f32_e32 v47, v47
	v_cvt_i32_f32_sdwa v51, v51 dst_sel:WORD_1 dst_unused:UNUSED_PAD src0_sel:DWORD
	v_cvt_i32_f32_sdwa v29, v29 dst_sel:BYTE_3 dst_unused:UNUSED_PAD src0_sel:DWORD
	v_cvt_i32_f32_sdwa v37, v37 dst_sel:BYTE_3 dst_unused:UNUSED_PAD src0_sel:DWORD
	v_cvt_i32_f32_sdwa v44, v44 dst_sel:BYTE_3 dst_unused:UNUSED_PAD src0_sel:DWORD
	s_waitcnt lgkmcnt(0)
	v_cvt_i32_f32_sdwa v52, v52 dst_sel:BYTE_3 dst_unused:UNUSED_PAD src0_sel:DWORD
	v_cvt_i32_f32_sdwa v45, v45 dst_sel:BYTE_3 dst_unused:UNUSED_PAD src0_sel:DWORD
	v_cvt_i32_f32_sdwa v53, v53 dst_sel:BYTE_3 dst_unused:UNUSED_PAD src0_sel:DWORD
	v_lshlrev_b32_e32 v14, 8, v14
	v_lshlrev_b32_e32 v32, 8, v32
	v_and_b32_e32 v26, 0xff0000, v26
	v_and_b32_e32 v34, 0xff0000, v34
	v_lshlrev_b32_e32 v15, 8, v15
	v_lshlrev_b32_e32 v33, 8, v33
	v_lshlrev_b32_e32 v40, 8, v40
	v_lshlrev_b32_e32 v48, 8, v48
	v_lshlrev_b32_e32 v41, 8, v41
	v_lshlrev_b32_e32 v49, 8, v49
	v_perm_b32 v12, v14, v12, s28
	v_perm_b32 v14, v32, v30, s28
	v_and_b32_e32 v27, 0xff0000, v27
	v_and_b32_e32 v35, 0xff0000, v35
	v_and_b32_e32 v42, 0xff0000, v42
	v_and_b32_e32 v50, 0xff0000, v50
	v_and_b32_e32 v43, 0xff0000, v43
	v_and_b32_e32 v51, 0xff0000, v51
	v_perm_b32 v15, v15, v13, s28
	v_perm_b32 v30, v33, v31, s28
	v_perm_b32 v31, v40, v38, s28
	v_perm_b32 v32, v48, v46, s28
	v_perm_b32 v33, v41, v39, s28
	v_perm_b32 v38, v49, v47, s28
	v_or3_b32 v12, v12, v26, v28
	v_or3_b32 v13, v14, v34, v36
	v_or3_b32 v14, v15, v27, v29
	v_or3_b32 v15, v30, v35, v37
	v_or3_b32 v26, v31, v42, v44
	v_or3_b32 v27, v32, v50, v52
	v_or3_b32 v28, v33, v43, v45
	v_or3_b32 v29, v38, v51, v53
	global_store_dwordx2 v[16:17], v[12:13], off
	global_store_dwordx2 v[18:19], v[14:15], off
	global_store_dwordx2 v[58:59], v[26:27], off
	global_store_dwordx2 v[60:61], v[28:29], off
	s_waitcnt lgkmcnt(0)
	v_add_u32_e32 v77, 0x420, v25
	v_add_u32_e32 v79, 0x428, v25
	v_add_u32_e32 v81, 0x840, v25
	v_add_u32_e32 v83, 0x848, v25
	v_add_u32_e32 v85, 0xc60, v25
	v_add_u32_e32 v87, 0xc68, v25
	v_add_u32_e32 v89, 0x1080, v25
	v_add_u32_e32 v91, 0x1088, v25
	v_add_u32_e32 v92, 0x14a0, v25
	v_add_u32_e32 v93, 0x14a8, v25
	v_add_u32_e32 v94, 0x18c0, v25
	v_add_u32_e32 v95, 0x18c8, v25
	v_add_u32_e32 v96, 0x1ce0, v25
	v_add_u32_e32 v97, 0x1ce8, v25
	v_lshl_add_u64 v[16:17], v[10:11], 0, s[26:27]
	v_lshl_add_u64 v[18:19], v[8:9], 0, s[26:27]
	v_lshl_add_u64 v[58:59], v[6:7], 0, s[26:27]
	v_lshl_add_u64 v[60:61], v[4:5], 0, s[26:27]
	v_lshl_add_u64 v[4:5], v[4:5], 0, 64
	v_lshl_add_u64 v[6:7], v[6:7], 0, 64
	v_lshl_add_u64 v[8:9], v[8:9], 0, 64
	v_lshl_add_u64 v[10:11], v[10:11], 0, 64
	s_waitcnt vmcnt(24)
	v_pk_mul_f32 v[14:15], v[106:107], v[170:171] op_sel_hi:[1,0]
	v_pk_mul_f32 v[12:13], v[108:109], v[170:171] op_sel_hi:[1,0]
	v_mul_f32_e32 v62, v20, v14
	v_mul_f32_e32 v63, v21, v15
	v_mul_f32_e32 v64, v22, v12
	v_mul_f32_e32 v65, v23, v13
	v_pk_mul_f32 v[14:15], v[110:111], v[172:173] op_sel_hi:[1,0]
	v_pk_mul_f32 v[12:13], v[112:113], v[172:173] op_sel_hi:[1,0]
	v_pk_mul_f32 v[26:27], v[116:117], v[174:175] op_sel_hi:[1,0]
	v_pk_mul_f32 v[28:29], v[114:115], v[174:175] op_sel_hi:[1,0]
	v_pk_mul_f32 v[30:31], v[120:121], v[176:177] op_sel_hi:[1,0]
	v_pk_mul_f32 v[32:33], v[118:119], v[176:177] op_sel_hi:[1,0]
	v_pk_mul_f32 v[34:35], v[124:125], v[178:179] op_sel_hi:[1,0]
	v_pk_mul_f32 v[36:37], v[122:123], v[178:179] op_sel_hi:[1,0]
	v_pk_mul_f32 v[38:39], v[128:129], v[180:181] op_sel_hi:[1,0]
	v_pk_mul_f32 v[40:41], v[126:127], v[180:181] op_sel_hi:[1,0]
	v_pk_mul_f32 v[42:43], v[132:133], v[182:183] op_sel_hi:[1,0]
	v_pk_mul_f32 v[44:45], v[130:131], v[182:183] op_sel_hi:[1,0]
	v_pk_mul_f32 v[46:47], v[136:137], v[184:185] op_sel_hi:[1,0]
	v_pk_mul_f32 v[48:49], v[134:135], v[184:185] op_sel_hi:[1,0]
	s_add_u32 s4, s4, 0x16000
	s_addc_u32 s5, s5, 0
	global_load_dwordx4 v[106:109], v250, s[4:5] nt
	global_load_dword v170, v251, s[6:7] offset:3584
	s_add_u32 s4, s4, 0x16000
	s_addc_u32 s5, s5, 0
	global_load_dwordx4 v[110:113], v250, s[4:5] nt
	global_load_dword v172, v251, s[6:7] offset:3616
	s_add_u32 s4, s4, 0x16000
	s_addc_u32 s5, s5, 0
	global_load_dwordx4 v[114:117], v250, s[4:5] nt
	global_load_dword v174, v251, s[6:7] offset:3648
	s_add_u32 s4, s4, 0x16000
	s_addc_u32 s5, s5, 0
	global_load_dwordx4 v[118:121], v250, s[4:5] nt
	global_load_dword v176, v251, s[6:7] offset:3680
	s_add_u32 s4, s4, 0x16000
	s_addc_u32 s5, s5, 0
	global_load_dwordx4 v[122:125], v250, s[4:5] nt
	global_load_dword v178, v251, s[6:7] offset:3712
	s_add_u32 s4, s4, 0x16000
	s_addc_u32 s5, s5, 0
	global_load_dwordx4 v[126:129], v250, s[4:5] nt
; #define LAS __attribute__((address_space(3)))
; #define GAS __attribute__((address_space(1)))
; #define LDS_WAIT() asm volatile("s_waitcnt lgkmcnt(0)" ::: "memory")
;     ...
;     for (int kb = 0; kb < D / 64; ++kb) {
; #pragma unroll
;         for (int i = 0; i < 8; ++i) { const int kk = 8 * i + kr; const int k = 64 * kb + kk; const f32x4 v = __builtin_nontemporal_load((const f32x4*)(W + (size_t)k * pitch)) * g[k];
;             LAS float* p = scr + kk * 33 + 4 * (lane & 7); p[0] = __builtin_rintf(v[0] * inv[0]); p[1] = __builtin_rintf(v[1] * inv[1]); p[2] = __builtin_rintf(v[2] * inv[2]); p[3] = __builtin_rintf(v[3] * inv[3]); }
;         LDS_WAIT(); asm volatile("" ::: "memory");
;         const int c = lane & 7;
; #pragma unroll
;         for (int j = 0; j < 4; ++j) { const int n = (lane >> 3) + 8 * j; const LAS float* sp = scr + (8 * c) * 33 + n;
;             u32x2 o;
;             o.x = ((unsigned)(int)sp[0 * 33] & 0xFFu) | (((unsigned)(int)sp[1 * 33] & 0xFFu) << 8) | (((unsigned)(int)sp[2 * 33] & 0xFFu) << 16) | (((unsigned)(int)sp[3 * 33] & 0xFFu) << 24);
;             o.y = ((unsigned)(int)sp[4 * 33] & 0xFFu) | (((unsigned)(int)sp[5 * 33] & 0xFFu) << 8) | (((unsigned)(int)sp[6 * 33] & 0xFFu) << 16) | (((unsigned)(int)sp[7 * 33] & 0xFFu) << 24);
;             *(GAS u32x2*)(dst + (size_t)(n0 + n) * D + 64 * kb + 8 * c) = o; }
;         LDS_WAIT(); asm volatile("" ::: "memory");
	global_load_dword v180, v251, s[6:7] offset:3744
	s_add_u32 s4, s4, 0x16000
	s_addc_u32 s5, s5, 0
	global_load_dwordx4 v[130:133], v250, s[4:5] nt
	global_load_dword v182, v251, s[6:7] offset:3776
	s_add_u32 s4, s4, 0x16000
	s_addc_u32 s5, s5, 0
	global_load_dwordx4 v[134:137], v250, s[4:5] nt
	global_load_dword v184, v251, s[6:7] offset:3808
	v_mul_f32_e32 v14, v20, v14
	v_mul_f32_e32 v15, v21, v15
	v_rndne_f32_e32 v50, v62
	v_rndne_f32_e32 v51, v63
	v_mul_f32_e32 v12, v22, v12
	v_mul_f32_e32 v13, v23, v13
	v_mul_f32_e32 v28, v20, v28
	v_mul_f32_e32 v29, v21, v29
	v_mul_f32_e32 v26, v22, v26
	v_mul_f32_e32 v27, v23, v27
	v_mul_f32_e32 v32, v20, v32
	v_mul_f32_e32 v33, v21, v33
	v_mul_f32_e32 v30, v22, v30
	v_mul_f32_e32 v31, v23, v31
	v_mul_f32_e32 v36, v20, v36
	v_mul_f32_e32 v37, v21, v37
	v_mul_f32_e32 v34, v22, v34
	v_mul_f32_e32 v35, v23, v35
	v_mul_f32_e32 v40, v20, v40
	v_mul_f32_e32 v41, v21, v41
	v_mul_f32_e32 v38, v22, v38
	v_mul_f32_e32 v39, v23, v39
	v_mul_f32_e32 v44, v20, v44
	v_mul_f32_e32 v45, v21, v45
	v_mul_f32_e32 v42, v22, v42
	v_mul_f32_e32 v43, v23, v43
	v_mul_f32_e32 v48, v20, v48
	v_mul_f32_e32 v49, v21, v49
	v_mul_f32_e32 v46, v22, v46
	v_mul_f32_e32 v47, v23, v47
	v_rndne_f32_e32 v14, v14
	v_rndne_f32_e32 v15, v15
	v_rndne_f32_e32 v52, v64
	v_rndne_f32_e32 v53, v65
	ds_write2_b32 v25, v50, v51 offset1:1
	ds_write2_b32 v25, v52, v53 offset0:2 offset1:3
	v_rndne_f32_e32 v12, v12
	v_rndne_f32_e32 v13, v13
	v_rndne_f32_e32 v28, v28
	v_rndne_f32_e32 v29, v29
	v_rndne_f32_e32 v26, v26
	v_rndne_f32_e32 v27, v27
	v_rndne_f32_e32 v32, v32
	v_rndne_f32_e32 v33, v33
	v_rndne_f32_e32 v30, v30
	v_rndne_f32_e32 v31, v31
	v_rndne_f32_e32 v36, v36
	v_rndne_f32_e32 v37, v37
	v_rndne_f32_e32 v34, v34
	v_rndne_f32_e32 v35, v35
	v_rndne_f32_e32 v40, v40
	v_rndne_f32_e32 v41, v41
	v_rndne_f32_e32 v38, v38
	v_rndne_f32_e32 v39, v39
	v_rndne_f32_e32 v44, v44
	v_rndne_f32_e32 v45, v45
	v_rndne_f32_e32 v42, v42
	v_rndne_f32_e32 v43, v43
	v_rndne_f32_e32 v48, v48
	v_rndne_f32_e32 v49, v49
	v_rndne_f32_e32 v46, v46
	v_rndne_f32_e32 v47, v47
	ds_write2_b32 v77, v14, v15 offset1:1
	ds_write2_b32 v79, v12, v13 offset1:1
	ds_write2_b32 v81, v28, v29 offset1:1
	ds_write2_b32 v83, v26, v27 offset1:1
	ds_write2_b32 v85, v32, v33 offset1:1
	ds_write2_b32 v87, v30, v31 offset1:1
	ds_write2_b32 v89, v36, v37 offset1:1
	ds_write2_b32 v91, v34, v35 offset1:1
	ds_write2_b32 v92, v40, v41 offset1:1
	ds_write2_b32 v93, v38, v39 offset1:1
	ds_write2_b32 v94, v44, v45 offset1:1
	ds_write2_b32 v95, v42, v43 offset1:1
	ds_write2_b32 v96, v48, v49 offset1:1
	ds_write2_b32 v97, v46, v47 offset1:1
	s_waitcnt lgkmcnt(0)
	ds_read2_b32 v[12:13], v24 offset1:8
	ds_read2_b32 v[14:15], v24 offset0:33 offset1:41
	ds_read2_b32 v[26:27], v24 offset0:66 offset1:74
	ds_read2_b32 v[28:29], v24 offset0:99 offset1:107
	ds_read2_b32 v[30:31], v24 offset0:132 offset1:140
	ds_read2_b32 v[32:33], v24 offset0:165 offset1:173
	ds_read2_b32 v[34:35], v24 offset0:198 offset1:206
	ds_read2_b32 v[36:37], v24 offset0:231 offset1:239
	ds_read2_b32 v[38:39], v24 offset0:16 offset1:24
	ds_read2_b32 v[40:41], v24 offset0:49 offset1:57
	ds_read2_b32 v[42:43], v24 offset0:82 offset1:90
	ds_read2_b32 v[44:45], v24 offset0:115 offset1:123
	ds_read2_b32 v[46:47], v24 offset0:148 offset1:156
	ds_read2_b32 v[48:49], v24 offset0:181 offset1:189
	ds_read2_b32 v[50:51], v24 offset0:214 offset1:222
	ds_read2_b32 v[52:53], v24 offset0:247 offset1:255
	s_waitcnt lgkmcnt(14)
	v_cvt_i32_f32_e32 v14, v14
	s_waitcnt lgkmcnt(10)
	v_cvt_i32_f32_e32 v32, v32
	v_cvt_i32_f32_e32 v12, v12
	v_cvt_i32_f32_sdwa v26, v26 dst_sel:WORD_1 dst_unused:UNUSED_PAD src0_sel:DWORD
	v_cvt_i32_f32_e32 v30, v30
	s_waitcnt lgkmcnt(9)
	v_cvt_i32_f32_sdwa v34, v34 dst_sel:WORD_1 dst_unused:UNUSED_PAD src0_sel:DWORD
	v_cvt_i32_f32_e32 v15, v15
	v_cvt_i32_f32_e32 v33, v33
	s_waitcnt lgkmcnt(6)
	v_cvt_i32_f32_e32 v40, v40
	s_waitcnt lgkmcnt(2)
	v_cvt_i32_f32_e32 v48, v48
	v_cvt_i32_f32_e32 v41, v41
	v_cvt_i32_f32_e32 v49, v49
	v_cvt_i32_f32_sdwa v28, v28 dst_sel:BYTE_3 dst_unused:UNUSED_PAD src0_sel:DWORD
	v_cvt_i32_f32_sdwa v36, v36 dst_sel:BYTE_3 dst_unused:UNUSED_PAD src0_sel:DWORD
	v_cvt_i32_f32_e32 v13, v13
	v_cvt_i32_f32_sdwa v27, v27 dst_sel:WORD_1 dst_unused:UNUSED_PAD src0_sel:DWORD
	v_cvt_i32_f32_e32 v31, v31
	v_cvt_i32_f32_sdwa v35, v35 dst_sel:WORD_1 dst_unused:UNUSED_PAD src0_sel:DWORD
	v_cvt_i32_f32_e32 v38, v38
	v_cvt_i32_f32_sdwa v42, v42 dst_sel:WORD_1 dst_unused:UNUSED_PAD src0_sel:DWORD
	v_cvt_i32_f32_e32 v46, v46
	s_waitcnt lgkmcnt(1)
	v_cvt_i32_f32_sdwa v50, v50 dst_sel:WORD_1 dst_unused:UNUSED_PAD src0_sel:DWORD
	v_cvt_i32_f32_e32 v39, v39
	v_cvt_i32_f32_sdwa v43, v43 dst_sel:WORD_1 dst_unused:UNUSED_PAD src0_sel:DWORD
	v_cvt_i32_f32_e32 v47, v47
	v_cvt_i32_f32_sdwa v51, v51 dst_sel:WORD_1 dst_unused:UNUSED_PAD src0_sel:DWORD
	v_cvt_i32_f32_sdwa v29, v29 dst_sel:BYTE_3 dst_unused:UNUSED_PAD src0_sel:DWORD
	v_cvt_i32_f32_sdwa v37, v37 dst_sel:BYTE_3 dst_unused:UNUSED_PAD src0_sel:DWORD
	v_cvt_i32_f32_sdwa v44, v44 dst_sel:BYTE_3 dst_unused:UNUSED_PAD src0_sel:DWORD
	s_waitcnt lgkmcnt(0)
; #define LAS __attribute__((address_space(3)))
; #define GAS __attribute__((address_space(1)))
; #define LDS_WAIT() asm volatile("s_waitcnt lgkmcnt(0)" ::: "memory")
;     ...
;     for (int kb = 0; kb < D / 64; ++kb) {
; #pragma unroll
;         for (int i = 0; i < 8; ++i) { const int kk = 8 * i + kr; const int k = 64 * kb + kk; const f32x4 v = __builtin_nontemporal_load((const f32x4*)(W + (size_t)k * pitch)) * g[k];
;             LAS float* p = scr + kk * 33 + 4 * (lane & 7); p[0] = __builtin_rintf(v[0] * inv[0]); p[1] = __builtin_rintf(v[1] * inv[1]); p[2] = __builtin_rintf(v[2] * inv[2]); p[3] = __builtin_rintf(v[3] * inv[3]); }
;         LDS_WAIT(); asm volatile("" ::: "memory");
;         const int c = lane & 7;
; #pragma unroll
;         for (int j = 0; j < 4; ++j) { const int n = (lane >> 3) + 8 * j; const LAS float* sp = scr + (8 * c) * 33 + n;
;             u32x2 o;
;             o.x = ((unsigned)(int)sp[0 * 33] & 0xFFu) | (((unsigned)(int)sp[1 * 33] & 0xFFu) << 8) | (((unsigned)(int)sp[2 * 33] & 0xFFu) << 16) | (((unsigned)(int)sp[3 * 33] & 0xFFu) << 24);
;             o.y = ((unsigned)(int)sp[4 * 33] & 0xFFu) | (((unsigned)(int)sp[5 * 33] & 0xFFu) << 8) | (((unsigned)(int)sp[6 * 33] & 0xFFu) << 16) | (((unsigned)(int)sp[7 * 33] & 0xFFu) << 24);
;             *(GAS u32x2*)(dst + (size_t)(n0 + n) * D + 64 * kb + 8 * c) = o; }
;         LDS_WAIT(); asm volatile("" ::: "memory");
	v_cvt_i32_f32_sdwa v52, v52 dst_sel:BYTE_3 dst_unused:UNUSED_PAD src0_sel:DWORD
	v_cvt_i32_f32_sdwa v45, v45 dst_sel:BYTE_3 dst_unused:UNUSED_PAD src0_sel:DWORD
	v_cvt_i32_f32_sdwa v53, v53 dst_sel:BYTE_3 dst_unused:UNUSED_PAD src0_sel:DWORD
	v_lshlrev_b32_e32 v14, 8, v14
	v_lshlrev_b32_e32 v32, 8, v32
	v_and_b32_e32 v26, 0xff0000, v26
	v_and_b32_e32 v34, 0xff0000, v34
	v_lshlrev_b32_e32 v15, 8, v15
	v_lshlrev_b32_e32 v33, 8, v33
	v_lshlrev_b32_e32 v40, 8, v40
	v_lshlrev_b32_e32 v48, 8, v48
	v_lshlrev_b32_e32 v41, 8, v41
	v_lshlrev_b32_e32 v49, 8, v49
	v_perm_b32 v12, v14, v12, s28
	v_perm_b32 v14, v32, v30, s28
	v_and_b32_e32 v27, 0xff0000, v27
	v_and_b32_e32 v35, 0xff0000, v35
	v_and_b32_e32 v42, 0xff0000, v42
	v_and_b32_e32 v50, 0xff0000, v50
	v_and_b32_e32 v43, 0xff0000, v43
	v_and_b32_e32 v51, 0xff0000, v51
	v_perm_b32 v15, v15, v13, s28
	v_perm_b32 v30, v33, v31, s28
	v_perm_b32 v31, v40, v38, s28
	v_perm_b32 v32, v48, v46, s28
	v_perm_b32 v33, v41, v39, s28
	v_perm_b32 v38, v49, v47, s28
	v_or3_b32 v12, v12, v26, v28
	v_or3_b32 v13, v14, v34, v36
	v_or3_b32 v14, v15, v27, v29
	v_or3_b32 v15, v30, v35, v37
	v_or3_b32 v26, v31, v42, v44
	v_or3_b32 v27, v32, v50, v52
	v_or3_b32 v28, v33, v43, v45
	v_or3_b32 v29, v38, v51, v53
	global_store_dwordx2 v[16:17], v[12:13], off
	global_store_dwordx2 v[18:19], v[14:15], off
	global_store_dwordx2 v[58:59], v[26:27], off
	global_store_dwordx2 v[60:61], v[28:29], off
	s_waitcnt lgkmcnt(0)
	v_add_u32_e32 v77, 0x420, v25
	v_add_u32_e32 v79, 0x428, v25
	v_add_u32_e32 v81, 0x840, v25
	v_add_u32_e32 v83, 0x848, v25
	v_add_u32_e32 v85, 0xc60, v25
	v_add_u32_e32 v87, 0xc68, v25
	v_add_u32_e32 v89, 0x1080, v25
	v_add_u32_e32 v91, 0x1088, v25
	v_add_u32_e32 v92, 0x14a0, v25
	v_add_u32_e32 v93, 0x14a8, v25
	v_add_u32_e32 v94, 0x18c0, v25
	v_add_u32_e32 v95, 0x18c8, v25
	v_add_u32_e32 v96, 0x1ce0, v25
	v_add_u32_e32 v97, 0x1ce8, v25
	v_lshl_add_u64 v[16:17], v[10:11], 0, s[26:27]
	v_lshl_add_u64 v[18:19], v[8:9], 0, s[26:27]
	v_lshl_add_u64 v[58:59], v[6:7], 0, s[26:27]
	v_lshl_add_u64 v[60:61], v[4:5], 0, s[26:27]
	v_lshl_add_u64 v[4:5], v[4:5], 0, 64
	v_lshl_add_u64 v[6:7], v[6:7], 0, 64
	v_lshl_add_u64 v[8:9], v[8:9], 0, 64
	v_lshl_add_u64 v[10:11], v[10:11], 0, 64
	s_waitcnt vmcnt(24)
	v_pk_mul_f32 v[14:15], v[138:139], v[186:187] op_sel_hi:[1,0]
	v_pk_mul_f32 v[12:13], v[140:141], v[186:187] op_sel_hi:[1,0]
	v_mul_f32_e32 v62, v20, v14
	v_mul_f32_e32 v63, v21, v15
	v_mul_f32_e32 v64, v22, v12
	v_mul_f32_e32 v65, v23, v13
	v_pk_mul_f32 v[14:15], v[142:143], v[188:189] op_sel_hi:[1,0]
	v_pk_mul_f32 v[12:13], v[144:145], v[188:189] op_sel_hi:[1,0]
	v_pk_mul_f32 v[26:27], v[148:149], v[190:191] op_sel_hi:[1,0]
	v_pk_mul_f32 v[28:29], v[146:147], v[190:191] op_sel_hi:[1,0]
	v_pk_mul_f32 v[30:31], v[152:153], v[192:193] op_sel_hi:[1,0]
	v_pk_mul_f32 v[32:33], v[150:151], v[192:193] op_sel_hi:[1,0]
	v_pk_mul_f32 v[34:35], v[156:157], v[194:195] op_sel_hi:[1,0]
	v_pk_mul_f32 v[36:37], v[154:155], v[194:195] op_sel_hi:[1,0]
	v_pk_mul_f32 v[38:39], v[160:161], v[196:197] op_sel_hi:[1,0]
	v_pk_mul_f32 v[40:41], v[158:159], v[196:197] op_sel_hi:[1,0]
	v_pk_mul_f32 v[42:43], v[164:165], v[198:199] op_sel_hi:[1,0]
	v_pk_mul_f32 v[44:45], v[162:163], v[198:199] op_sel_hi:[1,0]
	v_pk_mul_f32 v[46:47], v[168:169], v[200:201] op_sel_hi:[1,0]
	v_pk_mul_f32 v[48:49], v[166:167], v[200:201] op_sel_hi:[1,0]
	s_add_u32 s4, s4, 0x16000
	s_addc_u32 s5, s5, 0
	global_load_dwordx4 v[138:141], v250, s[4:5] nt
	global_load_dword v186, v251, s[6:7] offset:3840
	s_add_u32 s4, s4, 0x16000
	s_addc_u32 s5, s5, 0
	global_load_dwordx4 v[142:145], v250, s[4:5] nt
	global_load_dword v188, v251, s[6:7] offset:3872
	s_add_u32 s4, s4, 0x16000
	s_addc_u32 s5, s5, 0
	global_load_dwordx4 v[146:149], v250, s[4:5] nt
	global_load_dword v190, v251, s[6:7] offset:3904
	s_add_u32 s4, s4, 0x16000
	s_addc_u32 s5, s5, 0
	global_load_dwordx4 v[150:153], v250, s[4:5] nt
	global_load_dword v192, v251, s[6:7] offset:3936
	s_add_u32 s4, s4, 0x16000
	s_addc_u32 s5, s5, 0
	global_load_dwordx4 v[154:157], v250, s[4:5] nt
	global_load_dword v194, v251, s[6:7] offset:3968
	s_add_u32 s4, s4, 0x16000
	s_addc_u32 s5, s5, 0
	global_load_dwordx4 v[158:161], v250, s[4:5] nt
	global_load_dword v196, v251, s[6:7] offset:4000
	s_add_u32 s4, s4, 0x16000
	s_addc_u32 s5, s5, 0
	global_load_dwordx4 v[162:165], v250, s[4:5] nt
	global_load_dword v198, v251, s[6:7] offset:4032
	s_add_u32 s4, s4, 0x16000
	s_addc_u32 s5, s5, 0
	global_load_dwordx4 v[166:169], v250, s[4:5] nt
	global_load_dword v200, v251, s[6:7] offset:4064
	v_mul_f32_e32 v14, v20, v14
	v_mul_f32_e32 v15, v21, v15
	v_rndne_f32_e32 v50, v62
	v_rndne_f32_e32 v51, v63
	v_mul_f32_e32 v12, v22, v12
	v_mul_f32_e32 v13, v23, v13
	v_mul_f32_e32 v28, v20, v28
	v_mul_f32_e32 v29, v21, v29
	v_mul_f32_e32 v26, v22, v26
	v_mul_f32_e32 v27, v23, v27
	v_mul_f32_e32 v32, v20, v32
	v_mul_f32_e32 v33, v21, v33
	v_mul_f32_e32 v30, v22, v30
	v_mul_f32_e32 v31, v23, v31
	v_mul_f32_e32 v36, v20, v36
	v_mul_f32_e32 v37, v21, v37
	v_mul_f32_e32 v34, v22, v34
	v_mul_f32_e32 v35, v23, v35
	v_mul_f32_e32 v40, v20, v40
	v_mul_f32_e32 v41, v21, v41
	v_mul_f32_e32 v38, v22, v38
	v_mul_f32_e32 v39, v23, v39
	v_mul_f32_e32 v44, v20, v44
	v_mul_f32_e32 v45, v21, v45
	v_mul_f32_e32 v42, v22, v42
	v_mul_f32_e32 v43, v23, v43
	v_mul_f32_e32 v48, v20, v48
	v_mul_f32_e32 v49, v21, v49
	v_mul_f32_e32 v46, v22, v46
	v_mul_f32_e32 v47, v23, v47
	v_rndne_f32_e32 v14, v14
	v_rndne_f32_e32 v15, v15
	v_rndne_f32_e32 v52, v64
	v_rndne_f32_e32 v53, v65
	ds_write2_b32 v25, v50, v51 offset1:1
	ds_write2_b32 v25, v52, v53 offset0:2 offset1:3
	v_rndne_f32_e32 v12, v12
	v_rndne_f32_e32 v13, v13
	v_rndne_f32_e32 v28, v28
	v_rndne_f32_e32 v29, v29
	v_rndne_f32_e32 v26, v26
	v_rndne_f32_e32 v27, v27
	v_rndne_f32_e32 v32, v32
	v_rndne_f32_e32 v33, v33
	v_rndne_f32_e32 v30, v30
	v_rndne_f32_e32 v31, v31
	v_rndne_f32_e32 v36, v36
	v_rndne_f32_e32 v37, v37
	v_rndne_f32_e32 v34, v34
	v_rndne_f32_e32 v35, v35
	v_rndne_f32_e32 v40, v40
	v_rndne_f32_e32 v41, v41
	v_rndne_f32_e32 v38, v38
	v_rndne_f32_e32 v39, v39
	v_rndne_f32_e32 v44, v44
	v_rndne_f32_e32 v45, v45
	v_rndne_f32_e32 v42, v42
	v_rndne_f32_e32 v43, v43
	v_rndne_f32_e32 v48, v48
	v_rndne_f32_e32 v49, v49
	v_rndne_f32_e32 v46, v46
	v_rndne_f32_e32 v47, v47
	ds_write2_b32 v77, v14, v15 offset1:1
	ds_write2_b32 v79, v12, v13 offset1:1
	ds_write2_b32 v81, v28, v29 offset1:1
	ds_write2_b32 v83, v26, v27 offset1:1
	ds_write2_b32 v85, v32, v33 offset1:1
	ds_write2_b32 v87, v30, v31 offset1:1
	ds_write2_b32 v89, v36, v37 offset1:1
	ds_write2_b32 v91, v34, v35 offset1:1
	ds_write2_b32 v92, v40, v41 offset1:1
	ds_write2_b32 v93, v38, v39 offset1:1
	ds_write2_b32 v94, v44, v45 offset1:1
	ds_write2_b32 v95, v42, v43 offset1:1
	ds_write2_b32 v96, v48, v49 offset1:1
	ds_write2_b32 v97, v46, v47 offset1:1
	s_waitcnt lgkmcnt(0)
; #define LAS __attribute__((address_space(3)))
; #define GAS __attribute__((address_space(1)))
; #define LDS_WAIT() asm volatile("s_waitcnt lgkmcnt(0)" ::: "memory")
;     ...
;     for (int kb = 0; kb < D / 64; ++kb) {
; #pragma unroll
;         for (int i = 0; i < 8; ++i) { const int kk = 8 * i + kr; const int k = 64 * kb + kk; const f32x4 v = __builtin_nontemporal_load((const f32x4*)(W + (size_t)k * pitch)) * g[k];
;             LAS float* p = scr + kk * 33 + 4 * (lane & 7); p[0] = __builtin_rintf(v[0] * inv[0]); p[1] = __builtin_rintf(v[1] * inv[1]); p[2] = __builtin_rintf(v[2] * inv[2]); p[3] = __builtin_rintf(v[3] * inv[3]); }
;         LDS_WAIT(); asm volatile("" ::: "memory");
;         const int c = lane & 7;
; #pragma unroll
;         for (int j = 0; j < 4; ++j) { const int n = (lane >> 3) + 8 * j; const LAS float* sp = scr + (8 * c) * 33 + n;
;             u32x2 o;
;             o.x = ((unsigned)(int)sp[0 * 33] & 0xFFu) | (((unsigned)(int)sp[1 * 33] & 0xFFu) << 8) | (((unsigned)(int)sp[2 * 33] & 0xFFu) << 16) | (((unsigned)(int)sp[3 * 33] & 0xFFu) << 24);
;             o.y = ((unsigned)(int)sp[4 * 33] & 0xFFu) | (((unsigned)(int)sp[5 * 33] & 0xFFu) << 8) | (((unsigned)(int)sp[6 * 33] & 0xFFu) << 16) | (((unsigned)(int)sp[7 * 33] & 0xFFu) << 24);
;             *(GAS u32x2*)(dst + (size_t)(n0 + n) * D + 64 * kb + 8 * c) = o; }
;         LDS_WAIT(); asm volatile("" ::: "memory");
	ds_read2_b32 v[12:13], v24 offset1:8
	ds_read2_b32 v[14:15], v24 offset0:33 offset1:41
	ds_read2_b32 v[26:27], v24 offset0:66 offset1:74
	ds_read2_b32 v[28:29], v24 offset0:99 offset1:107
	ds_read2_b32 v[30:31], v24 offset0:132 offset1:140
	ds_read2_b32 v[32:33], v24 offset0:165 offset1:173
	ds_read2_b32 v[34:35], v24 offset0:198 offset1:206
	ds_read2_b32 v[36:37], v24 offset0:231 offset1:239
	ds_read2_b32 v[38:39], v24 offset0:16 offset1:24
	ds_read2_b32 v[40:41], v24 offset0:49 offset1:57
	ds_read2_b32 v[42:43], v24 offset0:82 offset1:90
	ds_read2_b32 v[44:45], v24 offset0:115 offset1:123
	ds_read2_b32 v[46:47], v24 offset0:148 offset1:156
	ds_read2_b32 v[48:49], v24 offset0:181 offset1:189
	ds_read2_b32 v[50:51], v24 offset0:214 offset1:222
	ds_read2_b32 v[52:53], v24 offset0:247 offset1:255
	s_waitcnt lgkmcnt(14)
	v_cvt_i32_f32_e32 v14, v14
	s_waitcnt lgkmcnt(10)
	v_cvt_i32_f32_e32 v32, v32
	v_cvt_i32_f32_e32 v12, v12
	v_cvt_i32_f32_sdwa v26, v26 dst_sel:WORD_1 dst_unused:UNUSED_PAD src0_sel:DWORD
	v_cvt_i32_f32_e32 v30, v30
	s_waitcnt lgkmcnt(9)
	v_cvt_i32_f32_sdwa v34, v34 dst_sel:WORD_1 dst_unused:UNUSED_PAD src0_sel:DWORD
	v_cvt_i32_f32_e32 v15, v15
	v_cvt_i32_f32_e32 v33, v33
	s_waitcnt lgkmcnt(6)
	v_cvt_i32_f32_e32 v40, v40
	s_waitcnt lgkmcnt(2)
	v_cvt_i32_f32_e32 v48, v48
	v_cvt_i32_f32_e32 v41, v41
	v_cvt_i32_f32_e32 v49, v49
	v_cvt_i32_f32_sdwa v28, v28 dst_sel:BYTE_3 dst_unused:UNUSED_PAD src0_sel:DWORD
	v_cvt_i32_f32_sdwa v36, v36 dst_sel:BYTE_3 dst_unused:UNUSED_PAD src0_sel:DWORD
	v_cvt_i32_f32_e32 v13, v13
	v_cvt_i32_f32_sdwa v27, v27 dst_sel:WORD_1 dst_unused:UNUSED_PAD src0_sel:DWORD
	v_cvt_i32_f32_e32 v31, v31
	v_cvt_i32_f32_sdwa v35, v35 dst_sel:WORD_1 dst_unused:UNUSED_PAD src0_sel:DWORD
	v_cvt_i32_f32_e32 v38, v38
	v_cvt_i32_f32_sdwa v42, v42 dst_sel:WORD_1 dst_unused:UNUSED_PAD src0_sel:DWORD
	v_cvt_i32_f32_e32 v46, v46
	s_waitcnt lgkmcnt(1)
	v_cvt_i32_f32_sdwa v50, v50 dst_sel:WORD_1 dst_unused:UNUSED_PAD src0_sel:DWORD
	v_cvt_i32_f32_e32 v39, v39
	v_cvt_i32_f32_sdwa v43, v43 dst_sel:WORD_1 dst_unused:UNUSED_PAD src0_sel:DWORD
	v_cvt_i32_f32_e32 v47, v47
	v_cvt_i32_f32_sdwa v51, v51 dst_sel:WORD_1 dst_unused:UNUSED_PAD src0_sel:DWORD
	v_cvt_i32_f32_sdwa v29, v29 dst_sel:BYTE_3 dst_unused:UNUSED_PAD src0_sel:DWORD
	v_cvt_i32_f32_sdwa v37, v37 dst_sel:BYTE_3 dst_unused:UNUSED_PAD src0_sel:DWORD
	v_cvt_i32_f32_sdwa v44, v44 dst_sel:BYTE_3 dst_unused:UNUSED_PAD src0_sel:DWORD
	s_waitcnt lgkmcnt(0)
	v_cvt_i32_f32_sdwa v52, v52 dst_sel:BYTE_3 dst_unused:UNUSED_PAD src0_sel:DWORD
	v_cvt_i32_f32_sdwa v45, v45 dst_sel:BYTE_3 dst_unused:UNUSED_PAD src0_sel:DWORD
	v_cvt_i32_f32_sdwa v53, v53 dst_sel:BYTE_3 dst_unused:UNUSED_PAD src0_sel:DWORD
	v_lshlrev_b32_e32 v14, 8, v14
	v_lshlrev_b32_e32 v32, 8, v32
	v_and_b32_e32 v26, 0xff0000, v26
	v_and_b32_e32 v34, 0xff0000, v34
	v_lshlrev_b32_e32 v15, 8, v15
	v_lshlrev_b32_e32 v33, 8, v33
	v_lshlrev_b32_e32 v40, 8, v40
	v_lshlrev_b32_e32 v48, 8, v48
	v_lshlrev_b32_e32 v41, 8, v41
	v_lshlrev_b32_e32 v49, 8, v49
	v_perm_b32 v12, v14, v12, s28
	v_perm_b32 v14, v32, v30, s28
	v_and_b32_e32 v27, 0xff0000, v27
	v_and_b32_e32 v35, 0xff0000, v35
	v_and_b32_e32 v42, 0xff0000, v42
	v_and_b32_e32 v50, 0xff0000, v50
	v_and_b32_e32 v43, 0xff0000, v43
	v_and_b32_e32 v51, 0xff0000, v51
	v_perm_b32 v15, v15, v13, s28
	v_perm_b32 v30, v33, v31, s28
	v_perm_b32 v31, v40, v38, s28
	v_perm_b32 v32, v48, v46, s28
	v_perm_b32 v33, v41, v39, s28
	v_perm_b32 v38, v49, v47, s28
	v_or3_b32 v12, v12, v26, v28
	v_or3_b32 v13, v14, v34, v36
	v_or3_b32 v14, v15, v27, v29
	v_or3_b32 v15, v30, v35, v37
	v_or3_b32 v26, v31, v42, v44
	v_or3_b32 v27, v32, v50, v52
	v_or3_b32 v28, v33, v43, v45
	v_or3_b32 v29, v38, v51, v53
	global_store_dwordx2 v[16:17], v[12:13], off
	global_store_dwordx2 v[18:19], v[14:15], off
	global_store_dwordx2 v[58:59], v[26:27], off
	global_store_dwordx2 v[60:61], v[28:29], off
	s_waitcnt lgkmcnt(0)
	v_add_u32_e32 v77, 0x420, v25
	v_add_u32_e32 v79, 0x428, v25
	v_add_u32_e32 v81, 0x840, v25
	v_add_u32_e32 v83, 0x848, v25
	v_add_u32_e32 v85, 0xc60, v25
	v_add_u32_e32 v87, 0xc68, v25
	v_add_u32_e32 v89, 0x1080, v25
	v_add_u32_e32 v91, 0x1088, v25
	v_add_u32_e32 v92, 0x14a0, v25
	v_add_u32_e32 v93, 0x14a8, v25
	v_add_u32_e32 v94, 0x18c0, v25
	v_add_u32_e32 v95, 0x18c8, v25
	v_add_u32_e32 v96, 0x1ce0, v25
	v_add_u32_e32 v97, 0x1ce8, v25
	v_lshl_add_u64 v[16:17], v[10:11], 0, s[26:27]
	v_lshl_add_u64 v[18:19], v[8:9], 0, s[26:27]
	v_lshl_add_u64 v[58:59], v[6:7], 0, s[26:27]
	v_lshl_add_u64 v[60:61], v[4:5], 0, s[26:27]
	v_lshl_add_u64 v[4:5], v[4:5], 0, 64
	v_lshl_add_u64 v[6:7], v[6:7], 0, 64
	v_lshl_add_u64 v[8:9], v[8:9], 0, 64
	v_lshl_add_u64 v[10:11], v[10:11], 0, 64
	s_waitcnt vmcnt(24)
; #define LAS __attribute__((address_space(3)))
; #define GAS __attribute__((address_space(1)))
; #define LDS_WAIT() asm volatile("s_waitcnt lgkmcnt(0)" ::: "memory")
;     ...
;     for (int kb = 0; kb < D / 64; ++kb) {
; #pragma unroll
;         for (int i = 0; i < 8; ++i) { const int kk = 8 * i + kr; const int k = 64 * kb + kk; const f32x4 v = __builtin_nontemporal_load((const f32x4*)(W + (size_t)k * pitch)) * g[k];
;             LAS float* p = scr + kk * 33 + 4 * (lane & 7); p[0] = __builtin_rintf(v[0] * inv[0]); p[1] = __builtin_rintf(v[1] * inv[1]); p[2] = __builtin_rintf(v[2] * inv[2]); p[3] = __builtin_rintf(v[3] * inv[3]); }
;         LDS_WAIT(); asm volatile("" ::: "memory");
;         const int c = lane & 7;
; #pragma unroll
;         for (int j = 0; j < 4; ++j) { const int n = (lane >> 3) + 8 * j; const LAS float* sp = scr + (8 * c) * 33 + n;
;             u32x2 o;
;             o.x = ((unsigned)(int)sp[0 * 33] & 0xFFu) | (((unsigned)(int)sp[1 * 33] & 0xFFu) << 8) | (((unsigned)(int)sp[2 * 33] & 0xFFu) << 16) | (((unsigned)(int)sp[3 * 33] & 0xFFu) << 24);
;             o.y = ((unsigned)(int)sp[4 * 33] & 0xFFu) | (((unsigned)(int)sp[5 * 33] & 0xFFu) << 8) | (((unsigned)(int)sp[6 * 33] & 0xFFu) << 16) | (((unsigned)(int)sp[7 * 33] & 0xFFu) << 24);
;             *(GAS u32x2*)(dst + (size_t)(n0 + n) * D + 64 * kb + 8 * c) = o; }
;         LDS_WAIT(); asm volatile("" ::: "memory");
	v_pk_mul_f32 v[14:15], v[106:107], v[170:171] op_sel_hi:[1,0]
	v_pk_mul_f32 v[12:13], v[108:109], v[170:171] op_sel_hi:[1,0]
	v_mul_f32_e32 v62, v20, v14
	v_mul_f32_e32 v63, v21, v15
	v_mul_f32_e32 v64, v22, v12
	v_mul_f32_e32 v65, v23, v13
	v_pk_mul_f32 v[14:15], v[110:111], v[172:173] op_sel_hi:[1,0]
	v_pk_mul_f32 v[12:13], v[112:113], v[172:173] op_sel_hi:[1,0]
	v_pk_mul_f32 v[26:27], v[116:117], v[174:175] op_sel_hi:[1,0]
	v_pk_mul_f32 v[28:29], v[114:115], v[174:175] op_sel_hi:[1,0]
	v_pk_mul_f32 v[30:31], v[120:121], v[176:177] op_sel_hi:[1,0]
	v_pk_mul_f32 v[32:33], v[118:119], v[176:177] op_sel_hi:[1,0]
	v_pk_mul_f32 v[34:35], v[124:125], v[178:179] op_sel_hi:[1,0]
	v_pk_mul_f32 v[36:37], v[122:123], v[178:179] op_sel_hi:[1,0]
	v_pk_mul_f32 v[38:39], v[128:129], v[180:181] op_sel_hi:[1,0]
	v_pk_mul_f32 v[40:41], v[126:127], v[180:181] op_sel_hi:[1,0]
	v_pk_mul_f32 v[42:43], v[132:133], v[182:183] op_sel_hi:[1,0]
	v_pk_mul_f32 v[44:45], v[130:131], v[182:183] op_sel_hi:[1,0]
	v_pk_mul_f32 v[46:47], v[136:137], v[184:185] op_sel_hi:[1,0]
	v_pk_mul_f32 v[48:49], v[134:135], v[184:185] op_sel_hi:[1,0]
	v_mul_f32_e32 v14, v20, v14
	v_mul_f32_e32 v15, v21, v15
	v_rndne_f32_e32 v50, v62
	v_rndne_f32_e32 v51, v63
	v_mul_f32_e32 v12, v22, v12
	v_mul_f32_e32 v13, v23, v13
	v_mul_f32_e32 v28, v20, v28
	v_mul_f32_e32 v29, v21, v29
	v_mul_f32_e32 v26, v22, v26
	v_mul_f32_e32 v27, v23, v27
	v_mul_f32_e32 v32, v20, v32
	v_mul_f32_e32 v33, v21, v33
	v_mul_f32_e32 v30, v22, v30
	v_mul_f32_e32 v31, v23, v31
	v_mul_f32_e32 v36, v20, v36
	v_mul_f32_e32 v37, v21, v37
	v_mul_f32_e32 v34, v22, v34
	v_mul_f32_e32 v35, v23, v35
	v_mul_f32_e32 v40, v20, v40
	v_mul_f32_e32 v41, v21, v41
	v_mul_f32_e32 v38, v22, v38
	v_mul_f32_e32 v39, v23, v39
	v_mul_f32_e32 v44, v20, v44
	v_mul_f32_e32 v45, v21, v45
	v_mul_f32_e32 v42, v22, v42
	v_mul_f32_e32 v43, v23, v43
	v_mul_f32_e32 v48, v20, v48
	v_mul_f32_e32 v49, v21, v49
	v_mul_f32_e32 v46, v22, v46
	v_mul_f32_e32 v47, v23, v47
	v_rndne_f32_e32 v14, v14
	v_rndne_f32_e32 v15, v15
	v_rndne_f32_e32 v52, v64
	v_rndne_f32_e32 v53, v65
	ds_write2_b32 v25, v50, v51 offset1:1
	ds_write2_b32 v25, v52, v53 offset0:2 offset1:3
	v_rndne_f32_e32 v12, v12
	v_rndne_f32_e32 v13, v13
	v_rndne_f32_e32 v28, v28
	v_rndne_f32_e32 v29, v29
	v_rndne_f32_e32 v26, v26
	v_rndne_f32_e32 v27, v27
	v_rndne_f32_e32 v32, v32
	v_rndne_f32_e32 v33, v33
	v_rndne_f32_e32 v30, v30
	v_rndne_f32_e32 v31, v31
	v_rndne_f32_e32 v36, v36
	v_rndne_f32_e32 v37, v37
	v_rndne_f32_e32 v34, v34
	v_rndne_f32_e32 v35, v35
	v_rndne_f32_e32 v40, v40
	v_rndne_f32_e32 v41, v41
	v_rndne_f32_e32 v38, v38
	v_rndne_f32_e32 v39, v39
	v_rndne_f32_e32 v44, v44
	v_rndne_f32_e32 v45, v45
	v_rndne_f32_e32 v42, v42
	v_rndne_f32_e32 v43, v43
	v_rndne_f32_e32 v48, v48
	v_rndne_f32_e32 v49, v49
	v_rndne_f32_e32 v46, v46
	v_rndne_f32_e32 v47, v47
	ds_write2_b32 v77, v14, v15 offset1:1
	ds_write2_b32 v79, v12, v13 offset1:1
	ds_write2_b32 v81, v28, v29 offset1:1
	ds_write2_b32 v83, v26, v27 offset1:1
	ds_write2_b32 v85, v32, v33 offset1:1
	ds_write2_b32 v87, v30, v31 offset1:1
	ds_write2_b32 v89, v36, v37 offset1:1
	ds_write2_b32 v91, v34, v35 offset1:1
	ds_write2_b32 v92, v40, v41 offset1:1
	ds_write2_b32 v93, v38, v39 offset1:1
	ds_write2_b32 v94, v44, v45 offset1:1
	ds_write2_b32 v95, v42, v43 offset1:1
	ds_write2_b32 v96, v48, v49 offset1:1
	ds_write2_b32 v97, v46, v47 offset1:1
	s_waitcnt lgkmcnt(0)
	ds_read2_b32 v[12:13], v24 offset1:8
	ds_read2_b32 v[14:15], v24 offset0:33 offset1:41
	ds_read2_b32 v[26:27], v24 offset0:66 offset1:74
	ds_read2_b32 v[28:29], v24 offset0:99 offset1:107
	ds_read2_b32 v[30:31], v24 offset0:132 offset1:140
	ds_read2_b32 v[32:33], v24 offset0:165 offset1:173
	ds_read2_b32 v[34:35], v24 offset0:198 offset1:206
	ds_read2_b32 v[36:37], v24 offset0:231 offset1:239
	ds_read2_b32 v[38:39], v24 offset0:16 offset1:24
	ds_read2_b32 v[40:41], v24 offset0:49 offset1:57
	ds_read2_b32 v[42:43], v24 offset0:82 offset1:90
	ds_read2_b32 v[44:45], v24 offset0:115 offset1:123
	ds_read2_b32 v[46:47], v24 offset0:148 offset1:156
	ds_read2_b32 v[48:49], v24 offset0:181 offset1:189
	ds_read2_b32 v[50:51], v24 offset0:214 offset1:222
	ds_read2_b32 v[52:53], v24 offset0:247 offset1:255
	s_waitcnt lgkmcnt(14)
	v_cvt_i32_f32_e32 v14, v14
	s_waitcnt lgkmcnt(10)
	v_cvt_i32_f32_e32 v32, v32
	v_cvt_i32_f32_e32 v12, v12
	v_cvt_i32_f32_sdwa v26, v26 dst_sel:WORD_1 dst_unused:UNUSED_PAD src0_sel:DWORD
	v_cvt_i32_f32_e32 v30, v30
	s_waitcnt lgkmcnt(9)
	v_cvt_i32_f32_sdwa v34, v34 dst_sel:WORD_1 dst_unused:UNUSED_PAD src0_sel:DWORD
	v_cvt_i32_f32_e32 v15, v15
	v_cvt_i32_f32_e32 v33, v33
	s_waitcnt lgkmcnt(6)
	v_cvt_i32_f32_e32 v40, v40
	s_waitcnt lgkmcnt(2)
	v_cvt_i32_f32_e32 v48, v48
	v_cvt_i32_f32_e32 v41, v41
	v_cvt_i32_f32_e32 v49, v49
	v_cvt_i32_f32_sdwa v28, v28 dst_sel:BYTE_3 dst_unused:UNUSED_PAD src0_sel:DWORD
	v_cvt_i32_f32_sdwa v36, v36 dst_sel:BYTE_3 dst_unused:UNUSED_PAD src0_sel:DWORD
	v_cvt_i32_f32_e32 v13, v13
	v_cvt_i32_f32_sdwa v27, v27 dst_sel:WORD_1 dst_unused:UNUSED_PAD src0_sel:DWORD
	v_cvt_i32_f32_e32 v31, v31
	v_cvt_i32_f32_sdwa v35, v35 dst_sel:WORD_1 dst_unused:UNUSED_PAD src0_sel:DWORD
	v_cvt_i32_f32_e32 v38, v38
	v_cvt_i32_f32_sdwa v42, v42 dst_sel:WORD_1 dst_unused:UNUSED_PAD src0_sel:DWORD
	v_cvt_i32_f32_e32 v46, v46
	s_waitcnt lgkmcnt(1)
	v_cvt_i32_f32_sdwa v50, v50 dst_sel:WORD_1 dst_unused:UNUSED_PAD src0_sel:DWORD
	v_cvt_i32_f32_e32 v39, v39
	v_cvt_i32_f32_sdwa v43, v43 dst_sel:WORD_1 dst_unused:UNUSED_PAD src0_sel:DWORD
	v_cvt_i32_f32_e32 v47, v47
	v_cvt_i32_f32_sdwa v51, v51 dst_sel:WORD_1 dst_unused:UNUSED_PAD src0_sel:DWORD
	v_cvt_i32_f32_sdwa v29, v29 dst_sel:BYTE_3 dst_unused:UNUSED_PAD src0_sel:DWORD
	v_cvt_i32_f32_sdwa v37, v37 dst_sel:BYTE_3 dst_unused:UNUSED_PAD src0_sel:DWORD
	v_cvt_i32_f32_sdwa v44, v44 dst_sel:BYTE_3 dst_unused:UNUSED_PAD src0_sel:DWORD
	s_waitcnt lgkmcnt(0)
; #define LAS __attribute__((address_space(3)))
; #define GAS __attribute__((address_space(1)))
; #define LDS_WAIT() asm volatile("s_waitcnt lgkmcnt(0)" ::: "memory")
;     ...
;     for (int kb = 0; kb < D / 64; ++kb) {
; #pragma unroll
;         for (int i = 0; i < 8; ++i) { const int kk = 8 * i + kr; const int k = 64 * kb + kk; const f32x4 v = __builtin_nontemporal_load((const f32x4*)(W + (size_t)k * pitch)) * g[k];
;             LAS float* p = scr + kk * 33 + 4 * (lane & 7); p[0] = __builtin_rintf(v[0] * inv[0]); p[1] = __builtin_rintf(v[1] * inv[1]); p[2] = __builtin_rintf(v[2] * inv[2]); p[3] = __builtin_rintf(v[3] * inv[3]); }
;         LDS_WAIT(); asm volatile("" ::: "memory");
;         const int c = lane & 7;
; #pragma unroll
;         for (int j = 0; j < 4; ++j) { const int n = (lane >> 3) + 8 * j; const LAS float* sp = scr + (8 * c) * 33 + n;
;             u32x2 o;
;             o.x = ((unsigned)(int)sp[0 * 33] & 0xFFu) | (((unsigned)(int)sp[1 * 33] & 0xFFu) << 8) | (((unsigned)(int)sp[2 * 33] & 0xFFu) << 16) | (((unsigned)(int)sp[3 * 33] & 0xFFu) << 24);
;             o.y = ((unsigned)(int)sp[4 * 33] & 0xFFu) | (((unsigned)(int)sp[5 * 33] & 0xFFu) << 8) | (((unsigned)(int)sp[6 * 33] & 0xFFu) << 16) | (((unsigned)(int)sp[7 * 33] & 0xFFu) << 24);
;             *(GAS u32x2*)(dst + (size_t)(n0 + n) * D + 64 * kb + 8 * c) = o; }
;         LDS_WAIT(); asm volatile("" ::: "memory");
	v_cvt_i32_f32_sdwa v52, v52 dst_sel:BYTE_3 dst_unused:UNUSED_PAD src0_sel:DWORD
	v_cvt_i32_f32_sdwa v45, v45 dst_sel:BYTE_3 dst_unused:UNUSED_PAD src0_sel:DWORD
	v_cvt_i32_f32_sdwa v53, v53 dst_sel:BYTE_3 dst_unused:UNUSED_PAD src0_sel:DWORD
	v_lshlrev_b32_e32 v14, 8, v14
	v_lshlrev_b32_e32 v32, 8, v32
	v_and_b32_e32 v26, 0xff0000, v26
	v_and_b32_e32 v34, 0xff0000, v34
	v_lshlrev_b32_e32 v15, 8, v15
	v_lshlrev_b32_e32 v33, 8, v33
	v_lshlrev_b32_e32 v40, 8, v40
	v_lshlrev_b32_e32 v48, 8, v48
	v_lshlrev_b32_e32 v41, 8, v41
	v_lshlrev_b32_e32 v49, 8, v49
	v_perm_b32 v12, v14, v12, s28
	v_perm_b32 v14, v32, v30, s28
	v_and_b32_e32 v27, 0xff0000, v27
	v_and_b32_e32 v35, 0xff0000, v35
	v_and_b32_e32 v42, 0xff0000, v42
	v_and_b32_e32 v50, 0xff0000, v50
	v_and_b32_e32 v43, 0xff0000, v43
	v_and_b32_e32 v51, 0xff0000, v51
	v_perm_b32 v15, v15, v13, s28
	v_perm_b32 v30, v33, v31, s28
	v_perm_b32 v31, v40, v38, s28
	v_perm_b32 v32, v48, v46, s28
	v_perm_b32 v33, v41, v39, s28
	v_perm_b32 v38, v49, v47, s28
	v_or3_b32 v12, v12, v26, v28
	v_or3_b32 v13, v14, v34, v36
	v_or3_b32 v14, v15, v27, v29
	v_or3_b32 v15, v30, v35, v37
	v_or3_b32 v26, v31, v42, v44
	v_or3_b32 v27, v32, v50, v52
	v_or3_b32 v28, v33, v43, v45
	v_or3_b32 v29, v38, v51, v53
	global_store_dwordx2 v[16:17], v[12:13], off
	global_store_dwordx2 v[18:19], v[14:15], off
	global_store_dwordx2 v[58:59], v[26:27], off
	global_store_dwordx2 v[60:61], v[28:29], off
	s_waitcnt lgkmcnt(0)
	v_add_u32_e32 v77, 0x420, v25
	v_add_u32_e32 v79, 0x428, v25
	v_add_u32_e32 v81, 0x840, v25
	v_add_u32_e32 v83, 0x848, v25
	v_add_u32_e32 v85, 0xc60, v25
	v_add_u32_e32 v87, 0xc68, v25
	v_add_u32_e32 v89, 0x1080, v25
	v_add_u32_e32 v91, 0x1088, v25
	v_add_u32_e32 v92, 0x14a0, v25
	v_add_u32_e32 v93, 0x14a8, v25
	v_add_u32_e32 v94, 0x18c0, v25
	v_add_u32_e32 v95, 0x18c8, v25
	v_add_u32_e32 v96, 0x1ce0, v25
	v_add_u32_e32 v97, 0x1ce8, v25
	v_lshl_add_u64 v[16:17], v[10:11], 0, s[26:27]
	v_lshl_add_u64 v[18:19], v[8:9], 0, s[26:27]
	v_lshl_add_u64 v[58:59], v[6:7], 0, s[26:27]
	v_lshl_add_u64 v[60:61], v[4:5], 0, s[26:27]
	v_lshl_add_u64 v[4:5], v[4:5], 0, 64
	v_lshl_add_u64 v[6:7], v[6:7], 0, 64
	v_lshl_add_u64 v[8:9], v[8:9], 0, 64
	v_lshl_add_u64 v[10:11], v[10:11], 0, 64
	s_waitcnt vmcnt(8)
	v_pk_mul_f32 v[14:15], v[138:139], v[186:187] op_sel_hi:[1,0]
	v_pk_mul_f32 v[12:13], v[140:141], v[186:187] op_sel_hi:[1,0]
	v_mul_f32_e32 v62, v20, v14
	v_mul_f32_e32 v63, v21, v15
	v_mul_f32_e32 v64, v22, v12
	v_mul_f32_e32 v65, v23, v13
	v_pk_mul_f32 v[14:15], v[142:143], v[188:189] op_sel_hi:[1,0]
	v_pk_mul_f32 v[12:13], v[144:145], v[188:189] op_sel_hi:[1,0]
	v_pk_mul_f32 v[26:27], v[148:149], v[190:191] op_sel_hi:[1,0]
	v_pk_mul_f32 v[28:29], v[146:147], v[190:191] op_sel_hi:[1,0]
	v_pk_mul_f32 v[30:31], v[152:153], v[192:193] op_sel_hi:[1,0]
	v_pk_mul_f32 v[32:33], v[150:151], v[192:193] op_sel_hi:[1,0]
	v_pk_mul_f32 v[34:35], v[156:157], v[194:195] op_sel_hi:[1,0]
	v_pk_mul_f32 v[36:37], v[154:155], v[194:195] op_sel_hi:[1,0]
	v_pk_mul_f32 v[38:39], v[160:161], v[196:197] op_sel_hi:[1,0]
	v_pk_mul_f32 v[40:41], v[158:159], v[196:197] op_sel_hi:[1,0]
	v_pk_mul_f32 v[42:43], v[164:165], v[198:199] op_sel_hi:[1,0]
	v_pk_mul_f32 v[44:45], v[162:163], v[198:199] op_sel_hi:[1,0]
	v_pk_mul_f32 v[46:47], v[168:169], v[200:201] op_sel_hi:[1,0]
	v_pk_mul_f32 v[48:49], v[166:167], v[200:201] op_sel_hi:[1,0]
	v_mul_f32_e32 v14, v20, v14
	v_mul_f32_e32 v15, v21, v15
	v_rndne_f32_e32 v50, v62
	v_rndne_f32_e32 v51, v63
	v_mul_f32_e32 v12, v22, v12
	v_mul_f32_e32 v13, v23, v13
	v_mul_f32_e32 v28, v20, v28
	v_mul_f32_e32 v29, v21, v29
	v_mul_f32_e32 v26, v22, v26
	v_mul_f32_e32 v27, v23, v27
	v_mul_f32_e32 v32, v20, v32
	v_mul_f32_e32 v33, v21, v33
	v_mul_f32_e32 v30, v22, v30
	v_mul_f32_e32 v31, v23, v31
	v_mul_f32_e32 v36, v20, v36
	v_mul_f32_e32 v37, v21, v37
	v_mul_f32_e32 v34, v22, v34
	v_mul_f32_e32 v35, v23, v35
	v_mul_f32_e32 v40, v20, v40
	v_mul_f32_e32 v41, v21, v41
	v_mul_f32_e32 v38, v22, v38
	v_mul_f32_e32 v39, v23, v39
	v_mul_f32_e32 v44, v20, v44
	v_mul_f32_e32 v45, v21, v45
	v_mul_f32_e32 v42, v22, v42
	v_mul_f32_e32 v43, v23, v43
	v_mul_f32_e32 v48, v20, v48
	v_mul_f32_e32 v49, v21, v49
	v_mul_f32_e32 v46, v22, v46
	v_mul_f32_e32 v47, v23, v47
	v_rndne_f32_e32 v14, v14
	v_rndne_f32_e32 v15, v15
	v_rndne_f32_e32 v52, v64
	v_rndne_f32_e32 v53, v65
	ds_write2_b32 v25, v50, v51 offset1:1
	ds_write2_b32 v25, v52, v53 offset0:2 offset1:3
	v_rndne_f32_e32 v12, v12
	v_rndne_f32_e32 v13, v13
	v_rndne_f32_e32 v28, v28
	v_rndne_f32_e32 v29, v29
	v_rndne_f32_e32 v26, v26
	v_rndne_f32_e32 v27, v27
	v_rndne_f32_e32 v32, v32
	v_rndne_f32_e32 v33, v33
	v_rndne_f32_e32 v30, v30
	v_rndne_f32_e32 v31, v31
	v_rndne_f32_e32 v36, v36
	v_rndne_f32_e32 v37, v37
	v_rndne_f32_e32 v34, v34
	v_rndne_f32_e32 v35, v35
	v_rndne_f32_e32 v40, v40
	v_rndne_f32_e32 v41, v41
	v_rndne_f32_e32 v38, v38
	v_rndne_f32_e32 v39, v39
	v_rndne_f32_e32 v44, v44
	v_rndne_f32_e32 v45, v45
	v_rndne_f32_e32 v42, v42
	v_rndne_f32_e32 v43, v43
	v_rndne_f32_e32 v48, v48
	v_rndne_f32_e32 v49, v49
	v_rndne_f32_e32 v46, v46
	v_rndne_f32_e32 v47, v47
	ds_write2_b32 v77, v14, v15 offset1:1
	ds_write2_b32 v79, v12, v13 offset1:1
	ds_write2_b32 v81, v28, v29 offset1:1
	ds_write2_b32 v83, v26, v27 offset1:1
	ds_write2_b32 v85, v32, v33 offset1:1
	ds_write2_b32 v87, v30, v31 offset1:1
	ds_write2_b32 v89, v36, v37 offset1:1
	ds_write2_b32 v91, v34, v35 offset1:1
	ds_write2_b32 v92, v40, v41 offset1:1
	ds_write2_b32 v93, v38, v39 offset1:1
	ds_write2_b32 v94, v44, v45 offset1:1
	ds_write2_b32 v95, v42, v43 offset1:1
	ds_write2_b32 v96, v48, v49 offset1:1
	ds_write2_b32 v97, v46, v47 offset1:1
	s_waitcnt lgkmcnt(0)
; #define LAS __attribute__((address_space(3)))
; #define GAS __attribute__((address_space(1)))
; #define LDS_WAIT() asm volatile("s_waitcnt lgkmcnt(0)" ::: "memory")
;     ...
;         LDS_WAIT(); asm volatile("" ::: "memory");
;         const int c = lane & 7;
; #pragma unroll
;         for (int j = 0; j < 4; ++j) { const int n = (lane >> 3) + 8 * j; const LAS float* sp = scr + (8 * c) * 33 + n;
;             u32x2 o;
;             o.x = ((unsigned)(int)sp[0 * 33] & 0xFFu) | (((unsigned)(int)sp[1 * 33] & 0xFFu) << 8) | (((unsigned)(int)sp[2 * 33] & 0xFFu) << 16) | (((unsigned)(int)sp[3 * 33] & 0xFFu) << 24);
;             o.y = ((unsigned)(int)sp[4 * 33] & 0xFFu) | (((unsigned)(int)sp[5 * 33] & 0xFFu) << 8) | (((unsigned)(int)sp[6 * 33] & 0xFFu) << 16) | (((unsigned)(int)sp[7 * 33] & 0xFFu) << 24);
;             *(GAS u32x2*)(dst + (size_t)(n0 + n) * D + 64 * kb + 8 * c) = o; }
;         LDS_WAIT(); asm volatile("" ::: "memory");
	ds_read2_b32 v[12:13], v24 offset1:8
	ds_read2_b32 v[14:15], v24 offset0:33 offset1:41
	ds_read2_b32 v[26:27], v24 offset0:66 offset1:74
	ds_read2_b32 v[28:29], v24 offset0:99 offset1:107
	ds_read2_b32 v[30:31], v24 offset0:132 offset1:140
	ds_read2_b32 v[32:33], v24 offset0:165 offset1:173
	ds_read2_b32 v[34:35], v24 offset0:198 offset1:206
	ds_read2_b32 v[36:37], v24 offset0:231 offset1:239
	ds_read2_b32 v[38:39], v24 offset0:16 offset1:24
	ds_read2_b32 v[40:41], v24 offset0:49 offset1:57
	ds_read2_b32 v[42:43], v24 offset0:82 offset1:90
	ds_read2_b32 v[44:45], v24 offset0:115 offset1:123
	ds_read2_b32 v[46:47], v24 offset0:148 offset1:156
	ds_read2_b32 v[48:49], v24 offset0:181 offset1:189
	ds_read2_b32 v[50:51], v24 offset0:214 offset1:222
	ds_read2_b32 v[52:53], v24 offset0:247 offset1:255
	s_waitcnt lgkmcnt(14)
	v_cvt_i32_f32_e32 v14, v14
	s_waitcnt lgkmcnt(10)
	v_cvt_i32_f32_e32 v32, v32
	v_cvt_i32_f32_e32 v12, v12
	v_cvt_i32_f32_sdwa v26, v26 dst_sel:WORD_1 dst_unused:UNUSED_PAD src0_sel:DWORD
	v_cvt_i32_f32_e32 v30, v30
	s_waitcnt lgkmcnt(9)
	v_cvt_i32_f32_sdwa v34, v34 dst_sel:WORD_1 dst_unused:UNUSED_PAD src0_sel:DWORD
	v_cvt_i32_f32_e32 v15, v15
	v_cvt_i32_f32_e32 v33, v33
	s_waitcnt lgkmcnt(6)
	v_cvt_i32_f32_e32 v40, v40
	s_waitcnt lgkmcnt(2)
	v_cvt_i32_f32_e32 v48, v48
	v_cvt_i32_f32_e32 v41, v41
	v_cvt_i32_f32_e32 v49, v49
	v_cvt_i32_f32_sdwa v28, v28 dst_sel:BYTE_3 dst_unused:UNUSED_PAD src0_sel:DWORD
	v_cvt_i32_f32_sdwa v36, v36 dst_sel:BYTE_3 dst_unused:UNUSED_PAD src0_sel:DWORD
	v_cvt_i32_f32_e32 v13, v13
	v_cvt_i32_f32_sdwa v27, v27 dst_sel:WORD_1 dst_unused:UNUSED_PAD src0_sel:DWORD
	v_cvt_i32_f32_e32 v31, v31
	v_cvt_i32_f32_sdwa v35, v35 dst_sel:WORD_1 dst_unused:UNUSED_PAD src0_sel:DWORD
	v_cvt_i32_f32_e32 v38, v38
	v_cvt_i32_f32_sdwa v42, v42 dst_sel:WORD_1 dst_unused:UNUSED_PAD src0_sel:DWORD
	v_cvt_i32_f32_e32 v46, v46
	s_waitcnt lgkmcnt(1)
	v_cvt_i32_f32_sdwa v50, v50 dst_sel:WORD_1 dst_unused:UNUSED_PAD src0_sel:DWORD
	v_cvt_i32_f32_e32 v39, v39
	v_cvt_i32_f32_sdwa v43, v43 dst_sel:WORD_1 dst_unused:UNUSED_PAD src0_sel:DWORD
	v_cvt_i32_f32_e32 v47, v47
	v_cvt_i32_f32_sdwa v51, v51 dst_sel:WORD_1 dst_unused:UNUSED_PAD src0_sel:DWORD
	v_cvt_i32_f32_sdwa v29, v29 dst_sel:BYTE_3 dst_unused:UNUSED_PAD src0_sel:DWORD
	v_cvt_i32_f32_sdwa v37, v37 dst_sel:BYTE_3 dst_unused:UNUSED_PAD src0_sel:DWORD
	v_cvt_i32_f32_sdwa v44, v44 dst_sel:BYTE_3 dst_unused:UNUSED_PAD src0_sel:DWORD
	s_waitcnt lgkmcnt(0)
	v_cvt_i32_f32_sdwa v52, v52 dst_sel:BYTE_3 dst_unused:UNUSED_PAD src0_sel:DWORD
	v_cvt_i32_f32_sdwa v45, v45 dst_sel:BYTE_3 dst_unused:UNUSED_PAD src0_sel:DWORD
	v_cvt_i32_f32_sdwa v53, v53 dst_sel:BYTE_3 dst_unused:UNUSED_PAD src0_sel:DWORD
	v_lshlrev_b32_e32 v14, 8, v14
	v_lshlrev_b32_e32 v32, 8, v32
	v_and_b32_e32 v26, 0xff0000, v26
	v_and_b32_e32 v34, 0xff0000, v34
	v_lshlrev_b32_e32 v15, 8, v15
	v_lshlrev_b32_e32 v33, 8, v33
	v_lshlrev_b32_e32 v40, 8, v40
	v_lshlrev_b32_e32 v48, 8, v48
	v_lshlrev_b32_e32 v41, 8, v41
	v_lshlrev_b32_e32 v49, 8, v49
	v_perm_b32 v12, v14, v12, s28
	v_perm_b32 v14, v32, v30, s28
	v_and_b32_e32 v27, 0xff0000, v27
	v_and_b32_e32 v35, 0xff0000, v35
	v_and_b32_e32 v42, 0xff0000, v42
	v_and_b32_e32 v50, 0xff0000, v50
	v_and_b32_e32 v43, 0xff0000, v43
	v_and_b32_e32 v51, 0xff0000, v51
	v_perm_b32 v15, v15, v13, s28
	v_perm_b32 v30, v33, v31, s28
	v_perm_b32 v31, v40, v38, s28
	v_perm_b32 v32, v48, v46, s28
	v_perm_b32 v33, v41, v39, s28
	v_perm_b32 v38, v49, v47, s28
	v_or3_b32 v12, v12, v26, v28
	v_or3_b32 v13, v14, v34, v36
	v_or3_b32 v14, v15, v27, v29
	v_or3_b32 v15, v30, v35, v37
	v_or3_b32 v26, v31, v42, v44
	v_or3_b32 v27, v32, v50, v52
	v_or3_b32 v28, v33, v43, v45
	v_or3_b32 v29, v38, v51, v53
	global_store_dwordx2 v[16:17], v[12:13], off
	global_store_dwordx2 v[18:19], v[14:15], off
	global_store_dwordx2 v[58:59], v[26:27], off
	global_store_dwordx2 v[60:61], v[28:29], off
	s_waitcnt lgkmcnt(0)
